# flat->global in GEMM epilogues; PP GEMM spread over all 256 WGs in dense-up phase
# speedup vs baseline: 1.0077x; 1.0077x over previous
; #define GAS __attribute__((address_space(1)))
; template <int MODE, int KL>
; __device__ __forceinline__ void p0_cvt_item(const float* W, int K, int N, unsigned char* WT, int il, int which, int item, int lane, const float* gk, float scale, int ldk, int koff) {
;     const int nblk = N >> 6, kb = item / nblk, nb = item - kb * nblk, nq = lane & 15, kr = lane >> 4, k0 = 4 * KL * kb + KL * kr, n0 = 64 * nb + 4 * nq;
;     const GAS f32x4* src = (const GAS f32x4*)(W + (size_t)k0 * N + n0);
;     f32x4 v[KL];
; #pragma unroll
;     for (int i = 0; i < KL; ++i) v[i] = src[(size_t)i * (N >> 2)];
;     if (MODE == 1) {
; #pragma unroll
;         for (int q = 0; q < KL / 4; ++q) { const f32x4 g = *(const GAS f32x4*)(gk + k0 + 4 * q); v[4 * q] *= g.x; v[4 * q + 1] *= g.y; v[4 * q + 2] *= g.z; v[4 * q + 3] *= g.w; } }
;     if (MODE == 2) {
; #pragma unroll
;         for (int i = 0; i < KL; ++i) v[i] *= scale; }
; #pragma unroll
;     for (int c = 0; c < 4; ++c) { const int n = n0 + c, row = il ? ((n >> 4) * 32 + which * 16 + (n & 15)) : n;
;         if (MODE == 2) { GAS v4u* dst = (GAS v4u*)(WT + (size_t)row * ldk + koff + k0);
; #pragma unroll
;             for (int q = 0; q < KL / 16; ++q) { v4u o;
;                 o.x = pg8::pk4_fp8(v[16 * q][c], v[16 * q + 1][c], v[16 * q + 2][c], v[16 * q + 3][c]);     o.y = pg8::pk4_fp8(v[16 * q + 4][c], v[16 * q + 5][c], v[16 * q + 6][c], v[16 * q + 7][c]);
;                 o.z = pg8::pk4_fp8(v[16 * q + 8][c], v[16 * q + 9][c], v[16 * q + 10][c], v[16 * q + 11][c]); o.w = pg8::pk4_fp8(v[16 * q + 12][c], v[16 * q + 13][c], v[16 * q + 14][c], v[16 * q + 15][c]);
;                 dst[q] = o; } }
;         else { GAS v4u* dst = (GAS v4u*)(WT + ((size_t)row * ldk + koff + k0) * 2);
; #pragma unroll
;             for (int q = 0; q < KL / 8; ++q) { v4u o;
;                 if (MODE == 1) { o.x = pg8::pk_f16(v[8 * q][c], v[8 * q + 1][c]); o.y = pg8::pk_f16(v[8 * q + 2][c], v[8 * q + 3][c]); o.z = pg8::pk_f16(v[8 * q + 4][c], v[8 * q + 5][c]); o.w = pg8::pk_f16(v[8 * q + 6][c], v[8 * q + 7][c]); }
;                 else { o.x = pk2(v[8 * q][c], v[8 * q + 1][c]); o.y = pk2(v[8 * q + 2][c], v[8 * q + 3][c]); o.z = pk2(v[8 * q + 4][c], v[8 * q + 5][c]); o.w = pk2(v[8 * q + 6][c], v[8 * q + 7][c]); }
;                 dst[q] = o; } } }
; }
; __device__ __forceinline__ void moe_cvt_tile(const Args& a, int set, int id, int lane) {
.LBB0_137:
	s_mul_hi_i32 s0, s3, 0x92492493
	s_add_i32 s0, s0, s3
	s_lshr_b32 s1, s0, 31
	s_ashr_i32 s7, s0, 8
	s_add_i32 s7, s7, s1
	s_mul_i32 s0, s7, 0xfffffe40
	s_add_i32 s6, s3, s0
	s_cmpk_gt_i32 s3, 0x1bff
	s_mov_b64 s[0:1], -1
	s_cbranch_scc0 .LBB0_139
	v_mov_b64_e32 v[0:1], s[66:67]
	global_load_dwordx2 v[2:3], v[0:1], off offset:152
	global_load_dwordx2 v[74:75], v[0:1], off offset:192
	s_ashr_i32 s0, s6, 31
	s_lshr_b32 s0, s0, 28
	s_add_i32 s0, s6, s0
	s_ashr_i32 s0, s0, 4
	s_mul_i32 s1, s7, 0x7000
	v_lshl_add_u32 v76, s0, 7, v148
	s_lshl_b32 s0, s0, 10
	s_add_i32 s0, s0, s1
	s_sub_i32 s0, s2, s0
	s_add_i32 s8, s5, s7
	v_ashrrev_i32_e32 v77, 31, v76
	v_add_u32_e32 v152, s0, v151
	v_lshlrev_b64 v[0:1], 12, v[76:77]
	v_add_u32_e32 v68, 0xfffe8000, v152
	v_ashrrev_i32_e32 v69, 31, v68
	v_mov_b32_e32 v64, v81
	v_mov_b32_e32 v65, v81
	v_mov_b32_e32 v66, v81
	v_mov_b32_e32 v67, v81
	s_waitcnt vmcnt(0) lgkmcnt(0)
	v_mad_i64_i32 v[2:3], s[0:1], s8, v192, v[2:3]
	v_lshl_add_u64 v[0:1], v[2:3], 0, v[0:1]
	v_lshl_add_u64 v[72:73], v[68:69], 2, v[0:1]
	v_add_co_u32_e32 v8, vcc, s50, v72
	s_mov_b32 s0, 0xc000
	s_nop 0
	v_addc_co_u32_e32 v9, vcc, 0, v73, vcc
	v_add_co_u32_e32 v16, vcc, s49, v72
	global_load_dwordx4 v[0:3], v[72:73], off
	s_nop 0
	v_addc_co_u32_e32 v17, vcc, 0, v73, vcc
	v_add_co_u32_e32 v24, vcc, s52, v72
	s_waitcnt vmcnt(0)
	v_pk_mul_f32 v[138:139], v[0:1], s[82:83] op_sel_hi:[1,0]
	v_addc_co_u32_e32 v25, vcc, 0, v73, vcc
	v_add_co_u32_e32 v32, vcc, s33, v72
	s_nop 1
	v_addc_co_u32_e32 v33, vcc, 0, v73, vcc
	v_add_co_u32_e32 v40, vcc, s97, v72
	s_nop 1
	v_addc_co_u32_e32 v41, vcc, 0, v73, vcc
	v_add_co_u32_e32 v48, vcc, s0, v72
	s_mov_b32 s0, 0xe000
	s_nop 0
	v_addc_co_u32_e32 v49, vcc, 0, v73, vcc
	v_add_co_u32_e32 v56, vcc, s0, v72
	v_mad_i64_i32 v[74:75], s[0:1], s8, v193, v[74:75]
	s_nop 0
	v_addc_co_u32_e32 v57, vcc, 0, v73, vcc
	v_add_co_u32_e32 v70, vcc, s53, v72
	v_lshl_add_u64 v[74:75], v[74:75], 0, v[76:77]
	s_nop 0
	v_addc_co_u32_e32 v71, vcc, 0, v73, vcc
	v_add_co_u32_e32 v76, vcc, s70, v72
	s_mov_b64 s[0:1], 0x33f00000
	s_nop 0
	v_addc_co_u32_e32 v77, vcc, 0, v73, vcc
	v_add_co_u32_e32 v86, vcc, s71, v72
	v_lshl_add_u64 v[134:135], v[74:75], 0, s[0:1]
	s_nop 0
	v_addc_co_u32_e32 v87, vcc, 0, v73, vcc
	s_mov_b32 s0, 0x16000
	v_add_co_u32_e32 v94, vcc, s0, v72
	s_mov_b32 s0, 0x18000
	s_nop 0
	v_addc_co_u32_e32 v95, vcc, 0, v73, vcc
	v_add_co_u32_e32 v102, vcc, s0, v72
	s_mov_b32 s0, 0x1a000
	s_nop 0
	v_addc_co_u32_e32 v103, vcc, 0, v73, vcc
	global_load_dwordx4 v[4:7], v[8:9], off offset:-4096
	s_nop 0
	global_load_dwordx4 v[8:11], v[8:9], off
	s_nop 0
	global_load_dwordx4 v[12:15], v[16:17], off offset:-4096
	s_nop 0
	global_load_dwordx4 v[16:19], v[16:17], off
	s_nop 0
	global_load_dwordx4 v[20:23], v[24:25], off offset:-4096
	s_nop 0
	global_load_dwordx4 v[24:27], v[24:25], off
	s_nop 0
	global_load_dwordx4 v[28:31], v[32:33], off offset:-4096
	s_nop 0
	global_load_dwordx4 v[32:35], v[32:33], off
	s_nop 0
	global_load_dwordx4 v[36:39], v[40:41], off offset:-4096
	s_nop 0
	global_load_dwordx4 v[40:43], v[40:41], off
	s_nop 0
	global_load_dwordx4 v[44:47], v[48:49], off offset:-4096
	s_nop 0
	global_load_dwordx4 v[48:51], v[48:49], off
	s_nop 0
	global_load_dwordx4 v[52:55], v[56:57], off offset:-4096
	s_nop 0
	global_load_dwordx4 v[56:59], v[56:57], off
	s_nop 0
	global_load_dwordx4 v[60:63], v[70:71], off offset:-4096
	v_add_co_u32_e32 v114, vcc, s0, v72
	s_mov_b32 s0, 0x1c000
	s_nop 0
	v_addc_co_u32_e32 v115, vcc, 0, v73, vcc
	v_add_co_u32_e32 v122, vcc, s0, v72
	s_mov_b32 s0, 0x1e000
	s_nop 0
	v_addc_co_u32_e32 v123, vcc, 0, v73, vcc
	v_add_co_u32_e32 v130, vcc, s0, v72
	s_mov_b32 s0, 0x1f000
	s_nop 0
	v_addc_co_u32_e32 v131, vcc, 0, v73, vcc
	v_add_co_u32_e32 v104, vcc, s0, v72
	s_movk_i32 s8, 0xe00
	s_nop 0
	v_addc_co_u32_e32 v105, vcc, 0, v73, vcc
	v_mad_i64_i32 v[136:137], s[0:1], v68, s8, v[134:135]
	global_load_dwordx4 v[68:71], v[70:71], off
	s_nop 0
	global_load_dwordx4 v[72:75], v[76:77], off offset:-4096
	s_nop 0
	global_load_dwordx4 v[76:79], v[76:77], off
	s_nop 0
	global_load_dwordx4 v[82:85], v[86:87], off offset:-4096
	s_nop 0
	global_load_dwordx4 v[86:89], v[86:87], off
	s_nop 0
	global_load_dwordx4 v[90:93], v[94:95], off offset:-4096
	s_nop 0
	global_load_dwordx4 v[94:97], v[94:95], off
	s_nop 0
	global_load_dwordx4 v[98:101], v[102:103], off offset:-4096
	global_load_dwordx4 v[106:109], v[102:103], off
	s_nop 0
	global_load_dwordx4 v[102:105], v[104:105], off
	s_nop 0
	global_load_dwordx4 v[110:113], v[114:115], off offset:-4096
	s_nop 0
	global_load_dwordx4 v[114:117], v[114:115], off
	s_nop 0
	global_load_dwordx4 v[118:121], v[122:123], off offset:-4096
	s_nop 0
	global_load_dwordx4 v[122:125], v[122:123], off
	s_nop 0
	global_load_dwordx4 v[126:129], v[130:131], off offset:-4096
	s_nop 0
	global_load_dwordx4 v[130:133], v[130:131], off
	s_waitcnt vmcnt(30)
	v_pk_mul_f32 v[142:143], v[4:5], s[82:83] op_sel_hi:[1,0]
	s_nop 0
	v_cvt_pk_fp8_f32 v64, v138, v142
	s_waitcnt vmcnt(29)
	v_pk_mul_f32 v[0:1], v[8:9], s[82:83] op_sel_hi:[1,0]
	s_waitcnt vmcnt(27)
	v_pk_mul_f32 v[140:141], v[16:17], s[82:83] op_sel_hi:[1,0]
	s_waitcnt vmcnt(26)
	v_pk_mul_f32 v[144:145], v[20:21], s[82:83] op_sel_hi:[1,0]
	v_pk_mul_f32 v[4:5], v[12:13], s[82:83] op_sel_hi:[1,0]
	v_cvt_pk_fp8_f32 v65, v140, v144
	s_waitcnt vmcnt(23)
	v_pk_mul_f32 v[32:33], v[32:33], s[82:83] op_sel_hi:[1,0]
	s_waitcnt vmcnt(22)
	v_pk_mul_f32 v[146:147], v[36:37], s[82:83] op_sel_hi:[1,0]
	s_waitcnt vmcnt(21)
	v_pk_mul_f32 v[16:17], v[40:41], s[82:83] op_sel_hi:[1,0]
	v_cvt_pk_fp8_f32 v66, v32, v146
	s_waitcnt vmcnt(19)
; __device__ __forceinline__ unsigned pk4_fp8(float a, float b, float c, float d) { int w = 0; w = __builtin_amdgcn_cvt_pk_fp8_f32(a, b, w, false); w = __builtin_amdgcn_cvt_pk_fp8_f32(c, d, w, true); return (unsigned)w; }
; #define GAS __attribute__((address_space(1)))
; __device__ __forceinline__ unsigned pk2(float lo, float hi) { return f2bf(lo) | (f2bf(hi) << 16); }
; template <int MODE, int KL>
; __device__ __forceinline__ void p0_cvt_item(const float* W, int K, int N, unsigned char* WT, int il, int which, int item, int lane, const float* gk, float scale, int ldk, int koff) {
;     ...
;     for (int c = 0; c < 4; ++c) { const int n = n0 + c, row = il ? ((n >> 4) * 32 + which * 16 + (n & 15)) : n;
;         if (MODE == 2) { GAS v4u* dst = (GAS v4u*)(WT + (size_t)row * ldk + koff + k0);
; #pragma unroll
;             for (int q = 0; q < KL / 16; ++q) { v4u o;
;                 o.x = pg8::pk4_fp8(v[16 * q][c], v[16 * q + 1][c], v[16 * q + 2][c], v[16 * q + 3][c]);     o.y = pg8::pk4_fp8(v[16 * q + 4][c], v[16 * q + 5][c], v[16 * q + 6][c], v[16 * q + 7][c]);
;                 o.z = pg8::pk4_fp8(v[16 * q + 8][c], v[16 * q + 9][c], v[16 * q + 10][c], v[16 * q + 11][c]); o.w = pg8::pk4_fp8(v[16 * q + 12][c], v[16 * q + 13][c], v[16 * q + 14][c], v[16 * q + 15][c]);
;                 dst[q] = o; } }
;         else { GAS v4u* dst = (GAS v4u*)(WT + ((size_t)row * ldk + koff + k0) * 2);
; #pragma unroll
;             for (int q = 0; q < KL / 8; ++q) { v4u o;
;                 if (MODE == 1) { o.x = pg8::pk_f16(v[8 * q][c], v[8 * q + 1][c]); o.y = pg8::pk_f16(v[8 * q + 2][c], v[8 * q + 3][c]); o.z = pg8::pk_f16(v[8 * q + 4][c], v[8 * q + 5][c]); o.w = pg8::pk_f16(v[8 * q + 6][c], v[8 * q + 7][c]); }
;                 else { o.x = pk2(v[8 * q][c], v[8 * q + 1][c]); o.y = pk2(v[8 * q + 2][c], v[8 * q + 3][c]); o.z = pk2(v[8 * q + 4][c], v[8 * q + 5][c]); o.w = pk2(v[8 * q + 6][c], v[8 * q + 7][c]); }
;                 dst[q] = o; } } }
	v_pk_mul_f32 v[36:37], v[48:49], s[82:83] op_sel_hi:[1,0]
	s_waitcnt vmcnt(18)
	v_pk_mul_f32 v[40:41], v[52:53], s[82:83] op_sel_hi:[1,0]
	v_pk_mul_f32 v[8:9], v[24:25], s[82:83] op_sel_hi:[1,0]
	v_cvt_pk_fp8_f32 v67, v36, v40
	v_pk_mul_f32 v[12:13], v[28:29], s[82:83] op_sel_hi:[1,0]
	v_pk_mul_f32 v[20:21], v[44:45], s[82:83] op_sel_hi:[1,0]
	s_waitcnt vmcnt(17)
	v_pk_mul_f32 v[24:25], v[56:57], s[82:83] op_sel_hi:[1,0]
	s_waitcnt vmcnt(16)
	v_pk_mul_f32 v[28:29], v[60:61], s[82:83] op_sel_hi:[1,0]
	v_cvt_pk_fp8_f32 v64, v0, v4 op_sel:[0,0,1]
	v_cvt_pk_fp8_f32 v65, v8, v12 op_sel:[0,0,1]
	v_cvt_pk_fp8_f32 v66, v16, v20 op_sel:[0,0,1]
	v_cvt_pk_fp8_f32 v67, v24, v28 op_sel:[0,0,1]
	v_mov_b32_e32 v140, v81
	v_mov_b32_e32 v138, v81
	v_cvt_pk_fp8_f32 v138, v33, v147
	global_store_dwordx4 v[136:137], v[64:67], off
	v_mov_b32_e32 v142, v81
	s_waitcnt vmcnt(16)
	v_pk_mul_f32 v[44:45], v[68:69], s[82:83] op_sel_hi:[1,0]
	v_mov_b32_e32 v64, v81
	v_mov_b32_e32 v65, v81
	v_mov_b32_e32 v66, v81
	v_mov_b32_e32 v67, v81
	s_waitcnt vmcnt(15)
	v_pk_mul_f32 v[48:49], v[72:73], s[82:83] op_sel_hi:[1,0]
	s_waitcnt vmcnt(12)
	v_pk_mul_f32 v[52:53], v[86:87], s[82:83] op_sel_hi:[1,0]
	s_waitcnt vmcnt(11)
	v_pk_mul_f32 v[56:57], v[90:91], s[82:83] op_sel_hi:[1,0]
	s_waitcnt vmcnt(8)
	v_pk_mul_f32 v[60:61], v[106:107], s[82:83] op_sel_hi:[1,0]
	s_waitcnt vmcnt(6)
	v_pk_mul_f32 v[68:69], v[110:111], s[82:83] op_sel_hi:[1,0]
	s_waitcnt vmcnt(3)
	v_pk_mul_f32 v[72:73], v[122:123], s[82:83] op_sel_hi:[1,0]
	s_waitcnt vmcnt(2)
	v_pk_mul_f32 v[86:87], v[126:127], s[82:83] op_sel_hi:[1,0]
	v_cvt_pk_fp8_f32 v64, v44, v48
	v_cvt_pk_fp8_f32 v65, v52, v56
	v_cvt_pk_fp8_f32 v66, v60, v68
	v_cvt_pk_fp8_f32 v67, v72, v86
	v_pk_mul_f32 v[106:107], v[76:77], s[82:83] op_sel_hi:[1,0]
	v_pk_mul_f32 v[82:83], v[82:83], s[82:83] op_sel_hi:[1,0]
	v_pk_mul_f32 v[110:111], v[94:95], s[82:83] op_sel_hi:[1,0]
	v_pk_mul_f32 v[122:123], v[98:99], s[82:83] op_sel_hi:[1,0]
	v_pk_mul_f32 v[114:115], v[114:115], s[82:83] op_sel_hi:[1,0]
	v_pk_mul_f32 v[118:119], v[118:119], s[82:83] op_sel_hi:[1,0]
	s_waitcnt vmcnt(1)
	v_pk_mul_f32 v[126:127], v[130:131], s[82:83] op_sel_hi:[1,0]
	v_pk_mul_f32 v[102:103], v[102:103], s[82:83] op_sel_hi:[1,0]
	v_cvt_pk_fp8_f32 v64, v106, v82 op_sel:[0,0,1]
	v_cvt_pk_fp8_f32 v65, v110, v122 op_sel:[0,0,1]
	v_cvt_pk_fp8_f32 v66, v114, v118 op_sel:[0,0,1]
	v_cvt_pk_fp8_f32 v67, v126, v102 op_sel:[0,0,1]
	v_cvt_pk_fp8_f32 v140, v45, v49
	v_cvt_pk_fp8_f32 v142, v61, v69
	v_pk_mul_f32 v[68:69], v[18:19], s[82:83] op_sel_hi:[1,0]
	global_store_dwordx4 v[136:137], v[64:67], off offset:16
	v_mov_b32_e32 v136, v81
	v_cvt_pk_fp8_f32 v136, v139, v143
	v_mov_b32_e32 v139, v81
	v_cvt_pk_fp8_f32 v139, v37, v41
	v_mov_b32_e32 v137, v81
	v_cvt_pk_fp8_f32 v137, v141, v145
	v_mov_b32_e32 v141, v81
	v_mov_b32_e32 v143, v81
	v_cvt_pk_fp8_f32 v141, v53, v57
	v_cvt_pk_fp8_f32 v143, v73, v87
	v_pk_mul_f32 v[64:65], v[2:3], s[82:83] op_sel_hi:[1,0]
	v_pk_mul_f32 v[86:87], v[6:7], s[82:83] op_sel_hi:[1,0]
	v_pk_mul_f32 v[90:91], v[22:23], s[82:83] op_sel_hi:[1,0]
	v_pk_mul_f32 v[72:73], v[34:35], s[82:83] op_sel_hi:[1,0]
	v_pk_mul_f32 v[94:95], v[38:39], s[82:83] op_sel_hi:[1,0]
	v_pk_mul_f32 v[76:77], v[50:51], s[82:83] op_sel_hi:[1,0]
	v_pk_mul_f32 v[98:99], v[54:55], s[82:83] op_sel_hi:[1,0]
	v_mov_b32_e32 v48, v81
	v_mov_b32_e32 v49, v81
	v_mov_b32_e32 v50, v81
	v_mov_b32_e32 v51, v81
	v_cvt_pk_fp8_f32 v136, v1, v5 op_sel:[0,0,1]
	v_cvt_pk_fp8_f32 v139, v25, v29 op_sel:[0,0,1]
	v_pk_mul_f32 v[40:41], v[30:31], s[82:83] op_sel_hi:[1,0]
	v_pk_mul_f32 v[52:53], v[42:43], s[82:83] op_sel_hi:[1,0]
	v_pk_mul_f32 v[56:57], v[46:47], s[82:83] op_sel_hi:[1,0]
	v_pk_mul_f32 v[28:29], v[70:71], s[82:83] op_sel_hi:[1,0]
	v_pk_mul_f32 v[42:43], v[74:75], s[82:83] op_sel_hi:[1,0]
	v_pk_mul_f32 v[4:5], v[84:85], s[82:83] op_sel_hi:[1,0]
	v_pk_mul_f32 v[30:31], v[88:89], s[82:83] op_sel_hi:[1,0]
	v_pk_mul_f32 v[44:45], v[92:93], s[82:83] op_sel_hi:[1,0]
	v_pk_mul_f32 v[32:33], v[108:109], s[82:83] op_sel_hi:[1,0]
	v_pk_mul_f32 v[46:47], v[112:113], s[82:83] op_sel_hi:[1,0]
	v_pk_mul_f32 v[34:35], v[124:125], s[82:83] op_sel_hi:[1,0]
	v_pk_mul_f32 v[36:37], v[128:129], s[82:83] op_sel_hi:[1,0]
	v_cvt_pk_fp8_f32 v140, v107, v83 op_sel:[0,0,1]
	v_cvt_pk_fp8_f32 v48, v64, v86
	v_cvt_pk_fp8_f32 v49, v68, v90
	v_cvt_pk_fp8_f32 v50, v72, v94
	v_cvt_pk_fp8_f32 v51, v76, v98
	v_mov_b32_e32 v82, v81
	v_mov_b32_e32 v83, v81
	v_mov_b32_e32 v84, v81
	v_mov_b32_e32 v85, v81
	v_cvt_pk_fp8_f32 v82, v28, v42
	v_cvt_pk_fp8_f32 v83, v30, v44
	v_cvt_pk_fp8_f32 v84, v32, v46
	v_cvt_pk_fp8_f32 v85, v34, v36
	v_cvt_pk_fp8_f32 v137, v9, v13 op_sel:[0,0,1]
	v_cvt_pk_fp8_f32 v138, v17, v21 op_sel:[0,0,1]
	v_pk_mul_f32 v[20:21], v[10:11], s[82:83] op_sel_hi:[1,0]
	v_pk_mul_f32 v[24:25], v[14:15], s[82:83] op_sel_hi:[1,0]
	v_pk_mul_f32 v[26:27], v[26:27], s[82:83] op_sel_hi:[1,0]
	v_pk_mul_f32 v[58:59], v[58:59], s[82:83] op_sel_hi:[1,0]
	v_pk_mul_f32 v[60:61], v[62:63], s[82:83] op_sel_hi:[1,0]
	v_cvt_pk_fp8_f32 v141, v111, v123 op_sel:[0,0,1]
	v_cvt_pk_fp8_f32 v142, v115, v119 op_sel:[0,0,1]
	v_cvt_pk_fp8_f32 v143, v127, v103 op_sel:[0,0,1]
	v_pk_mul_f32 v[2:3], v[78:79], s[82:83] op_sel_hi:[1,0]
	v_pk_mul_f32 v[6:7], v[96:97], s[82:83] op_sel_hi:[1,0]
	v_pk_mul_f32 v[8:9], v[100:101], s[82:83] op_sel_hi:[1,0]
	v_pk_mul_f32 v[10:11], v[116:117], s[82:83] op_sel_hi:[1,0]
	v_pk_mul_f32 v[12:13], v[120:121], s[82:83] op_sel_hi:[1,0]
	v_pk_mul_f32 v[14:15], v[132:133], s[82:83] op_sel_hi:[1,0]
	v_pk_mul_f32 v[16:17], v[104:105], s[82:83] op_sel_hi:[1,0]
	v_add_u32_e32 v0, 0xfffe8001, v152
	v_cvt_pk_fp8_f32 v48, v20, v24 op_sel:[0,0,1]
	v_cvt_pk_fp8_f32 v49, v26, v40 op_sel:[0,0,1]
	v_cvt_pk_fp8_f32 v50, v52, v56 op_sel:[0,0,1]
	v_cvt_pk_fp8_f32 v51, v58, v60 op_sel:[0,0,1]
	v_mad_i64_i32 v[0:1], s[0:1], v0, s8, v[134:135]
	v_cvt_pk_fp8_f32 v82, v2, v4 op_sel:[0,0,1]
	v_cvt_pk_fp8_f32 v83, v6, v8 op_sel:[0,0,1]
	v_cvt_pk_fp8_f32 v84, v10, v12 op_sel:[0,0,1]
	v_cvt_pk_fp8_f32 v85, v14, v16 op_sel:[0,0,1]
	global_store_dwordx4 v[0:1], v[136:139], off
	global_store_dwordx4 v[0:1], v[140:143], off offset:16
	v_add_u32_e32 v0, 0xfffe8002, v152
	v_mad_i64_i32 v[0:1], s[0:1], v0, s8, v[134:135]
	global_store_dwordx4 v[0:1], v[48:51], off
	global_store_dwordx4 v[0:1], v[82:85], off offset:16
	v_add_u32_e32 v0, 0xfffe8003, v152
	v_mad_i64_i32 v[0:1], s[0:1], v0, s8, v[134:135]
	s_mov_b64 s[0:1], 0
; #define GAS __attribute__((address_space(1)))
; template <int MODE, int KL>
; __device__ __forceinline__ void p0_cvt_item(const float* W, int K, int N, unsigned char* WT, int il, int which, int item, int lane, const float* gk, float scale, int ldk, int koff) {
;     const int nblk = N >> 6, kb = item / nblk, nb = item - kb * nblk, nq = lane & 15, kr = lane >> 4, k0 = 4 * KL * kb + KL * kr, n0 = 64 * nb + 4 * nq;
;     const GAS f32x4* src = (const GAS f32x4*)(W + (size_t)k0 * N + n0);
;     f32x4 v[KL];
; #pragma unroll
;     for (int i = 0; i < KL; ++i) v[i] = src[(size_t)i * (N >> 2)];
;     if (MODE == 1) {
; #pragma unroll
;         for (int q = 0; q < KL / 4; ++q) { const f32x4 g = *(const GAS f32x4*)(gk + k0 + 4 * q); v[4 * q] *= g.x; v[4 * q + 1] *= g.y; v[4 * q + 2] *= g.z; v[4 * q + 3] *= g.w; } }
;     if (MODE == 2) {
; #pragma unroll
;         for (int i = 0; i < KL; ++i) v[i] *= scale; }
; #pragma unroll
; __device__ __forceinline__ void moe_cvt_tile(const Args& a, int set, int id, int lane) {
;     const int j = id / MT_PER, item = id - j * MT_PER;
;     if (j < 16) { const int e = set * 8 + (j & 7), wh = j >> 3;
;         p0_cvt_item<2, 32>(a.in[17 + wh] + (size_t)e * D * FE, D, FE, a.ws + W_13M + (size_t)e * 2 * FE * D, 1, wh, item, lane, nullptr, 32.f, D, 0); }
.LBB0_139:
	s_andn2_b64 vcc, exec, s[0:1]
	s_cbranch_vccnz .LBB0_136
	s_and_b32 s0, s7, 7
	s_or_b32 s10, s0, s4
	s_ashr_i32 s0, s7, 3
	s_ashr_i32 s1, s0, 31
	s_lshl_b64 s[8:9], s[0:1], 3
	s_add_u32 s8, s66, s8
	s_addc_u32 s9, s67, s9
	v_mov_b64_e32 v[0:1], s[8:9]
	global_load_dwordx2 v[0:1], v[0:1], off offset:136
	v_mov_b64_e32 v[2:3], s[66:67]
	global_load_dwordx2 v[2:3], v[2:3], off offset:192
	s_mul_hi_i32 s1, s6, 0x92492493
	s_add_i32 s1, s1, s6
	s_lshr_b32 s6, s1, 31
	s_ashr_i32 s1, s1, 5
	s_add_i32 s1, s1, s6
	s_mulk_i32 s7, 0x1c0
	s_mul_i32 s6, s1, 0xffffffc8
	v_lshl_add_u32 v98, s1, 7, v148
	s_sub_i32 s1, s6, s7
	s_mul_i32 s62, s10, 0xe00000
	s_add_i32 s1, s3, s1
	v_lshl_or_b32 v100, s1, 6, v149
	s_movk_i32 s1, 0x3800
	v_ashrrev_i32_e32 v101, 31, v100
	v_ashrrev_i32_e32 v99, 31, v98
	s_waitcnt vmcnt(0) lgkmcnt(0)
	v_lshl_add_u64 v[0:1], v[0:1], 0, s[62:63]
	v_mad_i64_i32 v[0:1], s[6:7], v98, s1, v[0:1]
	v_lshl_add_u64 v[112:113], v[100:101], 2, v[0:1]
	s_movk_i32 s1, 0x3000
	v_add_co_u32_e32 v4, vcc, s1, v112
	s_movk_i32 s1, 0x7000
	s_nop 0
	v_addc_co_u32_e32 v5, vcc, 0, v113, vcc
	v_add_co_u32_e32 v8, vcc, s1, v112
	s_mov_b32 s1, 0xe000
	s_nop 0
	v_addc_co_u32_e32 v9, vcc, 0, v113, vcc
	v_add_co_u32_e32 v12, vcc, s97, v112
	s_mul_i32 s62, s10, 0x700000
	s_nop 0
	v_addc_co_u32_e32 v13, vcc, 0, v113, vcc
	v_add_co_u32_e32 v16, vcc, s1, v112
	s_mov_b32 s1, 0x11000
	s_nop 0
	v_addc_co_u32_e32 v17, vcc, 0, v113, vcc
	v_add_co_u32_e32 v20, vcc, s1, v112
	s_mov_b32 s1, 0x15000
	s_nop 0
	v_addc_co_u32_e32 v21, vcc, 0, v113, vcc
	v_add_co_u32_e32 v24, vcc, s1, v112
	s_mov_b32 s1, 0x18000
	s_nop 0
	v_addc_co_u32_e32 v25, vcc, 0, v113, vcc
	v_add_co_u32_e32 v28, vcc, s1, v112
	s_mov_b32 s1, 0x1c000
	s_nop 0
	v_addc_co_u32_e32 v29, vcc, 0, v113, vcc
	v_add_co_u32_e32 v32, vcc, s1, v112
	s_mov_b32 s1, 0x1f000
	s_nop 0
	v_addc_co_u32_e32 v33, vcc, 0, v113, vcc
	v_add_co_u32_e32 v36, vcc, s1, v112
	s_mov_b32 s1, 0x23000
	s_nop 0
	v_addc_co_u32_e32 v37, vcc, 0, v113, vcc
	v_add_co_u32_e32 v40, vcc, s1, v112
	s_mov_b32 s1, 0x26000
	s_nop 0
	v_addc_co_u32_e32 v41, vcc, 0, v113, vcc
	v_add_co_u32_e32 v44, vcc, s1, v112
	v_lshl_add_u64 v[110:111], v[2:3], 0, s[62:63]
	s_nop 0
	v_addc_co_u32_e32 v45, vcc, 0, v113, vcc
	global_load_dwordx4 v[0:3], v[112:113], off
	s_nop 0
	global_load_dwordx4 v[4:7], v[4:5], off offset:2048
	s_nop 0
	global_load_dwordx4 v[8:11], v[8:9], off
	s_nop 0
	global_load_dwordx4 v[12:15], v[12:13], off offset:2048
	s_nop 0
	global_load_dwordx4 v[16:19], v[16:17], off
	s_nop 0
	global_load_dwordx4 v[20:23], v[20:21], off offset:2048
	s_nop 0
	global_load_dwordx4 v[24:27], v[24:25], off
	s_nop 0
	global_load_dwordx4 v[28:31], v[28:29], off offset:2048
	s_nop 0
	global_load_dwordx4 v[32:35], v[32:33], off
	s_nop 0
	global_load_dwordx4 v[36:39], v[36:37], off offset:2048
	s_nop 0
	global_load_dwordx4 v[40:43], v[40:41], off
	s_nop 0
	global_load_dwordx4 v[44:47], v[44:45], off offset:2048
	s_mov_b32 s1, 0x2a000
	v_add_co_u32_e32 v48, vcc, s1, v112
	s_mov_b32 s1, 0x2d000
	s_nop 0
	v_addc_co_u32_e32 v49, vcc, 0, v113, vcc
	v_add_co_u32_e32 v52, vcc, s1, v112
	s_mov_b32 s1, 0x31000
	s_nop 0
	v_addc_co_u32_e32 v53, vcc, 0, v113, vcc
	v_add_co_u32_e32 v56, vcc, s1, v112
	s_mov_b32 s1, 0x34000
	s_nop 0
	v_addc_co_u32_e32 v57, vcc, 0, v113, vcc
	v_add_co_u32_e32 v60, vcc, s1, v112
	s_mov_b32 s1, 0x38000
	s_nop 0
	v_addc_co_u32_e32 v61, vcc, 0, v113, vcc
	v_add_co_u32_e32 v64, vcc, s1, v112
	s_mov_b32 s1, 0x3b000
	s_nop 0
	v_addc_co_u32_e32 v65, vcc, 0, v113, vcc
	v_add_co_u32_e32 v68, vcc, s1, v112
	s_mov_b32 s1, 0x3f000
	s_nop 0
	v_addc_co_u32_e32 v69, vcc, 0, v113, vcc
	v_add_co_u32_e32 v72, vcc, s1, v112
	s_mov_b32 s1, 0x42000
	s_nop 0
	v_addc_co_u32_e32 v73, vcc, 0, v113, vcc
	v_add_co_u32_e32 v76, vcc, s1, v112
	s_mov_b32 s1, 0x46000
	s_nop 0
	v_addc_co_u32_e32 v77, vcc, 0, v113, vcc
	v_add_co_u32_e32 v82, vcc, s1, v112
	s_mov_b32 s1, 0x49000
	s_nop 0
	v_addc_co_u32_e32 v83, vcc, 0, v113, vcc
	v_add_co_u32_e32 v86, vcc, s1, v112
	s_mov_b32 s1, 0x4d000
	s_nop 0
	v_addc_co_u32_e32 v87, vcc, 0, v113, vcc
	v_add_co_u32_e32 v90, vcc, s1, v112
	s_mov_b32 s1, 0x50000
	s_nop 0
	v_addc_co_u32_e32 v91, vcc, 0, v113, vcc
	v_add_co_u32_e32 v94, vcc, s1, v112
	s_mov_b32 s1, 0x54000
	s_nop 0
	v_addc_co_u32_e32 v95, vcc, 0, v113, vcc
	v_add_co_u32_e32 v102, vcc, s1, v112
	s_mov_b32 s1, 0x57000
	s_nop 0
	v_addc_co_u32_e32 v103, vcc, 0, v113, vcc
	v_add_co_u32_e32 v104, vcc, s1, v112
	global_load_dwordx4 v[48:51], v[48:49], off
	s_nop 0
	global_load_dwordx4 v[52:55], v[52:53], off offset:2048
	v_addc_co_u32_e32 v105, vcc, 0, v113, vcc
	s_mov_b32 s1, 0x5b000
	v_add_co_u32_e32 v130, vcc, s1, v112
	s_mov_b32 s1, 0x5e000
	s_nop 0
	v_addc_co_u32_e32 v131, vcc, 0, v113, vcc
	v_add_co_u32_e32 v132, vcc, s1, v112
	global_load_dwordx4 v[56:59], v[56:57], off
	s_nop 0
	global_load_dwordx4 v[60:63], v[60:61], off offset:2048
	v_addc_co_u32_e32 v133, vcc, 0, v113, vcc
	s_mov_b32 s1, 0x62000
	v_add_co_u32_e32 v106, vcc, s1, v112
	s_mov_b32 s1, 0x65000
	s_nop 0
	v_addc_co_u32_e32 v107, vcc, 0, v113, vcc
	v_add_co_u32_e32 v108, vcc, s1, v112
	s_mov_b32 s1, 0x69000
	s_nop 0
	v_addc_co_u32_e32 v109, vcc, 0, v113, vcc
	global_load_dwordx4 v[64:67], v[64:65], off
	s_nop 0
	global_load_dwordx4 v[68:71], v[68:69], off offset:2048
	s_nop 0
	global_load_dwordx4 v[72:75], v[72:73], off
	s_nop 0
	global_load_dwordx4 v[76:79], v[76:77], off offset:2048
	s_nop 0
	global_load_dwordx4 v[82:85], v[82:83], off
	s_nop 0
	global_load_dwordx4 v[86:89], v[86:87], off offset:2048
	v_add_co_u32_e32 v134, vcc, s1, v112
	s_mov_b32 s1, 0x6c000
	s_nop 0
	v_addc_co_u32_e32 v135, vcc, 0, v113, vcc
	v_add_co_u32_e32 v136, vcc, s1, v112
	s_waitcnt vmcnt(21)
; __device__ __forceinline__ unsigned pk4_fp8(float a, float b, float c, float d) { int w = 0; w = __builtin_amdgcn_cvt_pk_fp8_f32(a, b, w, false); w = __builtin_amdgcn_cvt_pk_fp8_f32(c, d, w, true); return (unsigned)w; }
; #define GAS __attribute__((address_space(1)))
; __device__ __forceinline__ unsigned pk2(float lo, float hi) { return f2bf(lo) | (f2bf(hi) << 16); }
; template <int MODE, int KL>
; __device__ __forceinline__ void p0_cvt_item(const float* W, int K, int N, unsigned char* WT, int il, int which, int item, int lane, const float* gk, float scale, int ldk, int koff) {
;     ...
;     for (int c = 0; c < 4; ++c) { const int n = n0 + c, row = il ? ((n >> 4) * 32 + which * 16 + (n & 15)) : n;
;         if (MODE == 2) { GAS v4u* dst = (GAS v4u*)(WT + (size_t)row * ldk + koff + k0);
; #pragma unroll
;             for (int q = 0; q < KL / 16; ++q) { v4u o;
;                 o.x = pg8::pk4_fp8(v[16 * q][c], v[16 * q + 1][c], v[16 * q + 2][c], v[16 * q + 3][c]);     o.y = pg8::pk4_fp8(v[16 * q + 4][c], v[16 * q + 5][c], v[16 * q + 6][c], v[16 * q + 7][c]);
;                 o.z = pg8::pk4_fp8(v[16 * q + 8][c], v[16 * q + 9][c], v[16 * q + 10][c], v[16 * q + 11][c]); o.w = pg8::pk4_fp8(v[16 * q + 12][c], v[16 * q + 13][c], v[16 * q + 14][c], v[16 * q + 15][c]);
;                 dst[q] = o; } }
;         else { GAS v4u* dst = (GAS v4u*)(WT + ((size_t)row * ldk + koff + k0) * 2);
; #pragma unroll
;             for (int q = 0; q < KL / 8; ++q) { v4u o;
;                 if (MODE == 1) { o.x = pg8::pk_f16(v[8 * q][c], v[8 * q + 1][c]); o.y = pg8::pk_f16(v[8 * q + 2][c], v[8 * q + 3][c]); o.z = pg8::pk_f16(v[8 * q + 4][c], v[8 * q + 5][c]); o.w = pg8::pk_f16(v[8 * q + 6][c], v[8 * q + 7][c]); }
;                 else { o.x = pk2(v[8 * q][c], v[8 * q + 1][c]); o.y = pk2(v[8 * q + 2][c], v[8 * q + 3][c]); o.z = pk2(v[8 * q + 4][c], v[8 * q + 5][c]); o.w = pk2(v[8 * q + 6][c], v[8 * q + 7][c]); }
;                 dst[q] = o; } } }
	v_pk_mul_f32 v[126:127], v[0:1], s[96:97] op_sel_hi:[1,0]
	v_lshlrev_b32_e32 v0, 1, v100
	v_addc_co_u32_e32 v137, vcc, 0, v113, vcc
	v_and_b32_e32 v0, 0xffffffe0, v0
	global_load_dwordx4 v[90:93], v[90:91], off
	s_nop 0
	global_load_dwordx4 v[94:97], v[94:95], off offset:2048
	s_waitcnt vmcnt(19)
	v_pk_mul_f32 v[120:121], v[16:17], s[96:97] op_sel_hi:[1,0]
	s_waitcnt vmcnt(12)
	v_pk_mul_f32 v[16:17], v[44:45], s[96:97] op_sel_hi:[1,0]
	v_lshl_add_u32 v44, s0, 4, v0
	v_lshl_add_u64 v[0:1], v[110:111], 0, v[98:99]
	global_load_dwordx4 v[110:113], v[102:103], off
	global_load_dwordx4 v[114:117], v[104:105], off offset:2048
	s_nop 0
	global_load_dwordx4 v[102:105], v[106:107], off
	s_nop 0
	global_load_dwordx4 v[106:109], v[108:109], off offset:2048
	s_nop 0
	global_load_dwordx4 v[138:141], v[130:131], off
	s_nop 0
	global_load_dwordx4 v[130:133], v[132:133], off offset:2048
	s_nop 0
	global_load_dwordx4 v[142:145], v[134:135], off
	s_nop 0
	global_load_dwordx4 v[134:137], v[136:137], off offset:2048
	v_pk_mul_f32 v[128:129], v[4:5], s[96:97] op_sel_hi:[1,0]
	v_pk_mul_f32 v[118:119], v[8:9], s[96:97] op_sel_hi:[1,0]
	v_pk_mul_f32 v[122:123], v[12:13], s[96:97] op_sel_hi:[1,0]
	v_pk_mul_f32 v[124:125], v[20:21], s[96:97] op_sel_hi:[1,0]
	v_pk_mul_f32 v[8:9], v[28:29], s[96:97] op_sel_hi:[1,0]
	v_pk_mul_f32 v[28:29], v[32:33], s[96:97] op_sel_hi:[1,0]
	v_pk_mul_f32 v[36:37], v[36:37], s[96:97] op_sel_hi:[1,0]
	v_pk_mul_f32 v[12:13], v[40:41], s[96:97] op_sel_hi:[1,0]
	v_mov_b32_e32 v98, v81
	v_mov_b32_e32 v99, v81
	v_mov_b32_e32 v100, v81
	v_mov_b32_e32 v101, v81
	v_cvt_pk_fp8_f32 v98, v126, v128
	v_cvt_pk_fp8_f32 v99, v120, v124
	v_cvt_pk_fp8_f32 v100, v28, v36
	v_pk_mul_f32 v[4:5], v[24:25], s[96:97] op_sel_hi:[1,0]
	v_cvt_pk_fp8_f32 v98, v118, v122 op_sel:[0,0,1]
	v_cvt_pk_fp8_f32 v99, v4, v8 op_sel:[0,0,1]
	v_cvt_pk_fp8_f32 v100, v12, v16 op_sel:[0,0,1]
	s_mov_b64 s[0:1], 0x25f00000
	v_lshl_add_u64 v[0:1], v[0:1], 0, s[0:1]
	v_mov_b32_e32 v118, v81
	v_mov_b32_e32 v120, v81
	v_pk_mul_f32 v[26:27], v[26:27], s[96:97] op_sel_hi:[1,0]
	s_waitcnt vmcnt(19)
	v_pk_mul_f32 v[32:33], v[48:49], s[96:97] op_sel_hi:[1,0]
	s_waitcnt vmcnt(18)
	v_pk_mul_f32 v[40:41], v[52:53], s[96:97] op_sel_hi:[1,0]
	v_or_b32_e32 v48, v44, v150
	v_cvt_pk_fp8_f32 v101, v32, v40
	v_ashrrev_i32_e32 v49, 31, v48
	v_lshlrev_b64 v[44:45], 10, v[48:49]
	v_lshl_add_u64 v[44:45], v[0:1], 0, v[44:45]
	s_waitcnt vmcnt(17)
	v_pk_mul_f32 v[20:21], v[56:57], s[96:97] op_sel_hi:[1,0]
	s_waitcnt vmcnt(16)
	v_pk_mul_f32 v[24:25], v[60:61], s[96:97] op_sel_hi:[1,0]
	v_pk_mul_f32 v[58:59], v[58:59], s[96:97] op_sel_hi:[1,0]
	v_cvt_pk_fp8_f32 v101, v20, v24 op_sel:[0,0,1]
	global_store_dwordx4 v[44:45], v[98:101], off
	s_nop 1
	v_mov_b32_e32 v98, v81
	v_mov_b32_e32 v99, v81
	v_mov_b32_e32 v100, v81
	v_mov_b32_e32 v101, v81
	s_waitcnt vmcnt(16)
	v_pk_mul_f32 v[52:53], v[64:65], s[96:97] op_sel_hi:[1,0]
	s_waitcnt vmcnt(15)
	v_pk_mul_f32 v[56:57], v[68:69], s[96:97] op_sel_hi:[1,0]
	s_waitcnt vmcnt(12)
	v_pk_mul_f32 v[60:61], v[82:83], s[96:97] op_sel_hi:[1,0]
	s_waitcnt vmcnt(11)
	v_pk_mul_f32 v[64:65], v[86:87], s[96:97] op_sel_hi:[1,0]
	v_pk_mul_f32 v[68:69], v[72:73], s[96:97] op_sel_hi:[1,0]
	v_pk_mul_f32 v[72:73], v[76:77], s[96:97] op_sel_hi:[1,0]
	v_cvt_pk_fp8_f32 v98, v52, v56
	v_cvt_pk_fp8_f32 v99, v60, v64
	v_cvt_pk_fp8_f32 v118, v53, v57
	v_pk_mul_f32 v[52:53], v[42:43], s[96:97] op_sel_hi:[1,0]
	v_cvt_pk_fp8_f32 v98, v68, v72 op_sel:[0,0,1]
	v_pk_mul_f32 v[56:57], v[46:47], s[96:97] op_sel_hi:[1,0]
	v_cvt_pk_fp8_f32 v118, v69, v73 op_sel:[0,0,1]
	v_pk_mul_f32 v[68:69], v[18:19], s[96:97] op_sel_hi:[1,0]
	s_waitcnt vmcnt(8)
	v_pk_mul_f32 v[76:77], v[110:111], s[96:97] op_sel_hi:[1,0]
	s_waitcnt vmcnt(7)
	v_pk_mul_f32 v[86:87], v[114:115], s[96:97] op_sel_hi:[1,0]
	s_waitcnt vmcnt(6)
	v_pk_mul_f32 v[110:111], v[102:103], s[96:97] op_sel_hi:[1,0]
	s_waitcnt vmcnt(5)
	v_pk_mul_f32 v[106:107], v[106:107], s[96:97] op_sel_hi:[1,0]
	v_cvt_pk_fp8_f32 v100, v76, v86
	v_cvt_pk_fp8_f32 v101, v110, v106
	v_pk_mul_f32 v[82:83], v[90:91], s[96:97] op_sel_hi:[1,0]
	v_pk_mul_f32 v[146:147], v[94:95], s[96:97] op_sel_hi:[1,0]
	s_waitcnt vmcnt(4)
	v_pk_mul_f32 v[114:115], v[138:139], s[96:97] op_sel_hi:[1,0]
	s_waitcnt vmcnt(3)
; __device__ __forceinline__ unsigned pk4_fp8(float a, float b, float c, float d) { int w = 0; w = __builtin_amdgcn_cvt_pk_fp8_f32(a, b, w, false); w = __builtin_amdgcn_cvt_pk_fp8_f32(c, d, w, true); return (unsigned)w; }
; #define GAS __attribute__((address_space(1)))
; __device__ __forceinline__ unsigned pk2(float lo, float hi) { return f2bf(lo) | (f2bf(hi) << 16); }
; template <int MODE, int KL>
; __device__ __forceinline__ void p0_cvt_item(const float* W, int K, int N, unsigned char* WT, int il, int which, int item, int lane, const float* gk, float scale, int ldk, int koff) {
;     ...
;     for (int c = 0; c < 4; ++c) { const int n = n0 + c, row = il ? ((n >> 4) * 32 + which * 16 + (n & 15)) : n;
;         if (MODE == 2) { GAS v4u* dst = (GAS v4u*)(WT + (size_t)row * ldk + koff + k0);
; #pragma unroll
;             for (int q = 0; q < KL / 16; ++q) { v4u o;
;                 o.x = pg8::pk4_fp8(v[16 * q][c], v[16 * q + 1][c], v[16 * q + 2][c], v[16 * q + 3][c]);     o.y = pg8::pk4_fp8(v[16 * q + 4][c], v[16 * q + 5][c], v[16 * q + 6][c], v[16 * q + 7][c]);
;                 o.z = pg8::pk4_fp8(v[16 * q + 8][c], v[16 * q + 9][c], v[16 * q + 10][c], v[16 * q + 11][c]); o.w = pg8::pk4_fp8(v[16 * q + 12][c], v[16 * q + 13][c], v[16 * q + 14][c], v[16 * q + 15][c]);
;                 dst[q] = o; } }
;         else { GAS v4u* dst = (GAS v4u*)(WT + ((size_t)row * ldk + koff + k0) * 2);
; #pragma unroll
;             for (int q = 0; q < KL / 8; ++q) { v4u o;
;                 if (MODE == 1) { o.x = pg8::pk_f16(v[8 * q][c], v[8 * q + 1][c]); o.y = pg8::pk_f16(v[8 * q + 2][c], v[8 * q + 3][c]); o.z = pg8::pk_f16(v[8 * q + 4][c], v[8 * q + 5][c]); o.w = pg8::pk_f16(v[8 * q + 6][c], v[8 * q + 7][c]); }
;                 else { o.x = pk2(v[8 * q][c], v[8 * q + 1][c]); o.y = pk2(v[8 * q + 2][c], v[8 * q + 3][c]); o.z = pk2(v[8 * q + 4][c], v[8 * q + 5][c]); o.w = pk2(v[8 * q + 6][c], v[8 * q + 7][c]); }
;                 dst[q] = o; } } }
	v_pk_mul_f32 v[130:131], v[130:131], s[96:97] op_sel_hi:[1,0]
	s_waitcnt vmcnt(2)
	v_pk_mul_f32 v[138:139], v[142:143], s[96:97] op_sel_hi:[1,0]
	s_waitcnt vmcnt(1)
	v_pk_mul_f32 v[134:135], v[134:135], s[96:97] op_sel_hi:[1,0]
	v_cvt_pk_fp8_f32 v99, v82, v146 op_sel:[0,0,1]
	v_cvt_pk_fp8_f32 v100, v114, v130 op_sel:[0,0,1]
	v_cvt_pk_fp8_f32 v101, v138, v134 op_sel:[0,0,1]
	v_mov_b32_e32 v102, v81
	v_mov_b32_e32 v103, v81
	v_cvt_pk_fp8_f32 v102, v29, v37
	global_store_dwordx4 v[44:45], v[98:101], off offset:16
	v_cvt_pk_fp8_f32 v103, v33, v41
	v_cvt_pk_fp8_f32 v120, v77, v87
	v_mov_b32_e32 v100, v81
	v_cvt_pk_fp8_f32 v100, v127, v129
	v_mov_b32_e32 v101, v81
	v_cvt_pk_fp8_f32 v101, v121, v125
	v_mov_b32_e32 v121, v81
	v_cvt_pk_fp8_f32 v100, v119, v123 op_sel:[0,0,1]
	v_mov_b32_e32 v119, v81
	v_cvt_pk_fp8_f32 v119, v61, v65
	v_cvt_pk_fp8_f32 v121, v111, v107
	v_cvt_pk_fp8_f32 v101, v5, v9 op_sel:[0,0,1]
	v_cvt_pk_fp8_f32 v102, v13, v17 op_sel:[0,0,1]
	v_cvt_pk_fp8_f32 v103, v21, v25 op_sel:[0,0,1]
	v_or_b32_e32 v18, 1, v48
	v_ashrrev_i32_e32 v19, 31, v18
	v_cvt_pk_fp8_f32 v119, v83, v147 op_sel:[0,0,1]
	v_cvt_pk_fp8_f32 v120, v115, v131 op_sel:[0,0,1]
	v_cvt_pk_fp8_f32 v121, v139, v135 op_sel:[0,0,1]
	v_lshlrev_b64 v[18:19], 10, v[18:19]
	v_pk_mul_f32 v[64:65], v[2:3], s[96:97] op_sel_hi:[1,0]
	v_pk_mul_f32 v[86:87], v[6:7], s[96:97] op_sel_hi:[1,0]
	v_pk_mul_f32 v[90:91], v[22:23], s[96:97] op_sel_hi:[1,0]
	v_pk_mul_f32 v[40:41], v[30:31], s[96:97] op_sel_hi:[1,0]
	v_pk_mul_f32 v[72:73], v[34:35], s[96:97] op_sel_hi:[1,0]
	v_pk_mul_f32 v[94:95], v[38:39], s[96:97] op_sel_hi:[1,0]
	v_pk_mul_f32 v[76:77], v[50:51], s[96:97] op_sel_hi:[1,0]
	v_pk_mul_f32 v[98:99], v[54:55], s[96:97] op_sel_hi:[1,0]
	v_pk_mul_f32 v[30:31], v[84:85], s[96:97] op_sel_hi:[1,0]
	v_lshl_add_u64 v[18:19], v[0:1], 0, v[18:19]
	v_mov_b32_e32 v82, v81
	v_mov_b32_e32 v83, v81
	v_mov_b32_e32 v84, v81
	v_mov_b32_e32 v85, v81
	v_pk_mul_f32 v[28:29], v[66:67], s[96:97] op_sel_hi:[1,0]
	v_pk_mul_f32 v[42:43], v[70:71], s[96:97] op_sel_hi:[1,0]
	v_pk_mul_f32 v[44:45], v[88:89], s[96:97] op_sel_hi:[1,0]
	v_pk_mul_f32 v[32:33], v[112:113], s[96:97] op_sel_hi:[1,0]
	v_pk_mul_f32 v[46:47], v[116:117], s[96:97] op_sel_hi:[1,0]
	v_pk_mul_f32 v[34:35], v[104:105], s[96:97] op_sel_hi:[1,0]
	v_pk_mul_f32 v[36:37], v[108:109], s[96:97] op_sel_hi:[1,0]
	global_store_dwordx4 v[18:19], v[100:103], off
	global_store_dwordx4 v[18:19], v[118:121], off offset:16
	v_cvt_pk_fp8_f32 v82, v64, v86
	v_cvt_pk_fp8_f32 v83, v68, v90
	v_cvt_pk_fp8_f32 v84, v72, v94
	v_cvt_pk_fp8_f32 v85, v76, v98
	v_mov_b32_e32 v100, v81
	v_mov_b32_e32 v101, v81
	v_mov_b32_e32 v102, v81
	v_mov_b32_e32 v103, v81
	v_cvt_pk_fp8_f32 v100, v28, v42
	v_cvt_pk_fp8_f32 v101, v30, v44
	v_cvt_pk_fp8_f32 v102, v32, v46
	v_cvt_pk_fp8_f32 v103, v34, v36
	v_pk_mul_f32 v[20:21], v[10:11], s[96:97] op_sel_hi:[1,0]
	v_pk_mul_f32 v[24:25], v[14:15], s[96:97] op_sel_hi:[1,0]
	v_pk_mul_f32 v[60:61], v[62:63], s[96:97] op_sel_hi:[1,0]
	v_pk_mul_f32 v[2:3], v[74:75], s[96:97] op_sel_hi:[1,0]
	v_pk_mul_f32 v[4:5], v[78:79], s[96:97] op_sel_hi:[1,0]
	v_pk_mul_f32 v[6:7], v[92:93], s[96:97] op_sel_hi:[1,0]
	v_pk_mul_f32 v[8:9], v[96:97], s[96:97] op_sel_hi:[1,0]
	v_pk_mul_f32 v[10:11], v[140:141], s[96:97] op_sel_hi:[1,0]
	v_pk_mul_f32 v[12:13], v[132:133], s[96:97] op_sel_hi:[1,0]
	v_pk_mul_f32 v[14:15], v[144:145], s[96:97] op_sel_hi:[1,0]
	v_pk_mul_f32 v[16:17], v[136:137], s[96:97] op_sel_hi:[1,0]
	v_or_b32_e32 v18, 2, v48
	v_cvt_pk_fp8_f32 v82, v20, v24 op_sel:[0,0,1]
	v_cvt_pk_fp8_f32 v83, v26, v40 op_sel:[0,0,1]
	v_cvt_pk_fp8_f32 v84, v52, v56 op_sel:[0,0,1]
	v_cvt_pk_fp8_f32 v85, v58, v60 op_sel:[0,0,1]
	v_ashrrev_i32_e32 v19, 31, v18
	v_cvt_pk_fp8_f32 v100, v2, v4 op_sel:[0,0,1]
	v_cvt_pk_fp8_f32 v101, v6, v8 op_sel:[0,0,1]
	v_cvt_pk_fp8_f32 v102, v10, v12 op_sel:[0,0,1]
	v_cvt_pk_fp8_f32 v103, v14, v16 op_sel:[0,0,1]
	v_lshlrev_b64 v[18:19], 10, v[18:19]
	v_lshl_add_u64 v[18:19], v[0:1], 0, v[18:19]
	global_store_dwordx4 v[18:19], v[82:85], off
	global_store_dwordx4 v[18:19], v[100:103], off offset:16
	v_or_b32_e32 v18, 3, v48
	v_ashrrev_i32_e32 v19, 31, v18
	v_lshlrev_b64 v[18:19], 10, v[18:19]
	v_lshl_add_u64 v[0:1], v[0:1], 0, v[18:19]
	s_branch .LBB0_136

; __device__ __forceinline__ float row_rstd(const float* ssp, size_t row) {
;     const f32x4* p = (const f32x4*)(ssp + row * 16); const f32x4 a = p[0], b = p[1], c = p[2], d = p[3];
;     const float s = (((a[0] + a[1]) + (a[2] + a[3])) + ((b[0] + b[1]) + (b[2] + b[3]))) + (((c[0] + c[1]) + (c[2] + c[3])) + ((d[0] + d[1]) + (d[2] + d[3])));
;     return rsqrtf(s * (1.f / 1024.f) + 1e-6f);
; }
.LBB0_143:
	v_readlane_b32 s2, v254, 25
	s_nop 1
	v_add_u32_e32 v0, s2, v80
	s_movk_i32 s2, 0x100
	v_cmp_gt_i32_e32 vcc, s2, v0
	s_and_saveexec_b64 s[2:3], vcc
	s_cbranch_execz .LBB0_145
	v_ashrrev_i32_e32 v1, 31, v0
	v_lshl_add_u64 v[2:3], s[4:5], 0, v[0:1]
	v_lshlrev_b64 v[2:3], 6, v[2:3]
	v_lshl_add_u64 v[10:11], s[80:81], 0, v[2:3]
	s_mov_b64 s[4:5], 0x400000
	v_lshl_add_u64 v[14:15], v[10:11], 0, s[4:5]
	v_add_co_u32_e32 v10, vcc, 0x400000, v10
	s_waitcnt lgkmcnt(0)
	global_load_dwordx4 v[2:5], v[14:15], off offset:16
	global_load_dwordx4 v[6:9], v[14:15], off offset:32
	v_addc_co_u32_e32 v11, vcc, 0, v11, vcc
	global_load_dwordx4 v[10:13], v[10:11], off
	s_nop 0
	global_load_dwordx4 v[14:17], v[14:15], off offset:48
	s_waitcnt vmcnt(0) lgkmcnt(0)
	v_mov_b32_e32 v22, v2
	v_mov_b32_e32 v19, v6
	v_mov_b32_e32 v21, v8
	v_mov_b32_e32 v2, v4
	v_mov_b32_e32 v18, v10
	v_mov_b32_e32 v6, v11
	v_mov_b32_e32 v20, v12
	v_mov_b32_e32 v8, v13
	v_mov_b32_e32 v23, v14
	v_mov_b32_e32 v14, v3
	v_mov_b32_e32 v3, v16
	v_mov_b32_e32 v16, v5
	v_pk_add_f32 v[4:5], v[18:19], v[6:7]
	v_pk_add_f32 v[6:7], v[20:21], v[8:9]
	v_pk_add_f32 v[8:9], v[22:23], v[14:15]
	v_pk_add_f32 v[2:3], v[2:3], v[16:17]
	v_pk_add_f32 v[4:5], v[4:5], v[6:7]
	v_pk_add_f32 v[2:3], v[8:9], v[2:3]
	s_nop 0
	v_pk_add_f32 v[2:3], v[4:5], v[2:3]
	s_nop 0
	v_add_f32_e32 v1, v2, v3
	v_fmamk_f32 v1, v1, 0x3a800000, v162
	v_mul_f32_e32 v2, 0x4b800000, v1
	v_cmp_gt_f32_e32 vcc, s85, v1
	s_nop 1
	v_cndmask_b32_e32 v1, v1, v2, vcc
	v_rsq_f32_e32 v1, v1
	v_lshl_add_u32 v2, v0, 2, 0
	v_add_u32_e32 v2, 0x20400, v2
	v_mul_f32_e32 v3, 0x45800000, v1
	v_cndmask_b32_e32 v1, v1, v3, vcc
	ds_write_b32 v2, v1

; __device__ __forceinline__ float sigm(float x) { return __builtin_amdgcn_rcpf(1.f + __expf(-x)); }
;     __device__ __forceinline__ void operator()(const f32x4 (&acc)[2][2][4][2], const Unit& u, int wr, int wc, int fr, int fq) const {
;     ...
;         } else { const int col0 = (u.pn - 11) * BM + wc * 32 + 8 * fq;
; #pragma unroll
;             for (int ai = 0; ai < 2; ++ai)
; #pragma unroll
;                 for (int m = 0; m < 4; ++m) { const size_t r = (size_t)(row0 + ai * HALF + m * 16); const float s = tbl[wr * 64 + fr + ai * HALF + m * 16]; unsigned char* rowp = GZ + (size_t)(u.pn - 11) * ldc + r * 256 + (wc * 32 + 8 * fq);
; #pragma unroll
;                     for (int bj = 0; bj < 2; ++bj) { const f32x4 v0 = acc[ai][bj][m][0] * s, v1 = acc[ai][bj][m][1] * s;
;                         unsigned q[8];
; #pragma unroll
;                         for (int i = 0; i < 4; ++i) { q[i] = (unsigned)(sigm(v0[i]) * 255.f + 0.5f); q[4 + i] = (unsigned)(sigm(v1[i]) * 255.f + 0.5f); if (u.pn >= 15) { q[i] = q[i] < 1u ? 1u : q[i]; q[4 + i] = q[4 + i] < 1u ? 1u : q[4 + i]; } }
;                         u32x2 w; w.x = q[0] | (q[1] << 8) | (q[2] << 16) | (q[3] << 24); w.y = q[4] | (q[5] << 8) | (q[6] << 16) | (q[7] << 24);
;                         *(u32x2*)(rowp + bj * HALF) = w; } }
.LBB0_160:
	s_waitcnt lgkmcnt(0)
	v_mul_f32_e32 v80, v126, v150
	v_mul_f32_e32 v80, 0xbfb8aa3b, v80
	v_exp_f32_e32 v80, v80
	s_add_i32 s62, s18, -11
	s_lshl_b64 s[0:1], s[62:63], 22
	s_add_u32 s4, s35, s0
	v_add_f32_e32 v80, 1.0, v80
	v_rcp_f32_e32 v154, v80
	v_mul_f32_e32 v80, v122, v150
	v_mul_f32_e32 v80, 0xbfb8aa3b, v80
	v_exp_f32_e32 v80, v80
	s_addc_u32 s5, s36, s1
	s_cmp_gt_u32 s18, 14
	s_cselect_b64 vcc, -1, 0
	v_add_f32_e32 v80, 1.0, v80
	v_rcp_f32_e32 v155, v80
	v_lshlrev_b64 v[152:153], 8, v[144:145]
	v_lshl_add_u64 v[152:153], s[4:5], 0, v[152:153]
	v_lshl_add_u64 v[152:153], v[152:153], 0, v[138:139]
	v_pk_fma_f32 v[154:155], v[154:155], s[90:91], 0.5 op_sel_hi:[1,0,0]
	s_mov_b64 s[0:1], 0x8000
	v_cvt_u32_f32_e32 v147, v154
	v_cvt_u32_f32_e32 v80, v155
	v_max_u32_e32 v149, 1, v147
	v_cndmask_b32_e32 v147, v147, v149, vcc
	v_mul_f32_e32 v149, v127, v150
	v_mul_f32_e32 v149, 0xbfb8aa3b, v149
	v_exp_f32_e32 v149, v149
	v_max_u32_e32 v154, 1, v80
	v_cndmask_b32_e32 v80, v80, v154, vcc
	v_add_f32_e32 v149, 1.0, v149
	v_rcp_f32_e32 v154, v149
	v_mul_f32_e32 v149, v123, v150
	v_mul_f32_e32 v149, 0xbfb8aa3b, v149
	v_exp_f32_e32 v149, v149
	s_nop 0
	v_add_f32_e32 v149, 1.0, v149
	v_rcp_f32_e32 v155, v149
	s_nop 0
	v_pk_fma_f32 v[154:155], v[154:155], s[90:91], 0.5 op_sel_hi:[1,0,0]
	s_nop 0
	v_cvt_u32_f32_e32 v149, v155
	v_cvt_u32_f32_e32 v154, v154
	v_max_u32_e32 v159, 1, v149
	v_max_u32_e32 v155, 1, v154
	v_cndmask_b32_e32 v149, v149, v159, vcc
	v_cndmask_b32_e32 v159, v154, v155, vcc
	v_mul_f32_e32 v154, v128, v150
	v_mul_f32_e32 v155, v124, v150
	v_mul_f32_e32 v154, 0xbfb8aa3b, v154
	v_mul_f32_e32 v155, 0xbfb8aa3b, v155
	v_exp_f32_e32 v154, v154
	v_exp_f32_e32 v155, v155
	v_lshl_or_b32 v147, v159, 8, v147
	v_lshl_or_b32 v80, v149, 8, v80
	v_add_f32_e32 v154, 1.0, v154
	v_add_f32_e32 v155, 1.0, v155
	v_rcp_f32_e32 v154, v154
	v_rcp_f32_e32 v155, v155
	s_nop 0
	v_pk_fma_f32 v[154:155], v[154:155], s[90:91], 0.5 op_sel_hi:[1,0,0]
	s_nop 0
	v_cvt_u32_f32_e32 v155, v155
	v_cvt_u32_f32_e32 v154, v154
	v_max_u32_e32 v161, 1, v155
	v_max_u32_e32 v160, 1, v154
	v_cndmask_b32_e32 v161, v155, v161, vcc
	v_cndmask_b32_e32 v160, v154, v160, vcc
	v_mul_f32_e32 v154, v129, v150
	v_mul_f32_e32 v155, v125, v150
	v_mul_f32_e32 v154, 0xbfb8aa3b, v154
	v_mul_f32_e32 v155, 0xbfb8aa3b, v155
	v_exp_f32_e32 v154, v154
	v_exp_f32_e32 v155, v155
	v_lshlrev_b32_e32 v159, 16, v160
	v_add_f32_e32 v154, 1.0, v154
	v_add_f32_e32 v155, 1.0, v155
	v_rcp_f32_e32 v154, v154
	v_rcp_f32_e32 v155, v155
	s_nop 0
	v_pk_fma_f32 v[154:155], v[154:155], s[90:91], 0.5 op_sel_hi:[1,0,0]
	s_nop 0
	v_cvt_u32_f32_e32 v154, v154
	v_cvt_u32_f32_e32 v155, v155
	v_max_u32_e32 v174, 1, v154
	v_max_u32_e32 v175, 1, v155
	v_cndmask_b32_e32 v154, v154, v174, vcc
	v_cndmask_b32_e32 v155, v155, v175, vcc
	v_lshlrev_b32_e32 v154, 24, v154
	v_or3_b32 v154, v147, v159, v154
	v_lshlrev_b32_e32 v147, 16, v161
	v_lshlrev_b32_e32 v149, 24, v155
	v_or3_b32 v155, v80, v147, v149
	v_mul_f32_e32 v80, v118, v150
	v_mul_f32_e32 v80, 0xbfb8aa3b, v80
	v_exp_f32_e32 v80, v80
	global_store_dwordx2 v[152:153], v[154:155], off
	v_add_f32_e32 v80, 1.0, v80
	v_rcp_f32_e32 v154, v80
	v_mul_f32_e32 v80, v110, v150
	v_mul_f32_e32 v80, 0xbfb8aa3b, v80
	v_exp_f32_e32 v80, v80
	s_nop 0
	v_add_f32_e32 v80, 1.0, v80
	v_rcp_f32_e32 v155, v80
	s_nop 0
	v_pk_fma_f32 v[154:155], v[154:155], s[90:91], 0.5 op_sel_hi:[1,0,0]
	s_nop 0
	v_cvt_u32_f32_e32 v147, v154
	v_cvt_u32_f32_e32 v80, v155
	v_max_u32_e32 v149, 1, v147
	v_cndmask_b32_e32 v147, v147, v149, vcc
	v_mul_f32_e32 v149, v119, v150
	v_mul_f32_e32 v149, 0xbfb8aa3b, v149
	v_exp_f32_e32 v149, v149
	v_max_u32_e32 v154, 1, v80
	v_cndmask_b32_e32 v80, v80, v154, vcc
	v_add_f32_e32 v149, 1.0, v149
	v_rcp_f32_e32 v154, v149
	v_mul_f32_e32 v149, v111, v150
	v_mul_f32_e32 v149, 0xbfb8aa3b, v149
	v_exp_f32_e32 v149, v149
	s_nop 0
	v_add_f32_e32 v149, 1.0, v149
	v_rcp_f32_e32 v155, v149
	s_nop 0
	v_pk_fma_f32 v[154:155], v[154:155], s[90:91], 0.5 op_sel_hi:[1,0,0]
	s_nop 0
	v_cvt_u32_f32_e32 v149, v155
	v_cvt_u32_f32_e32 v154, v154
	v_max_u32_e32 v159, 1, v149
	v_max_u32_e32 v155, 1, v154
	v_cndmask_b32_e32 v149, v149, v159, vcc
	v_cndmask_b32_e32 v159, v154, v155, vcc
	v_mul_f32_e32 v154, v120, v150
	v_mul_f32_e32 v155, v112, v150
	v_mul_f32_e32 v154, 0xbfb8aa3b, v154
	v_mul_f32_e32 v155, 0xbfb8aa3b, v155
	v_exp_f32_e32 v154, v154
	v_exp_f32_e32 v155, v155
	v_lshl_or_b32 v147, v159, 8, v147
	v_lshl_or_b32 v80, v149, 8, v80
	v_add_f32_e32 v154, 1.0, v154
	v_add_f32_e32 v155, 1.0, v155
	v_rcp_f32_e32 v154, v154
	v_rcp_f32_e32 v155, v155
	s_nop 0
	v_pk_fma_f32 v[154:155], v[154:155], s[90:91], 0.5 op_sel_hi:[1,0,0]
	s_nop 0
	v_cvt_u32_f32_e32 v155, v155
	v_cvt_u32_f32_e32 v154, v154
	v_max_u32_e32 v161, 1, v155
	v_max_u32_e32 v160, 1, v154
	v_cndmask_b32_e32 v161, v155, v161, vcc
	v_cndmask_b32_e32 v160, v154, v160, vcc
	v_mul_f32_e32 v154, v121, v150
	v_mul_f32_e32 v155, v113, v150
	v_mul_f32_e32 v154, 0xbfb8aa3b, v154
	v_mul_f32_e32 v155, 0xbfb8aa3b, v155
	v_exp_f32_e32 v154, v154
	v_exp_f32_e32 v155, v155
	v_lshlrev_b32_e32 v159, 16, v160
	v_add_f32_e32 v154, 1.0, v154
	v_add_f32_e32 v155, 1.0, v155
	v_rcp_f32_e32 v154, v154
	v_rcp_f32_e32 v155, v155
	s_nop 0
	v_pk_fma_f32 v[154:155], v[154:155], s[90:91], 0.5 op_sel_hi:[1,0,0]
	s_nop 0
	v_cvt_u32_f32_e32 v154, v154
	v_cvt_u32_f32_e32 v155, v155
	v_max_u32_e32 v174, 1, v154
	v_max_u32_e32 v175, 1, v155
	v_cndmask_b32_e32 v154, v154, v174, vcc
	v_cndmask_b32_e32 v155, v155, v175, vcc
	v_lshlrev_b32_e32 v154, 24, v154
	v_or3_b32 v154, v147, v159, v154
	v_lshlrev_b32_e32 v147, 16, v161
	v_lshlrev_b32_e32 v149, 24, v155
	v_or3_b32 v155, v80, v147, v149
	global_store_dwordx2 v[152:153], v[154:155], off offset:128
	ds_read_b32 v80, v157 offset:64
	v_ashrrev_i32_e32 v149, 31, v148
	v_lshlrev_b64 v[154:155], 8, v[148:149]
	v_lshl_add_u64 v[154:155], s[4:5], 0, v[154:155]
	v_lshl_add_u64 v[154:155], v[154:155], 0, v[138:139]
	s_waitcnt lgkmcnt(0)
; __device__ __forceinline__ float sigm(float x) { return __builtin_amdgcn_rcpf(1.f + __expf(-x)); }
;     __device__ __forceinline__ void operator()(const f32x4 (&acc)[2][2][4][2], const Unit& u, int wr, int wc, int fr, int fq) const {
;     ...
;         } else { const int col0 = (u.pn - 11) * BM + wc * 32 + 8 * fq;
; #pragma unroll
;             for (int ai = 0; ai < 2; ++ai)
; #pragma unroll
;                 for (int m = 0; m < 4; ++m) { const size_t r = (size_t)(row0 + ai * HALF + m * 16); const float s = tbl[wr * 64 + fr + ai * HALF + m * 16]; unsigned char* rowp = GZ + (size_t)(u.pn - 11) * ldc + r * 256 + (wc * 32 + 8 * fq);
; #pragma unroll
;                     for (int bj = 0; bj < 2; ++bj) { const f32x4 v0 = acc[ai][bj][m][0] * s, v1 = acc[ai][bj][m][1] * s;
;                         unsigned q[8];
; #pragma unroll
;                         for (int i = 0; i < 4; ++i) { q[i] = (unsigned)(sigm(v0[i]) * 255.f + 0.5f); q[4 + i] = (unsigned)(sigm(v1[i]) * 255.f + 0.5f); if (u.pn >= 15) { q[i] = q[i] < 1u ? 1u : q[i]; q[4 + i] = q[4 + i] < 1u ? 1u : q[4 + i]; } }
;                         u32x2 w; w.x = q[0] | (q[1] << 8) | (q[2] << 16) | (q[3] << 24); w.y = q[4] | (q[5] << 8) | (q[6] << 16) | (q[7] << 24);
;                         *(u32x2*)(rowp + bj * HALF) = w; } }
	v_mul_f32_e32 v147, v114, v80
	v_mul_f32_e32 v147, 0xbfb8aa3b, v147
	v_exp_f32_e32 v147, v147
	s_nop 0
	v_add_f32_e32 v147, 1.0, v147
	v_rcp_f32_e32 v160, v147
	v_mul_f32_e32 v147, v106, v80
	v_mul_f32_e32 v147, 0xbfb8aa3b, v147
	v_exp_f32_e32 v147, v147
	s_nop 0
	v_add_f32_e32 v147, 1.0, v147
	v_rcp_f32_e32 v161, v147
	s_nop 0
	v_pk_fma_f32 v[160:161], v[160:161], s[90:91], 0.5 op_sel_hi:[1,0,0]
	s_nop 0
	v_cvt_u32_f32_e32 v149, v160
	v_cvt_u32_f32_e32 v147, v161
	v_max_u32_e32 v159, 1, v149
	v_cndmask_b32_e32 v149, v149, v159, vcc
	v_mul_f32_e32 v159, v115, v80
	v_mul_f32_e32 v159, 0xbfb8aa3b, v159
	v_exp_f32_e32 v159, v159
	v_max_u32_e32 v160, 1, v147
	v_cndmask_b32_e32 v147, v147, v160, vcc
	v_add_f32_e32 v159, 1.0, v159
	v_rcp_f32_e32 v160, v159
	v_mul_f32_e32 v159, v107, v80
	v_mul_f32_e32 v159, 0xbfb8aa3b, v159
	v_exp_f32_e32 v159, v159
	s_nop 0
	v_add_f32_e32 v159, 1.0, v159
	v_rcp_f32_e32 v161, v159
	s_nop 0
	v_pk_fma_f32 v[160:161], v[160:161], s[90:91], 0.5 op_sel_hi:[1,0,0]
	s_nop 0
	v_cvt_u32_f32_e32 v159, v161
	v_cvt_u32_f32_e32 v160, v160
	v_max_u32_e32 v174, 1, v159
	v_max_u32_e32 v161, 1, v160
	v_cndmask_b32_e32 v159, v159, v174, vcc
	v_cndmask_b32_e32 v174, v160, v161, vcc
	v_mul_f32_e32 v160, v116, v80
	v_mul_f32_e32 v161, v108, v80
	v_mul_f32_e32 v160, 0xbfb8aa3b, v160
	v_mul_f32_e32 v161, 0xbfb8aa3b, v161
	v_exp_f32_e32 v160, v160
	v_exp_f32_e32 v161, v161
	v_lshl_or_b32 v149, v174, 8, v149
	v_lshl_or_b32 v147, v159, 8, v147
	v_add_f32_e32 v160, 1.0, v160
	v_add_f32_e32 v161, 1.0, v161
	v_rcp_f32_e32 v160, v160
	v_rcp_f32_e32 v161, v161
	s_nop 0
	v_pk_fma_f32 v[160:161], v[160:161], s[90:91], 0.5 op_sel_hi:[1,0,0]
	s_nop 0
	v_cvt_u32_f32_e32 v161, v161
	v_cvt_u32_f32_e32 v160, v160
	v_max_u32_e32 v176, 1, v161
	v_max_u32_e32 v175, 1, v160
	v_cndmask_b32_e32 v176, v161, v176, vcc
	v_cndmask_b32_e32 v175, v160, v175, vcc
	v_mul_f32_e32 v160, v117, v80
	v_mul_f32_e32 v161, v109, v80
	v_mul_f32_e32 v160, 0xbfb8aa3b, v160
	v_mul_f32_e32 v161, 0xbfb8aa3b, v161
	v_exp_f32_e32 v160, v160
	v_exp_f32_e32 v161, v161
	v_lshlrev_b32_e32 v174, 16, v175
	v_add_f32_e32 v160, 1.0, v160
	v_add_f32_e32 v161, 1.0, v161
	v_rcp_f32_e32 v160, v160
	v_rcp_f32_e32 v161, v161
	s_nop 0
	v_pk_fma_f32 v[160:161], v[160:161], s[90:91], 0.5 op_sel_hi:[1,0,0]
	s_nop 0
	v_cvt_u32_f32_e32 v160, v160
	v_cvt_u32_f32_e32 v161, v161
	v_max_u32_e32 v177, 1, v160
	v_max_u32_e32 v178, 1, v161
	v_cndmask_b32_e32 v160, v160, v177, vcc
	v_cndmask_b32_e32 v161, v161, v178, vcc
	v_lshlrev_b32_e32 v160, 24, v160
	v_or3_b32 v160, v149, v174, v160
	v_lshlrev_b32_e32 v149, 16, v176
	v_lshlrev_b32_e32 v159, 24, v161
	v_or3_b32 v161, v147, v149, v159
	v_mul_f32_e32 v147, v102, v80
	v_mul_f32_e32 v147, 0xbfb8aa3b, v147
	v_exp_f32_e32 v147, v147
	global_store_dwordx2 v[154:155], v[160:161], off
	v_add_f32_e32 v147, 1.0, v147
	v_rcp_f32_e32 v160, v147
	v_mul_f32_e32 v147, v94, v80
	v_mul_f32_e32 v147, 0xbfb8aa3b, v147
	v_exp_f32_e32 v147, v147
	s_nop 0
	v_add_f32_e32 v147, 1.0, v147
	v_rcp_f32_e32 v161, v147
	s_nop 0
	v_pk_fma_f32 v[160:161], v[160:161], s[90:91], 0.5 op_sel_hi:[1,0,0]
	s_nop 0
	v_cvt_u32_f32_e32 v149, v160
	v_cvt_u32_f32_e32 v147, v161
	v_max_u32_e32 v159, 1, v149
	v_cndmask_b32_e32 v149, v149, v159, vcc
	v_mul_f32_e32 v159, v103, v80
	v_mul_f32_e32 v159, 0xbfb8aa3b, v159
	v_exp_f32_e32 v159, v159
	v_max_u32_e32 v160, 1, v147
	v_cndmask_b32_e32 v147, v147, v160, vcc
	v_add_f32_e32 v159, 1.0, v159
	v_rcp_f32_e32 v160, v159
	v_mul_f32_e32 v159, v95, v80
	v_mul_f32_e32 v159, 0xbfb8aa3b, v159
	v_exp_f32_e32 v159, v159
	s_nop 0
	v_add_f32_e32 v159, 1.0, v159
	v_rcp_f32_e32 v161, v159
	s_nop 0
	v_pk_fma_f32 v[160:161], v[160:161], s[90:91], 0.5 op_sel_hi:[1,0,0]
	s_nop 0
	v_cvt_u32_f32_e32 v159, v161
	v_cvt_u32_f32_e32 v160, v160
	v_max_u32_e32 v174, 1, v159
	v_max_u32_e32 v161, 1, v160
	v_cndmask_b32_e32 v159, v159, v174, vcc
	v_cndmask_b32_e32 v174, v160, v161, vcc
	v_mul_f32_e32 v160, v104, v80
	v_mul_f32_e32 v161, v96, v80
	v_mul_f32_e32 v160, 0xbfb8aa3b, v160
	v_mul_f32_e32 v161, 0xbfb8aa3b, v161
	v_exp_f32_e32 v160, v160
	v_exp_f32_e32 v161, v161
	v_lshl_or_b32 v149, v174, 8, v149
	v_lshl_or_b32 v147, v159, 8, v147
	v_add_f32_e32 v160, 1.0, v160
	v_add_f32_e32 v161, 1.0, v161
	v_rcp_f32_e32 v160, v160
	v_rcp_f32_e32 v161, v161
	s_nop 0
	v_pk_fma_f32 v[160:161], v[160:161], s[90:91], 0.5 op_sel_hi:[1,0,0]
	s_nop 0
	v_cvt_u32_f32_e32 v160, v160
	v_cvt_u32_f32_e32 v161, v161
	v_max_u32_e32 v175, 1, v160
	v_cndmask_b32_e32 v175, v160, v175, vcc
	v_mul_f32_e32 v160, v105, v80
	v_mul_f32_e32 v80, v97, v80
	v_mul_f32_e32 v160, 0xbfb8aa3b, v160
	v_mul_f32_e32 v80, 0xbfb8aa3b, v80
	v_exp_f32_e32 v160, v160
	v_exp_f32_e32 v80, v80
	v_max_u32_e32 v176, 1, v161
	v_cndmask_b32_e32 v176, v161, v176, vcc
	v_add_f32_e32 v160, 1.0, v160
	v_add_f32_e32 v80, 1.0, v80
	v_rcp_f32_e32 v160, v160
	v_rcp_f32_e32 v161, v80
	s_nop 0
	v_pk_fma_f32 v[160:161], v[160:161], s[90:91], 0.5 op_sel_hi:[1,0,0]
	s_nop 0
	v_cvt_u32_f32_e32 v160, v160
	v_cvt_u32_f32_e32 v80, v161
	v_max_u32_e32 v161, 1, v160
	v_max_u32_e32 v177, 1, v80
	v_cndmask_b32_e32 v160, v160, v161, vcc
	v_cndmask_b32_e32 v80, v80, v177, vcc
	v_lshlrev_b32_e32 v161, 16, v175
	v_lshlrev_b32_e32 v160, 24, v160
	v_or3_b32 v160, v149, v161, v160
	v_lshlrev_b32_e32 v149, 16, v176
	v_lshlrev_b32_e32 v80, 24, v80
	v_or3_b32 v161, v147, v149, v80
	global_store_dwordx2 v[154:155], v[160:161], off offset:128
	ds_read_b32 v80, v157 offset:128
	v_ashrrev_i32_e32 v147, 31, v146
	v_lshlrev_b64 v[154:155], 8, v[146:147]
	v_lshl_add_u64 v[154:155], s[4:5], 0, v[154:155]
	v_lshl_add_u64 v[154:155], v[154:155], 0, v[138:139]
	s_waitcnt lgkmcnt(0)
; __device__ __forceinline__ float sigm(float x) { return __builtin_amdgcn_rcpf(1.f + __expf(-x)); }
;     __device__ __forceinline__ void operator()(const f32x4 (&acc)[2][2][4][2], const Unit& u, int wr, int wc, int fr, int fq) const {
;     ...
;         } else { const int col0 = (u.pn - 11) * BM + wc * 32 + 8 * fq;
; #pragma unroll
;             for (int ai = 0; ai < 2; ++ai)
; #pragma unroll
;                 for (int m = 0; m < 4; ++m) { const size_t r = (size_t)(row0 + ai * HALF + m * 16); const float s = tbl[wr * 64 + fr + ai * HALF + m * 16]; unsigned char* rowp = GZ + (size_t)(u.pn - 11) * ldc + r * 256 + (wc * 32 + 8 * fq);
; #pragma unroll
;                     for (int bj = 0; bj < 2; ++bj) { const f32x4 v0 = acc[ai][bj][m][0] * s, v1 = acc[ai][bj][m][1] * s;
;                         unsigned q[8];
; #pragma unroll
;                         for (int i = 0; i < 4; ++i) { q[i] = (unsigned)(sigm(v0[i]) * 255.f + 0.5f); q[4 + i] = (unsigned)(sigm(v1[i]) * 255.f + 0.5f); if (u.pn >= 15) { q[i] = q[i] < 1u ? 1u : q[i]; q[4 + i] = q[4 + i] < 1u ? 1u : q[4 + i]; } }
;                         u32x2 w; w.x = q[0] | (q[1] << 8) | (q[2] << 16) | (q[3] << 24); w.y = q[4] | (q[5] << 8) | (q[6] << 16) | (q[7] << 24);
;                         *(u32x2*)(rowp + bj * HALF) = w; } }
	v_mul_f32_e32 v147, v98, v80
	v_mul_f32_e32 v147, 0xbfb8aa3b, v147
	v_exp_f32_e32 v147, v147
	s_nop 0
	v_add_f32_e32 v147, 1.0, v147
	v_rcp_f32_e32 v160, v147
	v_mul_f32_e32 v147, v90, v80
	v_mul_f32_e32 v147, 0xbfb8aa3b, v147
	v_exp_f32_e32 v147, v147
	s_nop 0
	v_add_f32_e32 v147, 1.0, v147
	v_rcp_f32_e32 v161, v147
	s_nop 0
	v_pk_fma_f32 v[160:161], v[160:161], s[90:91], 0.5 op_sel_hi:[1,0,0]
	s_nop 0
	v_cvt_u32_f32_e32 v149, v160
	v_cvt_u32_f32_e32 v147, v161
	v_max_u32_e32 v159, 1, v149
	v_cndmask_b32_e32 v149, v149, v159, vcc
	v_mul_f32_e32 v159, v99, v80
	v_mul_f32_e32 v159, 0xbfb8aa3b, v159
	v_exp_f32_e32 v159, v159
	v_max_u32_e32 v160, 1, v147
	v_cndmask_b32_e32 v147, v147, v160, vcc
	v_add_f32_e32 v159, 1.0, v159
	v_rcp_f32_e32 v160, v159
	v_mul_f32_e32 v159, v91, v80
	v_mul_f32_e32 v159, 0xbfb8aa3b, v159
	v_exp_f32_e32 v159, v159
	s_nop 0
	v_add_f32_e32 v159, 1.0, v159
	v_rcp_f32_e32 v161, v159
	s_nop 0
	v_pk_fma_f32 v[160:161], v[160:161], s[90:91], 0.5 op_sel_hi:[1,0,0]
	s_nop 0
	v_cvt_u32_f32_e32 v159, v161
	v_cvt_u32_f32_e32 v160, v160
	v_max_u32_e32 v174, 1, v159
	v_max_u32_e32 v161, 1, v160
	v_cndmask_b32_e32 v159, v159, v174, vcc
	v_cndmask_b32_e32 v174, v160, v161, vcc
	v_mul_f32_e32 v160, v100, v80
	v_mul_f32_e32 v161, v92, v80
	v_mul_f32_e32 v160, 0xbfb8aa3b, v160
	v_mul_f32_e32 v161, 0xbfb8aa3b, v161
	v_exp_f32_e32 v160, v160
	v_exp_f32_e32 v161, v161
	v_lshl_or_b32 v149, v174, 8, v149
	v_lshl_or_b32 v147, v159, 8, v147
	v_add_f32_e32 v160, 1.0, v160
	v_add_f32_e32 v161, 1.0, v161
	v_rcp_f32_e32 v160, v160
	v_rcp_f32_e32 v161, v161
	s_nop 0
	v_pk_fma_f32 v[160:161], v[160:161], s[90:91], 0.5 op_sel_hi:[1,0,0]
	s_nop 0
	v_cvt_u32_f32_e32 v161, v161
	v_cvt_u32_f32_e32 v160, v160
	v_max_u32_e32 v176, 1, v161
	v_max_u32_e32 v175, 1, v160
	v_cndmask_b32_e32 v176, v161, v176, vcc
	v_cndmask_b32_e32 v175, v160, v175, vcc
	v_mul_f32_e32 v160, v101, v80
	v_mul_f32_e32 v161, v93, v80
	v_mul_f32_e32 v160, 0xbfb8aa3b, v160
	v_mul_f32_e32 v161, 0xbfb8aa3b, v161
	v_exp_f32_e32 v160, v160
	v_exp_f32_e32 v161, v161
	v_lshlrev_b32_e32 v174, 16, v175
	v_add_f32_e32 v160, 1.0, v160
	v_add_f32_e32 v161, 1.0, v161
	v_rcp_f32_e32 v160, v160
	v_rcp_f32_e32 v161, v161
	s_nop 0
	v_pk_fma_f32 v[160:161], v[160:161], s[90:91], 0.5 op_sel_hi:[1,0,0]
	s_nop 0
	v_cvt_u32_f32_e32 v160, v160
	v_cvt_u32_f32_e32 v161, v161
	v_max_u32_e32 v177, 1, v160
	v_max_u32_e32 v178, 1, v161
	v_cndmask_b32_e32 v160, v160, v177, vcc
	v_cndmask_b32_e32 v161, v161, v178, vcc
	v_lshlrev_b32_e32 v160, 24, v160
	v_or3_b32 v160, v149, v174, v160
	v_lshlrev_b32_e32 v149, 16, v176
	v_lshlrev_b32_e32 v159, 24, v161
	v_or3_b32 v161, v147, v149, v159
	v_mul_f32_e32 v147, v86, v80
	v_mul_f32_e32 v147, 0xbfb8aa3b, v147
	v_exp_f32_e32 v147, v147
	global_store_dwordx2 v[154:155], v[160:161], off
	v_add_f32_e32 v147, 1.0, v147
	v_rcp_f32_e32 v160, v147
	v_mul_f32_e32 v147, v76, v80
	v_mul_f32_e32 v147, 0xbfb8aa3b, v147
	v_exp_f32_e32 v147, v147
	s_nop 0
	v_add_f32_e32 v147, 1.0, v147
	v_rcp_f32_e32 v161, v147
	s_nop 0
	v_pk_fma_f32 v[160:161], v[160:161], s[90:91], 0.5 op_sel_hi:[1,0,0]
	s_nop 0
	v_cvt_u32_f32_e32 v149, v160
	v_cvt_u32_f32_e32 v147, v161
	v_max_u32_e32 v159, 1, v149
	v_cndmask_b32_e32 v149, v149, v159, vcc
	v_mul_f32_e32 v159, v87, v80
	v_mul_f32_e32 v159, 0xbfb8aa3b, v159
	v_exp_f32_e32 v159, v159
	v_max_u32_e32 v160, 1, v147
	v_cndmask_b32_e32 v147, v147, v160, vcc
	v_add_f32_e32 v159, 1.0, v159
	v_rcp_f32_e32 v160, v159
	v_mul_f32_e32 v159, v77, v80
	v_mul_f32_e32 v159, 0xbfb8aa3b, v159
	v_exp_f32_e32 v159, v159
	s_nop 0
	v_add_f32_e32 v159, 1.0, v159
	v_rcp_f32_e32 v161, v159
	s_nop 0
	v_pk_fma_f32 v[160:161], v[160:161], s[90:91], 0.5 op_sel_hi:[1,0,0]
	s_nop 0
	v_cvt_u32_f32_e32 v159, v161
	v_cvt_u32_f32_e32 v160, v160
	v_max_u32_e32 v174, 1, v159
	v_max_u32_e32 v161, 1, v160
	v_cndmask_b32_e32 v159, v159, v174, vcc
	v_cndmask_b32_e32 v174, v160, v161, vcc
	v_mul_f32_e32 v160, v88, v80
	v_mul_f32_e32 v161, v78, v80
	v_mul_f32_e32 v160, 0xbfb8aa3b, v160
	v_mul_f32_e32 v161, 0xbfb8aa3b, v161
	v_exp_f32_e32 v160, v160
	v_exp_f32_e32 v161, v161
	v_lshl_or_b32 v149, v174, 8, v149
	v_lshl_or_b32 v147, v159, 8, v147
	v_add_f32_e32 v160, 1.0, v160
	v_add_f32_e32 v161, 1.0, v161
	v_rcp_f32_e32 v160, v160
	v_rcp_f32_e32 v161, v161
	s_nop 0
	v_pk_fma_f32 v[160:161], v[160:161], s[90:91], 0.5 op_sel_hi:[1,0,0]
	s_nop 0
	v_cvt_u32_f32_e32 v160, v160
	v_cvt_u32_f32_e32 v161, v161
	v_max_u32_e32 v175, 1, v160
	v_cndmask_b32_e32 v175, v160, v175, vcc
	v_mul_f32_e32 v160, v89, v80
	v_mul_f32_e32 v80, v79, v80
	v_mul_f32_e32 v160, 0xbfb8aa3b, v160
	v_mul_f32_e32 v80, 0xbfb8aa3b, v80
	v_exp_f32_e32 v160, v160
	v_exp_f32_e32 v80, v80
	v_max_u32_e32 v176, 1, v161
	v_cndmask_b32_e32 v176, v161, v176, vcc
	v_add_f32_e32 v160, 1.0, v160
	v_add_f32_e32 v80, 1.0, v80
	v_rcp_f32_e32 v160, v160
	v_rcp_f32_e32 v161, v80
	s_nop 0
	v_pk_fma_f32 v[160:161], v[160:161], s[90:91], 0.5 op_sel_hi:[1,0,0]
	s_nop 0
	v_cvt_u32_f32_e32 v160, v160
	v_cvt_u32_f32_e32 v80, v161
	v_max_u32_e32 v161, 1, v160
	v_max_u32_e32 v177, 1, v80
	v_cndmask_b32_e32 v160, v160, v161, vcc
	v_cndmask_b32_e32 v80, v80, v177, vcc
	v_lshlrev_b32_e32 v161, 16, v175
	v_lshlrev_b32_e32 v160, 24, v160
	v_or3_b32 v160, v149, v161, v160
	v_lshlrev_b32_e32 v149, 16, v176
	v_lshlrev_b32_e32 v80, 24, v80
	v_or3_b32 v161, v147, v149, v80
	global_store_dwordx2 v[154:155], v[160:161], off offset:128
	ds_read_b32 v80, v157 offset:192
	v_or_b32_e32 v154, 48, v144
	v_ashrrev_i32_e32 v155, 31, v154
	v_lshlrev_b64 v[154:155], 8, v[154:155]
	v_lshl_add_u64 v[154:155], s[4:5], 0, v[154:155]
	s_waitcnt lgkmcnt(0)
; __device__ __forceinline__ float sigm(float x) { return __builtin_amdgcn_rcpf(1.f + __expf(-x)); }
;     __device__ __forceinline__ void operator()(const f32x4 (&acc)[2][2][4][2], const Unit& u, int wr, int wc, int fr, int fq) const {
;     ...
;         } else { const int col0 = (u.pn - 11) * BM + wc * 32 + 8 * fq;
; #pragma unroll
;             for (int ai = 0; ai < 2; ++ai)
; #pragma unroll
;                 for (int m = 0; m < 4; ++m) { const size_t r = (size_t)(row0 + ai * HALF + m * 16); const float s = tbl[wr * 64 + fr + ai * HALF + m * 16]; unsigned char* rowp = GZ + (size_t)(u.pn - 11) * ldc + r * 256 + (wc * 32 + 8 * fq);
; #pragma unroll
;                     for (int bj = 0; bj < 2; ++bj) { const f32x4 v0 = acc[ai][bj][m][0] * s, v1 = acc[ai][bj][m][1] * s;
;                         unsigned q[8];
; #pragma unroll
;                         for (int i = 0; i < 4; ++i) { q[i] = (unsigned)(sigm(v0[i]) * 255.f + 0.5f); q[4 + i] = (unsigned)(sigm(v1[i]) * 255.f + 0.5f); if (u.pn >= 15) { q[i] = q[i] < 1u ? 1u : q[i]; q[4 + i] = q[4 + i] < 1u ? 1u : q[4 + i]; } }
;                         u32x2 w; w.x = q[0] | (q[1] << 8) | (q[2] << 16) | (q[3] << 24); w.y = q[4] | (q[5] << 8) | (q[6] << 16) | (q[7] << 24);
;                         *(u32x2*)(rowp + bj * HALF) = w; } }
	v_mul_f32_e32 v147, v82, v80
	v_mul_f32_e32 v147, 0xbfb8aa3b, v147
	v_exp_f32_e32 v147, v147
	v_lshl_add_u64 v[154:155], v[154:155], 0, v[138:139]
	v_add_f32_e32 v147, 1.0, v147
	v_rcp_f32_e32 v160, v147
	v_mul_f32_e32 v147, v72, v80
	v_mul_f32_e32 v147, 0xbfb8aa3b, v147
	v_exp_f32_e32 v147, v147
	s_nop 0
	v_add_f32_e32 v147, 1.0, v147
	v_rcp_f32_e32 v161, v147
	s_nop 0
	v_pk_fma_f32 v[160:161], v[160:161], s[90:91], 0.5 op_sel_hi:[1,0,0]
	s_nop 0
	v_cvt_u32_f32_e32 v149, v160
	v_cvt_u32_f32_e32 v147, v161
	v_max_u32_e32 v159, 1, v149
	v_cndmask_b32_e32 v149, v149, v159, vcc
	v_mul_f32_e32 v159, v83, v80
	v_mul_f32_e32 v159, 0xbfb8aa3b, v159
	v_exp_f32_e32 v159, v159
	v_max_u32_e32 v160, 1, v147
	v_cndmask_b32_e32 v147, v147, v160, vcc
	v_add_f32_e32 v159, 1.0, v159
	v_rcp_f32_e32 v160, v159
	v_mul_f32_e32 v159, v73, v80
	v_mul_f32_e32 v159, 0xbfb8aa3b, v159
	v_exp_f32_e32 v159, v159
	s_nop 0
	v_add_f32_e32 v159, 1.0, v159
	v_rcp_f32_e32 v161, v159
	s_nop 0
	v_pk_fma_f32 v[160:161], v[160:161], s[90:91], 0.5 op_sel_hi:[1,0,0]
	s_nop 0
	v_cvt_u32_f32_e32 v159, v161
	v_cvt_u32_f32_e32 v160, v160
	v_max_u32_e32 v174, 1, v159
	v_max_u32_e32 v161, 1, v160
	v_cndmask_b32_e32 v159, v159, v174, vcc
	v_cndmask_b32_e32 v174, v160, v161, vcc
	v_mul_f32_e32 v160, v84, v80
	v_mul_f32_e32 v161, v74, v80
	v_mul_f32_e32 v160, 0xbfb8aa3b, v160
	v_mul_f32_e32 v161, 0xbfb8aa3b, v161
	v_exp_f32_e32 v160, v160
	v_exp_f32_e32 v161, v161
	v_lshl_or_b32 v149, v174, 8, v149
	v_lshl_or_b32 v147, v159, 8, v147
	v_add_f32_e32 v160, 1.0, v160
	v_add_f32_e32 v161, 1.0, v161
	v_rcp_f32_e32 v160, v160
	v_rcp_f32_e32 v161, v161
	s_nop 0
	v_pk_fma_f32 v[160:161], v[160:161], s[90:91], 0.5 op_sel_hi:[1,0,0]
	s_nop 0
	v_cvt_u32_f32_e32 v161, v161
	v_cvt_u32_f32_e32 v160, v160
	v_max_u32_e32 v176, 1, v161
	v_max_u32_e32 v175, 1, v160
	v_cndmask_b32_e32 v176, v161, v176, vcc
	v_cndmask_b32_e32 v175, v160, v175, vcc
	v_mul_f32_e32 v160, v85, v80
	v_mul_f32_e32 v161, v75, v80
	v_mul_f32_e32 v160, 0xbfb8aa3b, v160
	v_mul_f32_e32 v161, 0xbfb8aa3b, v161
	v_exp_f32_e32 v160, v160
	v_exp_f32_e32 v161, v161
	v_lshlrev_b32_e32 v174, 16, v175
	v_add_f32_e32 v160, 1.0, v160
	v_add_f32_e32 v161, 1.0, v161
	v_rcp_f32_e32 v160, v160
	v_rcp_f32_e32 v161, v161
	s_nop 0
	v_pk_fma_f32 v[160:161], v[160:161], s[90:91], 0.5 op_sel_hi:[1,0,0]
	s_nop 0
	v_cvt_u32_f32_e32 v160, v160
	v_cvt_u32_f32_e32 v161, v161
	v_max_u32_e32 v177, 1, v160
	v_max_u32_e32 v178, 1, v161
	v_cndmask_b32_e32 v160, v160, v177, vcc
	v_cndmask_b32_e32 v161, v161, v178, vcc
	v_lshlrev_b32_e32 v160, 24, v160
	v_or3_b32 v160, v149, v174, v160
	v_lshlrev_b32_e32 v149, 16, v176
	v_lshlrev_b32_e32 v159, 24, v161
	v_or3_b32 v161, v147, v149, v159
	v_mul_f32_e32 v147, v68, v80
	v_mul_f32_e32 v147, 0xbfb8aa3b, v147
	v_exp_f32_e32 v147, v147
	global_store_dwordx2 v[154:155], v[160:161], off
	v_add_f32_e32 v147, 1.0, v147
	v_rcp_f32_e32 v160, v147
	v_mul_f32_e32 v147, v64, v80
	v_mul_f32_e32 v147, 0xbfb8aa3b, v147
	v_exp_f32_e32 v147, v147
	s_nop 0
	v_add_f32_e32 v147, 1.0, v147
	v_rcp_f32_e32 v161, v147
	s_nop 0
	v_pk_fma_f32 v[160:161], v[160:161], s[90:91], 0.5 op_sel_hi:[1,0,0]
	s_nop 0
	v_cvt_u32_f32_e32 v149, v160
	v_cvt_u32_f32_e32 v147, v161
	v_max_u32_e32 v159, 1, v149
	v_cndmask_b32_e32 v149, v149, v159, vcc
	v_mul_f32_e32 v159, v69, v80
	v_mul_f32_e32 v159, 0xbfb8aa3b, v159
	v_exp_f32_e32 v159, v159
	v_max_u32_e32 v160, 1, v147
	v_cndmask_b32_e32 v147, v147, v160, vcc
	v_add_f32_e32 v159, 1.0, v159
	v_rcp_f32_e32 v160, v159
	v_mul_f32_e32 v159, v65, v80
	v_mul_f32_e32 v159, 0xbfb8aa3b, v159
	v_exp_f32_e32 v159, v159
	s_nop 0
	v_add_f32_e32 v159, 1.0, v159
	v_rcp_f32_e32 v161, v159
	s_nop 0
	v_pk_fma_f32 v[160:161], v[160:161], s[90:91], 0.5 op_sel_hi:[1,0,0]
	s_nop 0
	v_cvt_u32_f32_e32 v159, v161
	v_cvt_u32_f32_e32 v160, v160
	v_max_u32_e32 v174, 1, v159
	v_max_u32_e32 v161, 1, v160
	v_cndmask_b32_e32 v159, v159, v174, vcc
	v_cndmask_b32_e32 v174, v160, v161, vcc
	v_mul_f32_e32 v160, v70, v80
	v_mul_f32_e32 v161, v66, v80
	v_mul_f32_e32 v160, 0xbfb8aa3b, v160
	v_mul_f32_e32 v161, 0xbfb8aa3b, v161
	v_exp_f32_e32 v160, v160
	v_exp_f32_e32 v161, v161
	v_lshl_or_b32 v149, v174, 8, v149
	v_lshl_or_b32 v147, v159, 8, v147
	v_add_f32_e32 v160, 1.0, v160
	v_add_f32_e32 v161, 1.0, v161
	v_rcp_f32_e32 v160, v160
	v_rcp_f32_e32 v161, v161
	s_nop 0
	v_pk_fma_f32 v[160:161], v[160:161], s[90:91], 0.5 op_sel_hi:[1,0,0]
	s_nop 0
	v_cvt_u32_f32_e32 v160, v160
	v_cvt_u32_f32_e32 v161, v161
	v_max_u32_e32 v175, 1, v160
	v_cndmask_b32_e32 v175, v160, v175, vcc
	v_mul_f32_e32 v160, v71, v80
	v_mul_f32_e32 v80, v67, v80
	v_mul_f32_e32 v160, 0xbfb8aa3b, v160
	v_mul_f32_e32 v80, 0xbfb8aa3b, v80
	v_exp_f32_e32 v160, v160
	v_exp_f32_e32 v80, v80
	v_max_u32_e32 v176, 1, v161
	v_cndmask_b32_e32 v176, v161, v176, vcc
	v_add_f32_e32 v160, 1.0, v160
	v_add_f32_e32 v80, 1.0, v80
	v_rcp_f32_e32 v160, v160
	v_rcp_f32_e32 v161, v80
	s_nop 0
	v_pk_fma_f32 v[160:161], v[160:161], s[90:91], 0.5 op_sel_hi:[1,0,0]
	s_nop 0
	v_cvt_u32_f32_e32 v160, v160
	v_cvt_u32_f32_e32 v80, v161
	v_max_u32_e32 v161, 1, v160
	v_max_u32_e32 v177, 1, v80
	v_cndmask_b32_e32 v160, v160, v161, vcc
	v_cndmask_b32_e32 v80, v80, v177, vcc
	v_lshlrev_b32_e32 v161, 16, v175
	v_lshlrev_b32_e32 v160, 24, v160
	v_or3_b32 v160, v149, v161, v160
	v_lshlrev_b32_e32 v149, 16, v176
	v_lshlrev_b32_e32 v80, 24, v80
	v_or3_b32 v161, v147, v149, v80
	global_store_dwordx2 v[154:155], v[160:161], off offset:128
	ds_read_b32 v80, v157 offset:512
	v_lshl_add_u64 v[154:155], v[152:153], 0, s[0:1]
	s_mov_b64 s[0:1], 0x9000
	s_waitcnt lgkmcnt(0)
; __device__ __forceinline__ float sigm(float x) { return __builtin_amdgcn_rcpf(1.f + __expf(-x)); }
;     __device__ __forceinline__ void operator()(const f32x4 (&acc)[2][2][4][2], const Unit& u, int wr, int wc, int fr, int fq) const {
;     ...
;         } else { const int col0 = (u.pn - 11) * BM + wc * 32 + 8 * fq;
; #pragma unroll
;             for (int ai = 0; ai < 2; ++ai)
; #pragma unroll
;                 for (int m = 0; m < 4; ++m) { const size_t r = (size_t)(row0 + ai * HALF + m * 16); const float s = tbl[wr * 64 + fr + ai * HALF + m * 16]; unsigned char* rowp = GZ + (size_t)(u.pn - 11) * ldc + r * 256 + (wc * 32 + 8 * fq);
; #pragma unroll
;                     for (int bj = 0; bj < 2; ++bj) { const f32x4 v0 = acc[ai][bj][m][0] * s, v1 = acc[ai][bj][m][1] * s;
;                         unsigned q[8];
; #pragma unroll
;                         for (int i = 0; i < 4; ++i) { q[i] = (unsigned)(sigm(v0[i]) * 255.f + 0.5f); q[4 + i] = (unsigned)(sigm(v1[i]) * 255.f + 0.5f); if (u.pn >= 15) { q[i] = q[i] < 1u ? 1u : q[i]; q[4 + i] = q[4 + i] < 1u ? 1u : q[4 + i]; } }
;                         u32x2 w; w.x = q[0] | (q[1] << 8) | (q[2] << 16) | (q[3] << 24); w.y = q[4] | (q[5] << 8) | (q[6] << 16) | (q[7] << 24);
;                         *(u32x2*)(rowp + bj * HALF) = w; } }
	v_mul_f32_e32 v147, v60, v80
	v_mul_f32_e32 v147, 0xbfb8aa3b, v147
	v_exp_f32_e32 v147, v147
	s_nop 0
	v_add_f32_e32 v147, 1.0, v147
	v_rcp_f32_e32 v160, v147
	v_mul_f32_e32 v147, v56, v80
	v_mul_f32_e32 v147, 0xbfb8aa3b, v147
	v_exp_f32_e32 v147, v147
	s_nop 0
	v_add_f32_e32 v147, 1.0, v147
	v_rcp_f32_e32 v161, v147
	s_nop 0
	v_pk_fma_f32 v[160:161], v[160:161], s[90:91], 0.5 op_sel_hi:[1,0,0]
	s_nop 0
	v_cvt_u32_f32_e32 v149, v160
	v_cvt_u32_f32_e32 v147, v161
	v_max_u32_e32 v159, 1, v149
	v_cndmask_b32_e32 v149, v149, v159, vcc
	v_mul_f32_e32 v159, v61, v80
	v_mul_f32_e32 v159, 0xbfb8aa3b, v159
	v_exp_f32_e32 v159, v159
	v_max_u32_e32 v160, 1, v147
	v_cndmask_b32_e32 v147, v147, v160, vcc
	v_add_f32_e32 v159, 1.0, v159
	v_rcp_f32_e32 v160, v159
	v_mul_f32_e32 v159, v57, v80
	v_mul_f32_e32 v159, 0xbfb8aa3b, v159
	v_exp_f32_e32 v159, v159
	s_nop 0
	v_add_f32_e32 v159, 1.0, v159
	v_rcp_f32_e32 v161, v159
	s_nop 0
	v_pk_fma_f32 v[160:161], v[160:161], s[90:91], 0.5 op_sel_hi:[1,0,0]
	s_nop 0
	v_cvt_u32_f32_e32 v159, v161
	v_cvt_u32_f32_e32 v160, v160
	v_max_u32_e32 v174, 1, v159
	v_max_u32_e32 v161, 1, v160
	v_cndmask_b32_e32 v159, v159, v174, vcc
	v_cndmask_b32_e32 v174, v160, v161, vcc
	v_mul_f32_e32 v160, v62, v80
	v_mul_f32_e32 v161, v58, v80
	v_mul_f32_e32 v160, 0xbfb8aa3b, v160
	v_mul_f32_e32 v161, 0xbfb8aa3b, v161
	v_exp_f32_e32 v160, v160
	v_exp_f32_e32 v161, v161
	v_lshl_or_b32 v149, v174, 8, v149
	v_lshl_or_b32 v147, v159, 8, v147
	v_add_f32_e32 v160, 1.0, v160
	v_add_f32_e32 v161, 1.0, v161
	v_rcp_f32_e32 v160, v160
	v_rcp_f32_e32 v161, v161
	s_nop 0
	v_pk_fma_f32 v[160:161], v[160:161], s[90:91], 0.5 op_sel_hi:[1,0,0]
	s_nop 0
	v_cvt_u32_f32_e32 v161, v161
	v_cvt_u32_f32_e32 v160, v160
	v_max_u32_e32 v176, 1, v161
	v_max_u32_e32 v175, 1, v160
	v_cndmask_b32_e32 v176, v161, v176, vcc
	v_cndmask_b32_e32 v175, v160, v175, vcc
	v_mul_f32_e32 v160, v63, v80
	v_mul_f32_e32 v161, v59, v80
	v_mul_f32_e32 v160, 0xbfb8aa3b, v160
	v_mul_f32_e32 v161, 0xbfb8aa3b, v161
	v_exp_f32_e32 v160, v160
	v_exp_f32_e32 v161, v161
	v_lshlrev_b32_e32 v174, 16, v175
	v_add_f32_e32 v160, 1.0, v160
	v_add_f32_e32 v161, 1.0, v161
	v_rcp_f32_e32 v160, v160
	v_rcp_f32_e32 v161, v161
	s_nop 0
	v_pk_fma_f32 v[160:161], v[160:161], s[90:91], 0.5 op_sel_hi:[1,0,0]
	s_nop 0
	v_cvt_u32_f32_e32 v160, v160
	v_cvt_u32_f32_e32 v161, v161
	v_max_u32_e32 v177, 1, v160
	v_max_u32_e32 v178, 1, v161
	v_cndmask_b32_e32 v160, v160, v177, vcc
	v_cndmask_b32_e32 v161, v161, v178, vcc
	v_lshlrev_b32_e32 v160, 24, v160
	v_or3_b32 v160, v149, v174, v160
	v_lshlrev_b32_e32 v149, 16, v176
	v_lshlrev_b32_e32 v159, 24, v161
	v_or3_b32 v161, v147, v149, v159
	v_mul_f32_e32 v147, v48, v80
	v_mul_f32_e32 v147, 0xbfb8aa3b, v147
	v_exp_f32_e32 v147, v147
	v_add_co_u32_e64 v174, s[4:5], s33, v152
	v_add_f32_e32 v147, 1.0, v147
	s_nop 0
	v_addc_co_u32_e64 v175, s[4:5], 0, v153, s[4:5]
	global_store_dwordx2 v[174:175], v[160:161], off
	v_rcp_f32_e32 v160, v147
	v_mul_f32_e32 v147, v40, v80
	v_mul_f32_e32 v147, 0xbfb8aa3b, v147
	v_exp_f32_e32 v147, v147
	s_nop 0
	v_add_f32_e32 v147, 1.0, v147
	v_rcp_f32_e32 v161, v147
	s_nop 0
	v_pk_fma_f32 v[160:161], v[160:161], s[90:91], 0.5 op_sel_hi:[1,0,0]
	s_nop 0
	v_cvt_u32_f32_e32 v149, v160
	v_cvt_u32_f32_e32 v147, v161
	v_max_u32_e32 v159, 1, v149
	v_cndmask_b32_e32 v149, v149, v159, vcc
	v_mul_f32_e32 v159, v49, v80
	v_mul_f32_e32 v159, 0xbfb8aa3b, v159
	v_exp_f32_e32 v159, v159
	v_max_u32_e32 v160, 1, v147
	v_cndmask_b32_e32 v147, v147, v160, vcc
	v_add_f32_e32 v159, 1.0, v159
	v_rcp_f32_e32 v160, v159
	v_mul_f32_e32 v159, v41, v80
	v_mul_f32_e32 v159, 0xbfb8aa3b, v159
	v_exp_f32_e32 v159, v159
	s_nop 0
	v_add_f32_e32 v159, 1.0, v159
	v_rcp_f32_e32 v161, v159
	s_nop 0
	v_pk_fma_f32 v[160:161], v[160:161], s[90:91], 0.5 op_sel_hi:[1,0,0]
	s_nop 0
	v_cvt_u32_f32_e32 v159, v161
	v_cvt_u32_f32_e32 v160, v160
	v_max_u32_e32 v174, 1, v159
	v_max_u32_e32 v161, 1, v160
	v_cndmask_b32_e32 v159, v159, v174, vcc
	v_cndmask_b32_e32 v174, v160, v161, vcc
	v_mul_f32_e32 v160, v50, v80
	v_mul_f32_e32 v161, v42, v80
	v_mul_f32_e32 v160, 0xbfb8aa3b, v160
	v_mul_f32_e32 v161, 0xbfb8aa3b, v161
	v_exp_f32_e32 v160, v160
	v_exp_f32_e32 v161, v161
	v_lshl_or_b32 v149, v174, 8, v149
	v_lshl_or_b32 v147, v159, 8, v147
	v_add_f32_e32 v160, 1.0, v160
	v_add_f32_e32 v161, 1.0, v161
	v_rcp_f32_e32 v160, v160
	v_rcp_f32_e32 v161, v161
	s_nop 0
	v_pk_fma_f32 v[160:161], v[160:161], s[90:91], 0.5 op_sel_hi:[1,0,0]
	s_nop 0
	v_cvt_u32_f32_e32 v160, v160
	v_cvt_u32_f32_e32 v161, v161
	v_max_u32_e32 v175, 1, v160
	v_cndmask_b32_e32 v175, v160, v175, vcc
	v_mul_f32_e32 v160, v51, v80
	v_mul_f32_e32 v80, v43, v80
	v_mul_f32_e32 v160, 0xbfb8aa3b, v160
	v_mul_f32_e32 v80, 0xbfb8aa3b, v80
	v_exp_f32_e32 v160, v160
	v_exp_f32_e32 v80, v80
	v_max_u32_e32 v176, 1, v161
	v_cndmask_b32_e32 v176, v161, v176, vcc
	v_add_f32_e32 v160, 1.0, v160
	v_add_f32_e32 v80, 1.0, v80
	v_rcp_f32_e32 v160, v160
	v_rcp_f32_e32 v161, v80
	s_nop 0
	v_pk_fma_f32 v[160:161], v[160:161], s[90:91], 0.5 op_sel_hi:[1,0,0]
	s_nop 0
	v_cvt_u32_f32_e32 v160, v160
	v_cvt_u32_f32_e32 v80, v161
	v_max_u32_e32 v161, 1, v160
	v_max_u32_e32 v177, 1, v80
	v_cndmask_b32_e32 v160, v160, v161, vcc
	v_cndmask_b32_e32 v80, v80, v177, vcc
	v_lshlrev_b32_e32 v161, 16, v175
	v_lshlrev_b32_e32 v160, 24, v160
	v_or3_b32 v160, v149, v161, v160
	v_lshlrev_b32_e32 v149, 16, v176
	v_lshlrev_b32_e32 v80, 24, v80
	v_or3_b32 v161, v147, v149, v80
	global_store_dwordx2 v[154:155], v[160:161], off offset:128
	ds_read_b32 v80, v157 offset:576
	v_lshl_add_u64 v[154:155], v[152:153], 0, s[0:1]
	s_mov_b32 s0, 0x9000
	s_waitcnt lgkmcnt(0)
; __device__ __forceinline__ float sigm(float x) { return __builtin_amdgcn_rcpf(1.f + __expf(-x)); }
;     __device__ __forceinline__ void operator()(const f32x4 (&acc)[2][2][4][2], const Unit& u, int wr, int wc, int fr, int fq) const {
;     ...
;         } else { const int col0 = (u.pn - 11) * BM + wc * 32 + 8 * fq;
; #pragma unroll
;             for (int ai = 0; ai < 2; ++ai)
; #pragma unroll
;                 for (int m = 0; m < 4; ++m) { const size_t r = (size_t)(row0 + ai * HALF + m * 16); const float s = tbl[wr * 64 + fr + ai * HALF + m * 16]; unsigned char* rowp = GZ + (size_t)(u.pn - 11) * ldc + r * 256 + (wc * 32 + 8 * fq);
; #pragma unroll
;                     for (int bj = 0; bj < 2; ++bj) { const f32x4 v0 = acc[ai][bj][m][0] * s, v1 = acc[ai][bj][m][1] * s;
;                         unsigned q[8];
; #pragma unroll
;                         for (int i = 0; i < 4; ++i) { q[i] = (unsigned)(sigm(v0[i]) * 255.f + 0.5f); q[4 + i] = (unsigned)(sigm(v1[i]) * 255.f + 0.5f); if (u.pn >= 15) { q[i] = q[i] < 1u ? 1u : q[i]; q[4 + i] = q[4 + i] < 1u ? 1u : q[4 + i]; } }
;                         u32x2 w; w.x = q[0] | (q[1] << 8) | (q[2] << 16) | (q[3] << 24); w.y = q[4] | (q[5] << 8) | (q[6] << 16) | (q[7] << 24);
;                         *(u32x2*)(rowp + bj * HALF) = w; } }
	v_mul_f32_e32 v147, v52, v80
	v_mul_f32_e32 v147, 0xbfb8aa3b, v147
	v_exp_f32_e32 v147, v147
	s_nop 0
	v_add_f32_e32 v147, 1.0, v147
	v_rcp_f32_e32 v160, v147
	v_mul_f32_e32 v147, v44, v80
	v_mul_f32_e32 v147, 0xbfb8aa3b, v147
	v_exp_f32_e32 v147, v147
	s_nop 0
	v_add_f32_e32 v147, 1.0, v147
	v_rcp_f32_e32 v161, v147
	s_nop 0
	v_pk_fma_f32 v[160:161], v[160:161], s[90:91], 0.5 op_sel_hi:[1,0,0]
	s_nop 0
	v_cvt_u32_f32_e32 v149, v160
	v_cvt_u32_f32_e32 v147, v161
	v_max_u32_e32 v159, 1, v149
	v_cndmask_b32_e32 v149, v149, v159, vcc
	v_mul_f32_e32 v159, v53, v80
	v_mul_f32_e32 v159, 0xbfb8aa3b, v159
	v_exp_f32_e32 v159, v159
	v_max_u32_e32 v160, 1, v147
	v_cndmask_b32_e32 v147, v147, v160, vcc
	v_add_f32_e32 v159, 1.0, v159
	v_rcp_f32_e32 v160, v159
	v_mul_f32_e32 v159, v45, v80
	v_mul_f32_e32 v159, 0xbfb8aa3b, v159
	v_exp_f32_e32 v159, v159
	s_nop 0
	v_add_f32_e32 v159, 1.0, v159
	v_rcp_f32_e32 v161, v159
	s_nop 0
	v_pk_fma_f32 v[160:161], v[160:161], s[90:91], 0.5 op_sel_hi:[1,0,0]
	s_nop 0
	v_cvt_u32_f32_e32 v159, v161
	v_cvt_u32_f32_e32 v160, v160
	v_max_u32_e32 v174, 1, v159
	v_max_u32_e32 v161, 1, v160
	v_cndmask_b32_e32 v159, v159, v174, vcc
	v_cndmask_b32_e32 v174, v160, v161, vcc
	v_mul_f32_e32 v160, v54, v80
	v_mul_f32_e32 v161, v46, v80
	v_mul_f32_e32 v160, 0xbfb8aa3b, v160
	v_mul_f32_e32 v161, 0xbfb8aa3b, v161
	v_exp_f32_e32 v160, v160
	v_exp_f32_e32 v161, v161
	v_lshl_or_b32 v149, v174, 8, v149
	v_lshl_or_b32 v147, v159, 8, v147
	v_add_f32_e32 v160, 1.0, v160
	v_add_f32_e32 v161, 1.0, v161
	v_rcp_f32_e32 v160, v160
	v_rcp_f32_e32 v161, v161
	s_nop 0
	v_pk_fma_f32 v[160:161], v[160:161], s[90:91], 0.5 op_sel_hi:[1,0,0]
	s_nop 0
	v_cvt_u32_f32_e32 v161, v161
	v_cvt_u32_f32_e32 v160, v160
	v_max_u32_e32 v176, 1, v161
	v_max_u32_e32 v175, 1, v160
	v_cndmask_b32_e32 v176, v161, v176, vcc
	v_cndmask_b32_e32 v175, v160, v175, vcc
	v_mul_f32_e32 v160, v55, v80
	v_mul_f32_e32 v161, v47, v80
	v_mul_f32_e32 v160, 0xbfb8aa3b, v160
	v_mul_f32_e32 v161, 0xbfb8aa3b, v161
	v_exp_f32_e32 v160, v160
	v_exp_f32_e32 v161, v161
	v_lshlrev_b32_e32 v174, 16, v175
	v_add_f32_e32 v160, 1.0, v160
	v_add_f32_e32 v161, 1.0, v161
	v_rcp_f32_e32 v160, v160
	v_rcp_f32_e32 v161, v161
	s_nop 0
	v_pk_fma_f32 v[160:161], v[160:161], s[90:91], 0.5 op_sel_hi:[1,0,0]
	s_nop 0
	v_cvt_u32_f32_e32 v160, v160
	v_cvt_u32_f32_e32 v161, v161
	v_max_u32_e32 v177, 1, v160
	v_max_u32_e32 v178, 1, v161
	v_cndmask_b32_e32 v160, v160, v177, vcc
	v_cndmask_b32_e32 v161, v161, v178, vcc
	v_lshlrev_b32_e32 v160, 24, v160
	v_or3_b32 v160, v149, v174, v160
	v_lshlrev_b32_e32 v149, 16, v176
	v_lshlrev_b32_e32 v159, 24, v161
	v_or3_b32 v161, v147, v149, v159
	v_mul_f32_e32 v147, v32, v80
	v_mul_f32_e32 v147, 0xbfb8aa3b, v147
	v_exp_f32_e32 v147, v147
	v_add_co_u32_e64 v174, s[4:5], s0, v152
	s_mov_b64 s[0:1], 0xa000
	s_nop 0
	v_addc_co_u32_e64 v175, s[4:5], 0, v153, s[4:5]
	v_add_f32_e32 v147, 1.0, v147
	global_store_dwordx2 v[174:175], v[160:161], off
	v_rcp_f32_e32 v160, v147
	v_mul_f32_e32 v147, v24, v80
	v_mul_f32_e32 v147, 0xbfb8aa3b, v147
	v_exp_f32_e32 v147, v147
	s_nop 0
	v_add_f32_e32 v147, 1.0, v147
	v_rcp_f32_e32 v161, v147
	s_nop 0
	v_pk_fma_f32 v[160:161], v[160:161], s[90:91], 0.5 op_sel_hi:[1,0,0]
	s_nop 0
	v_cvt_u32_f32_e32 v149, v160
	v_cvt_u32_f32_e32 v147, v161
	v_max_u32_e32 v159, 1, v149
	v_cndmask_b32_e32 v149, v149, v159, vcc
	v_mul_f32_e32 v159, v33, v80
	v_mul_f32_e32 v159, 0xbfb8aa3b, v159
	v_exp_f32_e32 v159, v159
	v_max_u32_e32 v160, 1, v147
	v_cndmask_b32_e32 v147, v147, v160, vcc
	v_add_f32_e32 v159, 1.0, v159
	v_rcp_f32_e32 v160, v159
	v_mul_f32_e32 v159, v25, v80
	v_mul_f32_e32 v159, 0xbfb8aa3b, v159
	v_exp_f32_e32 v159, v159
	s_nop 0
	v_add_f32_e32 v159, 1.0, v159
	v_rcp_f32_e32 v161, v159
	s_nop 0
	v_pk_fma_f32 v[160:161], v[160:161], s[90:91], 0.5 op_sel_hi:[1,0,0]
	s_nop 0
	v_cvt_u32_f32_e32 v159, v161
	v_cvt_u32_f32_e32 v160, v160
	v_max_u32_e32 v174, 1, v159
	v_max_u32_e32 v161, 1, v160
	v_cndmask_b32_e32 v159, v159, v174, vcc
	v_cndmask_b32_e32 v174, v160, v161, vcc
	v_mul_f32_e32 v160, v34, v80
	v_mul_f32_e32 v161, v26, v80
	v_mul_f32_e32 v160, 0xbfb8aa3b, v160
	v_mul_f32_e32 v161, 0xbfb8aa3b, v161
	v_exp_f32_e32 v160, v160
	v_exp_f32_e32 v161, v161
	v_lshl_or_b32 v149, v174, 8, v149
	v_lshl_or_b32 v147, v159, 8, v147
	v_add_f32_e32 v160, 1.0, v160
	v_add_f32_e32 v161, 1.0, v161
	v_rcp_f32_e32 v160, v160
	v_rcp_f32_e32 v161, v161
	s_nop 0
	v_pk_fma_f32 v[160:161], v[160:161], s[90:91], 0.5 op_sel_hi:[1,0,0]
	s_nop 0
	v_cvt_u32_f32_e32 v160, v160
	v_cvt_u32_f32_e32 v161, v161
	v_max_u32_e32 v175, 1, v160
	v_cndmask_b32_e32 v175, v160, v175, vcc
	v_mul_f32_e32 v160, v35, v80
	v_mul_f32_e32 v80, v27, v80
	v_mul_f32_e32 v160, 0xbfb8aa3b, v160
	v_mul_f32_e32 v80, 0xbfb8aa3b, v80
	v_exp_f32_e32 v160, v160
	v_exp_f32_e32 v80, v80
	v_max_u32_e32 v176, 1, v161
	v_cndmask_b32_e32 v176, v161, v176, vcc
	v_add_f32_e32 v160, 1.0, v160
	v_add_f32_e32 v80, 1.0, v80
	v_rcp_f32_e32 v160, v160
	v_rcp_f32_e32 v161, v80
	s_nop 0
	v_pk_fma_f32 v[160:161], v[160:161], s[90:91], 0.5 op_sel_hi:[1,0,0]
	s_nop 0
	v_cvt_u32_f32_e32 v160, v160
	v_cvt_u32_f32_e32 v80, v161
	v_max_u32_e32 v161, 1, v160
	v_max_u32_e32 v177, 1, v80
	v_cndmask_b32_e32 v160, v160, v161, vcc
	v_cndmask_b32_e32 v80, v80, v177, vcc
	v_lshlrev_b32_e32 v161, 16, v175
	v_lshlrev_b32_e32 v160, 24, v160
	v_or3_b32 v160, v149, v161, v160
	v_lshlrev_b32_e32 v149, 16, v176
	v_lshlrev_b32_e32 v80, 24, v80
	v_or3_b32 v161, v147, v149, v80
	global_store_dwordx2 v[154:155], v[160:161], off offset:128
	ds_read_b32 v80, v157 offset:640
	v_lshl_add_u64 v[154:155], v[152:153], 0, s[0:1]
	s_mov_b64 s[0:1], 0xb000
	s_waitcnt lgkmcnt(0)
; __device__ __forceinline__ float sigm(float x) { return __builtin_amdgcn_rcpf(1.f + __expf(-x)); }
;     __device__ __forceinline__ void operator()(const f32x4 (&acc)[2][2][4][2], const Unit& u, int wr, int wc, int fr, int fq) const {
;     ...
;         } else { const int col0 = (u.pn - 11) * BM + wc * 32 + 8 * fq;
; #pragma unroll
;             for (int ai = 0; ai < 2; ++ai)
; #pragma unroll
;                 for (int m = 0; m < 4; ++m) { const size_t r = (size_t)(row0 + ai * HALF + m * 16); const float s = tbl[wr * 64 + fr + ai * HALF + m * 16]; unsigned char* rowp = GZ + (size_t)(u.pn - 11) * ldc + r * 256 + (wc * 32 + 8 * fq);
; #pragma unroll
;                     for (int bj = 0; bj < 2; ++bj) { const f32x4 v0 = acc[ai][bj][m][0] * s, v1 = acc[ai][bj][m][1] * s;
;                         unsigned q[8];
; #pragma unroll
;                         for (int i = 0; i < 4; ++i) { q[i] = (unsigned)(sigm(v0[i]) * 255.f + 0.5f); q[4 + i] = (unsigned)(sigm(v1[i]) * 255.f + 0.5f); if (u.pn >= 15) { q[i] = q[i] < 1u ? 1u : q[i]; q[4 + i] = q[4 + i] < 1u ? 1u : q[4 + i]; } }
;                         u32x2 w; w.x = q[0] | (q[1] << 8) | (q[2] << 16) | (q[3] << 24); w.y = q[4] | (q[5] << 8) | (q[6] << 16) | (q[7] << 24);
;                         *(u32x2*)(rowp + bj * HALF) = w; } }
	v_mul_f32_e32 v147, v36, v80
	v_mul_f32_e32 v147, 0xbfb8aa3b, v147
	v_exp_f32_e32 v147, v147
	s_nop 0
	v_add_f32_e32 v147, 1.0, v147
	v_rcp_f32_e32 v160, v147
	v_mul_f32_e32 v147, v28, v80
	v_mul_f32_e32 v147, 0xbfb8aa3b, v147
	v_exp_f32_e32 v147, v147
	s_nop 0
	v_add_f32_e32 v147, 1.0, v147
	v_rcp_f32_e32 v161, v147
	s_nop 0
	v_pk_fma_f32 v[160:161], v[160:161], s[90:91], 0.5 op_sel_hi:[1,0,0]
	s_nop 0
	v_cvt_u32_f32_e32 v149, v160
	v_cvt_u32_f32_e32 v147, v161
	v_max_u32_e32 v159, 1, v149
	v_cndmask_b32_e32 v149, v149, v159, vcc
	v_mul_f32_e32 v159, v37, v80
	v_mul_f32_e32 v159, 0xbfb8aa3b, v159
	v_exp_f32_e32 v159, v159
	v_max_u32_e32 v160, 1, v147
	v_cndmask_b32_e32 v147, v147, v160, vcc
	v_add_f32_e32 v159, 1.0, v159
	v_rcp_f32_e32 v160, v159
	v_mul_f32_e32 v159, v29, v80
	v_mul_f32_e32 v159, 0xbfb8aa3b, v159
	v_exp_f32_e32 v159, v159
	s_nop 0
	v_add_f32_e32 v159, 1.0, v159
	v_rcp_f32_e32 v161, v159
	s_nop 0
	v_pk_fma_f32 v[160:161], v[160:161], s[90:91], 0.5 op_sel_hi:[1,0,0]
	s_nop 0
	v_cvt_u32_f32_e32 v159, v161
	v_cvt_u32_f32_e32 v160, v160
	v_max_u32_e32 v174, 1, v159
	v_max_u32_e32 v161, 1, v160
	v_cndmask_b32_e32 v159, v159, v174, vcc
	v_cndmask_b32_e32 v174, v160, v161, vcc
	v_mul_f32_e32 v160, v38, v80
	v_mul_f32_e32 v161, v30, v80
	v_mul_f32_e32 v160, 0xbfb8aa3b, v160
	v_mul_f32_e32 v161, 0xbfb8aa3b, v161
	v_exp_f32_e32 v160, v160
	v_exp_f32_e32 v161, v161
	v_lshl_or_b32 v149, v174, 8, v149
	v_lshl_or_b32 v147, v159, 8, v147
	v_add_f32_e32 v160, 1.0, v160
	v_add_f32_e32 v161, 1.0, v161
	v_rcp_f32_e32 v160, v160
	v_rcp_f32_e32 v161, v161
	s_nop 0
	v_pk_fma_f32 v[160:161], v[160:161], s[90:91], 0.5 op_sel_hi:[1,0,0]
	s_nop 0
	v_cvt_u32_f32_e32 v161, v161
	v_cvt_u32_f32_e32 v160, v160
	v_max_u32_e32 v176, 1, v161
	v_max_u32_e32 v175, 1, v160
	v_cndmask_b32_e32 v176, v161, v176, vcc
	v_cndmask_b32_e32 v175, v160, v175, vcc
	v_mul_f32_e32 v160, v39, v80
	v_mul_f32_e32 v161, v31, v80
	v_mul_f32_e32 v160, 0xbfb8aa3b, v160
	v_mul_f32_e32 v161, 0xbfb8aa3b, v161
	v_exp_f32_e32 v160, v160
	v_exp_f32_e32 v161, v161
	v_lshlrev_b32_e32 v174, 16, v175
	v_add_f32_e32 v160, 1.0, v160
	v_add_f32_e32 v161, 1.0, v161
	v_rcp_f32_e32 v160, v160
	v_rcp_f32_e32 v161, v161
	s_nop 0
	v_pk_fma_f32 v[160:161], v[160:161], s[90:91], 0.5 op_sel_hi:[1,0,0]
	s_nop 0
	v_cvt_u32_f32_e32 v160, v160
	v_cvt_u32_f32_e32 v161, v161
	v_max_u32_e32 v177, 1, v160
	v_max_u32_e32 v178, 1, v161
	v_cndmask_b32_e32 v160, v160, v177, vcc
	v_cndmask_b32_e32 v161, v161, v178, vcc
	v_lshlrev_b32_e32 v160, 24, v160
	v_or3_b32 v160, v149, v174, v160
	v_lshlrev_b32_e32 v149, 16, v176
	v_lshlrev_b32_e32 v159, 24, v161
	v_or3_b32 v161, v147, v149, v159
	v_mul_f32_e32 v147, v16, v80
	v_mul_f32_e32 v147, 0xbfb8aa3b, v147
	v_exp_f32_e32 v147, v147
	v_add_co_u32_e64 v174, s[4:5], s97, v152
	v_add_f32_e32 v147, 1.0, v147
	s_nop 0
	v_addc_co_u32_e64 v175, s[4:5], 0, v153, s[4:5]
	global_store_dwordx2 v[174:175], v[160:161], off
	v_rcp_f32_e32 v160, v147
	v_mul_f32_e32 v147, v8, v80
	v_mul_f32_e32 v147, 0xbfb8aa3b, v147
	v_exp_f32_e32 v147, v147
	s_nop 0
	v_add_f32_e32 v147, 1.0, v147
	v_rcp_f32_e32 v161, v147
	s_nop 0
	v_pk_fma_f32 v[160:161], v[160:161], s[90:91], 0.5 op_sel_hi:[1,0,0]
	s_nop 0
	v_cvt_u32_f32_e32 v149, v160
	v_cvt_u32_f32_e32 v147, v161
	v_max_u32_e32 v159, 1, v149
	v_cndmask_b32_e32 v149, v149, v159, vcc
	v_mul_f32_e32 v159, v17, v80
	v_mul_f32_e32 v159, 0xbfb8aa3b, v159
	v_exp_f32_e32 v159, v159
	v_max_u32_e32 v160, 1, v147
	v_cndmask_b32_e32 v147, v147, v160, vcc
	v_add_f32_e32 v159, 1.0, v159
	v_rcp_f32_e32 v160, v159
	v_mul_f32_e32 v159, v9, v80
	v_mul_f32_e32 v159, 0xbfb8aa3b, v159
	v_exp_f32_e32 v159, v159
	s_nop 0
	v_add_f32_e32 v159, 1.0, v159
	v_rcp_f32_e32 v161, v159
	s_nop 0
	v_pk_fma_f32 v[160:161], v[160:161], s[90:91], 0.5 op_sel_hi:[1,0,0]
	s_nop 0
	v_cvt_u32_f32_e32 v159, v161
	v_cvt_u32_f32_e32 v160, v160
	v_max_u32_e32 v174, 1, v159
	v_max_u32_e32 v161, 1, v160
	v_cndmask_b32_e32 v159, v159, v174, vcc
	v_cndmask_b32_e32 v174, v160, v161, vcc
	v_mul_f32_e32 v160, v18, v80
	v_mul_f32_e32 v161, v10, v80
	v_mul_f32_e32 v160, 0xbfb8aa3b, v160
	v_mul_f32_e32 v161, 0xbfb8aa3b, v161
	v_exp_f32_e32 v160, v160
	v_exp_f32_e32 v161, v161
	v_lshl_or_b32 v149, v174, 8, v149
	v_lshl_or_b32 v147, v159, 8, v147
	v_add_f32_e32 v160, 1.0, v160
	v_add_f32_e32 v161, 1.0, v161
	v_rcp_f32_e32 v160, v160
	v_rcp_f32_e32 v161, v161
	s_nop 0
	v_pk_fma_f32 v[160:161], v[160:161], s[90:91], 0.5 op_sel_hi:[1,0,0]
	s_nop 0
	v_cvt_u32_f32_e32 v160, v160
	v_cvt_u32_f32_e32 v161, v161
	v_max_u32_e32 v175, 1, v160
	v_cndmask_b32_e32 v175, v160, v175, vcc
	v_mul_f32_e32 v160, v19, v80
	v_mul_f32_e32 v80, v11, v80
	v_mul_f32_e32 v160, 0xbfb8aa3b, v160
	v_mul_f32_e32 v80, 0xbfb8aa3b, v80
	v_exp_f32_e32 v160, v160
	v_exp_f32_e32 v80, v80
	v_max_u32_e32 v176, 1, v161
	v_cndmask_b32_e32 v176, v161, v176, vcc
	v_add_f32_e32 v160, 1.0, v160
	v_add_f32_e32 v80, 1.0, v80
	v_rcp_f32_e32 v160, v160
	v_rcp_f32_e32 v161, v80
	s_nop 0
	v_pk_fma_f32 v[160:161], v[160:161], s[90:91], 0.5 op_sel_hi:[1,0,0]
	s_nop 0
	v_cvt_u32_f32_e32 v160, v160
	v_cvt_u32_f32_e32 v80, v161
	v_max_u32_e32 v161, 1, v160
	v_max_u32_e32 v177, 1, v80
	v_cndmask_b32_e32 v160, v160, v161, vcc
	v_cndmask_b32_e32 v80, v80, v177, vcc
	v_lshlrev_b32_e32 v161, 16, v175
	v_lshlrev_b32_e32 v160, 24, v160
	v_or3_b32 v160, v149, v161, v160
	v_lshlrev_b32_e32 v149, 16, v176
	v_lshlrev_b32_e32 v80, 24, v80
	v_or3_b32 v161, v147, v149, v80
	global_store_dwordx2 v[154:155], v[160:161], off offset:128
	ds_read_b32 v80, v157 offset:704
	v_lshl_add_u64 v[154:155], v[152:153], 0, s[0:1]
	v_add_co_u32_e64 v152, s[4:5], s83, v152
	s_waitcnt lgkmcnt(0)
; __device__ __forceinline__ float sigm(float x) { return __builtin_amdgcn_rcpf(1.f + __expf(-x)); }
;     __device__ __forceinline__ void operator()(const f32x4 (&acc)[2][2][4][2], const Unit& u, int wr, int wc, int fr, int fq) const {
;     ...
;         } else { const int col0 = (u.pn - 11) * BM + wc * 32 + 8 * fq;
; #pragma unroll
;             for (int ai = 0; ai < 2; ++ai)
; #pragma unroll
;                 for (int m = 0; m < 4; ++m) { const size_t r = (size_t)(row0 + ai * HALF + m * 16); const float s = tbl[wr * 64 + fr + ai * HALF + m * 16]; unsigned char* rowp = GZ + (size_t)(u.pn - 11) * ldc + r * 256 + (wc * 32 + 8 * fq);
; #pragma unroll
;                     for (int bj = 0; bj < 2; ++bj) { const f32x4 v0 = acc[ai][bj][m][0] * s, v1 = acc[ai][bj][m][1] * s;
;                         unsigned q[8];
; #pragma unroll
;                         for (int i = 0; i < 4; ++i) { q[i] = (unsigned)(sigm(v0[i]) * 255.f + 0.5f); q[4 + i] = (unsigned)(sigm(v1[i]) * 255.f + 0.5f); if (u.pn >= 15) { q[i] = q[i] < 1u ? 1u : q[i]; q[4 + i] = q[4 + i] < 1u ? 1u : q[4 + i]; } }
;                         u32x2 w; w.x = q[0] | (q[1] << 8) | (q[2] << 16) | (q[3] << 24); w.y = q[4] | (q[5] << 8) | (q[6] << 16) | (q[7] << 24);
;                         *(u32x2*)(rowp + bj * HALF) = w; } }
	v_mul_f32_e32 v147, v20, v80
	v_mul_f32_e32 v147, 0xbfb8aa3b, v147
	v_exp_f32_e32 v147, v147
	v_addc_co_u32_e64 v153, s[4:5], 0, v153, s[4:5]
	v_add_f32_e32 v147, 1.0, v147
	v_rcp_f32_e32 v160, v147
	v_mul_f32_e32 v147, v12, v80
	v_mul_f32_e32 v147, 0xbfb8aa3b, v147
	v_exp_f32_e32 v147, v147
	s_nop 0
	v_add_f32_e32 v147, 1.0, v147
	v_rcp_f32_e32 v161, v147
	s_nop 0
	v_pk_fma_f32 v[160:161], v[160:161], s[90:91], 0.5 op_sel_hi:[1,0,0]
	s_nop 0
	v_cvt_u32_f32_e32 v149, v160
	v_cvt_u32_f32_e32 v147, v161
	v_max_u32_e32 v159, 1, v149
	v_cndmask_b32_e32 v149, v149, v159, vcc
	v_mul_f32_e32 v159, v21, v80
	v_mul_f32_e32 v159, 0xbfb8aa3b, v159
	v_exp_f32_e32 v159, v159
	v_max_u32_e32 v160, 1, v147
	v_cndmask_b32_e32 v147, v147, v160, vcc
	v_add_f32_e32 v159, 1.0, v159
	v_rcp_f32_e32 v160, v159
	v_mul_f32_e32 v159, v13, v80
	v_mul_f32_e32 v159, 0xbfb8aa3b, v159
	v_exp_f32_e32 v159, v159
	s_nop 0
	v_add_f32_e32 v159, 1.0, v159
	v_rcp_f32_e32 v161, v159
	s_nop 0
	v_pk_fma_f32 v[160:161], v[160:161], s[90:91], 0.5 op_sel_hi:[1,0,0]
	s_nop 0
	v_cvt_u32_f32_e32 v159, v161
	v_cvt_u32_f32_e32 v160, v160
	v_max_u32_e32 v174, 1, v159
	v_max_u32_e32 v161, 1, v160
	v_cndmask_b32_e32 v159, v159, v174, vcc
	v_cndmask_b32_e32 v174, v160, v161, vcc
	v_mul_f32_e32 v160, v22, v80
	v_mul_f32_e32 v161, v14, v80
	v_mul_f32_e32 v160, 0xbfb8aa3b, v160
	v_mul_f32_e32 v161, 0xbfb8aa3b, v161
	v_exp_f32_e32 v160, v160
	v_exp_f32_e32 v161, v161
	v_lshl_or_b32 v149, v174, 8, v149
	v_lshl_or_b32 v147, v159, 8, v147
	v_add_f32_e32 v160, 1.0, v160
	v_add_f32_e32 v161, 1.0, v161
	v_rcp_f32_e32 v160, v160
	v_rcp_f32_e32 v161, v161
	s_nop 0
	v_pk_fma_f32 v[160:161], v[160:161], s[90:91], 0.5 op_sel_hi:[1,0,0]
	s_nop 0
	v_cvt_u32_f32_e32 v161, v161
	v_cvt_u32_f32_e32 v160, v160
	v_max_u32_e32 v176, 1, v161
	v_max_u32_e32 v175, 1, v160
	v_cndmask_b32_e32 v176, v161, v176, vcc
	v_cndmask_b32_e32 v175, v160, v175, vcc
	v_mul_f32_e32 v160, v23, v80
	v_mul_f32_e32 v161, v15, v80
	v_mul_f32_e32 v160, 0xbfb8aa3b, v160
	v_mul_f32_e32 v161, 0xbfb8aa3b, v161
	v_exp_f32_e32 v160, v160
	v_exp_f32_e32 v161, v161
	v_lshlrev_b32_e32 v174, 16, v175
	v_add_f32_e32 v160, 1.0, v160
	v_add_f32_e32 v161, 1.0, v161
	v_rcp_f32_e32 v160, v160
	v_rcp_f32_e32 v161, v161
	s_nop 0
	v_pk_fma_f32 v[160:161], v[160:161], s[90:91], 0.5 op_sel_hi:[1,0,0]
	s_nop 0
	v_cvt_u32_f32_e32 v160, v160
	v_cvt_u32_f32_e32 v161, v161
	v_max_u32_e32 v177, 1, v160
	v_max_u32_e32 v178, 1, v161
	v_cndmask_b32_e32 v160, v160, v177, vcc
	v_cndmask_b32_e32 v161, v161, v178, vcc
	v_lshlrev_b32_e32 v160, 24, v160
	v_or3_b32 v160, v149, v174, v160
	v_lshlrev_b32_e32 v149, 16, v176
	v_lshlrev_b32_e32 v159, 24, v161
	v_or3_b32 v161, v147, v149, v159
	v_mul_f32_e32 v147, v4, v80
	v_mul_f32_e32 v147, 0xbfb8aa3b, v147
	v_exp_f32_e32 v147, v147
	global_store_dwordx2 v[152:153], v[160:161], off
	v_add_f32_e32 v147, 1.0, v147
	v_rcp_f32_e32 v152, v147
	v_mul_f32_e32 v147, v0, v80
	v_mul_f32_e32 v147, 0xbfb8aa3b, v147
	v_exp_f32_e32 v147, v147
	s_nop 0
	v_add_f32_e32 v147, 1.0, v147
	v_rcp_f32_e32 v153, v147
	s_nop 0
	v_pk_fma_f32 v[152:153], v[152:153], s[90:91], 0.5 op_sel_hi:[1,0,0]
	s_nop 0
	v_cvt_u32_f32_e32 v147, v153
	v_cvt_u32_f32_e32 v149, v152
	v_max_u32_e32 v153, 1, v147
	v_max_u32_e32 v152, 1, v149
	v_cndmask_b32_e32 v147, v147, v153, vcc
	v_cndmask_b32_e32 v149, v149, v152, vcc
	v_mul_f32_e32 v152, v5, v80
	v_mul_f32_e32 v153, v1, v80
	v_mul_f32_e32 v152, 0xbfb8aa3b, v152
	v_mul_f32_e32 v153, 0xbfb8aa3b, v153
	v_exp_f32_e32 v152, v152
	v_exp_f32_e32 v153, v153
	v_add_f32_e32 v152, 1.0, v152
	v_add_f32_e32 v153, 1.0, v153
	v_rcp_f32_e32 v152, v152
	v_rcp_f32_e32 v153, v153
	s_nop 0
	v_pk_fma_f32 v[152:153], v[152:153], s[90:91], 0.5 op_sel_hi:[1,0,0]
	s_nop 0
	v_cvt_u32_f32_e32 v153, v153
	v_cvt_u32_f32_e32 v152, v152
	v_max_u32_e32 v160, 1, v153
	v_max_u32_e32 v159, 1, v152
	v_cndmask_b32_e32 v160, v153, v160, vcc
	v_cndmask_b32_e32 v159, v152, v159, vcc
	v_mul_f32_e32 v152, v6, v80
	v_mul_f32_e32 v153, v2, v80
	v_mul_f32_e32 v152, 0xbfb8aa3b, v152
	v_mul_f32_e32 v153, 0xbfb8aa3b, v153
	v_exp_f32_e32 v152, v152
	v_exp_f32_e32 v153, v153
	v_lshl_or_b32 v149, v159, 8, v149
	v_lshl_or_b32 v147, v160, 8, v147
	v_add_f32_e32 v152, 1.0, v152
	v_add_f32_e32 v153, 1.0, v153
	v_rcp_f32_e32 v152, v152
	v_rcp_f32_e32 v153, v153
	s_nop 0
	v_pk_fma_f32 v[152:153], v[152:153], s[90:91], 0.5 op_sel_hi:[1,0,0]
	s_nop 0
	v_cvt_u32_f32_e32 v152, v152
	v_cvt_u32_f32_e32 v153, v153
	v_max_u32_e32 v161, 1, v152
	v_cndmask_b32_e32 v161, v152, v161, vcc
	v_mul_f32_e32 v152, v7, v80
	v_mul_f32_e32 v80, v3, v80
	v_mul_f32_e32 v152, 0xbfb8aa3b, v152
	v_mul_f32_e32 v80, 0xbfb8aa3b, v80
	v_exp_f32_e32 v152, v152
	v_exp_f32_e32 v80, v80
	v_max_u32_e32 v174, 1, v153
	v_cndmask_b32_e32 v174, v153, v174, vcc
	v_add_f32_e32 v152, 1.0, v152
	v_add_f32_e32 v80, 1.0, v80
	v_rcp_f32_e32 v152, v152
	v_rcp_f32_e32 v153, v80
	s_nop 0
	v_pk_fma_f32 v[152:153], v[152:153], s[90:91], 0.5 op_sel_hi:[1,0,0]
	s_nop 0
	v_cvt_u32_f32_e32 v152, v152
	v_cvt_u32_f32_e32 v80, v153
	v_max_u32_e32 v153, 1, v152
	v_max_u32_e32 v175, 1, v80
	v_cndmask_b32_e32 v152, v152, v153, vcc
	v_cndmask_b32_e32 v80, v80, v175, vcc
	v_lshlrev_b32_e32 v153, 16, v161
	v_lshlrev_b32_e32 v152, 24, v152
	v_or3_b32 v152, v149, v153, v152
	v_lshlrev_b32_e32 v149, 16, v174
	v_lshlrev_b32_e32 v80, 24, v80
	v_or3_b32 v153, v147, v149, v80
	global_store_dwordx2 v[154:155], v[152:153], off offset:128
	s_cbranch_execnz .LBB0_159
; __device__ __forceinline__ unsigned cvtpk(float lo, float hi) { f32x2_t v = {lo, hi}; bf16x2_t b = __builtin_convertvector(v, bf16x2_t); return __builtin_bit_cast(unsigned, b); }
;     __device__ __forceinline__ void operator()(const f32x4 (&acc)[2][2][4][2], const Unit& u, int wr, int wc, int fr, int fq) const {
;     ...
;         if (u.pn < 11) { const int col0 = u.pn * BM + wc * 32 + 8 * fq;
; #pragma unroll
;             for (int ai = 0; ai < 2; ++ai)
; #pragma unroll
;                 for (int m = 0; m < 4; ++m) { const size_t r = (size_t)(row0 + ai * HALF + m * 16); const float s = tbl[wr * 64 + fr + ai * HALF + m * 16]; bf16_t* rowp = O + (size_t)u.pn * ldc + r * 256 + (wc * 32 + 8 * fq);
; #pragma unroll
;                     for (int bj = 0; bj < 2; ++bj) { const f32x4 v0 = acc[ai][bj][m][0] * s, v1 = acc[ai][bj][m][1] * s;
;                         u32x4 w; w.x = cvtpk(v0[0], v0[1]); w.y = cvtpk(v0[2], v0[3]); w.z = cvtpk(v1[0], v1[1]); w.w = cvtpk(v1[2], v1[3]);
;                         *(u32x4*)(rowp + bj * HALF) = w; } }
.LBB0_161:
	s_ashr_i32 s19, s18, 31
	s_lshl_b64 s[0:1], s[18:19], 23
	s_add_u32 s0, s68, s0
	s_addc_u32 s1, s69, s1
	v_lshlrev_b64 v[152:153], 9, v[144:145]
	v_lshl_add_u64 v[152:153], s[0:1], 0, v[152:153]
	v_lshlrev_b32_e32 v80, 1, v138
	s_waitcnt lgkmcnt(0)
	v_pk_mul_f32 v[128:129], v[128:129], v[150:151] op_sel_hi:[1,0]
	v_pk_mul_f32 v[126:127], v[126:127], v[150:151] op_sel_hi:[1,0]
	v_pk_mul_f32 v[154:155], v[124:125], v[150:151] op_sel_hi:[1,0]
	v_pk_mul_f32 v[124:125], v[122:123], v[150:151] op_sel_hi:[1,0]
	v_lshl_add_u64 v[152:153], v[152:153], 0, v[80:81]
	v_cvt_pk_bf16_f32 v122, v126, v127
	v_cvt_pk_bf16_f32 v123, v128, v129
	v_cvt_pk_bf16_f32 v124, v124, v125
	v_cvt_pk_bf16_f32 v125, v154, v155
	global_store_dwordx4 v[152:153], v[122:125], off
	v_pk_mul_f32 v[120:121], v[120:121], v[150:151] op_sel_hi:[1,0]
	v_pk_mul_f32 v[118:119], v[118:119], v[150:151] op_sel_hi:[1,0]
	v_pk_mul_f32 v[122:123], v[112:113], v[150:151] op_sel_hi:[1,0]
	v_pk_mul_f32 v[112:113], v[110:111], v[150:151] op_sel_hi:[1,0]
	v_cvt_pk_bf16_f32 v110, v118, v119
	v_cvt_pk_bf16_f32 v111, v120, v121
	v_cvt_pk_bf16_f32 v112, v112, v113
	v_cvt_pk_bf16_f32 v113, v122, v123
	global_store_dwordx4 v[152:153], v[110:113], off offset:256
	ds_read_b32 v110, v157 offset:64
	v_ashrrev_i32_e32 v149, 31, v148
	v_lshlrev_b64 v[112:113], 9, v[148:149]
	v_lshl_add_u64 v[112:113], s[0:1], 0, v[112:113]
	v_lshl_add_u64 v[112:113], v[112:113], 0, v[80:81]
	s_waitcnt lgkmcnt(0)
	v_pk_mul_f32 v[116:117], v[116:117], v[110:111] op_sel_hi:[1,0]
	v_pk_mul_f32 v[114:115], v[114:115], v[110:111] op_sel_hi:[1,0]
	v_pk_mul_f32 v[118:119], v[108:109], v[110:111] op_sel_hi:[1,0]
	v_pk_mul_f32 v[108:109], v[106:107], v[110:111] op_sel_hi:[1,0]
	v_cvt_pk_bf16_f32 v106, v114, v115
	v_cvt_pk_bf16_f32 v107, v116, v117
	v_cvt_pk_bf16_f32 v108, v108, v109
	v_cvt_pk_bf16_f32 v109, v118, v119
	global_store_dwordx4 v[112:113], v[106:109], off
	v_pk_mul_f32 v[104:105], v[104:105], v[110:111] op_sel_hi:[1,0]
	v_pk_mul_f32 v[102:103], v[102:103], v[110:111] op_sel_hi:[1,0]
	v_pk_mul_f32 v[106:107], v[96:97], v[110:111] op_sel_hi:[1,0]
	v_pk_mul_f32 v[96:97], v[94:95], v[110:111] op_sel_hi:[1,0]
	v_cvt_pk_bf16_f32 v94, v102, v103
	v_cvt_pk_bf16_f32 v95, v104, v105
	v_cvt_pk_bf16_f32 v96, v96, v97
	v_cvt_pk_bf16_f32 v97, v106, v107
	global_store_dwordx4 v[112:113], v[94:97], off offset:256
	ds_read_b32 v94, v157 offset:128
	v_ashrrev_i32_e32 v147, 31, v146
	v_lshlrev_b64 v[96:97], 9, v[146:147]
	v_lshl_add_u64 v[96:97], s[0:1], 0, v[96:97]
	v_lshl_add_u64 v[96:97], v[96:97], 0, v[80:81]
	s_waitcnt lgkmcnt(0)
	v_pk_mul_f32 v[100:101], v[100:101], v[94:95] op_sel_hi:[1,0]
	v_pk_mul_f32 v[98:99], v[98:99], v[94:95] op_sel_hi:[1,0]
	v_pk_mul_f32 v[102:103], v[92:93], v[94:95] op_sel_hi:[1,0]
	v_pk_mul_f32 v[92:93], v[90:91], v[94:95] op_sel_hi:[1,0]
	v_cvt_pk_bf16_f32 v90, v98, v99
	v_cvt_pk_bf16_f32 v91, v100, v101
	v_cvt_pk_bf16_f32 v92, v92, v93
	v_cvt_pk_bf16_f32 v93, v102, v103
	global_store_dwordx4 v[96:97], v[90:93], off
	v_pk_mul_f32 v[88:89], v[88:89], v[94:95] op_sel_hi:[1,0]
	v_pk_mul_f32 v[86:87], v[86:87], v[94:95] op_sel_hi:[1,0]
	v_pk_mul_f32 v[90:91], v[78:79], v[94:95] op_sel_hi:[1,0]
	v_pk_mul_f32 v[78:79], v[76:77], v[94:95] op_sel_hi:[1,0]
	v_cvt_pk_bf16_f32 v76, v86, v87
	v_cvt_pk_bf16_f32 v77, v88, v89
	v_cvt_pk_bf16_f32 v78, v78, v79
	v_cvt_pk_bf16_f32 v79, v90, v91
	global_store_dwordx4 v[96:97], v[76:79], off offset:256
	ds_read_b32 v78, v157 offset:192
	s_waitcnt lgkmcnt(0)
	v_pk_mul_f32 v[84:85], v[84:85], v[78:79] op_sel_hi:[1,0]
	v_or_b32_e32 v76, 48, v144
	v_ashrrev_i32_e32 v77, 31, v76
	v_lshlrev_b64 v[76:77], 9, v[76:77]
	v_lshl_add_u64 v[76:77], s[0:1], 0, v[76:77]
	v_pk_mul_f32 v[82:83], v[82:83], v[78:79] op_sel_hi:[1,0]
	v_pk_mul_f32 v[86:87], v[74:75], v[78:79] op_sel_hi:[1,0]
	v_pk_mul_f32 v[74:75], v[72:73], v[78:79] op_sel_hi:[1,0]
	v_lshl_add_u64 v[76:77], v[76:77], 0, v[80:81]
	v_cvt_pk_bf16_f32 v72, v82, v83
	v_cvt_pk_bf16_f32 v73, v84, v85
	v_cvt_pk_bf16_f32 v74, v74, v75
	v_cvt_pk_bf16_f32 v75, v86, v87
	global_store_dwordx4 v[76:77], v[72:75], off
	v_pk_mul_f32 v[70:71], v[70:71], v[78:79] op_sel_hi:[1,0]
	v_pk_mul_f32 v[68:69], v[68:69], v[78:79] op_sel_hi:[1,0]
	v_pk_mul_f32 v[72:73], v[66:67], v[78:79] op_sel_hi:[1,0]
	v_pk_mul_f32 v[66:67], v[64:65], v[78:79] op_sel_hi:[1,0]
	v_cvt_pk_bf16_f32 v64, v68, v69
	v_cvt_pk_bf16_f32 v65, v70, v71
	v_cvt_pk_bf16_f32 v66, v66, v67
	v_cvt_pk_bf16_f32 v67, v72, v73
	global_store_dwordx4 v[76:77], v[64:67], off offset:256
	ds_read_b32 v64, v157 offset:512
	s_mov_b64 s[0:1], 0x10000
	v_lshl_add_u64 v[66:67], v[152:153], 0, s[0:1]
	s_mov_b64 s[0:1], 0x12000
	s_waitcnt lgkmcnt(0)
; __device__ __forceinline__ unsigned cvtpk(float lo, float hi) { f32x2_t v = {lo, hi}; bf16x2_t b = __builtin_convertvector(v, bf16x2_t); return __builtin_bit_cast(unsigned, b); }
;     __device__ __forceinline__ void operator()(const f32x4 (&acc)[2][2][4][2], const Unit& u, int wr, int wc, int fr, int fq) const {
;     ...
;         if (u.pn < 11) { const int col0 = u.pn * BM + wc * 32 + 8 * fq;
; #pragma unroll
;             for (int ai = 0; ai < 2; ++ai)
; #pragma unroll
;                 for (int m = 0; m < 4; ++m) { const size_t r = (size_t)(row0 + ai * HALF + m * 16); const float s = tbl[wr * 64 + fr + ai * HALF + m * 16]; bf16_t* rowp = O + (size_t)u.pn * ldc + r * 256 + (wc * 32 + 8 * fq);
; #pragma unroll
;                     for (int bj = 0; bj < 2; ++bj) { const f32x4 v0 = acc[ai][bj][m][0] * s, v1 = acc[ai][bj][m][1] * s;
;                         u32x4 w; w.x = cvtpk(v0[0], v0[1]); w.y = cvtpk(v0[2], v0[3]); w.z = cvtpk(v1[0], v1[1]); w.w = cvtpk(v1[2], v1[3]);
;                         *(u32x4*)(rowp + bj * HALF) = w; } }
	v_pk_mul_f32 v[60:61], v[60:61], v[64:65] op_sel_hi:[1,0]
	v_pk_mul_f32 v[62:63], v[62:63], v[64:65] op_sel_hi:[1,0]
	v_pk_mul_f32 v[68:69], v[58:59], v[64:65] op_sel_hi:[1,0]
	v_pk_mul_f32 v[58:59], v[56:57], v[64:65] op_sel_hi:[1,0]
	v_cvt_pk_bf16_f32 v56, v60, v61
	v_add_co_u32_e32 v60, vcc, s53, v152
	v_cvt_pk_bf16_f32 v57, v62, v63
	v_cvt_pk_bf16_f32 v58, v58, v59
	v_cvt_pk_bf16_f32 v59, v68, v69
	v_addc_co_u32_e32 v61, vcc, 0, v153, vcc
	global_store_dwordx4 v[60:61], v[56:59], off
	v_pk_mul_f32 v[50:51], v[50:51], v[64:65] op_sel_hi:[1,0]
	v_pk_mul_f32 v[48:49], v[48:49], v[64:65] op_sel_hi:[1,0]
	v_pk_mul_f32 v[56:57], v[42:43], v[64:65] op_sel_hi:[1,0]
	v_pk_mul_f32 v[42:43], v[40:41], v[64:65] op_sel_hi:[1,0]
	v_cvt_pk_bf16_f32 v40, v48, v49
	v_cvt_pk_bf16_f32 v41, v50, v51
	v_cvt_pk_bf16_f32 v42, v42, v43
	v_cvt_pk_bf16_f32 v43, v56, v57
	global_store_dwordx4 v[66:67], v[40:43], off offset:256
	ds_read_b32 v48, v157 offset:576
	v_lshl_add_u64 v[50:51], v[152:153], 0, s[0:1]
	s_mov_b64 s[0:1], 0x14000
	s_waitcnt lgkmcnt(0)
	v_pk_mul_f32 v[42:43], v[54:55], v[48:49] op_sel_hi:[1,0]
	v_pk_mul_f32 v[40:41], v[52:53], v[48:49] op_sel_hi:[1,0]
	v_pk_mul_f32 v[44:45], v[44:45], v[48:49] op_sel_hi:[1,0]
	v_pk_mul_f32 v[46:47], v[46:47], v[48:49] op_sel_hi:[1,0]
	v_cvt_pk_bf16_f32 v40, v40, v41
	v_cvt_pk_bf16_f32 v41, v42, v43
	v_cvt_pk_bf16_f32 v42, v44, v45
	v_add_co_u32_e32 v44, vcc, s70, v152
	v_cvt_pk_bf16_f32 v43, v46, v47
	s_nop 0
	v_addc_co_u32_e32 v45, vcc, 0, v153, vcc
	global_store_dwordx4 v[44:45], v[40:43], off
	v_pk_mul_f32 v[34:35], v[34:35], v[48:49] op_sel_hi:[1,0]
	v_pk_mul_f32 v[32:33], v[32:33], v[48:49] op_sel_hi:[1,0]
	v_pk_mul_f32 v[40:41], v[26:27], v[48:49] op_sel_hi:[1,0]
	v_pk_mul_f32 v[26:27], v[24:25], v[48:49] op_sel_hi:[1,0]
	v_cvt_pk_bf16_f32 v24, v32, v33
	v_cvt_pk_bf16_f32 v25, v34, v35
	v_cvt_pk_bf16_f32 v26, v26, v27
	v_cvt_pk_bf16_f32 v27, v40, v41
	global_store_dwordx4 v[50:51], v[24:27], off offset:256
	ds_read_b32 v32, v157 offset:640
	v_lshl_add_u64 v[34:35], v[152:153], 0, s[0:1]
	s_mov_b64 s[0:1], 0x16000
	s_waitcnt lgkmcnt(0)
	v_pk_mul_f32 v[26:27], v[38:39], v[32:33] op_sel_hi:[1,0]
	v_pk_mul_f32 v[24:25], v[36:37], v[32:33] op_sel_hi:[1,0]
	v_pk_mul_f32 v[28:29], v[28:29], v[32:33] op_sel_hi:[1,0]
	v_pk_mul_f32 v[30:31], v[30:31], v[32:33] op_sel_hi:[1,0]
	v_cvt_pk_bf16_f32 v24, v24, v25
	v_cvt_pk_bf16_f32 v25, v26, v27
	v_cvt_pk_bf16_f32 v26, v28, v29
	v_add_co_u32_e32 v28, vcc, s71, v152
	v_cvt_pk_bf16_f32 v27, v30, v31
	s_nop 0
	v_addc_co_u32_e32 v29, vcc, 0, v153, vcc
	global_store_dwordx4 v[28:29], v[24:27], off
	v_pk_mul_f32 v[18:19], v[18:19], v[32:33] op_sel_hi:[1,0]
	v_pk_mul_f32 v[16:17], v[16:17], v[32:33] op_sel_hi:[1,0]
	v_pk_mul_f32 v[24:25], v[10:11], v[32:33] op_sel_hi:[1,0]
	v_pk_mul_f32 v[10:11], v[8:9], v[32:33] op_sel_hi:[1,0]
	v_cvt_pk_bf16_f32 v8, v16, v17
	v_cvt_pk_bf16_f32 v9, v18, v19
	v_cvt_pk_bf16_f32 v10, v10, v11
	v_cvt_pk_bf16_f32 v11, v24, v25
	global_store_dwordx4 v[34:35], v[8:11], off offset:256
	ds_read_b32 v16, v157 offset:704
	v_lshl_add_u64 v[18:19], v[152:153], 0, s[0:1]
	s_mov_b32 s0, 0x16000
	s_waitcnt lgkmcnt(0)
	v_pk_mul_f32 v[10:11], v[22:23], v[16:17] op_sel_hi:[1,0]
	v_pk_mul_f32 v[8:9], v[20:21], v[16:17] op_sel_hi:[1,0]
	v_pk_mul_f32 v[12:13], v[12:13], v[16:17] op_sel_hi:[1,0]
	v_pk_mul_f32 v[14:15], v[14:15], v[16:17] op_sel_hi:[1,0]
	v_cvt_pk_bf16_f32 v8, v8, v9
	v_cvt_pk_bf16_f32 v9, v10, v11
	v_cvt_pk_bf16_f32 v10, v12, v13
	v_add_co_u32_e32 v12, vcc, s0, v152
	v_cvt_pk_bf16_f32 v11, v14, v15
	s_nop 0
	v_addc_co_u32_e32 v13, vcc, 0, v153, vcc
	global_store_dwordx4 v[12:13], v[8:11], off
	v_pk_mul_f32 v[6:7], v[6:7], v[16:17] op_sel_hi:[1,0]
	v_pk_mul_f32 v[4:5], v[4:5], v[16:17] op_sel_hi:[1,0]
	v_pk_mul_f32 v[8:9], v[2:3], v[16:17] op_sel_hi:[1,0]
	v_pk_mul_f32 v[2:3], v[0:1], v[16:17] op_sel_hi:[1,0]
	v_cvt_pk_bf16_f32 v0, v4, v5
	v_cvt_pk_bf16_f32 v1, v6, v7
	v_cvt_pk_bf16_f32 v2, v2, v3
	v_cvt_pk_bf16_f32 v3, v8, v9
	global_store_dwordx4 v[18:19], v[0:3], off offset:256
	s_andn2_b64 vcc, exec, s[2:3]
	s_mov_b64 s[0:1], -1
	s_cbranch_vccnz .LBB0_150

; #define GM_R(w, sh) ((float)(((a.w) >> (sh)) & 255u) * __builtin_amdgcn_rcpf((float)(((b.w) >> (sh)) & 255u)))
;     __device__ __forceinline__ void mid(f32x4 (&acc)[2][2][4][2], const Unit& u, int wr, int wc) const {
;         int fr, fq; { int z_ = 0; asm volatile("" : "+v"(z_)); const int l_ = (int)__builtin_amdgcn_mbcnt_hi(~0u, __builtin_amdgcn_mbcnt_lo(~0u, (unsigned)z_)); fr = l_ & 15; fq = l_ >> 4; }
;         const int row0 = u.pm * BM + wr * 64 + fr, col0 = u.pn * BM + wc * 32 + 8 * fq;
; #pragma unroll
;         for (int ai = 0; ai < 2; ++ai) {
;             u32x2 ga[4][2], gb[4][2];
; #pragma unroll
;             for (int m = 0; m < 4; ++m)
; #pragma unroll
;                 for (int bj = 0; bj < 2; ++bj) { const unsigned char* gp = G + (size_t)u.pn * ldg + (size_t)(row0 + ai * HALF + m * 16) * 256 + (wc * 32 + 8 * fq) + bj * HALF; ga[m][bj] = *(const u32x2*)gp; gb[m][bj] = *(const u32x2*)(gp + (size_t)4 * ldg); }
; #pragma unroll
;             for (int m = 0; m < 4; ++m)
; #pragma unroll
;                 for (int bj = 0; bj < 2; ++bj) { const u32x2 a = ga[m][bj], b = gb[m][bj];
;     ...
;                     acc[ai][bj][m][0][0] *= GM_R(x, 0); acc[ai][bj][m][0][1] *= GM_R(x, 8); acc[ai][bj][m][0][2] *= GM_R(x, 16); acc[ai][bj][m][0][3] *= GM_R(x, 24);
;                     acc[ai][bj][m][1][0] *= GM_R(y, 0); acc[ai][bj][m][1][1] *= GM_R(y, 8); acc[ai][bj][m][1][2] *= GM_R(y, 16); acc[ai][bj][m][1][3] *= GM_R(y, 24);
;     ...
;                 }
;         }
;     }
.LBB0_468:
	s_cmpk_lg_i32 s22, 0x400
	s_cbranch_scc1 .LBB0_467
	v_mov_b32_e32 v80, v81
	s_mov_b64 s[0:1], 0x8000
	v_mbcnt_lo_u32_b32 v80, -1, v80
	v_mbcnt_hi_u32_b32 v80, -1, v80
	v_ashrrev_i32_e32 v82, 1, v80
	v_and_b32_e32 v82, -8, v82
	v_and_or_b32 v80, v80, 15, s39
	v_add_u32_e32 v152, s9, v80
	v_add_u32_e32 v82, s40, v82
	v_ashrrev_i32_e32 v83, 31, v82
	v_ashrrev_i32_e32 v153, 31, v152
	v_lshl_add_u64 v[154:155], s[20:21], 0, v[82:83]
	v_lshlrev_b64 v[82:83], 8, v[152:153]
	v_lshl_add_u64 v[82:83], v[154:155], 0, v[82:83]
	v_add_co_u32_e32 v148, vcc, s91, v82
	global_load_dwordx2 v[188:189], v[82:83], off
	s_nop 0
	v_addc_co_u32_e32 v149, vcc, 0, v83, vcc
	global_load_dwordx2 v[190:191], v[148:149], off
	global_load_dwordx2 v[184:185], v[82:83], off offset:128
	global_load_dwordx2 v[186:187], v[148:149], off offset:128
	v_or_b32_e32 v148, 16, v152
	v_ashrrev_i32_e32 v149, 31, v148
	v_lshlrev_b64 v[148:149], 8, v[148:149]
	v_lshl_add_u64 v[148:149], v[154:155], 0, v[148:149]
	v_add_co_u32_e32 v150, vcc, s91, v148
	global_load_dwordx2 v[180:181], v[148:149], off
	s_nop 0
	v_addc_co_u32_e32 v151, vcc, 0, v149, vcc
	global_load_dwordx2 v[182:183], v[150:151], off
	global_load_dwordx2 v[174:175], v[148:149], off offset:128
	global_load_dwordx2 v[178:179], v[150:151], off offset:128
	v_or_b32_e32 v148, 32, v152
	v_ashrrev_i32_e32 v149, 31, v148
	v_lshlrev_b64 v[148:149], 8, v[148:149]
	v_lshl_add_u64 v[148:149], v[154:155], 0, v[148:149]
	v_add_co_u32_e32 v150, vcc, s91, v148
	global_load_dwordx2 v[156:157], v[148:149], off
	s_nop 0
	v_addc_co_u32_e32 v151, vcc, 0, v149, vcc
	global_load_dwordx2 v[160:161], v[150:151], off
	s_nop 0
	global_load_dwordx2 v[148:149], v[148:149], off offset:128
	s_nop 0
	global_load_dwordx2 v[150:151], v[150:151], off offset:128
	v_or_b32_e32 v152, 48, v152
	v_ashrrev_i32_e32 v153, 31, v152
	v_lshlrev_b64 v[152:153], 8, v[152:153]
	v_lshl_add_u64 v[154:155], v[154:155], 0, v[152:153]
	v_add_co_u32_e32 v176, vcc, s91, v154
	global_load_dwordx2 v[152:153], v[154:155], off
	s_nop 0
	v_addc_co_u32_e32 v177, vcc, 0, v155, vcc
	global_load_dwordx2 v[158:159], v[176:177], off
	s_nop 0
	global_load_dwordx2 v[154:155], v[154:155], off offset:128
	s_nop 0
	global_load_dwordx2 v[176:177], v[176:177], off offset:128
	s_waitcnt vmcnt(0) lgkmcnt(0)
	v_cvt_f32_ubyte1_e32 v215, v188
	v_cvt_f32_ubyte0_e32 v80, v190
	v_rcp_iflag_f32_e32 v208, v80
	v_cvt_f32_ubyte1_e32 v80, v190
	v_rcp_iflag_f32_e32 v209, v80
	v_cvt_f32_ubyte2_e32 v80, v190
	v_rcp_iflag_f32_e32 v210, v80
	v_cvt_f32_ubyte3_e32 v80, v190
	v_cvt_f32_ubyte0_e32 v214, v188
	v_rcp_iflag_f32_e32 v211, v80
	v_pk_mul_f32 v[208:209], v[208:209], v[214:215]
	v_cvt_f32_ubyte0_e32 v80, v191
	v_pk_mul_f32 v[128:129], v[128:129], v[208:209]
	v_rcp_iflag_f32_e32 v208, v80
	v_cvt_f32_ubyte1_e32 v80, v191
	v_rcp_iflag_f32_e32 v209, v80
	v_cvt_f32_ubyte3_e32 v213, v188
	v_cvt_f32_ubyte2_e32 v212, v188
	v_cvt_f32_ubyte2_e32 v80, v191
	v_pk_mul_f32 v[210:211], v[210:211], v[212:213]
	v_rcp_iflag_f32_e32 v190, v80
	v_cvt_f32_ubyte3_e32 v80, v191
	v_cvt_f32_ubyte1_e32 v213, v189
	v_cvt_f32_ubyte0_e32 v212, v189
	v_pk_mul_f32 v[130:131], v[130:131], v[210:211]
	v_rcp_iflag_f32_e32 v191, v80
	v_cvt_f32_ubyte3_e32 v211, v189
	v_cvt_f32_ubyte2_e32 v210, v189
	v_pk_mul_f32 v[188:189], v[208:209], v[212:213]
	v_cvt_f32_ubyte0_e32 v80, v186
	v_pk_mul_f32 v[124:125], v[124:125], v[188:189]
	v_rcp_iflag_f32_e32 v188, v80
	v_cvt_f32_ubyte1_e32 v80, v186
	v_rcp_iflag_f32_e32 v189, v80
	v_pk_mul_f32 v[190:191], v[190:191], v[210:211]
	v_cvt_f32_ubyte2_e32 v80, v186
	v_pk_mul_f32 v[126:127], v[126:127], v[190:191]
	v_rcp_iflag_f32_e32 v190, v80
	v_cvt_f32_ubyte3_e32 v80, v186
	v_cvt_f32_ubyte1_e32 v211, v184
	v_cvt_f32_ubyte0_e32 v210, v184
	v_rcp_iflag_f32_e32 v191, v80
	v_pk_mul_f32 v[188:189], v[188:189], v[210:211]
	v_cvt_f32_ubyte0_e32 v80, v187
	v_pk_mul_f32 v[120:121], v[120:121], v[188:189]
	v_rcp_iflag_f32_e32 v188, v80
	v_cvt_f32_ubyte1_e32 v80, v187
	v_rcp_iflag_f32_e32 v189, v80
	v_cvt_f32_ubyte3_e32 v209, v184
	v_cvt_f32_ubyte2_e32 v208, v184
	v_cvt_f32_ubyte2_e32 v80, v187
	v_pk_mul_f32 v[190:191], v[190:191], v[208:209]
	v_rcp_iflag_f32_e32 v186, v80
	v_cvt_f32_ubyte3_e32 v80, v187
	v_cvt_f32_ubyte1_e32 v209, v185
	v_cvt_f32_ubyte0_e32 v208, v185
	v_pk_mul_f32 v[122:123], v[122:123], v[190:191]
	v_rcp_iflag_f32_e32 v187, v80
	v_cvt_f32_ubyte3_e32 v191, v185
	v_cvt_f32_ubyte2_e32 v190, v185
	v_pk_mul_f32 v[184:185], v[188:189], v[208:209]
	v_cvt_f32_ubyte0_e32 v80, v182
	v_pk_mul_f32 v[116:117], v[116:117], v[184:185]
	v_rcp_iflag_f32_e32 v184, v80
	v_cvt_f32_ubyte1_e32 v80, v182
	v_rcp_iflag_f32_e32 v185, v80
	v_pk_mul_f32 v[186:187], v[186:187], v[190:191]
	v_cvt_f32_ubyte2_e32 v80, v182
	v_pk_mul_f32 v[118:119], v[118:119], v[186:187]
	v_rcp_iflag_f32_e32 v186, v80
	v_cvt_f32_ubyte3_e32 v80, v182
	v_cvt_f32_ubyte1_e32 v191, v180
	v_cvt_f32_ubyte0_e32 v190, v180
	v_rcp_iflag_f32_e32 v187, v80
	v_pk_mul_f32 v[184:185], v[184:185], v[190:191]
	v_cvt_f32_ubyte0_e32 v80, v183
	v_pk_mul_f32 v[112:113], v[112:113], v[184:185]
	v_rcp_iflag_f32_e32 v184, v80
	v_cvt_f32_ubyte1_e32 v80, v183
	v_rcp_iflag_f32_e32 v185, v80
	v_cvt_f32_ubyte3_e32 v189, v180
	v_cvt_f32_ubyte2_e32 v188, v180
	v_cvt_f32_ubyte2_e32 v80, v183
	v_pk_mul_f32 v[186:187], v[186:187], v[188:189]
	v_rcp_iflag_f32_e32 v182, v80
	v_cvt_f32_ubyte3_e32 v80, v183
	v_cvt_f32_ubyte1_e32 v189, v181
	v_cvt_f32_ubyte0_e32 v188, v181
	v_pk_mul_f32 v[114:115], v[114:115], v[186:187]
	v_rcp_iflag_f32_e32 v183, v80
	v_cvt_f32_ubyte3_e32 v187, v181
	v_cvt_f32_ubyte2_e32 v186, v181
	v_pk_mul_f32 v[180:181], v[184:185], v[188:189]
; #define GM_R(w, sh) ((float)(((a.w) >> (sh)) & 255u) * __builtin_amdgcn_rcpf((float)(((b.w) >> (sh)) & 255u)))
;     __device__ __forceinline__ void mid(f32x4 (&acc)[2][2][4][2], const Unit& u, int wr, int wc) const {
;     ...
;                 for (int bj = 0; bj < 2; ++bj) { const u32x2 a = ga[m][bj], b = gb[m][bj];
;     ...
;                     acc[ai][bj][m][0][0] *= GM_R(x, 0); acc[ai][bj][m][0][1] *= GM_R(x, 8); acc[ai][bj][m][0][2] *= GM_R(x, 16); acc[ai][bj][m][0][3] *= GM_R(x, 24);
;                     acc[ai][bj][m][1][0] *= GM_R(y, 0); acc[ai][bj][m][1][1] *= GM_R(y, 8); acc[ai][bj][m][1][2] *= GM_R(y, 16); acc[ai][bj][m][1][3] *= GM_R(y, 24);
;     ...
;                 }
	v_cvt_f32_ubyte0_e32 v80, v178
	v_pk_mul_f32 v[108:109], v[108:109], v[180:181]
	v_rcp_iflag_f32_e32 v180, v80
	v_cvt_f32_ubyte1_e32 v80, v178
	v_rcp_iflag_f32_e32 v181, v80
	v_pk_mul_f32 v[182:183], v[182:183], v[186:187]
	v_cvt_f32_ubyte2_e32 v80, v178
	v_pk_mul_f32 v[110:111], v[110:111], v[182:183]
	v_rcp_iflag_f32_e32 v182, v80
	v_cvt_f32_ubyte3_e32 v80, v178
	v_cvt_f32_ubyte1_e32 v187, v174
	v_cvt_f32_ubyte0_e32 v186, v174
	v_rcp_iflag_f32_e32 v183, v80
	v_pk_mul_f32 v[180:181], v[180:181], v[186:187]
	v_cvt_f32_ubyte0_e32 v80, v179
	v_pk_mul_f32 v[104:105], v[104:105], v[180:181]
	v_rcp_iflag_f32_e32 v180, v80
	v_cvt_f32_ubyte1_e32 v80, v179
	v_rcp_iflag_f32_e32 v181, v80
	v_cvt_f32_ubyte3_e32 v185, v174
	v_cvt_f32_ubyte2_e32 v184, v174
	v_cvt_f32_ubyte2_e32 v80, v179
	v_pk_mul_f32 v[182:183], v[182:183], v[184:185]
	v_rcp_iflag_f32_e32 v178, v80
	v_cvt_f32_ubyte3_e32 v80, v179
	v_cvt_f32_ubyte1_e32 v185, v175
	v_cvt_f32_ubyte0_e32 v184, v175
	v_pk_mul_f32 v[106:107], v[106:107], v[182:183]
	v_rcp_iflag_f32_e32 v179, v80
	v_cvt_f32_ubyte3_e32 v183, v175
	v_cvt_f32_ubyte2_e32 v182, v175
	v_pk_mul_f32 v[174:175], v[180:181], v[184:185]
	v_cvt_f32_ubyte0_e32 v80, v160
	v_pk_mul_f32 v[100:101], v[100:101], v[174:175]
	v_rcp_iflag_f32_e32 v174, v80
	v_cvt_f32_ubyte1_e32 v80, v160
	v_rcp_iflag_f32_e32 v175, v80
	v_pk_mul_f32 v[178:179], v[178:179], v[182:183]
	v_cvt_f32_ubyte2_e32 v80, v160
	v_pk_mul_f32 v[102:103], v[102:103], v[178:179]
	v_rcp_iflag_f32_e32 v178, v80
	v_cvt_f32_ubyte3_e32 v80, v160
	v_cvt_f32_ubyte1_e32 v183, v156
	v_cvt_f32_ubyte0_e32 v182, v156
	v_rcp_iflag_f32_e32 v179, v80
	v_pk_mul_f32 v[174:175], v[174:175], v[182:183]
	v_cvt_f32_ubyte0_e32 v80, v161
	v_pk_mul_f32 v[96:97], v[96:97], v[174:175]
	v_rcp_iflag_f32_e32 v174, v80
	v_cvt_f32_ubyte1_e32 v80, v161
	v_rcp_iflag_f32_e32 v175, v80
	v_cvt_f32_ubyte3_e32 v181, v156
	v_cvt_f32_ubyte2_e32 v180, v156
	v_cvt_f32_ubyte2_e32 v80, v161
	v_pk_mul_f32 v[178:179], v[178:179], v[180:181]
	v_rcp_iflag_f32_e32 v160, v80
	v_cvt_f32_ubyte3_e32 v80, v161
	v_cvt_f32_ubyte1_e32 v181, v157
	v_cvt_f32_ubyte0_e32 v180, v157
	v_pk_mul_f32 v[98:99], v[98:99], v[178:179]
	v_rcp_iflag_f32_e32 v161, v80
	v_cvt_f32_ubyte3_e32 v179, v157
	v_cvt_f32_ubyte2_e32 v178, v157
	v_pk_mul_f32 v[156:157], v[174:175], v[180:181]
	v_cvt_f32_ubyte0_e32 v80, v150
	v_pk_mul_f32 v[92:93], v[92:93], v[156:157]
	v_rcp_iflag_f32_e32 v156, v80
	v_cvt_f32_ubyte1_e32 v80, v150
	v_rcp_iflag_f32_e32 v157, v80
	v_pk_mul_f32 v[160:161], v[160:161], v[178:179]
	v_cvt_f32_ubyte2_e32 v80, v150
	v_pk_mul_f32 v[94:95], v[94:95], v[160:161]
	v_rcp_iflag_f32_e32 v160, v80
	v_cvt_f32_ubyte3_e32 v80, v150
	v_cvt_f32_ubyte1_e32 v179, v148
	v_cvt_f32_ubyte0_e32 v178, v148
	v_rcp_iflag_f32_e32 v161, v80
	v_pk_mul_f32 v[156:157], v[156:157], v[178:179]
	v_cvt_f32_ubyte0_e32 v80, v151
	v_pk_mul_f32 v[88:89], v[88:89], v[156:157]
	v_rcp_iflag_f32_e32 v156, v80
	v_cvt_f32_ubyte1_e32 v80, v151
	v_rcp_iflag_f32_e32 v157, v80
	v_cvt_f32_ubyte2_e32 v80, v151
	v_rcp_iflag_f32_e32 v150, v80
	v_cvt_f32_ubyte3_e32 v80, v151
	v_cvt_f32_ubyte3_e32 v175, v148
	v_cvt_f32_ubyte2_e32 v174, v148
	v_rcp_iflag_f32_e32 v151, v80
	v_pk_mul_f32 v[160:161], v[160:161], v[174:175]
	v_cvt_f32_ubyte1_e32 v175, v149
	v_cvt_f32_ubyte0_e32 v174, v149
	v_pk_mul_f32 v[90:91], v[90:91], v[160:161]
	v_cvt_f32_ubyte3_e32 v161, v149
	v_cvt_f32_ubyte2_e32 v160, v149
	v_pk_mul_f32 v[148:149], v[156:157], v[174:175]
	v_cvt_f32_ubyte0_e32 v80, v158
	v_pk_mul_f32 v[84:85], v[84:85], v[148:149]
	v_rcp_iflag_f32_e32 v148, v80
	v_cvt_f32_ubyte1_e32 v80, v158
	v_pk_mul_f32 v[150:151], v[150:151], v[160:161]
	v_rcp_iflag_f32_e32 v149, v80
	v_cvt_f32_ubyte2_e32 v80, v158
	v_pk_mul_f32 v[86:87], v[86:87], v[150:151]
	v_rcp_iflag_f32_e32 v150, v80
	v_cvt_f32_ubyte3_e32 v80, v158
	v_rcp_iflag_f32_e32 v151, v80
	v_cvt_f32_ubyte1_e32 v161, v152
	v_cvt_f32_ubyte0_e32 v160, v152
	v_pk_mul_f32 v[148:149], v[148:149], v[160:161]
	v_cvt_f32_ubyte0_e32 v80, v159
	v_cvt_f32_ubyte3_e32 v157, v152
	v_cvt_f32_ubyte2_e32 v156, v152
	v_pk_mul_f32 v[76:77], v[76:77], v[148:149]
	v_rcp_iflag_f32_e32 v148, v80
	v_cvt_f32_ubyte1_e32 v80, v159
	v_pk_mul_f32 v[150:151], v[150:151], v[156:157]
	v_rcp_iflag_f32_e32 v149, v80
	v_cvt_f32_ubyte2_e32 v80, v159
	v_pk_mul_f32 v[78:79], v[78:79], v[150:151]
	v_rcp_iflag_f32_e32 v150, v80
	v_cvt_f32_ubyte3_e32 v80, v159
	v_rcp_iflag_f32_e32 v151, v80
	v_cvt_f32_ubyte1_e32 v159, v153
	v_cvt_f32_ubyte0_e32 v158, v153
	v_pk_mul_f32 v[148:149], v[148:149], v[158:159]
	v_cvt_f32_ubyte0_e32 v80, v176
	v_cvt_f32_ubyte3_e32 v157, v153
	v_cvt_f32_ubyte2_e32 v156, v153
	v_pk_mul_f32 v[72:73], v[72:73], v[148:149]
	v_rcp_iflag_f32_e32 v148, v80
	v_cvt_f32_ubyte1_e32 v80, v176
	v_pk_mul_f32 v[150:151], v[150:151], v[156:157]
	v_rcp_iflag_f32_e32 v149, v80
	v_cvt_f32_ubyte2_e32 v80, v176
	v_pk_mul_f32 v[74:75], v[74:75], v[150:151]
	v_rcp_iflag_f32_e32 v150, v80
	v_cvt_f32_ubyte3_e32 v80, v176
	v_rcp_iflag_f32_e32 v151, v80
	v_cvt_f32_ubyte1_e32 v157, v154
	v_cvt_f32_ubyte0_e32 v156, v154
	v_pk_mul_f32 v[148:149], v[148:149], v[156:157]
	v_cvt_f32_ubyte0_e32 v80, v177
	v_cvt_f32_ubyte3_e32 v153, v154
	v_cvt_f32_ubyte2_e32 v152, v154
	v_pk_mul_f32 v[68:69], v[68:69], v[148:149]
	v_rcp_iflag_f32_e32 v148, v80
	v_cvt_f32_ubyte1_e32 v80, v177
	v_pk_mul_f32 v[150:151], v[150:151], v[152:153]
	v_rcp_iflag_f32_e32 v149, v80
	v_cvt_f32_ubyte2_e32 v80, v177
	v_pk_mul_f32 v[70:71], v[70:71], v[150:151]
	v_rcp_iflag_f32_e32 v150, v80
	v_cvt_f32_ubyte3_e32 v80, v177
	v_rcp_iflag_f32_e32 v151, v80
	v_cvt_f32_ubyte3_e32 v153, v155
	v_cvt_f32_ubyte2_e32 v152, v155
; #define GM_R(w, sh) ((float)(((a.w) >> (sh)) & 255u) * __builtin_amdgcn_rcpf((float)(((b.w) >> (sh)) & 255u)))
;     __device__ __forceinline__ void mid(f32x4 (&acc)[2][2][4][2], const Unit& u, int wr, int wc) const {
;     ...
;             for (int m = 0; m < 4; ++m)
; #pragma unroll
;                 for (int bj = 0; bj < 2; ++bj) { const unsigned char* gp = G + (size_t)u.pn * ldg + (size_t)(row0 + ai * HALF + m * 16) * 256 + (wc * 32 + 8 * fq) + bj * HALF; ga[m][bj] = *(const u32x2*)gp; gb[m][bj] = *(const u32x2*)(gp + (size_t)4 * ldg); }
; #pragma unroll
;             for (int m = 0; m < 4; ++m)
; #pragma unroll
;                 for (int bj = 0; bj < 2; ++bj) { const u32x2 a = ga[m][bj], b = gb[m][bj];
;     ...
;                     acc[ai][bj][m][0][0] *= GM_R(x, 0); acc[ai][bj][m][0][1] *= GM_R(x, 8); acc[ai][bj][m][0][2] *= GM_R(x, 16); acc[ai][bj][m][0][3] *= GM_R(x, 24);
;                     acc[ai][bj][m][1][0] *= GM_R(y, 0); acc[ai][bj][m][1][1] *= GM_R(y, 8); acc[ai][bj][m][1][2] *= GM_R(y, 16); acc[ai][bj][m][1][3] *= GM_R(y, 24);
;     ...
;                 }
	v_cvt_f32_ubyte1_e32 v157, v155
	v_cvt_f32_ubyte0_e32 v156, v155
	v_pk_mul_f32 v[150:151], v[150:151], v[152:153]
	v_pk_mul_f32 v[148:149], v[148:149], v[156:157]
	v_pk_mul_f32 v[66:67], v[66:67], v[150:151]
	v_add_co_u32_e32 v150, vcc, s33, v82
	v_pk_mul_f32 v[64:65], v[64:65], v[148:149]
	v_lshl_add_u64 v[148:149], v[82:83], 0, s[0:1]
	v_addc_co_u32_e32 v151, vcc, 0, v83, vcc
	s_mov_b32 s0, 0x1008000
	global_load_dwordx2 v[154:155], v[150:151], off
	v_add_co_u32_e32 v150, vcc, s0, v82
	s_mov_b64 s[0:1], 0x9000
	s_nop 0
	v_addc_co_u32_e32 v151, vcc, 0, v83, vcc
	global_load_dwordx2 v[182:183], v[150:151], off
	global_load_dwordx2 v[160:161], v[148:149], off offset:128
	global_load_dwordx2 v[184:185], v[150:151], off offset:128
	v_lshl_add_u64 v[148:149], v[82:83], 0, s[0:1]
	s_mov_b32 s0, 0x9000
	v_add_co_u32_e32 v150, vcc, s0, v82
	s_mov_b32 s0, 0x1009000
	s_nop 0
	v_addc_co_u32_e32 v151, vcc, 0, v83, vcc
	global_load_dwordx2 v[186:187], v[150:151], off
	v_add_co_u32_e32 v150, vcc, s0, v82
	s_mov_b64 s[0:1], 0xa000
	s_nop 0
	v_addc_co_u32_e32 v151, vcc, 0, v83, vcc
	global_load_dwordx2 v[188:189], v[150:151], off
	global_load_dwordx2 v[178:179], v[148:149], off offset:128
	global_load_dwordx2 v[180:181], v[150:151], off offset:128
	v_add_co_u32_e32 v150, vcc, s97, v82
	v_lshl_add_u64 v[148:149], v[82:83], 0, s[0:1]
	s_nop 0
	v_addc_co_u32_e32 v151, vcc, 0, v83, vcc
	s_mov_b32 s0, 0x100a000
	global_load_dwordx2 v[174:175], v[150:151], off
	v_add_co_u32_e32 v150, vcc, s0, v82
	s_mov_b64 s[0:1], 0xb000
	s_nop 0
	v_addc_co_u32_e32 v151, vcc, 0, v83, vcc
	global_load_dwordx2 v[176:177], v[150:151], off
	global_load_dwordx2 v[156:157], v[148:149], off offset:128
	global_load_dwordx2 v[158:159], v[150:151], off offset:128
	v_add_co_u32_e32 v150, vcc, s83, v82
	v_lshl_add_u64 v[148:149], v[82:83], 0, s[0:1]
	s_nop 0
	v_addc_co_u32_e32 v151, vcc, 0, v83, vcc
	s_mov_b32 s0, 0x100b000
	v_add_co_u32_e32 v190, vcc, s0, v82
	global_load_dwordx2 v[150:151], v[150:151], off
	s_nop 0
	v_addc_co_u32_e32 v191, vcc, 0, v83, vcc
	global_load_dwordx2 v[152:153], v[190:191], off
	global_load_dwordx2 v[82:83], v[148:149], off offset:128
	s_nop 0
	global_load_dwordx2 v[148:149], v[190:191], off offset:128
	s_waitcnt vmcnt(0) lgkmcnt(0)
	v_cvt_f32_ubyte1_e32 v213, v154
	v_cvt_f32_ubyte0_e32 v212, v154
	v_cvt_f32_ubyte3_e32 v211, v154
	v_cvt_f32_ubyte2_e32 v210, v154
	v_cvt_f32_ubyte0_e32 v80, v182
	v_rcp_iflag_f32_e32 v190, v80
	v_cvt_f32_ubyte1_e32 v80, v182
	v_rcp_iflag_f32_e32 v191, v80
	v_cvt_f32_ubyte2_e32 v80, v182
	v_rcp_iflag_f32_e32 v208, v80
	v_cvt_f32_ubyte3_e32 v80, v182
	v_rcp_iflag_f32_e32 v209, v80
	v_pk_mul_f32 v[190:191], v[190:191], v[212:213]
	v_cvt_f32_ubyte0_e32 v80, v183
	v_pk_mul_f32 v[60:61], v[60:61], v[190:191]
	v_rcp_iflag_f32_e32 v190, v80
	v_cvt_f32_ubyte1_e32 v80, v183
	v_rcp_iflag_f32_e32 v191, v80
	v_cvt_f32_ubyte2_e32 v80, v183
	v_pk_mul_f32 v[208:209], v[208:209], v[210:211]
	v_rcp_iflag_f32_e32 v182, v80
	v_cvt_f32_ubyte3_e32 v80, v183
	v_cvt_f32_ubyte1_e32 v211, v155
	v_cvt_f32_ubyte0_e32 v210, v155
	v_pk_mul_f32 v[62:63], v[62:63], v[208:209]
	v_rcp_iflag_f32_e32 v183, v80
	v_cvt_f32_ubyte3_e32 v209, v155
	v_cvt_f32_ubyte2_e32 v208, v155
	v_pk_mul_f32 v[154:155], v[190:191], v[210:211]
	v_cvt_f32_ubyte0_e32 v80, v184
	v_pk_mul_f32 v[56:57], v[56:57], v[154:155]
	v_rcp_iflag_f32_e32 v154, v80
	v_cvt_f32_ubyte1_e32 v80, v184
	v_rcp_iflag_f32_e32 v155, v80
	v_pk_mul_f32 v[182:183], v[182:183], v[208:209]
	v_cvt_f32_ubyte2_e32 v80, v184
	v_pk_mul_f32 v[58:59], v[58:59], v[182:183]
	v_rcp_iflag_f32_e32 v182, v80
	v_cvt_f32_ubyte3_e32 v80, v184
	v_cvt_f32_ubyte1_e32 v209, v160
	v_cvt_f32_ubyte0_e32 v208, v160
	v_rcp_iflag_f32_e32 v183, v80
	v_pk_mul_f32 v[154:155], v[154:155], v[208:209]
	v_cvt_f32_ubyte0_e32 v80, v185
	v_pk_mul_f32 v[52:53], v[52:53], v[154:155]
	v_rcp_iflag_f32_e32 v154, v80
	v_cvt_f32_ubyte1_e32 v80, v185
	v_rcp_iflag_f32_e32 v155, v80
	v_cvt_f32_ubyte3_e32 v191, v160
	v_cvt_f32_ubyte2_e32 v190, v160
	v_pk_mul_f32 v[182:183], v[182:183], v[190:191]
	v_cvt_f32_ubyte2_e32 v80, v185
	v_pk_mul_f32 v[54:55], v[54:55], v[182:183]
	v_rcp_iflag_f32_e32 v182, v80
	v_cvt_f32_ubyte3_e32 v80, v185
	v_cvt_f32_ubyte1_e32 v191, v161
	v_cvt_f32_ubyte0_e32 v190, v161
	v_rcp_iflag_f32_e32 v183, v80
	v_pk_mul_f32 v[154:155], v[154:155], v[190:191]
	v_cvt_f32_ubyte0_e32 v80, v188
	v_pk_mul_f32 v[48:49], v[48:49], v[154:155]
	v_rcp_iflag_f32_e32 v154, v80
	v_cvt_f32_ubyte1_e32 v80, v188
	v_rcp_iflag_f32_e32 v155, v80
	v_cvt_f32_ubyte3_e32 v185, v161
	v_cvt_f32_ubyte2_e32 v184, v161
	v_pk_mul_f32 v[160:161], v[182:183], v[184:185]
	v_cvt_f32_ubyte2_e32 v80, v188
	v_pk_mul_f32 v[50:51], v[50:51], v[160:161]
	v_rcp_iflag_f32_e32 v160, v80
	v_cvt_f32_ubyte3_e32 v80, v188
	v_cvt_f32_ubyte1_e32 v185, v186
	v_cvt_f32_ubyte0_e32 v184, v186
	v_rcp_iflag_f32_e32 v161, v80
	v_pk_mul_f32 v[154:155], v[154:155], v[184:185]
	v_cvt_f32_ubyte0_e32 v80, v189
	v_pk_mul_f32 v[44:45], v[44:45], v[154:155]
	v_rcp_iflag_f32_e32 v154, v80
	v_cvt_f32_ubyte1_e32 v80, v189
	v_rcp_iflag_f32_e32 v155, v80
	v_cvt_f32_ubyte3_e32 v183, v186
	v_cvt_f32_ubyte2_e32 v182, v186
	v_pk_mul_f32 v[160:161], v[160:161], v[182:183]
	v_cvt_f32_ubyte2_e32 v80, v189
	v_pk_mul_f32 v[46:47], v[46:47], v[160:161]
	v_rcp_iflag_f32_e32 v160, v80
	v_cvt_f32_ubyte3_e32 v80, v189
	v_cvt_f32_ubyte1_e32 v185, v187
	v_cvt_f32_ubyte0_e32 v184, v187
	v_rcp_iflag_f32_e32 v161, v80
	v_pk_mul_f32 v[154:155], v[154:155], v[184:185]
	v_cvt_f32_ubyte0_e32 v80, v180
	v_pk_mul_f32 v[40:41], v[40:41], v[154:155]
	v_rcp_iflag_f32_e32 v154, v80
	v_cvt_f32_ubyte1_e32 v80, v180
	v_rcp_iflag_f32_e32 v155, v80
; #define GM_R(w, sh) ((float)(((a.w) >> (sh)) & 255u) * __builtin_amdgcn_rcpf((float)(((b.w) >> (sh)) & 255u)))
;     __device__ __forceinline__ void mid(f32x4 (&acc)[2][2][4][2], const Unit& u, int wr, int wc) const {
;     ...
;                 for (int bj = 0; bj < 2; ++bj) { const u32x2 a = ga[m][bj], b = gb[m][bj];
;     ...
;                     acc[ai][bj][m][0][0] *= GM_R(x, 0); acc[ai][bj][m][0][1] *= GM_R(x, 8); acc[ai][bj][m][0][2] *= GM_R(x, 16); acc[ai][bj][m][0][3] *= GM_R(x, 24);
;                     acc[ai][bj][m][1][0] *= GM_R(y, 0); acc[ai][bj][m][1][1] *= GM_R(y, 8); acc[ai][bj][m][1][2] *= GM_R(y, 16); acc[ai][bj][m][1][3] *= GM_R(y, 24);
;     ...
;                 }
	v_cvt_f32_ubyte3_e32 v183, v187
	v_cvt_f32_ubyte2_e32 v182, v187
	v_pk_mul_f32 v[160:161], v[160:161], v[182:183]
	v_cvt_f32_ubyte2_e32 v80, v180
	v_pk_mul_f32 v[42:43], v[42:43], v[160:161]
	v_rcp_iflag_f32_e32 v160, v80
	v_cvt_f32_ubyte3_e32 v80, v180
	v_cvt_f32_ubyte1_e32 v185, v178
	v_cvt_f32_ubyte0_e32 v184, v178
	v_rcp_iflag_f32_e32 v161, v80
	v_pk_mul_f32 v[154:155], v[154:155], v[184:185]
	v_cvt_f32_ubyte0_e32 v80, v181
	v_pk_mul_f32 v[36:37], v[36:37], v[154:155]
	v_rcp_iflag_f32_e32 v154, v80
	v_cvt_f32_ubyte1_e32 v80, v181
	v_rcp_iflag_f32_e32 v155, v80
	v_cvt_f32_ubyte3_e32 v183, v178
	v_cvt_f32_ubyte2_e32 v182, v178
	v_pk_mul_f32 v[160:161], v[160:161], v[182:183]
	v_cvt_f32_ubyte2_e32 v80, v181
	v_pk_mul_f32 v[38:39], v[38:39], v[160:161]
	v_rcp_iflag_f32_e32 v160, v80
	v_cvt_f32_ubyte3_e32 v80, v181
	v_cvt_f32_ubyte1_e32 v183, v179
	v_cvt_f32_ubyte0_e32 v182, v179
	v_rcp_iflag_f32_e32 v161, v80
	v_pk_mul_f32 v[154:155], v[154:155], v[182:183]
	v_cvt_f32_ubyte0_e32 v80, v176
	v_pk_mul_f32 v[32:33], v[32:33], v[154:155]
	v_rcp_iflag_f32_e32 v154, v80
	v_cvt_f32_ubyte1_e32 v80, v176
	v_rcp_iflag_f32_e32 v155, v80
	v_cvt_f32_ubyte3_e32 v181, v179
	v_cvt_f32_ubyte2_e32 v180, v179
	v_pk_mul_f32 v[160:161], v[160:161], v[180:181]
	v_cvt_f32_ubyte2_e32 v80, v176
	v_pk_mul_f32 v[34:35], v[34:35], v[160:161]
	v_rcp_iflag_f32_e32 v160, v80
	v_cvt_f32_ubyte3_e32 v80, v176
	v_cvt_f32_ubyte1_e32 v181, v174
	v_cvt_f32_ubyte0_e32 v180, v174
	v_rcp_iflag_f32_e32 v161, v80
	v_pk_mul_f32 v[154:155], v[154:155], v[180:181]
	v_cvt_f32_ubyte0_e32 v80, v177
	v_pk_mul_f32 v[28:29], v[28:29], v[154:155]
	v_rcp_iflag_f32_e32 v154, v80
	v_cvt_f32_ubyte1_e32 v80, v177
	v_rcp_iflag_f32_e32 v155, v80
	v_cvt_f32_ubyte3_e32 v179, v174
	v_cvt_f32_ubyte2_e32 v178, v174
	v_pk_mul_f32 v[160:161], v[160:161], v[178:179]
	v_cvt_f32_ubyte2_e32 v80, v177
	v_pk_mul_f32 v[30:31], v[30:31], v[160:161]
	v_rcp_iflag_f32_e32 v160, v80
	v_cvt_f32_ubyte3_e32 v80, v177
	v_cvt_f32_ubyte1_e32 v179, v175
	v_cvt_f32_ubyte0_e32 v178, v175
	v_rcp_iflag_f32_e32 v161, v80
	v_pk_mul_f32 v[154:155], v[154:155], v[178:179]
	v_cvt_f32_ubyte0_e32 v80, v158
	v_pk_mul_f32 v[24:25], v[24:25], v[154:155]
	v_rcp_iflag_f32_e32 v154, v80
	v_cvt_f32_ubyte1_e32 v80, v158
	v_rcp_iflag_f32_e32 v155, v80
	v_cvt_f32_ubyte3_e32 v177, v175
	v_cvt_f32_ubyte2_e32 v176, v175
	v_pk_mul_f32 v[160:161], v[160:161], v[176:177]
	v_cvt_f32_ubyte2_e32 v80, v158
	v_pk_mul_f32 v[26:27], v[26:27], v[160:161]
	v_rcp_iflag_f32_e32 v160, v80
	v_cvt_f32_ubyte3_e32 v80, v158
	v_cvt_f32_ubyte1_e32 v177, v156
	v_cvt_f32_ubyte0_e32 v176, v156
	v_rcp_iflag_f32_e32 v161, v80
	v_pk_mul_f32 v[154:155], v[154:155], v[176:177]
	v_cvt_f32_ubyte0_e32 v80, v159
	v_pk_mul_f32 v[20:21], v[20:21], v[154:155]
	v_rcp_iflag_f32_e32 v154, v80
	v_cvt_f32_ubyte1_e32 v80, v159
	v_rcp_iflag_f32_e32 v155, v80
	v_cvt_f32_ubyte3_e32 v175, v156
	v_cvt_f32_ubyte2_e32 v174, v156
	v_cvt_f32_ubyte2_e32 v80, v159
	v_pk_mul_f32 v[160:161], v[160:161], v[174:175]
	v_rcp_iflag_f32_e32 v158, v80
	v_cvt_f32_ubyte3_e32 v80, v159
	v_cvt_f32_ubyte1_e32 v175, v157
	v_cvt_f32_ubyte0_e32 v174, v157
	v_rcp_iflag_f32_e32 v159, v80
	v_pk_mul_f32 v[154:155], v[154:155], v[174:175]
	v_cvt_f32_ubyte0_e32 v80, v152
	v_pk_mul_f32 v[16:17], v[16:17], v[154:155]
	v_rcp_iflag_f32_e32 v154, v80
	v_cvt_f32_ubyte1_e32 v80, v152
	v_rcp_iflag_f32_e32 v155, v80
	v_pk_mul_f32 v[22:23], v[22:23], v[160:161]
	v_cvt_f32_ubyte3_e32 v161, v157
	v_cvt_f32_ubyte2_e32 v160, v157
	v_pk_mul_f32 v[156:157], v[158:159], v[160:161]
	v_cvt_f32_ubyte2_e32 v80, v152
	v_pk_mul_f32 v[18:19], v[18:19], v[156:157]
	v_rcp_iflag_f32_e32 v156, v80
	v_cvt_f32_ubyte3_e32 v80, v152
	v_cvt_f32_ubyte1_e32 v161, v150
	v_cvt_f32_ubyte0_e32 v160, v150
	v_rcp_iflag_f32_e32 v157, v80
	v_pk_mul_f32 v[154:155], v[154:155], v[160:161]
	v_cvt_f32_ubyte0_e32 v80, v153
	v_pk_mul_f32 v[12:13], v[12:13], v[154:155]
	v_rcp_iflag_f32_e32 v154, v80
	v_cvt_f32_ubyte1_e32 v80, v153
	v_rcp_iflag_f32_e32 v155, v80
	v_cvt_f32_ubyte3_e32 v159, v150
	v_cvt_f32_ubyte2_e32 v158, v150
	v_cvt_f32_ubyte2_e32 v80, v153
	v_pk_mul_f32 v[156:157], v[156:157], v[158:159]
	v_rcp_iflag_f32_e32 v152, v80
	v_cvt_f32_ubyte3_e32 v80, v153
	v_cvt_f32_ubyte1_e32 v159, v151
	v_cvt_f32_ubyte0_e32 v158, v151
	v_pk_mul_f32 v[14:15], v[14:15], v[156:157]
	v_rcp_iflag_f32_e32 v153, v80
	v_cvt_f32_ubyte3_e32 v157, v151
	v_cvt_f32_ubyte2_e32 v156, v151
	v_pk_mul_f32 v[150:151], v[154:155], v[158:159]
	v_cvt_f32_ubyte0_e32 v80, v148
	v_pk_mul_f32 v[8:9], v[8:9], v[150:151]
	v_rcp_iflag_f32_e32 v150, v80
	v_cvt_f32_ubyte1_e32 v80, v148
	v_rcp_iflag_f32_e32 v151, v80
	v_pk_mul_f32 v[152:153], v[152:153], v[156:157]
	v_cvt_f32_ubyte2_e32 v80, v148
	v_pk_mul_f32 v[10:11], v[10:11], v[152:153]
	v_rcp_iflag_f32_e32 v152, v80
	v_cvt_f32_ubyte3_e32 v80, v148
	v_cvt_f32_ubyte1_e32 v157, v82
	v_cvt_f32_ubyte0_e32 v156, v82
	v_rcp_iflag_f32_e32 v153, v80
	v_pk_mul_f32 v[150:151], v[150:151], v[156:157]
	v_cvt_f32_ubyte0_e32 v80, v149
	v_pk_mul_f32 v[4:5], v[4:5], v[150:151]
	v_rcp_iflag_f32_e32 v150, v80
	v_cvt_f32_ubyte1_e32 v80, v149
	v_rcp_iflag_f32_e32 v151, v80
	v_cvt_f32_ubyte2_e32 v80, v149
	v_rcp_iflag_f32_e32 v148, v80
	v_cvt_f32_ubyte3_e32 v80, v149
	v_rcp_iflag_f32_e32 v149, v80
	v_cvt_f32_ubyte3_e32 v155, v82
	v_cvt_f32_ubyte2_e32 v154, v82
	v_pk_mul_f32 v[152:153], v[152:153], v[154:155]
	v_cvt_f32_ubyte1_e32 v155, v83
	v_pk_mul_f32 v[6:7], v[6:7], v[152:153]
	v_cvt_f32_ubyte3_e32 v153, v83
	v_cvt_f32_ubyte2_e32 v152, v83
	v_cvt_f32_ubyte0_e32 v154, v83
	v_pk_mul_f32 v[82:83], v[150:151], v[154:155]
	v_pk_mul_f32 v[148:149], v[148:149], v[152:153]
	v_pk_mul_f32 v[0:1], v[0:1], v[82:83]
	v_pk_mul_f32 v[2:3], v[2:3], v[148:149]
	s_branch .LBB0_467

; __device__ __forceinline__ unsigned cvtpk(float lo, float hi) { f32x2_t v = {lo, hi}; bf16x2_t b = __builtin_convertvector(v, bf16x2_t); return __builtin_bit_cast(unsigned, b); }
;     __device__ __forceinline__ void operator()(const f32x4 (&acc)[2][2][4][2], const Unit& u, int wr, int wc, int fr, int fq) const {
;         { int z_ = 0; asm volatile("" : "+v"(z_)); const int l_ = (int)__builtin_amdgcn_mbcnt_hi(~0u, __builtin_amdgcn_mbcnt_lo(~0u, (unsigned)z_)); fr = l_ & 15; fq = l_ >> 4; }
;         const int row0 = u.pm * BM + wr * 64 + fr, col0 = u.pn * BM + wc * 32 + 8 * fq;
; #pragma unroll
;         for (int ai = 0; ai < 2; ++ai) {
;             u32x2 gb[4][2];
; #pragma unroll
;             for (int m = 0; m < 4; ++m)
; #pragma unroll
;                 for (int bj = 0; bj < 2; ++bj) gb[m][bj] = *(const u32x2*)(G + (size_t)(4 + u.pn) * ldg + (size_t)(row0 + ai * HALF + m * 16) * 256 + (wc * 32 + 8 * fq) + bj * HALF);
; #pragma unroll
;             for (int m = 0; m < 4; ++m)
; #pragma unroll
;                 for (int bj = 0; bj < 2; ++bj) { const size_t r = (size_t)(row0 + ai * HALF + m * 16); const int c = col0 + bj * HALF; const u32x2 b = gb[m][bj]; const float k = 1.f / 255.f;
;                     f32x4 v0 = acc[ai][bj][m][0], v1 = acc[ai][bj][m][1];
;                     v0[0] *= (float)(b.x & 255u) * k; v0[1] *= (float)((b.x >> 8) & 255u) * k; v0[2] *= (float)((b.x >> 16) & 255u) * k; v0[3] *= (float)(b.x >> 24) * k;
;                     v1[0] *= (float)(b.y & 255u) * k; v1[1] *= (float)((b.y >> 8) & 255u) * k; v1[2] *= (float)((b.y >> 16) & 255u) * k; v1[3] *= (float)(b.y >> 24) * k;
;                     u32x4 w; w.x = cvtpk(v0[0], v0[1]); w.y = cvtpk(v0[2], v0[3]); w.z = cvtpk(v1[0], v1[1]); w.w = cvtpk(v1[2], v1[3]);
;                     *(u32x4*)(O + r * ldc + c) = w; }
;         }
;     }
.LBB0_472:
	v_mov_b32_e32 v80, v81
	s_add_i32 s9, s9, s39
	v_mbcnt_lo_u32_b32 v80, -1, v80
	v_mbcnt_hi_u32_b32 v80, -1, v80
	v_and_or_b32 v144, v80, 15, s9
	s_lshl_b32 s0, s18, 8
	v_ashrrev_i32_e32 v80, 1, v80
	s_or_b32 s0, s0, s40
	v_and_b32_e32 v80, -8, v80
	v_add_u32_e32 v82, s0, v80
	s_lshl_b64 s[0:1], s[18:19], 22
	v_add_u32_e32 v146, s40, v80
	s_add_u32 s0, s37, s0
	v_ashrrev_i32_e32 v147, 31, v146
	s_addc_u32 s1, s38, s1
	v_lshl_add_u64 v[146:147], s[0:1], 0, v[146:147]
	s_mov_b64 s[0:1], 0x1000000
	v_ashrrev_i32_e32 v145, 31, v144
	v_lshl_add_u64 v[146:147], v[146:147], 0, s[0:1]
	v_lshlrev_b64 v[148:149], 8, v[144:145]
	v_lshl_add_u64 v[148:149], v[146:147], 0, v[148:149]
	global_load_dwordx2 v[180:181], v[148:149], off
	global_load_dwordx2 v[178:179], v[148:149], off offset:128
	v_or_b32_e32 v174, 16, v144
	v_ashrrev_i32_e32 v175, 31, v174
	v_lshlrev_b64 v[148:149], 8, v[174:175]
	v_lshl_add_u64 v[148:149], v[146:147], 0, v[148:149]
	global_load_dwordx2 v[176:177], v[148:149], off
	global_load_dwordx2 v[160:161], v[148:149], off offset:128
	v_or_b32_e32 v156, 32, v144
	v_ashrrev_i32_e32 v157, 31, v156
	v_lshlrev_b64 v[148:149], 8, v[156:157]
	v_lshl_add_u64 v[148:149], v[146:147], 0, v[148:149]
	global_load_dwordx2 v[158:159], v[148:149], off
	global_load_dwordx2 v[154:155], v[148:149], off offset:128
	v_or_b32_e32 v150, 48, v144
	v_ashrrev_i32_e32 v151, 31, v150
	v_lshlrev_b64 v[148:149], 8, v[150:151]
	v_lshl_add_u64 v[148:149], v[146:147], 0, v[148:149]
	global_load_dwordx2 v[152:153], v[148:149], off
	s_nop 0
	global_load_dwordx2 v[148:149], v[148:149], off offset:128
	v_ashrrev_i32_e32 v83, 31, v82
	v_lshlrev_b64 v[82:83], 1, v[82:83]
	s_mov_b64 s[0:1], -1
	s_andn2_b64 vcc, exec, s[2:3]
	s_waitcnt vmcnt(0) lgkmcnt(0)
	v_cvt_f32_ubyte1_e32 v183, v180
	v_cvt_f32_ubyte0_e32 v182, v180
	v_pk_mul_f32 v[182:183], v[182:183], s[58:59] op_sel_hi:[1,0]
	s_nop 0
	v_pk_mul_f32 v[128:129], v[128:129], v[182:183]
	v_cvt_f32_ubyte3_e32 v183, v180
	v_cvt_f32_ubyte2_e32 v182, v180
	v_pk_mul_f32 v[182:183], v[182:183], s[58:59] op_sel_hi:[1,0]
	s_nop 0
	v_pk_mul_f32 v[130:131], v[130:131], v[182:183]
	v_cvt_f32_ubyte1_e32 v183, v181
	v_cvt_f32_ubyte0_e32 v182, v181
	v_pk_mul_f32 v[182:183], v[182:183], s[58:59] op_sel_hi:[1,0]
	s_nop 0
	v_pk_mul_f32 v[182:183], v[124:125], v[182:183]
	v_cvt_f32_ubyte3_e32 v125, v181
	v_cvt_f32_ubyte2_e32 v124, v181
	v_pk_mul_f32 v[124:125], v[124:125], s[58:59] op_sel_hi:[1,0]
	s_nop 0
	v_pk_mul_f32 v[180:181], v[126:127], v[124:125]
	v_cvt_pk_bf16_f32 v124, v128, v129
	v_lshlrev_b64 v[128:129], 11, v[144:145]
	v_lshl_add_u64 v[128:129], s[70:71], 0, v[128:129]
	v_cvt_pk_bf16_f32 v125, v130, v131
	v_cvt_pk_bf16_f32 v126, v182, v183
	v_cvt_pk_bf16_f32 v127, v180, v181
	v_lshl_add_u64 v[128:129], v[128:129], 0, v[82:83]
	global_store_dwordx4 v[128:129], v[124:127], off
	s_nop 1
	v_cvt_f32_ubyte1_e32 v125, v178
	v_cvt_f32_ubyte0_e32 v124, v178
	v_pk_mul_f32 v[124:125], v[124:125], s[58:59] op_sel_hi:[1,0]
	s_nop 0
	v_pk_mul_f32 v[120:121], v[120:121], v[124:125]
	v_cvt_f32_ubyte3_e32 v125, v178
	v_cvt_f32_ubyte2_e32 v124, v178
	v_pk_mul_f32 v[124:125], v[124:125], s[58:59] op_sel_hi:[1,0]
	s_nop 0
	v_pk_mul_f32 v[122:123], v[122:123], v[124:125]
	v_cvt_f32_ubyte1_e32 v125, v179
	v_cvt_f32_ubyte0_e32 v124, v179
	v_pk_mul_f32 v[124:125], v[124:125], s[58:59] op_sel_hi:[1,0]
	s_nop 0
	v_pk_mul_f32 v[124:125], v[116:117], v[124:125]
	v_cvt_f32_ubyte3_e32 v117, v179
	v_cvt_f32_ubyte2_e32 v116, v179
	v_pk_mul_f32 v[116:117], v[116:117], s[58:59] op_sel_hi:[1,0]
	s_nop 0
	v_pk_mul_f32 v[126:127], v[118:119], v[116:117]
	v_cvt_pk_bf16_f32 v116, v120, v121
	v_cvt_pk_bf16_f32 v117, v122, v123
	v_cvt_pk_bf16_f32 v118, v124, v125
	v_cvt_pk_bf16_f32 v119, v126, v127
	global_store_dwordx4 v[128:129], v[116:119], off offset:256
	s_nop 1
	v_cvt_f32_ubyte1_e32 v117, v176
	v_cvt_f32_ubyte0_e32 v116, v176
	v_pk_mul_f32 v[116:117], v[116:117], s[58:59] op_sel_hi:[1,0]
	s_nop 0
	v_pk_mul_f32 v[112:113], v[112:113], v[116:117]
	v_cvt_f32_ubyte3_e32 v117, v176
	v_cvt_f32_ubyte2_e32 v116, v176
	v_pk_mul_f32 v[116:117], v[116:117], s[58:59] op_sel_hi:[1,0]
	s_nop 0
	v_pk_mul_f32 v[114:115], v[114:115], v[116:117]
	v_cvt_f32_ubyte1_e32 v117, v177
	v_cvt_f32_ubyte0_e32 v116, v177
	v_pk_mul_f32 v[116:117], v[116:117], s[58:59] op_sel_hi:[1,0]
	s_nop 0
	v_pk_mul_f32 v[116:117], v[108:109], v[116:117]
	v_cvt_f32_ubyte3_e32 v109, v177
	v_cvt_f32_ubyte2_e32 v108, v177
	v_pk_mul_f32 v[108:109], v[108:109], s[58:59] op_sel_hi:[1,0]
	s_nop 0
	v_pk_mul_f32 v[118:119], v[110:111], v[108:109]
	v_cvt_pk_bf16_f32 v108, v112, v113
	v_lshlrev_b64 v[112:113], 11, v[174:175]
	v_lshl_add_u64 v[112:113], s[70:71], 0, v[112:113]
	v_cvt_pk_bf16_f32 v109, v114, v115
	v_cvt_pk_bf16_f32 v110, v116, v117
	v_cvt_pk_bf16_f32 v111, v118, v119
	v_lshl_add_u64 v[112:113], v[112:113], 0, v[82:83]
	global_store_dwordx4 v[112:113], v[108:111], off
	s_nop 1
	v_cvt_f32_ubyte1_e32 v109, v160
	v_cvt_f32_ubyte0_e32 v108, v160
	v_pk_mul_f32 v[108:109], v[108:109], s[58:59] op_sel_hi:[1,0]
	s_nop 0
	v_pk_mul_f32 v[104:105], v[104:105], v[108:109]
	v_cvt_f32_ubyte3_e32 v109, v160
	v_cvt_f32_ubyte2_e32 v108, v160
	v_pk_mul_f32 v[108:109], v[108:109], s[58:59] op_sel_hi:[1,0]
	s_nop 0
	v_pk_mul_f32 v[106:107], v[106:107], v[108:109]
	v_cvt_f32_ubyte1_e32 v109, v161
	v_cvt_f32_ubyte0_e32 v108, v161
	v_pk_mul_f32 v[108:109], v[108:109], s[58:59] op_sel_hi:[1,0]
	s_nop 0
	v_pk_mul_f32 v[108:109], v[100:101], v[108:109]
	v_cvt_f32_ubyte3_e32 v101, v161
	v_cvt_f32_ubyte2_e32 v100, v161
	v_pk_mul_f32 v[100:101], v[100:101], s[58:59] op_sel_hi:[1,0]
	s_nop 0
; __device__ __forceinline__ unsigned cvtpk(float lo, float hi) { f32x2_t v = {lo, hi}; bf16x2_t b = __builtin_convertvector(v, bf16x2_t); return __builtin_bit_cast(unsigned, b); }
;     __device__ __forceinline__ void operator()(const f32x4 (&acc)[2][2][4][2], const Unit& u, int wr, int wc, int fr, int fq) const {
;         { int z_ = 0; asm volatile("" : "+v"(z_)); const int l_ = (int)__builtin_amdgcn_mbcnt_hi(~0u, __builtin_amdgcn_mbcnt_lo(~0u, (unsigned)z_)); fr = l_ & 15; fq = l_ >> 4; }
;         const int row0 = u.pm * BM + wr * 64 + fr, col0 = u.pn * BM + wc * 32 + 8 * fq;
; #pragma unroll
;         for (int ai = 0; ai < 2; ++ai) {
;             u32x2 gb[4][2];
; #pragma unroll
;             for (int m = 0; m < 4; ++m)
; #pragma unroll
;                 for (int bj = 0; bj < 2; ++bj) gb[m][bj] = *(const u32x2*)(G + (size_t)(4 + u.pn) * ldg + (size_t)(row0 + ai * HALF + m * 16) * 256 + (wc * 32 + 8 * fq) + bj * HALF);
; #pragma unroll
;             for (int m = 0; m < 4; ++m)
; #pragma unroll
;                 for (int bj = 0; bj < 2; ++bj) { const size_t r = (size_t)(row0 + ai * HALF + m * 16); const int c = col0 + bj * HALF; const u32x2 b = gb[m][bj]; const float k = 1.f / 255.f;
;                     f32x4 v0 = acc[ai][bj][m][0], v1 = acc[ai][bj][m][1];
;                     v0[0] *= (float)(b.x & 255u) * k; v0[1] *= (float)((b.x >> 8) & 255u) * k; v0[2] *= (float)((b.x >> 16) & 255u) * k; v0[3] *= (float)(b.x >> 24) * k;
;                     v1[0] *= (float)(b.y & 255u) * k; v1[1] *= (float)((b.y >> 8) & 255u) * k; v1[2] *= (float)((b.y >> 16) & 255u) * k; v1[3] *= (float)(b.y >> 24) * k;
;                     u32x4 w; w.x = cvtpk(v0[0], v0[1]); w.y = cvtpk(v0[2], v0[3]); w.z = cvtpk(v1[0], v1[1]); w.w = cvtpk(v1[2], v1[3]);
;                     *(u32x4*)(O + r * ldc + c) = w; }
;         }
;     }
	v_pk_mul_f32 v[110:111], v[102:103], v[100:101]
	v_cvt_pk_bf16_f32 v100, v104, v105
	v_cvt_pk_bf16_f32 v101, v106, v107
	v_cvt_pk_bf16_f32 v102, v108, v109
	v_cvt_pk_bf16_f32 v103, v110, v111
	global_store_dwordx4 v[112:113], v[100:103], off offset:256
	s_nop 1
	v_cvt_f32_ubyte1_e32 v101, v158
	v_cvt_f32_ubyte0_e32 v100, v158
	v_pk_mul_f32 v[100:101], v[100:101], s[58:59] op_sel_hi:[1,0]
	s_nop 0
	v_pk_mul_f32 v[96:97], v[96:97], v[100:101]
	v_cvt_f32_ubyte3_e32 v101, v158
	v_cvt_f32_ubyte2_e32 v100, v158
	v_pk_mul_f32 v[100:101], v[100:101], s[58:59] op_sel_hi:[1,0]
	s_nop 0
	v_pk_mul_f32 v[98:99], v[98:99], v[100:101]
	v_cvt_f32_ubyte1_e32 v101, v159
	v_cvt_f32_ubyte0_e32 v100, v159
	v_pk_mul_f32 v[100:101], v[100:101], s[58:59] op_sel_hi:[1,0]
	s_nop 0
	v_pk_mul_f32 v[100:101], v[92:93], v[100:101]
	v_cvt_f32_ubyte3_e32 v93, v159
	v_cvt_f32_ubyte2_e32 v92, v159
	v_pk_mul_f32 v[92:93], v[92:93], s[58:59] op_sel_hi:[1,0]
	s_nop 0
	v_pk_mul_f32 v[102:103], v[94:95], v[92:93]
	v_cvt_pk_bf16_f32 v92, v96, v97
	v_lshlrev_b64 v[96:97], 11, v[156:157]
	v_lshl_add_u64 v[96:97], s[70:71], 0, v[96:97]
	v_cvt_pk_bf16_f32 v93, v98, v99
	v_cvt_pk_bf16_f32 v94, v100, v101
	v_cvt_pk_bf16_f32 v95, v102, v103
	v_lshl_add_u64 v[96:97], v[96:97], 0, v[82:83]
	global_store_dwordx4 v[96:97], v[92:95], off
	s_nop 1
	v_cvt_f32_ubyte1_e32 v93, v154
	v_cvt_f32_ubyte0_e32 v92, v154
	v_pk_mul_f32 v[92:93], v[92:93], s[58:59] op_sel_hi:[1,0]
	s_nop 0
	v_pk_mul_f32 v[88:89], v[88:89], v[92:93]
	v_cvt_f32_ubyte3_e32 v93, v154
	v_cvt_f32_ubyte2_e32 v92, v154
	v_pk_mul_f32 v[92:93], v[92:93], s[58:59] op_sel_hi:[1,0]
	s_nop 0
	v_pk_mul_f32 v[90:91], v[90:91], v[92:93]
	v_cvt_f32_ubyte1_e32 v93, v155
	v_cvt_f32_ubyte0_e32 v92, v155
	v_pk_mul_f32 v[92:93], v[92:93], s[58:59] op_sel_hi:[1,0]
	s_nop 0
	v_pk_mul_f32 v[92:93], v[84:85], v[92:93]
	v_cvt_f32_ubyte3_e32 v85, v155
	v_cvt_f32_ubyte2_e32 v84, v155
	v_pk_mul_f32 v[84:85], v[84:85], s[58:59] op_sel_hi:[1,0]
	s_nop 0
	v_pk_mul_f32 v[94:95], v[86:87], v[84:85]
	v_cvt_pk_bf16_f32 v84, v88, v89
	v_cvt_pk_bf16_f32 v85, v90, v91
	v_cvt_pk_bf16_f32 v86, v92, v93
	v_cvt_pk_bf16_f32 v87, v94, v95
	global_store_dwordx4 v[96:97], v[84:87], off offset:256
	s_nop 1
	v_cvt_f32_ubyte1_e32 v85, v152
	v_cvt_f32_ubyte0_e32 v84, v152
	v_pk_mul_f32 v[84:85], v[84:85], s[58:59] op_sel_hi:[1,0]
	s_nop 0
	v_pk_mul_f32 v[76:77], v[76:77], v[84:85]
	v_cvt_f32_ubyte3_e32 v85, v152
	v_cvt_f32_ubyte2_e32 v84, v152
	v_pk_mul_f32 v[84:85], v[84:85], s[58:59] op_sel_hi:[1,0]
	s_nop 0
	v_pk_mul_f32 v[78:79], v[78:79], v[84:85]
	v_cvt_f32_ubyte1_e32 v85, v153
	v_cvt_f32_ubyte0_e32 v84, v153
	v_pk_mul_f32 v[84:85], v[84:85], s[58:59] op_sel_hi:[1,0]
	s_nop 0
	v_pk_mul_f32 v[84:85], v[72:73], v[84:85]
	v_cvt_f32_ubyte3_e32 v73, v153
	v_cvt_f32_ubyte2_e32 v72, v153
	v_pk_mul_f32 v[72:73], v[72:73], s[58:59] op_sel_hi:[1,0]
	s_nop 0
	v_pk_mul_f32 v[86:87], v[74:75], v[72:73]
	v_cvt_pk_bf16_f32 v72, v76, v77
	v_lshlrev_b64 v[76:77], 11, v[150:151]
	v_lshl_add_u64 v[76:77], s[70:71], 0, v[76:77]
	v_cvt_pk_bf16_f32 v73, v78, v79
	v_cvt_pk_bf16_f32 v74, v84, v85
	v_cvt_pk_bf16_f32 v75, v86, v87
	v_lshl_add_u64 v[76:77], v[76:77], 0, v[82:83]
	global_store_dwordx4 v[76:77], v[72:75], off
	v_add_u32_e32 v84, 0xa0, v144
	v_ashrrev_i32_e32 v85, 31, v84
	v_cvt_f32_ubyte1_e32 v73, v148
	v_cvt_f32_ubyte0_e32 v72, v148
	v_pk_mul_f32 v[72:73], v[72:73], s[58:59] op_sel_hi:[1,0]
	s_nop 0
	v_pk_mul_f32 v[68:69], v[68:69], v[72:73]
	v_cvt_f32_ubyte3_e32 v73, v148
	v_cvt_f32_ubyte2_e32 v72, v148
	v_pk_mul_f32 v[72:73], v[72:73], s[58:59] op_sel_hi:[1,0]
	s_nop 0
	v_pk_mul_f32 v[70:71], v[70:71], v[72:73]
	v_cvt_f32_ubyte1_e32 v73, v149
	v_cvt_f32_ubyte0_e32 v72, v149
	v_pk_mul_f32 v[72:73], v[72:73], s[58:59] op_sel_hi:[1,0]
	s_nop 0
	v_pk_mul_f32 v[72:73], v[64:65], v[72:73]
	v_cvt_f32_ubyte3_e32 v65, v149
	v_cvt_f32_ubyte2_e32 v64, v149
	v_pk_mul_f32 v[64:65], v[64:65], s[58:59] op_sel_hi:[1,0]
	s_nop 0
	v_pk_mul_f32 v[74:75], v[66:67], v[64:65]
	v_cvt_pk_bf16_f32 v64, v68, v69
	v_add_u32_e32 v68, 0x80, v144
	v_cvt_pk_bf16_f32 v65, v70, v71
	v_cvt_pk_bf16_f32 v66, v72, v73
	v_cvt_pk_bf16_f32 v67, v74, v75
	v_ashrrev_i32_e32 v69, 31, v68
	global_store_dwordx4 v[76:77], v[64:67], off offset:256
	v_add_u32_e32 v74, 0x90, v144
	v_ashrrev_i32_e32 v75, 31, v74
	v_lshlrev_b64 v[64:65], 8, v[68:69]
	v_lshl_add_u64 v[64:65], v[146:147], 0, v[64:65]
	global_load_dwordx2 v[70:71], v[64:65], off
	global_load_dwordx2 v[72:73], v[64:65], off offset:128
	v_lshlrev_b64 v[64:65], 8, v[74:75]
	v_lshl_add_u64 v[64:65], v[146:147], 0, v[64:65]
	global_load_dwordx2 v[76:77], v[64:65], off
	global_load_dwordx2 v[78:79], v[64:65], off offset:128
	v_lshlrev_b64 v[64:65], 8, v[84:85]
	v_lshl_add_u64 v[64:65], v[146:147], 0, v[64:65]
	global_load_dwordx2 v[86:87], v[64:65], off
	global_load_dwordx2 v[88:89], v[64:65], off offset:128
	v_add_u32_e32 v66, 0xb0, v144
	v_ashrrev_i32_e32 v67, 31, v66
	v_lshlrev_b64 v[64:65], 8, v[66:67]
	v_lshl_add_u64 v[64:65], v[146:147], 0, v[64:65]
	global_load_dwordx2 v[90:91], v[64:65], off
	s_nop 0
	global_load_dwordx2 v[64:65], v[64:65], off offset:128
	s_waitcnt vmcnt(0) lgkmcnt(0)
; __device__ __forceinline__ unsigned cvtpk(float lo, float hi) { f32x2_t v = {lo, hi}; bf16x2_t b = __builtin_convertvector(v, bf16x2_t); return __builtin_bit_cast(unsigned, b); }
;     __device__ __forceinline__ void operator()(const f32x4 (&acc)[2][2][4][2], const Unit& u, int wr, int wc, int fr, int fq) const {
;     ...
;             for (int m = 0; m < 4; ++m)
; #pragma unroll
;                 for (int bj = 0; bj < 2; ++bj) { const size_t r = (size_t)(row0 + ai * HALF + m * 16); const int c = col0 + bj * HALF; const u32x2 b = gb[m][bj]; const float k = 1.f / 255.f;
;                     f32x4 v0 = acc[ai][bj][m][0], v1 = acc[ai][bj][m][1];
;                     v0[0] *= (float)(b.x & 255u) * k; v0[1] *= (float)((b.x >> 8) & 255u) * k; v0[2] *= (float)((b.x >> 16) & 255u) * k; v0[3] *= (float)(b.x >> 24) * k;
;                     v1[0] *= (float)(b.y & 255u) * k; v1[1] *= (float)((b.y >> 8) & 255u) * k; v1[2] *= (float)((b.y >> 16) & 255u) * k; v1[3] *= (float)(b.y >> 24) * k;
;                     u32x4 w; w.x = cvtpk(v0[0], v0[1]); w.y = cvtpk(v0[2], v0[3]); w.z = cvtpk(v1[0], v1[1]); w.w = cvtpk(v1[2], v1[3]);
;                     *(u32x4*)(O + r * ldc + c) = w; }
	v_cvt_f32_ubyte1_e32 v93, v70
	v_cvt_f32_ubyte0_e32 v92, v70
	v_pk_mul_f32 v[92:93], v[92:93], s[58:59] op_sel_hi:[1,0]
	s_nop 0
	v_pk_mul_f32 v[60:61], v[60:61], v[92:93]
	v_cvt_f32_ubyte3_e32 v93, v70
	v_cvt_f32_ubyte2_e32 v92, v70
	v_pk_mul_f32 v[92:93], v[92:93], s[58:59] op_sel_hi:[1,0]
	s_nop 0
	v_pk_mul_f32 v[62:63], v[62:63], v[92:93]
	v_cvt_f32_ubyte1_e32 v93, v71
	v_cvt_f32_ubyte0_e32 v92, v71
	v_pk_mul_f32 v[92:93], v[92:93], s[58:59] op_sel_hi:[1,0]
	s_nop 0
	v_pk_mul_f32 v[92:93], v[56:57], v[92:93]
	v_cvt_f32_ubyte3_e32 v57, v71
	v_cvt_f32_ubyte2_e32 v56, v71
	v_pk_mul_f32 v[56:57], v[56:57], s[58:59] op_sel_hi:[1,0]
	s_nop 0
	v_pk_mul_f32 v[70:71], v[58:59], v[56:57]
	v_cvt_pk_bf16_f32 v56, v60, v61
	v_lshlrev_b64 v[60:61], 11, v[68:69]
	v_lshl_add_u64 v[60:61], s[70:71], 0, v[60:61]
	v_cvt_pk_bf16_f32 v57, v62, v63
	v_cvt_pk_bf16_f32 v58, v92, v93
	v_cvt_pk_bf16_f32 v59, v70, v71
	v_lshl_add_u64 v[60:61], v[60:61], 0, v[82:83]
	global_store_dwordx4 v[60:61], v[56:59], off
	s_nop 1
	v_cvt_f32_ubyte1_e32 v57, v72
	v_cvt_f32_ubyte0_e32 v56, v72
	v_pk_mul_f32 v[56:57], v[56:57], s[58:59] op_sel_hi:[1,0]
	s_nop 0
	v_pk_mul_f32 v[52:53], v[52:53], v[56:57]
	v_cvt_f32_ubyte3_e32 v57, v72
	v_cvt_f32_ubyte2_e32 v56, v72
	v_pk_mul_f32 v[56:57], v[56:57], s[58:59] op_sel_hi:[1,0]
	s_nop 0
	v_pk_mul_f32 v[54:55], v[54:55], v[56:57]
	v_cvt_f32_ubyte1_e32 v57, v73
	v_cvt_f32_ubyte0_e32 v56, v73
	v_pk_mul_f32 v[56:57], v[56:57], s[58:59] op_sel_hi:[1,0]
	s_nop 0
	v_pk_mul_f32 v[56:57], v[48:49], v[56:57]
	v_cvt_f32_ubyte3_e32 v49, v73
	v_cvt_f32_ubyte2_e32 v48, v73
	v_pk_mul_f32 v[48:49], v[48:49], s[58:59] op_sel_hi:[1,0]
	s_nop 0
	v_pk_mul_f32 v[58:59], v[50:51], v[48:49]
	v_cvt_pk_bf16_f32 v48, v52, v53
	v_cvt_pk_bf16_f32 v49, v54, v55
	v_cvt_pk_bf16_f32 v50, v56, v57
	v_cvt_pk_bf16_f32 v51, v58, v59
	global_store_dwordx4 v[60:61], v[48:51], off offset:256
	s_nop 1
	v_cvt_f32_ubyte1_e32 v49, v76
	v_cvt_f32_ubyte0_e32 v48, v76
	v_pk_mul_f32 v[48:49], v[48:49], s[58:59] op_sel_hi:[1,0]
	s_nop 0
	v_pk_mul_f32 v[44:45], v[44:45], v[48:49]
	v_cvt_f32_ubyte3_e32 v49, v76
	v_cvt_f32_ubyte2_e32 v48, v76
	v_pk_mul_f32 v[48:49], v[48:49], s[58:59] op_sel_hi:[1,0]
	s_nop 0
	v_pk_mul_f32 v[46:47], v[46:47], v[48:49]
	v_cvt_f32_ubyte1_e32 v49, v77
	v_cvt_f32_ubyte0_e32 v48, v77
	v_pk_mul_f32 v[48:49], v[48:49], s[58:59] op_sel_hi:[1,0]
	s_nop 0
	v_pk_mul_f32 v[48:49], v[40:41], v[48:49]
	v_cvt_f32_ubyte3_e32 v41, v77
	v_cvt_f32_ubyte2_e32 v40, v77
	v_pk_mul_f32 v[40:41], v[40:41], s[58:59] op_sel_hi:[1,0]
	s_nop 0
	v_pk_mul_f32 v[50:51], v[42:43], v[40:41]
	v_cvt_pk_bf16_f32 v40, v44, v45
	v_lshlrev_b64 v[44:45], 11, v[74:75]
	v_lshl_add_u64 v[44:45], s[70:71], 0, v[44:45]
	v_cvt_pk_bf16_f32 v41, v46, v47
	v_cvt_pk_bf16_f32 v42, v48, v49
	v_cvt_pk_bf16_f32 v43, v50, v51
	v_lshl_add_u64 v[44:45], v[44:45], 0, v[82:83]
	global_store_dwordx4 v[44:45], v[40:43], off
	s_nop 1
	v_cvt_f32_ubyte1_e32 v41, v78
	v_cvt_f32_ubyte0_e32 v40, v78
	v_pk_mul_f32 v[40:41], v[40:41], s[58:59] op_sel_hi:[1,0]
	s_nop 0
	v_pk_mul_f32 v[36:37], v[36:37], v[40:41]
	v_cvt_f32_ubyte3_e32 v41, v78
	v_cvt_f32_ubyte2_e32 v40, v78
	v_pk_mul_f32 v[40:41], v[40:41], s[58:59] op_sel_hi:[1,0]
	s_nop 0
	v_pk_mul_f32 v[38:39], v[38:39], v[40:41]
	v_cvt_f32_ubyte1_e32 v41, v79
	v_cvt_f32_ubyte0_e32 v40, v79
	v_pk_mul_f32 v[40:41], v[40:41], s[58:59] op_sel_hi:[1,0]
	s_nop 0
	v_pk_mul_f32 v[40:41], v[32:33], v[40:41]
	v_cvt_f32_ubyte3_e32 v33, v79
	v_cvt_f32_ubyte2_e32 v32, v79
	v_pk_mul_f32 v[32:33], v[32:33], s[58:59] op_sel_hi:[1,0]
	s_nop 0
	v_pk_mul_f32 v[42:43], v[34:35], v[32:33]
	v_cvt_pk_bf16_f32 v32, v36, v37
	v_cvt_pk_bf16_f32 v33, v38, v39
	v_cvt_pk_bf16_f32 v34, v40, v41
	v_cvt_pk_bf16_f32 v35, v42, v43
	global_store_dwordx4 v[44:45], v[32:35], off offset:256
	s_nop 1
	v_cvt_f32_ubyte1_e32 v33, v86
; #define PG8_BAR __builtin_amdgcn_s_barrier()
; __device__ __forceinline__ unsigned cvtpk(float lo, float hi) { f32x2_t v = {lo, hi}; bf16x2_t b = __builtin_convertvector(v, bf16x2_t); return __builtin_bit_cast(unsigned, b); }
;     ...
;         if (!has_next) break;
; #pragma unroll
;         for (int a = 0; a < 2; ++a)
; #pragma unroll
;             for (int b = 0; b < 2; ++b)
; #pragma unroll
;                 for (int m = 0; m < 4; ++m)
; #pragma unroll
;                     for (int n = 0; n < 2; ++n) acc[a][b][m][n] = (f32x4){0.f, 0.f, 0.f, 0.f};
;         cur = nxt; cA = nA; cB = nB; ++ui;
;         if constexpr (ALIGN_EPI) { if (wr == 1) PG8_BAR; }
;     __device__ __forceinline__ void operator()(const f32x4 (&acc)[2][2][4][2], const Unit& u, int wr, int wc, int fr, int fq) const {
;     ...
;             for (int m = 0; m < 4; ++m)
; #pragma unroll
;                 for (int bj = 0; bj < 2; ++bj) { const size_t r = (size_t)(row0 + ai * HALF + m * 16); const int c = col0 + bj * HALF; const u32x2 b = gb[m][bj]; const float k = 1.f / 255.f;
;                     f32x4 v0 = acc[ai][bj][m][0], v1 = acc[ai][bj][m][1];
;                     v0[0] *= (float)(b.x & 255u) * k; v0[1] *= (float)((b.x >> 8) & 255u) * k; v0[2] *= (float)((b.x >> 16) & 255u) * k; v0[3] *= (float)(b.x >> 24) * k;
;                     v1[0] *= (float)(b.y & 255u) * k; v1[1] *= (float)((b.y >> 8) & 255u) * k; v1[2] *= (float)((b.y >> 16) & 255u) * k; v1[3] *= (float)(b.y >> 24) * k;
;                     u32x4 w; w.x = cvtpk(v0[0], v0[1]); w.y = cvtpk(v0[2], v0[3]); w.z = cvtpk(v1[0], v1[1]); w.w = cvtpk(v1[2], v1[3]);
;                     *(u32x4*)(O + r * ldc + c) = w; }
	v_cvt_f32_ubyte0_e32 v32, v86
	v_pk_mul_f32 v[32:33], v[32:33], s[58:59] op_sel_hi:[1,0]
	s_nop 0
	v_pk_mul_f32 v[28:29], v[28:29], v[32:33]
	v_cvt_f32_ubyte3_e32 v33, v86
	v_cvt_f32_ubyte2_e32 v32, v86
	v_pk_mul_f32 v[32:33], v[32:33], s[58:59] op_sel_hi:[1,0]
	s_nop 0
	v_pk_mul_f32 v[30:31], v[30:31], v[32:33]
	v_cvt_f32_ubyte1_e32 v33, v87
	v_cvt_f32_ubyte0_e32 v32, v87
	v_pk_mul_f32 v[32:33], v[32:33], s[58:59] op_sel_hi:[1,0]
	s_nop 0
	v_pk_mul_f32 v[32:33], v[24:25], v[32:33]
	v_cvt_f32_ubyte3_e32 v25, v87
	v_cvt_f32_ubyte2_e32 v24, v87
	v_pk_mul_f32 v[24:25], v[24:25], s[58:59] op_sel_hi:[1,0]
	s_nop 0
	v_pk_mul_f32 v[34:35], v[26:27], v[24:25]
	v_cvt_pk_bf16_f32 v24, v28, v29
	v_lshlrev_b64 v[28:29], 11, v[84:85]
	v_lshl_add_u64 v[28:29], s[70:71], 0, v[28:29]
	v_cvt_pk_bf16_f32 v25, v30, v31
	v_cvt_pk_bf16_f32 v26, v32, v33
	v_cvt_pk_bf16_f32 v27, v34, v35
	v_lshl_add_u64 v[28:29], v[28:29], 0, v[82:83]
	global_store_dwordx4 v[28:29], v[24:27], off
	s_nop 1
	v_cvt_f32_ubyte1_e32 v25, v88
	v_cvt_f32_ubyte0_e32 v24, v88
	v_pk_mul_f32 v[24:25], v[24:25], s[58:59] op_sel_hi:[1,0]
	s_nop 0
	v_pk_mul_f32 v[20:21], v[20:21], v[24:25]
	v_cvt_f32_ubyte3_e32 v25, v88
	v_cvt_f32_ubyte2_e32 v24, v88
	v_pk_mul_f32 v[24:25], v[24:25], s[58:59] op_sel_hi:[1,0]
	s_nop 0
	v_pk_mul_f32 v[22:23], v[22:23], v[24:25]
	v_cvt_f32_ubyte1_e32 v25, v89
	v_cvt_f32_ubyte0_e32 v24, v89
	v_pk_mul_f32 v[24:25], v[24:25], s[58:59] op_sel_hi:[1,0]
	s_nop 0
	v_pk_mul_f32 v[24:25], v[16:17], v[24:25]
	v_cvt_f32_ubyte3_e32 v17, v89
	v_cvt_f32_ubyte2_e32 v16, v89
	v_pk_mul_f32 v[16:17], v[16:17], s[58:59] op_sel_hi:[1,0]
	s_nop 0
	v_pk_mul_f32 v[26:27], v[18:19], v[16:17]
	v_cvt_pk_bf16_f32 v16, v20, v21
	v_cvt_pk_bf16_f32 v17, v22, v23
	v_cvt_pk_bf16_f32 v18, v24, v25
	v_cvt_pk_bf16_f32 v19, v26, v27
	global_store_dwordx4 v[28:29], v[16:19], off offset:256
	s_nop 1
	v_cvt_f32_ubyte1_e32 v17, v90
	v_cvt_f32_ubyte0_e32 v16, v90
	v_pk_mul_f32 v[16:17], v[16:17], s[58:59] op_sel_hi:[1,0]
	s_nop 0
	v_pk_mul_f32 v[12:13], v[12:13], v[16:17]
	v_cvt_f32_ubyte3_e32 v17, v90
	v_cvt_f32_ubyte2_e32 v16, v90
	v_pk_mul_f32 v[16:17], v[16:17], s[58:59] op_sel_hi:[1,0]
	s_nop 0
	v_pk_mul_f32 v[14:15], v[14:15], v[16:17]
	v_cvt_f32_ubyte1_e32 v17, v91
	v_cvt_f32_ubyte0_e32 v16, v91
	v_pk_mul_f32 v[16:17], v[16:17], s[58:59] op_sel_hi:[1,0]
	s_nop 0
	v_pk_mul_f32 v[16:17], v[8:9], v[16:17]
	v_cvt_f32_ubyte3_e32 v9, v91
	v_cvt_f32_ubyte2_e32 v8, v91
	v_pk_mul_f32 v[8:9], v[8:9], s[58:59] op_sel_hi:[1,0]
	s_nop 0
	v_pk_mul_f32 v[18:19], v[10:11], v[8:9]
	v_cvt_pk_bf16_f32 v8, v12, v13
	v_lshlrev_b64 v[12:13], 11, v[66:67]
	v_lshl_add_u64 v[12:13], s[70:71], 0, v[12:13]
	v_cvt_pk_bf16_f32 v9, v14, v15
	v_cvt_pk_bf16_f32 v10, v16, v17
	v_cvt_pk_bf16_f32 v11, v18, v19
	v_lshl_add_u64 v[12:13], v[12:13], 0, v[82:83]
	global_store_dwordx4 v[12:13], v[8:11], off
	s_nop 1
	v_cvt_f32_ubyte1_e32 v9, v64
	v_cvt_f32_ubyte0_e32 v8, v64
	v_pk_mul_f32 v[8:9], v[8:9], s[58:59] op_sel_hi:[1,0]
	s_nop 0
	v_pk_mul_f32 v[4:5], v[4:5], v[8:9]
	v_cvt_f32_ubyte3_e32 v9, v64
	v_cvt_f32_ubyte2_e32 v8, v64
	v_pk_mul_f32 v[8:9], v[8:9], s[58:59] op_sel_hi:[1,0]
	s_nop 0
	v_pk_mul_f32 v[6:7], v[6:7], v[8:9]
	v_cvt_f32_ubyte1_e32 v9, v65
	v_cvt_f32_ubyte0_e32 v8, v65
	v_pk_mul_f32 v[8:9], v[8:9], s[58:59] op_sel_hi:[1,0]
	s_nop 0
	v_pk_mul_f32 v[8:9], v[0:1], v[8:9]
	v_cvt_f32_ubyte3_e32 v1, v65
	v_cvt_f32_ubyte2_e32 v0, v65
	v_pk_mul_f32 v[0:1], v[0:1], s[58:59] op_sel_hi:[1,0]
	s_nop 0
	v_pk_mul_f32 v[10:11], v[2:3], v[0:1]
	v_cvt_pk_bf16_f32 v0, v4, v5
	v_cvt_pk_bf16_f32 v1, v6, v7
	v_cvt_pk_bf16_f32 v2, v8, v9
	v_cvt_pk_bf16_f32 v3, v10, v11
	global_store_dwordx4 v[12:13], v[0:3], off offset:256
	s_cbranch_vccnz .LBB0_459
	s_andn2_b64 vcc, exec, s[4:5]
	s_cbranch_vccnz .LBB0_458
	s_barrier
	s_branch .LBB0_458

; __device__ __forceinline__ float xor_add(float v, int lane, int o) { return v + __builtin_bit_cast(float, __builtin_amdgcn_ds_bpermute((lane ^ o) << 2, __builtin_bit_cast(int, v))); }
; __device__ __forceinline__ float f16_lo(unsigned u) { return (float)__builtin_bit_cast(h16x2, u)[0]; }
; __device__ __forceinline__ float f16_hi(unsigned u) { return (float)__builtin_bit_cast(h16x2, u)[1]; }
;     __device__ __forceinline__ void operator()(const f32x4 (&acc)[2][2][4][2], const Unit& u, int wr, int wc, int fr, int fq) const {
;     ...
;                     for (int bj = 0; bj < 2; ++bj) bsv[mm][bj] = *(const u32x4*)(base + (size_t)(row0 + ai * HALF + (2 * mp + mm) * 16) * ldc + col0 + bj * HALF);
; #pragma unroll
;                 for (int mm = 0; mm < 2; ++mm) { const int m = 2 * mp + mm; const size_t r = (size_t)(row0 + ai * HALF + m * 16), off = r * ldc + col0; float ss = 0.f;
; #pragma unroll
;                     for (int bj = 0; bj < 2; ++bj) { const u32x4 b = bsv[mm][bj]; const f32x4 a0 = acc[ai][bj][m][0] * sc, a1 = acc[ai][bj][m][1] * sc;
;                         f32x4 v0, v1; v0[0] = f16_lo(b.x) + a0[0]; v0[1] = f16_hi(b.x) + a0[1]; v0[2] = f16_lo(b.y) + a0[2]; v0[3] = f16_hi(b.y) + a0[3];
;                         v1[0] = f16_lo(b.z) + a1[0]; v1[1] = f16_hi(b.z) + a1[1]; v1[2] = f16_lo(b.w) + a1[2]; v1[3] = f16_hi(b.w) + a1[3];
;                         u32x4 w; w.x = pk_f16(v0[0], v0[1]); w.y = pk_f16(v0[2], v0[3]); w.z = pk_f16(v1[0], v1[1]); w.w = pk_f16(v1[2], v1[3]); *(u32x4*)(out + off + bj * HALF) = w;
;                         ss += ((v0[0] * v0[0] + v0[1] * v0[1]) + (v0[2] * v0[2] + v0[3] * v0[3])) + ((v1[0] * v1[0] + v1[1] * v1[1]) + (v1[2] * v1[2] + v1[3] * v1[3])); }
;                     ss = xor_add(ss, lane, 16); ss = xor_add(ss, lane, 32);
;                     if (fq == 0) ssp[r * 16 + (u.pn & 3) * 4 + wc] = ss; }
.LBB0_555:
	v_mov_b32_e32 v130, v81
	s_lshl_b32 s0, s20, 8
	v_mbcnt_lo_u32_b32 v130, -1, v130
	v_mbcnt_hi_u32_b32 v158, -1, v130
	s_add_i32 s0, s0, s35
	v_and_or_b32 v150, v158, 15, s0
	s_lshl_b32 s0, s18, 8
	v_ashrrev_i32_e32 v130, 1, v158
	s_or_b32 s0, s0, s36
	v_and_b32_e32 v130, -8, v130
	v_add_u32_e32 v148, s0, v130
	v_ashrrev_i32_e32 v149, 31, v148
	v_lshlrev_b64 v[160:161], 1, v[148:149]
	v_ashrrev_i32_e32 v151, 31, v150
	v_lshl_add_u64 v[152:153], s[56:57], 0, v[160:161]
	v_lshlrev_b64 v[182:183], 11, v[150:151]
	v_lshl_add_u64 v[130:131], v[152:153], 0, v[182:183]
	global_load_dwordx4 v[174:177], v[130:131], off
	global_load_dwordx4 v[178:181], v[130:131], off offset:256
	v_or_b32_e32 v154, 16, v150
	v_ashrrev_i32_e32 v155, 31, v154
	v_lshlrev_b64 v[130:131], 11, v[154:155]
	v_lshl_add_u64 v[130:131], v[152:153], 0, v[130:131]
	global_load_dwordx4 v[134:137], v[130:131], off
	s_nop 0
	global_load_dwordx4 v[130:133], v[130:131], off offset:256
	v_lshlrev_b32_e32 v170, 2, v158
	v_cmp_gt_u32_e32 vcc, 16, v158
	v_xor_b32_e32 v159, 64, v170
	v_xor_b32_e32 v158, 0x80, v170
	s_lshl_b32 s0, s18, 2
	s_and_b32 s11, s0, 12
	s_waitcnt vmcnt(0) lgkmcnt(0)
	v_cvt_f32_f16_e32 v184, v174
	v_cvt_f32_f16_sdwa v185, v174 dst_sel:DWORD dst_unused:UNUSED_PAD src0_sel:WORD_1
	v_cvt_f32_f16_e32 v174, v175
	v_cvt_f32_f16_sdwa v175, v175 dst_sel:DWORD dst_unused:UNUSED_PAD src0_sel:WORD_1
	v_cvt_f32_f16_e32 v186, v176
	v_cvt_f32_f16_sdwa v187, v176 dst_sel:DWORD dst_unused:UNUSED_PAD src0_sel:WORD_1
	v_cvt_f32_f16_e32 v176, v177
	v_cvt_f32_f16_sdwa v177, v177 dst_sel:DWORD dst_unused:UNUSED_PAD src0_sel:WORD_1
	v_cvt_f32_f16_e32 v188, v178
	v_cvt_f32_f16_sdwa v189, v178 dst_sel:DWORD dst_unused:UNUSED_PAD src0_sel:WORD_1
	v_cvt_f32_f16_e32 v178, v179
	v_cvt_f32_f16_sdwa v179, v179 dst_sel:DWORD dst_unused:UNUSED_PAD src0_sel:WORD_1
	v_cvt_f32_f16_e32 v190, v180
	v_cvt_f32_f16_sdwa v191, v180 dst_sel:DWORD dst_unused:UNUSED_PAD src0_sel:WORD_1
	v_cvt_f32_f16_e32 v180, v181
	v_cvt_f32_f16_sdwa v181, v181 dst_sel:DWORD dst_unused:UNUSED_PAD src0_sel:WORD_1
	v_pk_add_f32 v[126:127], v[126:127], v[184:185]
	v_pk_add_f32 v[128:129], v[128:129], v[174:175]
	v_pk_add_f32 v[122:123], v[122:123], v[186:187]
	v_pk_add_f32 v[124:125], v[124:125], v[176:177]
	v_pk_add_f32 v[118:119], v[118:119], v[188:189]
	v_pk_add_f32 v[120:121], v[120:121], v[178:179]
	v_pk_add_f32 v[174:175], v[114:115], v[190:191]
	v_pk_add_f32 v[176:177], v[116:117], v[180:181]
	v_cvt_pk_f16_f32 v114, v126, v127
	v_cvt_pk_f16_f32 v115, v128, v129
	v_cvt_pk_f16_f32 v116, v122, v123
	v_cvt_pk_f16_f32 v117, v124, v125
	v_pk_mul_f32 v[126:127], v[126:127], v[126:127]
	v_pk_mul_f32 v[128:129], v[128:129], v[128:129]
	v_pk_mul_f32 v[122:123], v[122:123], v[122:123]
	v_pk_mul_f32 v[124:125], v[124:125], v[124:125]
	v_pk_mul_f32 v[178:179], v[118:119], v[118:119]
	v_pk_mul_f32 v[180:181], v[120:121], v[120:121]
	v_pk_mul_f32 v[184:185], v[174:175], v[174:175]
	v_pk_mul_f32 v[186:187], v[176:177], v[176:177]
	v_add_f32_e32 v171, v184, v185
	v_add_f32_e32 v170, v186, v187
	v_add_f32_e32 v172, v180, v181
	v_add_f32_e32 v173, v178, v179
	v_add_f32_e32 v124, v124, v125
	v_add_f32_e32 v122, v122, v123
	v_add_f32_e32 v123, v128, v129
	v_add_f32_e32 v125, v126, v127
	v_add_f32_e32 v126, v171, v170
	v_add_f32_e32 v127, v173, v172
	v_add_f32_e32 v122, v122, v124
	v_add_f32_e32 v123, v125, v123
	v_add_f32_e32 v124, v127, v126
	v_add_f32_e32 v122, v123, v122
	v_add_f32_e32 v124, v122, v124
	ds_bpermute_b32 v125, v159, v124
	v_lshl_add_u64 v[122:123], s[72:73], 0, v[182:183]
	v_lshl_add_u64 v[122:123], v[122:123], 0, v[160:161]
	global_store_dwordx4 v[122:123], v[114:117], off
	s_waitcnt lgkmcnt(0)
	s_nop 0
	v_add_f32_e32 v114, v124, v125
	ds_bpermute_b32 v115, v158, v114
	v_cvt_pk_f16_f32 v116, v118, v119
	v_cvt_pk_f16_f32 v117, v120, v121
	v_cvt_pk_f16_f32 v118, v174, v175
	v_cvt_pk_f16_f32 v119, v176, v177
	global_store_dwordx4 v[122:123], v[116:119], off offset:256
	s_and_saveexec_b64 s[0:1], vcc
	s_cbranch_execz .LBB0_557
	v_lshlrev_b64 v[116:117], 6, v[150:151]
	v_lshl_add_u64 v[116:117], s[6:7], 0, v[116:117]
	s_lshl_b32 s62, s11, 2
	v_lshl_add_u64 v[116:117], v[116:117], 0, s[62:63]
	s_lshl_b32 s62, s34, 2
	v_lshl_add_u64 v[116:117], v[116:117], 0, s[62:63]
	s_waitcnt lgkmcnt(0)
	v_add_f32_e32 v114, v114, v115
	global_store_dword v[116:117], v114, off
; __device__ __forceinline__ float xor_add(float v, int lane, int o) { return v + __builtin_bit_cast(float, __builtin_amdgcn_ds_bpermute((lane ^ o) << 2, __builtin_bit_cast(int, v))); }
; __device__ __forceinline__ float f16_lo(unsigned u) { return (float)__builtin_bit_cast(h16x2, u)[0]; }
; __device__ __forceinline__ float f16_hi(unsigned u) { return (float)__builtin_bit_cast(h16x2, u)[1]; }
;     __device__ __forceinline__ void operator()(const f32x4 (&acc)[2][2][4][2], const Unit& u, int wr, int wc, int fr, int fq) const {
;     ...
;                     for (int bj = 0; bj < 2; ++bj) bsv[mm][bj] = *(const u32x4*)(base + (size_t)(row0 + ai * HALF + (2 * mp + mm) * 16) * ldc + col0 + bj * HALF);
; #pragma unroll
;                 for (int mm = 0; mm < 2; ++mm) { const int m = 2 * mp + mm; const size_t r = (size_t)(row0 + ai * HALF + m * 16), off = r * ldc + col0; float ss = 0.f;
; #pragma unroll
;                     for (int bj = 0; bj < 2; ++bj) { const u32x4 b = bsv[mm][bj]; const f32x4 a0 = acc[ai][bj][m][0] * sc, a1 = acc[ai][bj][m][1] * sc;
;                         f32x4 v0, v1; v0[0] = f16_lo(b.x) + a0[0]; v0[1] = f16_hi(b.x) + a0[1]; v0[2] = f16_lo(b.y) + a0[2]; v0[3] = f16_hi(b.y) + a0[3];
;                         v1[0] = f16_lo(b.z) + a1[0]; v1[1] = f16_hi(b.z) + a1[1]; v1[2] = f16_lo(b.w) + a1[2]; v1[3] = f16_hi(b.w) + a1[3];
;                         u32x4 w; w.x = pk_f16(v0[0], v0[1]); w.y = pk_f16(v0[2], v0[3]); w.z = pk_f16(v1[0], v1[1]); w.w = pk_f16(v1[2], v1[3]); *(u32x4*)(out + off + bj * HALF) = w;
;                         ss += ((v0[0] * v0[0] + v0[1] * v0[1]) + (v0[2] * v0[2] + v0[3] * v0[3])) + ((v1[0] * v1[0] + v1[1] * v1[1]) + (v1[2] * v1[2] + v1[3] * v1[3])); }
;                     ss = xor_add(ss, lane, 16); ss = xor_add(ss, lane, 32);
;                     if (fq == 0) ssp[r * 16 + (u.pn & 3) * 4 + wc] = ss; }
.LBB0_557:
	s_or_b64 exec, exec, s[0:1]
	v_cvt_f32_f16_sdwa v119, v135 dst_sel:DWORD dst_unused:UNUSED_PAD src0_sel:WORD_1
	v_cvt_f32_f16_e32 v118, v135
	v_cvt_f32_f16_sdwa v117, v134 dst_sel:DWORD dst_unused:UNUSED_PAD src0_sel:WORD_1
	v_cvt_f32_f16_e32 v116, v134
	v_cvt_f32_f16_sdwa v121, v137 dst_sel:DWORD dst_unused:UNUSED_PAD src0_sel:WORD_1
	v_pk_add_f32 v[118:119], v[112:113], v[118:119]
	v_cvt_f32_f16_sdwa v113, v136 dst_sel:DWORD dst_unused:UNUSED_PAD src0_sel:WORD_1
	v_cvt_f32_f16_e32 v112, v136
	v_cvt_f32_f16_e32 v120, v137
	s_waitcnt lgkmcnt(0)
	v_lshlrev_b64 v[114:115], 10, v[154:155]
	v_pk_add_f32 v[116:117], v[110:111], v[116:117]
	v_pk_add_f32 v[106:107], v[106:107], v[112:113]
	v_pk_add_f32 v[108:109], v[108:109], v[120:121]
	v_lshl_add_u64 v[114:115], v[114:115], 1, s[72:73]
	v_cvt_pk_f16_f32 v110, v116, v117
	v_cvt_pk_f16_f32 v111, v118, v119
	v_cvt_pk_f16_f32 v112, v106, v107
	v_cvt_pk_f16_f32 v113, v108, v109
	v_lshl_add_u64 v[114:115], v[148:149], 1, v[114:115]
	global_store_dwordx4 v[114:115], v[110:113], off
	v_cvt_f32_f16_sdwa v121, v133 dst_sel:DWORD dst_unused:UNUSED_PAD src0_sel:WORD_1
	v_cvt_f32_f16_e32 v120, v133
	v_pk_mul_f32 v[112:113], v[118:119], v[118:119]
	v_cvt_f32_f16_sdwa v119, v131 dst_sel:DWORD dst_unused:UNUSED_PAD src0_sel:WORD_1
	v_cvt_f32_f16_e32 v118, v131
	v_pk_mul_f32 v[110:111], v[116:117], v[116:117]
	v_cvt_f32_f16_sdwa v117, v130 dst_sel:DWORD dst_unused:UNUSED_PAD src0_sel:WORD_1
	v_cvt_f32_f16_e32 v116, v130
	v_pk_add_f32 v[118:119], v[104:105], v[118:119]
	v_cvt_f32_f16_sdwa v105, v132 dst_sel:DWORD dst_unused:UNUSED_PAD src0_sel:WORD_1
	v_cvt_f32_f16_e32 v104, v132
	v_pk_add_f32 v[116:117], v[102:103], v[116:117]
	v_pk_add_f32 v[100:101], v[100:101], v[120:121]
	v_cvt_pk_f16_f32 v102, v116, v117
	v_pk_add_f32 v[98:99], v[98:99], v[104:105]
	v_cvt_pk_f16_f32 v103, v118, v119
	v_cvt_pk_f16_f32 v104, v98, v99
	v_cvt_pk_f16_f32 v105, v100, v101
	v_pk_mul_f32 v[98:99], v[98:99], v[98:99]
	v_pk_mul_f32 v[100:101], v[100:101], v[100:101]
	global_store_dwordx4 v[114:115], v[102:105], off offset:256
	v_add_f32_e32 v100, v100, v101
	v_add_f32_e32 v98, v98, v99
	v_pk_mul_f32 v[102:103], v[116:117], v[116:117]
	v_pk_mul_f32 v[104:105], v[118:119], v[118:119]
	v_add_f32_e32 v98, v98, v100
	v_add_f32_e32 v99, v104, v105
	v_add_f32_e32 v100, v102, v103
	v_pk_mul_f32 v[106:107], v[106:107], v[106:107]
	v_pk_mul_f32 v[108:109], v[108:109], v[108:109]
	v_add_f32_e32 v99, v100, v99
	v_add_f32_e32 v98, v99, v98
	v_add_f32_e32 v99, v108, v109
	v_add_f32_e32 v100, v106, v107
	v_add_f32_e32 v99, v100, v99
	v_add_f32_e32 v100, v112, v113
	v_add_f32_e32 v101, v110, v111
	v_add_f32_e32 v100, v101, v100
	v_add_f32_e32 v99, v100, v99
	v_add_f32_e32 v98, v99, v98
	ds_bpermute_b32 v99, v159, v98
	s_waitcnt lgkmcnt(0)
	v_add_f32_e32 v98, v98, v99
	ds_bpermute_b32 v99, v158, v98
	s_and_saveexec_b64 s[0:1], vcc
	s_cbranch_execz .LBB0_559
	v_lshlrev_b64 v[100:101], 6, v[154:155]
	v_lshl_add_u64 v[100:101], s[6:7], 0, v[100:101]
	s_lshl_b32 s62, s11, 2
	v_lshl_add_u64 v[100:101], v[100:101], 0, s[62:63]
	s_lshl_b32 s62, s34, 2
	v_lshl_add_u64 v[100:101], v[100:101], 0, s[62:63]
	s_waitcnt lgkmcnt(0)
	v_add_f32_e32 v98, v98, v99
	global_store_dword v[100:101], v98, off
.LBB0_559:
	s_or_b64 exec, exec, s[0:1]
	v_or_b32_e32 v108, 32, v150
	v_ashrrev_i32_e32 v109, 31, v108
	v_lshlrev_b64 v[118:119], 11, v[108:109]
	s_waitcnt lgkmcnt(0)
	v_lshl_add_u64 v[98:99], v[152:153], 0, v[118:119]
	global_load_dwordx4 v[110:113], v[98:99], off
	global_load_dwordx4 v[114:117], v[98:99], off offset:256
	v_or_b32_e32 v106, 48, v150
	v_ashrrev_i32_e32 v107, 31, v106
	v_lshlrev_b64 v[98:99], 11, v[106:107]
	v_lshl_add_u64 v[98:99], v[152:153], 0, v[98:99]
	global_load_dwordx4 v[102:105], v[98:99], off
	s_nop 0
	global_load_dwordx4 v[98:101], v[98:99], off offset:256
	s_waitcnt vmcnt(0) lgkmcnt(0)
	v_cvt_f32_f16_e32 v120, v110
	v_cvt_f32_f16_sdwa v121, v110 dst_sel:DWORD dst_unused:UNUSED_PAD src0_sel:WORD_1
	v_cvt_f32_f16_e32 v110, v111
	v_cvt_f32_f16_sdwa v111, v111 dst_sel:DWORD dst_unused:UNUSED_PAD src0_sel:WORD_1
	v_pk_add_f32 v[120:121], v[94:95], v[120:121]
	s_nop 0
	v_cvt_pk_f16_f32 v94, v120, v121
	v_pk_add_f32 v[110:111], v[96:97], v[110:111]
	v_cvt_f32_f16_e32 v96, v112
	v_cvt_f32_f16_sdwa v97, v112 dst_sel:DWORD dst_unused:UNUSED_PAD src0_sel:WORD_1
	v_cvt_f32_f16_e32 v112, v113
	v_cvt_f32_f16_sdwa v113, v113 dst_sel:DWORD dst_unused:UNUSED_PAD src0_sel:WORD_1
	v_cvt_pk_f16_f32 v95, v110, v111
	v_pk_add_f32 v[90:91], v[90:91], v[96:97]
	v_pk_add_f32 v[92:93], v[92:93], v[112:113]
	v_lshl_add_u64 v[112:113], s[72:73], 0, v[118:119]
	v_cvt_pk_f16_f32 v96, v90, v91
	v_cvt_pk_f16_f32 v97, v92, v93
	v_lshl_add_u64 v[112:113], v[148:149], 1, v[112:113]
	global_store_dwordx4 v[112:113], v[94:97], off
	v_pk_mul_f32 v[90:91], v[90:91], v[90:91]
	v_pk_mul_f32 v[92:93], v[92:93], v[92:93]
	v_pk_mul_f32 v[96:97], v[110:111], v[110:111]
	v_cvt_f32_f16_e32 v110, v114
	v_cvt_f32_f16_sdwa v111, v114 dst_sel:DWORD dst_unused:UNUSED_PAD src0_sel:WORD_1
	v_cvt_f32_f16_e32 v114, v115
	v_cvt_f32_f16_sdwa v115, v115 dst_sel:DWORD dst_unused:UNUSED_PAD src0_sel:WORD_1
	v_pk_mul_f32 v[94:95], v[120:121], v[120:121]
	v_pk_add_f32 v[110:111], v[86:87], v[110:111]
	v_pk_add_f32 v[114:115], v[88:89], v[114:115]
	v_cvt_f32_f16_e32 v88, v116
	v_cvt_f32_f16_sdwa v89, v116 dst_sel:DWORD dst_unused:UNUSED_PAD src0_sel:WORD_1
	v_cvt_f32_f16_e32 v116, v117
	v_cvt_f32_f16_sdwa v117, v117 dst_sel:DWORD dst_unused:UNUSED_PAD src0_sel:WORD_1
	v_cvt_pk_f16_f32 v86, v110, v111
	v_pk_add_f32 v[82:83], v[82:83], v[88:89]
	v_cvt_pk_f16_f32 v87, v114, v115
	v_pk_add_f32 v[84:85], v[84:85], v[116:117]
	v_cvt_pk_f16_f32 v88, v82, v83
	v_cvt_pk_f16_f32 v89, v84, v85
	v_pk_mul_f32 v[82:83], v[82:83], v[82:83]
	v_pk_mul_f32 v[84:85], v[84:85], v[84:85]
	global_store_dwordx4 v[112:113], v[86:89], off offset:256
	v_add_f32_e32 v84, v84, v85
	v_add_f32_e32 v82, v82, v83
	v_pk_mul_f32 v[86:87], v[110:111], v[110:111]
	v_pk_mul_f32 v[88:89], v[114:115], v[114:115]
	v_add_f32_e32 v82, v82, v84
	v_add_f32_e32 v83, v88, v89
	v_add_f32_e32 v84, v86, v87
	v_add_f32_e32 v83, v84, v83
	v_add_f32_e32 v82, v83, v82
	v_add_f32_e32 v83, v92, v93
	v_add_f32_e32 v84, v90, v91
	v_add_f32_e32 v83, v84, v83
	v_add_f32_e32 v84, v96, v97
	v_add_f32_e32 v85, v94, v95
	v_add_f32_e32 v84, v85, v84
	v_add_f32_e32 v83, v84, v83
	v_add_f32_e32 v82, v83, v82
	ds_bpermute_b32 v83, v159, v82
	s_waitcnt lgkmcnt(0)
	v_add_f32_e32 v82, v82, v83
	ds_bpermute_b32 v83, v158, v82
	s_and_saveexec_b64 s[0:1], vcc
	s_cbranch_execz .LBB0_561
	v_lshlrev_b64 v[84:85], 6, v[108:109]
	v_lshl_add_u64 v[84:85], s[6:7], 0, v[84:85]
	s_lshl_b32 s62, s11, 2
	v_lshl_add_u64 v[84:85], v[84:85], 0, s[62:63]
	s_lshl_b32 s62, s34, 2
	v_lshl_add_u64 v[84:85], v[84:85], 0, s[62:63]
	s_waitcnt lgkmcnt(0)
	v_add_f32_e32 v82, v82, v83
	global_store_dword v[84:85], v82, off
; __device__ __forceinline__ float xor_add(float v, int lane, int o) { return v + __builtin_bit_cast(float, __builtin_amdgcn_ds_bpermute((lane ^ o) << 2, __builtin_bit_cast(int, v))); }
; __device__ __forceinline__ float f16_lo(unsigned u) { return (float)__builtin_bit_cast(h16x2, u)[0]; }
; __device__ __forceinline__ float f16_hi(unsigned u) { return (float)__builtin_bit_cast(h16x2, u)[1]; }
;     __device__ __forceinline__ void operator()(const f32x4 (&acc)[2][2][4][2], const Unit& u, int wr, int wc, int fr, int fq) const {
;     ...
;                     for (int bj = 0; bj < 2; ++bj) bsv[mm][bj] = *(const u32x4*)(base + (size_t)(row0 + ai * HALF + (2 * mp + mm) * 16) * ldc + col0 + bj * HALF);
; #pragma unroll
;                 for (int mm = 0; mm < 2; ++mm) { const int m = 2 * mp + mm; const size_t r = (size_t)(row0 + ai * HALF + m * 16), off = r * ldc + col0; float ss = 0.f;
; #pragma unroll
;                     for (int bj = 0; bj < 2; ++bj) { const u32x4 b = bsv[mm][bj]; const f32x4 a0 = acc[ai][bj][m][0] * sc, a1 = acc[ai][bj][m][1] * sc;
;                         f32x4 v0, v1; v0[0] = f16_lo(b.x) + a0[0]; v0[1] = f16_hi(b.x) + a0[1]; v0[2] = f16_lo(b.y) + a0[2]; v0[3] = f16_hi(b.y) + a0[3];
;                         v1[0] = f16_lo(b.z) + a1[0]; v1[1] = f16_hi(b.z) + a1[1]; v1[2] = f16_lo(b.w) + a1[2]; v1[3] = f16_hi(b.w) + a1[3];
;                         u32x4 w; w.x = pk_f16(v0[0], v0[1]); w.y = pk_f16(v0[2], v0[3]); w.z = pk_f16(v1[0], v1[1]); w.w = pk_f16(v1[2], v1[3]); *(u32x4*)(out + off + bj * HALF) = w;
;                         ss += ((v0[0] * v0[0] + v0[1] * v0[1]) + (v0[2] * v0[2] + v0[3] * v0[3])) + ((v1[0] * v1[0] + v1[1] * v1[1]) + (v1[2] * v1[2] + v1[3] * v1[3])); }
;                     ss = xor_add(ss, lane, 16); ss = xor_add(ss, lane, 32);
;                     if (fq == 0) ssp[r * 16 + (u.pn & 3) * 4 + wc] = ss; }
.LBB0_561:
	s_or_b64 exec, exec, s[0:1]
	v_cvt_f32_f16_sdwa v87, v103 dst_sel:DWORD dst_unused:UNUSED_PAD src0_sel:WORD_1
	v_cvt_f32_f16_e32 v86, v103
	v_cvt_f32_f16_sdwa v85, v102 dst_sel:DWORD dst_unused:UNUSED_PAD src0_sel:WORD_1
	v_cvt_f32_f16_e32 v84, v102
	v_cvt_f32_f16_sdwa v89, v105 dst_sel:DWORD dst_unused:UNUSED_PAD src0_sel:WORD_1
	v_pk_add_f32 v[86:87], v[78:79], v[86:87]
	v_cvt_f32_f16_sdwa v79, v104 dst_sel:DWORD dst_unused:UNUSED_PAD src0_sel:WORD_1
	v_cvt_f32_f16_e32 v78, v104
	v_cvt_f32_f16_e32 v88, v105
	s_waitcnt lgkmcnt(0)
	v_lshlrev_b64 v[82:83], 10, v[106:107]
	v_pk_add_f32 v[84:85], v[76:77], v[84:85]
	v_pk_add_f32 v[72:73], v[72:73], v[78:79]
	v_pk_add_f32 v[74:75], v[74:75], v[88:89]
	v_lshl_add_u64 v[82:83], v[82:83], 1, s[72:73]
	v_cvt_pk_f16_f32 v76, v84, v85
	v_cvt_pk_f16_f32 v77, v86, v87
	v_cvt_pk_f16_f32 v78, v72, v73
	v_cvt_pk_f16_f32 v79, v74, v75
	v_lshl_add_u64 v[82:83], v[148:149], 1, v[82:83]
	global_store_dwordx4 v[82:83], v[76:79], off
	v_cvt_f32_f16_sdwa v89, v101 dst_sel:DWORD dst_unused:UNUSED_PAD src0_sel:WORD_1
	v_cvt_f32_f16_e32 v88, v101
	v_pk_mul_f32 v[78:79], v[86:87], v[86:87]
	v_cvt_f32_f16_sdwa v87, v99 dst_sel:DWORD dst_unused:UNUSED_PAD src0_sel:WORD_1
	v_cvt_f32_f16_e32 v86, v99
	v_pk_mul_f32 v[76:77], v[84:85], v[84:85]
	v_cvt_f32_f16_sdwa v85, v98 dst_sel:DWORD dst_unused:UNUSED_PAD src0_sel:WORD_1
	v_cvt_f32_f16_e32 v84, v98
	v_pk_add_f32 v[86:87], v[70:71], v[86:87]
	v_cvt_f32_f16_sdwa v71, v100 dst_sel:DWORD dst_unused:UNUSED_PAD src0_sel:WORD_1
	v_cvt_f32_f16_e32 v70, v100
	v_pk_add_f32 v[84:85], v[68:69], v[84:85]
	v_pk_add_f32 v[66:67], v[66:67], v[88:89]
	v_cvt_pk_f16_f32 v68, v84, v85
	v_pk_add_f32 v[64:65], v[64:65], v[70:71]
	v_cvt_pk_f16_f32 v69, v86, v87
	v_cvt_pk_f16_f32 v70, v64, v65
	v_cvt_pk_f16_f32 v71, v66, v67
	v_pk_mul_f32 v[64:65], v[64:65], v[64:65]
	v_pk_mul_f32 v[66:67], v[66:67], v[66:67]
	global_store_dwordx4 v[82:83], v[68:71], off offset:256
	v_add_f32_e32 v66, v66, v67
	v_add_f32_e32 v64, v64, v65
	v_pk_mul_f32 v[68:69], v[84:85], v[84:85]
	v_pk_mul_f32 v[70:71], v[86:87], v[86:87]
	v_add_f32_e32 v64, v64, v66
	v_add_f32_e32 v65, v70, v71
	v_add_f32_e32 v66, v68, v69
	v_pk_mul_f32 v[72:73], v[72:73], v[72:73]
	v_pk_mul_f32 v[74:75], v[74:75], v[74:75]
	v_add_f32_e32 v65, v66, v65
	v_add_f32_e32 v64, v65, v64
	v_add_f32_e32 v65, v74, v75
	v_add_f32_e32 v66, v72, v73
	v_add_f32_e32 v65, v66, v65
	v_add_f32_e32 v66, v78, v79
	v_add_f32_e32 v67, v76, v77
	v_add_f32_e32 v66, v67, v66
	v_add_f32_e32 v65, v66, v65
	v_add_f32_e32 v64, v65, v64
	ds_bpermute_b32 v65, v159, v64
	s_waitcnt lgkmcnt(0)
	v_add_f32_e32 v64, v64, v65
	ds_bpermute_b32 v65, v158, v64
	s_and_saveexec_b64 s[0:1], vcc
	s_cbranch_execz .LBB0_563
	v_lshlrev_b64 v[66:67], 6, v[106:107]
	v_lshl_add_u64 v[66:67], s[6:7], 0, v[66:67]
	s_lshl_b32 s62, s11, 2
	v_lshl_add_u64 v[66:67], v[66:67], 0, s[62:63]
	s_lshl_b32 s62, s34, 2
	v_lshl_add_u64 v[66:67], v[66:67], 0, s[62:63]
	s_waitcnt lgkmcnt(0)
	v_add_f32_e32 v64, v64, v65
	global_store_dword v[66:67], v64, off
.LBB0_563:
	s_or_b64 exec, exec, s[0:1]
	v_add_u32_e32 v74, 0x80, v150
	v_ashrrev_i32_e32 v75, 31, v74
	v_lshlrev_b64 v[86:87], 11, v[74:75]
	s_waitcnt lgkmcnt(0)
	v_lshl_add_u64 v[64:65], v[152:153], 0, v[86:87]
	global_load_dwordx4 v[76:79], v[64:65], off
	global_load_dwordx4 v[82:85], v[64:65], off offset:256
	v_add_u32_e32 v72, 0x90, v150
	v_ashrrev_i32_e32 v73, 31, v72
	v_lshlrev_b64 v[64:65], 11, v[72:73]
	v_lshl_add_u64 v[64:65], v[152:153], 0, v[64:65]
	global_load_dwordx4 v[68:71], v[64:65], off
	s_nop 0
	global_load_dwordx4 v[64:67], v[64:65], off offset:256
	s_waitcnt vmcnt(0) lgkmcnt(0)
	v_cvt_f32_f16_e32 v88, v76
	v_cvt_f32_f16_sdwa v89, v76 dst_sel:DWORD dst_unused:UNUSED_PAD src0_sel:WORD_1
	v_cvt_f32_f16_e32 v76, v77
	v_cvt_f32_f16_sdwa v77, v77 dst_sel:DWORD dst_unused:UNUSED_PAD src0_sel:WORD_1
	v_pk_add_f32 v[88:89], v[60:61], v[88:89]
	s_nop 0
	v_cvt_pk_f16_f32 v60, v88, v89
	v_pk_add_f32 v[76:77], v[62:63], v[76:77]
	v_cvt_f32_f16_e32 v62, v78
	v_cvt_f32_f16_sdwa v63, v78 dst_sel:DWORD dst_unused:UNUSED_PAD src0_sel:WORD_1
	v_cvt_f32_f16_e32 v78, v79
	v_cvt_f32_f16_sdwa v79, v79 dst_sel:DWORD dst_unused:UNUSED_PAD src0_sel:WORD_1
	v_cvt_pk_f16_f32 v61, v76, v77
	v_pk_add_f32 v[56:57], v[56:57], v[62:63]
	v_pk_add_f32 v[58:59], v[58:59], v[78:79]
	v_lshl_add_u64 v[78:79], s[72:73], 0, v[86:87]
	v_cvt_pk_f16_f32 v62, v56, v57
	v_cvt_pk_f16_f32 v63, v58, v59
	v_lshl_add_u64 v[78:79], v[148:149], 1, v[78:79]
	global_store_dwordx4 v[78:79], v[60:63], off
	v_pk_mul_f32 v[56:57], v[56:57], v[56:57]
	v_pk_mul_f32 v[58:59], v[58:59], v[58:59]
	v_pk_mul_f32 v[62:63], v[76:77], v[76:77]
	v_cvt_f32_f16_e32 v76, v82
	v_cvt_f32_f16_sdwa v77, v82 dst_sel:DWORD dst_unused:UNUSED_PAD src0_sel:WORD_1
	v_cvt_f32_f16_e32 v82, v83
	v_cvt_f32_f16_sdwa v83, v83 dst_sel:DWORD dst_unused:UNUSED_PAD src0_sel:WORD_1
	v_pk_mul_f32 v[60:61], v[88:89], v[88:89]
	v_pk_add_f32 v[76:77], v[52:53], v[76:77]
	v_pk_add_f32 v[82:83], v[54:55], v[82:83]
	v_cvt_f32_f16_e32 v54, v84
	v_cvt_f32_f16_sdwa v55, v84 dst_sel:DWORD dst_unused:UNUSED_PAD src0_sel:WORD_1
	v_cvt_f32_f16_e32 v84, v85
	v_cvt_f32_f16_sdwa v85, v85 dst_sel:DWORD dst_unused:UNUSED_PAD src0_sel:WORD_1
	v_cvt_pk_f16_f32 v52, v76, v77
	v_pk_add_f32 v[48:49], v[48:49], v[54:55]
	v_cvt_pk_f16_f32 v53, v82, v83
	v_pk_add_f32 v[50:51], v[50:51], v[84:85]
	v_cvt_pk_f16_f32 v54, v48, v49
	v_cvt_pk_f16_f32 v55, v50, v51
	v_pk_mul_f32 v[48:49], v[48:49], v[48:49]
	v_pk_mul_f32 v[50:51], v[50:51], v[50:51]
	global_store_dwordx4 v[78:79], v[52:55], off offset:256
	v_add_f32_e32 v50, v50, v51
	v_add_f32_e32 v48, v48, v49
	v_pk_mul_f32 v[52:53], v[76:77], v[76:77]
	v_pk_mul_f32 v[54:55], v[82:83], v[82:83]
	v_add_f32_e32 v48, v48, v50
	v_add_f32_e32 v49, v54, v55
	v_add_f32_e32 v50, v52, v53
	v_add_f32_e32 v49, v50, v49
	v_add_f32_e32 v48, v49, v48
	v_add_f32_e32 v49, v58, v59
	v_add_f32_e32 v50, v56, v57
	v_add_f32_e32 v49, v50, v49
	v_add_f32_e32 v50, v62, v63
	v_add_f32_e32 v51, v60, v61
	v_add_f32_e32 v50, v51, v50
	v_add_f32_e32 v49, v50, v49
	v_add_f32_e32 v48, v49, v48
	ds_bpermute_b32 v49, v159, v48
	s_waitcnt lgkmcnt(0)
	v_add_f32_e32 v48, v48, v49
	ds_bpermute_b32 v49, v158, v48
	s_and_saveexec_b64 s[0:1], vcc
	s_cbranch_execz .LBB0_565
	v_lshlrev_b64 v[50:51], 6, v[74:75]
	v_lshl_add_u64 v[50:51], s[6:7], 0, v[50:51]
	s_lshl_b32 s62, s11, 2
	v_lshl_add_u64 v[50:51], v[50:51], 0, s[62:63]
	s_lshl_b32 s62, s34, 2
	v_lshl_add_u64 v[50:51], v[50:51], 0, s[62:63]
	s_waitcnt lgkmcnt(0)
	v_add_f32_e32 v48, v48, v49
	global_store_dword v[50:51], v48, off
; __device__ __forceinline__ float xor_add(float v, int lane, int o) { return v + __builtin_bit_cast(float, __builtin_amdgcn_ds_bpermute((lane ^ o) << 2, __builtin_bit_cast(int, v))); }
; __device__ __forceinline__ float f16_lo(unsigned u) { return (float)__builtin_bit_cast(h16x2, u)[0]; }
; __device__ __forceinline__ float f16_hi(unsigned u) { return (float)__builtin_bit_cast(h16x2, u)[1]; }
;     __device__ __forceinline__ void operator()(const f32x4 (&acc)[2][2][4][2], const Unit& u, int wr, int wc, int fr, int fq) const {
;     ...
;                     for (int bj = 0; bj < 2; ++bj) bsv[mm][bj] = *(const u32x4*)(base + (size_t)(row0 + ai * HALF + (2 * mp + mm) * 16) * ldc + col0 + bj * HALF);
; #pragma unroll
;                 for (int mm = 0; mm < 2; ++mm) { const int m = 2 * mp + mm; const size_t r = (size_t)(row0 + ai * HALF + m * 16), off = r * ldc + col0; float ss = 0.f;
; #pragma unroll
;                     for (int bj = 0; bj < 2; ++bj) { const u32x4 b = bsv[mm][bj]; const f32x4 a0 = acc[ai][bj][m][0] * sc, a1 = acc[ai][bj][m][1] * sc;
;                         f32x4 v0, v1; v0[0] = f16_lo(b.x) + a0[0]; v0[1] = f16_hi(b.x) + a0[1]; v0[2] = f16_lo(b.y) + a0[2]; v0[3] = f16_hi(b.y) + a0[3];
;                         v1[0] = f16_lo(b.z) + a1[0]; v1[1] = f16_hi(b.z) + a1[1]; v1[2] = f16_lo(b.w) + a1[2]; v1[3] = f16_hi(b.w) + a1[3];
;                         u32x4 w; w.x = pk_f16(v0[0], v0[1]); w.y = pk_f16(v0[2], v0[3]); w.z = pk_f16(v1[0], v1[1]); w.w = pk_f16(v1[2], v1[3]); *(u32x4*)(out + off + bj * HALF) = w;
;                         ss += ((v0[0] * v0[0] + v0[1] * v0[1]) + (v0[2] * v0[2] + v0[3] * v0[3])) + ((v1[0] * v1[0] + v1[1] * v1[1]) + (v1[2] * v1[2] + v1[3] * v1[3])); }
;                     ss = xor_add(ss, lane, 16); ss = xor_add(ss, lane, 32);
;                     if (fq == 0) ssp[r * 16 + (u.pn & 3) * 4 + wc] = ss; }
.LBB0_565:
	s_or_b64 exec, exec, s[0:1]
	v_cvt_f32_f16_sdwa v53, v69 dst_sel:DWORD dst_unused:UNUSED_PAD src0_sel:WORD_1
	v_cvt_f32_f16_e32 v52, v69
	v_cvt_f32_f16_sdwa v51, v68 dst_sel:DWORD dst_unused:UNUSED_PAD src0_sel:WORD_1
	v_cvt_f32_f16_e32 v50, v68
	v_cvt_f32_f16_sdwa v55, v71 dst_sel:DWORD dst_unused:UNUSED_PAD src0_sel:WORD_1
	v_pk_add_f32 v[52:53], v[46:47], v[52:53]
	v_cvt_f32_f16_sdwa v47, v70 dst_sel:DWORD dst_unused:UNUSED_PAD src0_sel:WORD_1
	v_cvt_f32_f16_e32 v46, v70
	v_cvt_f32_f16_e32 v54, v71
	s_waitcnt lgkmcnt(0)
	v_lshlrev_b64 v[48:49], 10, v[72:73]
	v_pk_add_f32 v[50:51], v[44:45], v[50:51]
	v_pk_add_f32 v[40:41], v[40:41], v[46:47]
	v_pk_add_f32 v[42:43], v[42:43], v[54:55]
	v_lshl_add_u64 v[48:49], v[48:49], 1, s[72:73]
	v_cvt_pk_f16_f32 v44, v50, v51
	v_cvt_pk_f16_f32 v45, v52, v53
	v_cvt_pk_f16_f32 v46, v40, v41
	v_cvt_pk_f16_f32 v47, v42, v43
	v_lshl_add_u64 v[48:49], v[148:149], 1, v[48:49]
	global_store_dwordx4 v[48:49], v[44:47], off
	v_cvt_f32_f16_sdwa v55, v67 dst_sel:DWORD dst_unused:UNUSED_PAD src0_sel:WORD_1
	v_cvt_f32_f16_e32 v54, v67
	v_pk_mul_f32 v[46:47], v[52:53], v[52:53]
	v_cvt_f32_f16_sdwa v53, v65 dst_sel:DWORD dst_unused:UNUSED_PAD src0_sel:WORD_1
	v_cvt_f32_f16_e32 v52, v65
	v_pk_mul_f32 v[44:45], v[50:51], v[50:51]
	v_cvt_f32_f16_sdwa v51, v64 dst_sel:DWORD dst_unused:UNUSED_PAD src0_sel:WORD_1
	v_cvt_f32_f16_e32 v50, v64
	v_pk_add_f32 v[52:53], v[38:39], v[52:53]
	v_cvt_f32_f16_sdwa v39, v66 dst_sel:DWORD dst_unused:UNUSED_PAD src0_sel:WORD_1
	v_cvt_f32_f16_e32 v38, v66
	v_pk_add_f32 v[50:51], v[36:37], v[50:51]
	v_pk_add_f32 v[34:35], v[34:35], v[54:55]
	v_cvt_pk_f16_f32 v36, v50, v51
	v_pk_add_f32 v[32:33], v[32:33], v[38:39]
	v_cvt_pk_f16_f32 v37, v52, v53
	v_cvt_pk_f16_f32 v38, v32, v33
	v_cvt_pk_f16_f32 v39, v34, v35
	v_pk_mul_f32 v[32:33], v[32:33], v[32:33]
	v_pk_mul_f32 v[34:35], v[34:35], v[34:35]
	global_store_dwordx4 v[48:49], v[36:39], off offset:256
	v_add_f32_e32 v34, v34, v35
	v_add_f32_e32 v32, v32, v33
	v_pk_mul_f32 v[36:37], v[50:51], v[50:51]
	v_pk_mul_f32 v[38:39], v[52:53], v[52:53]
	v_add_f32_e32 v32, v32, v34
	v_add_f32_e32 v33, v38, v39
	v_add_f32_e32 v34, v36, v37
	v_pk_mul_f32 v[40:41], v[40:41], v[40:41]
	v_pk_mul_f32 v[42:43], v[42:43], v[42:43]
	v_add_f32_e32 v33, v34, v33
	v_add_f32_e32 v32, v33, v32
	v_add_f32_e32 v33, v42, v43
	v_add_f32_e32 v34, v40, v41
	v_add_f32_e32 v33, v34, v33
	v_add_f32_e32 v34, v46, v47
	v_add_f32_e32 v35, v44, v45
	v_add_f32_e32 v34, v35, v34
	v_add_f32_e32 v33, v34, v33
	v_add_f32_e32 v32, v33, v32
	ds_bpermute_b32 v33, v159, v32
	s_waitcnt lgkmcnt(0)
	v_add_f32_e32 v32, v32, v33
	ds_bpermute_b32 v33, v158, v32
	s_and_saveexec_b64 s[0:1], vcc
	s_cbranch_execz .LBB0_567
	v_lshlrev_b64 v[34:35], 6, v[72:73]
	v_lshl_add_u64 v[34:35], s[6:7], 0, v[34:35]
	s_lshl_b32 s62, s11, 2
	v_lshl_add_u64 v[34:35], v[34:35], 0, s[62:63]
	s_lshl_b32 s62, s34, 2
	v_lshl_add_u64 v[34:35], v[34:35], 0, s[62:63]
	s_waitcnt lgkmcnt(0)
	v_add_f32_e32 v32, v32, v33
	global_store_dword v[34:35], v32, off
; __device__ __forceinline__ float xor_add(float v, int lane, int o) { return v + __builtin_bit_cast(float, __builtin_amdgcn_ds_bpermute((lane ^ o) << 2, __builtin_bit_cast(int, v))); }
; __device__ __forceinline__ float f16_lo(unsigned u) { return (float)__builtin_bit_cast(h16x2, u)[0]; }
; __device__ __forceinline__ float f16_hi(unsigned u) { return (float)__builtin_bit_cast(h16x2, u)[1]; }
;     __device__ __forceinline__ void operator()(const f32x4 (&acc)[2][2][4][2], const Unit& u, int wr, int wc, int fr, int fq) const {
;     ...
;                     for (int bj = 0; bj < 2; ++bj) bsv[mm][bj] = *(const u32x4*)(base + (size_t)(row0 + ai * HALF + (2 * mp + mm) * 16) * ldc + col0 + bj * HALF);
; #pragma unroll
;                 for (int mm = 0; mm < 2; ++mm) { const int m = 2 * mp + mm; const size_t r = (size_t)(row0 + ai * HALF + m * 16), off = r * ldc + col0; float ss = 0.f;
; #pragma unroll
;                     for (int bj = 0; bj < 2; ++bj) { const u32x4 b = bsv[mm][bj]; const f32x4 a0 = acc[ai][bj][m][0] * sc, a1 = acc[ai][bj][m][1] * sc;
;                         f32x4 v0, v1; v0[0] = f16_lo(b.x) + a0[0]; v0[1] = f16_hi(b.x) + a0[1]; v0[2] = f16_lo(b.y) + a0[2]; v0[3] = f16_hi(b.y) + a0[3];
;                         v1[0] = f16_lo(b.z) + a1[0]; v1[1] = f16_hi(b.z) + a1[1]; v1[2] = f16_lo(b.w) + a1[2]; v1[3] = f16_hi(b.w) + a1[3];
;                         u32x4 w; w.x = pk_f16(v0[0], v0[1]); w.y = pk_f16(v0[2], v0[3]); w.z = pk_f16(v1[0], v1[1]); w.w = pk_f16(v1[2], v1[3]); *(u32x4*)(out + off + bj * HALF) = w;
;                         ss += ((v0[0] * v0[0] + v0[1] * v0[1]) + (v0[2] * v0[2] + v0[3] * v0[3])) + ((v1[0] * v1[0] + v1[1] * v1[1]) + (v1[2] * v1[2] + v1[3] * v1[3])); }
;                     ss = xor_add(ss, lane, 16); ss = xor_add(ss, lane, 32);
;                     if (fq == 0) ssp[r * 16 + (u.pn & 3) * 4 + wc] = ss; }
.LBB0_567:
	s_or_b64 exec, exec, s[0:1]
	v_add_u32_e32 v42, 0xa0, v150
	v_ashrrev_i32_e32 v43, 31, v42
	v_lshlrev_b64 v[52:53], 11, v[42:43]
	s_waitcnt lgkmcnt(0)
	v_lshl_add_u64 v[32:33], v[152:153], 0, v[52:53]
	global_load_dwordx4 v[44:47], v[32:33], off
	global_load_dwordx4 v[48:51], v[32:33], off offset:256
	v_add_u32_e32 v40, 0xb0, v150
	v_ashrrev_i32_e32 v41, 31, v40
	v_lshlrev_b64 v[32:33], 11, v[40:41]
	v_lshl_add_u64 v[32:33], v[152:153], 0, v[32:33]
	global_load_dwordx4 v[36:39], v[32:33], off
	s_nop 0
	global_load_dwordx4 v[32:35], v[32:33], off offset:256
	s_waitcnt vmcnt(0) lgkmcnt(0)
	v_cvt_f32_f16_e32 v54, v44
	v_cvt_f32_f16_sdwa v55, v44 dst_sel:DWORD dst_unused:UNUSED_PAD src0_sel:WORD_1
	v_cvt_f32_f16_e32 v44, v45
	v_cvt_f32_f16_sdwa v45, v45 dst_sel:DWORD dst_unused:UNUSED_PAD src0_sel:WORD_1
	v_pk_add_f32 v[54:55], v[28:29], v[54:55]
	s_nop 0
	v_cvt_pk_f16_f32 v28, v54, v55
	v_pk_add_f32 v[44:45], v[30:31], v[44:45]
	v_cvt_f32_f16_e32 v30, v46
	v_cvt_f32_f16_sdwa v31, v46 dst_sel:DWORD dst_unused:UNUSED_PAD src0_sel:WORD_1
	v_cvt_f32_f16_e32 v46, v47
	v_cvt_f32_f16_sdwa v47, v47 dst_sel:DWORD dst_unused:UNUSED_PAD src0_sel:WORD_1
	v_cvt_pk_f16_f32 v29, v44, v45
	v_pk_add_f32 v[24:25], v[24:25], v[30:31]
	v_pk_add_f32 v[26:27], v[26:27], v[46:47]
	v_lshl_add_u64 v[46:47], s[72:73], 0, v[52:53]
	v_cvt_pk_f16_f32 v30, v24, v25
	v_cvt_pk_f16_f32 v31, v26, v27
	v_lshl_add_u64 v[46:47], v[148:149], 1, v[46:47]
	global_store_dwordx4 v[46:47], v[28:31], off
	v_pk_mul_f32 v[24:25], v[24:25], v[24:25]
	v_pk_mul_f32 v[26:27], v[26:27], v[26:27]
	v_pk_mul_f32 v[30:31], v[44:45], v[44:45]
	v_cvt_f32_f16_e32 v44, v48
	v_cvt_f32_f16_sdwa v45, v48 dst_sel:DWORD dst_unused:UNUSED_PAD src0_sel:WORD_1
	v_cvt_f32_f16_e32 v48, v49
	v_cvt_f32_f16_sdwa v49, v49 dst_sel:DWORD dst_unused:UNUSED_PAD src0_sel:WORD_1
	v_pk_mul_f32 v[28:29], v[54:55], v[54:55]
	v_pk_add_f32 v[44:45], v[20:21], v[44:45]
	v_pk_add_f32 v[48:49], v[22:23], v[48:49]
	v_cvt_f32_f16_e32 v22, v50
	v_cvt_f32_f16_sdwa v23, v50 dst_sel:DWORD dst_unused:UNUSED_PAD src0_sel:WORD_1
	v_cvt_f32_f16_e32 v50, v51
	v_cvt_f32_f16_sdwa v51, v51 dst_sel:DWORD dst_unused:UNUSED_PAD src0_sel:WORD_1
	v_cvt_pk_f16_f32 v20, v44, v45
	v_pk_add_f32 v[16:17], v[16:17], v[22:23]
	v_cvt_pk_f16_f32 v21, v48, v49
	v_pk_add_f32 v[18:19], v[18:19], v[50:51]
	v_cvt_pk_f16_f32 v22, v16, v17
	v_cvt_pk_f16_f32 v23, v18, v19
	v_pk_mul_f32 v[16:17], v[16:17], v[16:17]
	v_pk_mul_f32 v[18:19], v[18:19], v[18:19]
	global_store_dwordx4 v[46:47], v[20:23], off offset:256
	v_add_f32_e32 v18, v18, v19
	v_add_f32_e32 v16, v16, v17
	v_pk_mul_f32 v[20:21], v[44:45], v[44:45]
	v_pk_mul_f32 v[22:23], v[48:49], v[48:49]
	v_add_f32_e32 v16, v16, v18
	v_add_f32_e32 v17, v22, v23
	v_add_f32_e32 v18, v20, v21
	v_add_f32_e32 v17, v18, v17
	v_add_f32_e32 v16, v17, v16
	v_add_f32_e32 v17, v26, v27
	v_add_f32_e32 v18, v24, v25
	v_add_f32_e32 v17, v18, v17
	v_add_f32_e32 v18, v30, v31
	v_add_f32_e32 v19, v28, v29
	v_add_f32_e32 v18, v19, v18
	v_add_f32_e32 v17, v18, v17
	v_add_f32_e32 v16, v17, v16
	ds_bpermute_b32 v17, v159, v16
	s_waitcnt lgkmcnt(0)
	v_add_f32_e32 v16, v16, v17
	ds_bpermute_b32 v17, v158, v16
	s_and_saveexec_b64 s[0:1], vcc
	s_cbranch_execz .LBB0_569
	v_lshlrev_b64 v[18:19], 6, v[42:43]
	v_lshl_add_u64 v[18:19], s[6:7], 0, v[18:19]
	s_lshl_b32 s62, s11, 2
	v_lshl_add_u64 v[18:19], v[18:19], 0, s[62:63]
	s_lshl_b32 s62, s34, 2
	v_lshl_add_u64 v[18:19], v[18:19], 0, s[62:63]
	s_waitcnt lgkmcnt(0)
	v_add_f32_e32 v16, v16, v17
	global_store_dword v[18:19], v16, off
.LBB0_569:
	s_or_b64 exec, exec, s[0:1]
	v_cvt_f32_f16_sdwa v21, v37 dst_sel:DWORD dst_unused:UNUSED_PAD src0_sel:WORD_1
	v_cvt_f32_f16_e32 v20, v37
	v_cvt_f32_f16_sdwa v19, v36 dst_sel:DWORD dst_unused:UNUSED_PAD src0_sel:WORD_1
	v_cvt_f32_f16_e32 v18, v36
	v_cvt_f32_f16_sdwa v23, v39 dst_sel:DWORD dst_unused:UNUSED_PAD src0_sel:WORD_1
	v_pk_add_f32 v[20:21], v[14:15], v[20:21]
	v_cvt_f32_f16_sdwa v15, v38 dst_sel:DWORD dst_unused:UNUSED_PAD src0_sel:WORD_1
	v_cvt_f32_f16_e32 v14, v38
	v_cvt_f32_f16_e32 v22, v39
	s_waitcnt lgkmcnt(0)
	v_lshlrev_b64 v[16:17], 10, v[40:41]
	v_pk_add_f32 v[18:19], v[12:13], v[18:19]
	v_pk_add_f32 v[8:9], v[8:9], v[14:15]
	v_pk_add_f32 v[10:11], v[10:11], v[22:23]
	v_lshl_add_u64 v[16:17], v[16:17], 1, s[72:73]
	v_cvt_pk_f16_f32 v12, v18, v19
	v_cvt_pk_f16_f32 v13, v20, v21
	v_cvt_pk_f16_f32 v14, v8, v9
	v_cvt_pk_f16_f32 v15, v10, v11
	v_lshl_add_u64 v[16:17], v[148:149], 1, v[16:17]
	global_store_dwordx4 v[16:17], v[12:15], off
	v_cvt_f32_f16_sdwa v23, v35 dst_sel:DWORD dst_unused:UNUSED_PAD src0_sel:WORD_1
	v_cvt_f32_f16_e32 v22, v35
	v_pk_mul_f32 v[14:15], v[20:21], v[20:21]
	v_cvt_f32_f16_sdwa v21, v33 dst_sel:DWORD dst_unused:UNUSED_PAD src0_sel:WORD_1
	v_cvt_f32_f16_e32 v20, v33
	v_pk_mul_f32 v[12:13], v[18:19], v[18:19]
	v_cvt_f32_f16_sdwa v19, v32 dst_sel:DWORD dst_unused:UNUSED_PAD src0_sel:WORD_1
	v_cvt_f32_f16_e32 v18, v32
	v_pk_add_f32 v[20:21], v[6:7], v[20:21]
	v_cvt_f32_f16_sdwa v7, v34 dst_sel:DWORD dst_unused:UNUSED_PAD src0_sel:WORD_1
	v_cvt_f32_f16_e32 v6, v34
	v_pk_add_f32 v[18:19], v[4:5], v[18:19]
	v_pk_add_f32 v[2:3], v[2:3], v[22:23]
	v_cvt_pk_f16_f32 v4, v18, v19
	v_pk_add_f32 v[0:1], v[0:1], v[6:7]
	v_cvt_pk_f16_f32 v5, v20, v21
	v_cvt_pk_f16_f32 v6, v0, v1
	v_cvt_pk_f16_f32 v7, v2, v3
	v_pk_mul_f32 v[0:1], v[0:1], v[0:1]
	v_pk_mul_f32 v[2:3], v[2:3], v[2:3]
	global_store_dwordx4 v[16:17], v[4:7], off offset:256
	v_add_f32_e32 v2, v2, v3
	v_add_f32_e32 v0, v0, v1
	v_pk_mul_f32 v[4:5], v[18:19], v[18:19]
	v_pk_mul_f32 v[6:7], v[20:21], v[20:21]
	v_add_f32_e32 v0, v0, v2
	v_add_f32_e32 v1, v6, v7
	v_add_f32_e32 v2, v4, v5
	v_pk_mul_f32 v[8:9], v[8:9], v[8:9]
	v_pk_mul_f32 v[10:11], v[10:11], v[10:11]
	v_add_f32_e32 v1, v2, v1
	v_add_f32_e32 v0, v1, v0
	v_add_f32_e32 v1, v10, v11
	v_add_f32_e32 v2, v8, v9
	v_add_f32_e32 v1, v2, v1
	v_add_f32_e32 v2, v14, v15
	v_add_f32_e32 v3, v12, v13
	v_add_f32_e32 v2, v3, v2
	v_add_f32_e32 v1, v2, v1
	v_add_f32_e32 v0, v1, v0
	ds_bpermute_b32 v1, v159, v0
	s_waitcnt lgkmcnt(0)
	v_add_f32_e32 v0, v0, v1
	ds_bpermute_b32 v1, v158, v0
	s_and_saveexec_b64 s[0:1], vcc
	s_cbranch_execz .LBB0_571
	v_lshlrev_b64 v[2:3], 6, v[40:41]
	v_lshl_add_u64 v[2:3], s[6:7], 0, v[2:3]
	s_lshl_b32 s62, s11, 2
	v_lshl_add_u64 v[2:3], v[2:3], 0, s[62:63]
	s_lshl_b32 s62, s34, 2
	v_lshl_add_u64 v[2:3], v[2:3], 0, s[62:63]
	s_waitcnt lgkmcnt(0)
	v_add_f32_e32 v0, v0, v1
	global_store_dword v[2:3], v0, off

; __device__ __forceinline__ int ld_agent_i(const int* p) { return (int)__hip_atomic_load((const unsigned*)p, RLX_AGENT); }
; __global__ void __launch_bounds__(NWAVES * 64, 2) mk_fwd(Args args) {
;     ...
;                 const int nu = __builtin_amdgcn_readfirstlane(ld_agent_i((const int*)(ws + WS_TBL + T_NUN)));
;                 pg8::Gemm g{(const bf16*)(ws + WS_AG), (const bf16*)(ws + W_13M + (size_t)(l >> 1) * NE * 2 * FE * D), MOE_ROWS, NE * 2 * FE, D / 2};
;                 ULIST_FILL((const int*)(ws + WS_TBL + T_LISTU), nu);
.LBB0_900:
	s_andn2_b64 vcc, exec, s[0:1]
	v_readlane_b32 s0, v255, 45
	v_readlane_b32 s1, v255, 46
	s_waitcnt vmcnt(0)
	s_nop 0
	v_cndmask_b32_e64 v0, 0, 1, s[0:1]
	v_cmp_ne_u32_e64 s[2:3], 1, v0
	s_cbranch_vccnz .LBB0_1027
	v_mov_b32_e32 v188, v81
	v_readlane_b32 s28, v254, 2
	s_and_b64 vcc, exec, s[2:3]
	s_mov_b64 s[0:1], -1
	s_cbranch_vccnz .LBB0_926
	v_mov_b32_e32 v0, s80
	v_add_co_u32_e32 v0, vcc, 0x28a000, v0
	s_waitcnt lgkmcnt(0)
	v_mov_b32_e32 v1, s81
	v_mov_b32_e32 v2, v81
	v_readlane_b32 s10, v254, 2
	v_addc_co_u32_e32 v1, vcc, 0, v1, vcc
	global_load_dword v0, v[0:1], off sc1
	v_mbcnt_lo_u32_b32 v1, -1, v2
	v_mbcnt_hi_u32_b32 v1, -1, v1
	v_readlane_b32 s0, v254, 25
	s_nop 1
	v_add_u32_e32 v8, s0, v1
	v_cmp_gt_i32_e32 vcc, 32, v8
	s_waitcnt vmcnt(0) lgkmcnt(0)
	v_readfirstlane_b32 s0, v0
	s_and_saveexec_b64 s[4:5], vcc
	s_cbranch_execz .LBB0_909
	s_ashr_i32 s1, s10, 31
	v_mov_b32_e32 v0, s10
	v_mov_b32_e32 v1, s1
	v_mad_i64_i32 v[0:1], s[6:7], v8, s59, v[0:1]
	s_ashr_i32 s1, s0, 31
	v_cmp_gt_i64_e32 vcc, s[0:1], v[0:1]
	s_and_b64 exec, exec, vcc
	s_cbranch_execz .LBB0_909
	v_ashrrev_i32_e32 v1, 31, v0
	s_lshr_b32 s1, s1, 29
	v_lshrrev_b32_e32 v1, 29, v1
	s_add_i32 s1, s0, s1
	v_add_u32_e32 v1, v0, v1
	s_ashr_i32 s8, s1, 3
	s_and_b32 s1, s1, -8
	v_and_b32_e32 v2, -8, v1
	s_sub_i32 s9, s0, s1
	v_sub_u32_e32 v2, v0, v2
	v_cmp_le_i32_e32 vcc, s9, v2
	s_add_i32 s1, s8, 1
	s_and_saveexec_b64 s[6:7], vcc
	s_xor_b64 s[6:7], exec, s[6:7]
	v_subrev_u32_e32 v0, s9, v2
	s_mul_i32 s11, s1, s9
	v_mul_lo_u32 v0, v0, s8
	v_add_u32_e32 v0, s11, v0
	s_andn2_saveexec_b64 s[6:7], s[6:7]
	v_mul_lo_u32 v0, v2, s1
	s_or_b64 exec, exec, s[6:7]
	v_ashrrev_i32_e32 v1, 3, v1
	v_add_lshl_u32 v0, v0, v1, 1
	v_ashrrev_i32_e32 v1, 31, v0
	v_lshl_add_u64 v[0:1], v[0:1], 2, s[80:81]
	v_add_co_u32_e32 v2, vcc, 0x280000, v0
	s_mov_b64 s[6:7], 0x280000
	s_nop 0
	v_addc_co_u32_e32 v3, vcc, 0, v1, vcc
	global_load_dword v2, v[2:3], off sc1
	v_lshl_add_u32 v3, v8, 3, 0
	v_add_u32_e32 v3, 0x21000, v3
	v_lshl_add_u64 v[0:1], v[0:1], 0, s[6:7]
	s_waitcnt vmcnt(0) lgkmcnt(0)
	ds_write_b32 v3, v2
	global_load_dword v0, v[0:1], off offset:4 sc1
	s_waitcnt vmcnt(0) lgkmcnt(0)
	ds_write_b32 v3, v0 offset:4

; __device__ __forceinline__ unsigned pk4_fp8(float a, float b, float c, float d) { int w = 0; w = __builtin_amdgcn_cvt_pk_fp8_f32(a, b, w, false); w = __builtin_amdgcn_cvt_pk_fp8_f32(c, d, w, true); return (unsigned)w; }
; __device__ __forceinline__ f32x4 swiglu4(f32x4 a, f32x4 b, float k1, float k3) {
;     const f32x2v a0 = {a[0], a[1]}, a1 = {a[2], a[3]}, b0 = {b[0], b[1]}, b1 = {b[2], b[3]};
;     const f32x2v t0 = a0 * k1, t1 = a1 * k1;
;     const f32x2v e0 = {__builtin_amdgcn_exp2f(t0[0]), __builtin_amdgcn_exp2f(t0[1])}, e1 = {__builtin_amdgcn_exp2f(t1[0]), __builtin_amdgcn_exp2f(t1[1])};
;     const f32x2v d0 = e0 * k3 + k3, d1 = e1 * k3 + k3;
;     const f32x2v r0 = {__builtin_amdgcn_rcpf(d0[0]), __builtin_amdgcn_rcpf(d0[1])}, r1 = {__builtin_amdgcn_rcpf(d1[0]), __builtin_amdgcn_rcpf(d1[1])};
;     const f32x2v y0 = (a0 * b0) * r0, y1 = (a1 * b1) * r1;
;     return (f32x4){y0[0], y0[1], y1[0], y1[1]};
;     __device__ __forceinline__ void operator()(const f32x4 (&acc)[2][2][4][2], const Unit& u, int wr, int wc, int fr, int fq) const {
;     ...
;             for (int bj = 0; bj < 2; ++bj) { unsigned d[4];
; #pragma unroll
;                 for (int m = 0; m < 4; ++m) { const f32x4 y = swiglu4(acc[ai][bj][m][0], acc[ai][bj][m][1], k1, k3);
;                     d[m] = pk4_fp8(y[0], y[1], y[2], y[3]); }
;                 const u32x4 q = xpose4(d[0], d[1], d[2], d[3]);
;                 *(u32x4*)(O + (size_t)(row0 + ai * HALF + 16 * fq) * ldc + hc0 + bj * 64) = q; }
.LBB0_921:
	s_mul_hi_i32 s0, s22, 0x92492493
	s_add_i32 s0, s0, s22
	s_lshr_b32 s1, s0, 31
	s_lshr_b32 s0, s0, 4
	s_add_i32 s0, s0, s1
	s_mul_i32 s0, s0, 28
	s_sub_i32 s0, s22, s0
	s_mov_b32 s22, 0xbd38aa3b
	v_pk_mul_f32 v[0:1], v[158:159], s[22:23] op_sel_hi:[1,0]
	v_pk_mul_f32 v[2:3], v[160:161], s[22:23] op_sel_hi:[1,0]
	v_exp_f32_e32 v0, v0
	v_exp_f32_e32 v1, v1
	v_exp_f32_e32 v2, v2
	v_exp_f32_e32 v3, v3
	v_lshl_add_u32 v16, s20, 8, v191
	s_mov_b32 s20, 0x43800000
	v_pk_fma_f32 v[0:1], v[0:1], s[20:21], s[20:21] op_sel_hi:[1,0,0]
	v_pk_fma_f32 v[2:3], v[2:3], s[20:21], s[20:21] op_sel_hi:[1,0,0]
	v_rcp_f32_e32 v0, v0
	v_rcp_f32_e32 v1, v1
	v_rcp_f32_e32 v4, v2
	v_rcp_f32_e32 v5, v3
	v_pk_mul_f32 v[2:3], v[158:159], v[154:155]
	v_pk_mul_f32 v[8:9], v[152:153], s[22:23] op_sel_hi:[1,0]
	v_pk_mul_f32 v[0:1], v[2:3], v[0:1]
	v_mov_b32_e32 v2, v81
	v_cvt_pk_fp8_f32 v2, v0, v1
	v_pk_mul_f32 v[0:1], v[150:151], s[22:23] op_sel_hi:[1,0]
	v_exp_f32_e32 v8, v8
	v_exp_f32_e32 v0, v0
	v_exp_f32_e32 v1, v1
	v_exp_f32_e32 v9, v9
	v_pk_mul_f32 v[6:7], v[160:161], v[156:157]
	v_mov_b32_e32 v3, v81
	v_pk_fma_f32 v[0:1], v[0:1], s[20:21], s[20:21] op_sel_hi:[1,0,0]
	v_pk_mul_f32 v[4:5], v[6:7], v[4:5]
	v_rcp_f32_e32 v0, v0
	v_rcp_f32_e32 v1, v1
	v_cvt_pk_fp8_f32 v2, v4, v5 op_sel:[0,0,1]
	v_pk_fma_f32 v[4:5], v[8:9], s[20:21], s[20:21] op_sel_hi:[1,0,0]
	v_pk_mul_f32 v[8:9], v[150:151], v[146:147]
	v_rcp_f32_e32 v4, v4
	v_rcp_f32_e32 v5, v5
	v_pk_mul_f32 v[0:1], v[8:9], v[0:1]
	v_pk_mul_f32 v[8:9], v[144:145], s[22:23] op_sel_hi:[1,0]
	v_cvt_pk_fp8_f32 v3, v0, v1
	v_exp_f32_e32 v8, v8
	v_exp_f32_e32 v9, v9
	v_pk_mul_f32 v[6:7], v[152:153], v[148:149]
	v_pk_mul_f32 v[0:1], v[142:143], s[22:23] op_sel_hi:[1,0]
	v_pk_mul_f32 v[4:5], v[6:7], v[4:5]
	v_exp_f32_e32 v0, v0
	v_exp_f32_e32 v1, v1
	v_cvt_pk_fp8_f32 v3, v4, v5 op_sel:[0,0,1]
	v_pk_fma_f32 v[4:5], v[8:9], s[20:21], s[20:21] op_sel_hi:[1,0,0]
	v_pk_mul_f32 v[6:7], v[144:145], v[140:141]
	v_rcp_f32_e32 v4, v4
	v_rcp_f32_e32 v5, v5
	v_pk_fma_f32 v[0:1], v[0:1], s[20:21], s[20:21] op_sel_hi:[1,0,0]
	v_pk_mul_f32 v[8:9], v[142:143], v[138:139]
	v_rcp_f32_e32 v0, v0
	v_rcp_f32_e32 v1, v1
	v_pk_mul_f32 v[6:7], v[6:7], v[4:5]
	v_pk_mul_f32 v[4:5], v[134:135], s[22:23] op_sel_hi:[1,0]
	s_lshl_b32 s0, s0, 7
	v_exp_f32_e32 v10, v4
	v_exp_f32_e32 v11, v5
	v_pk_mul_f32 v[0:1], v[8:9], v[0:1]
	v_pk_mul_f32 v[8:9], v[136:137], s[22:23] op_sel_hi:[1,0]
	v_mov_b32_e32 v4, v81
	v_exp_f32_e32 v8, v8
	v_exp_f32_e32 v9, v9
	v_cvt_pk_fp8_f32 v4, v0, v1
	v_pk_fma_f32 v[0:1], v[10:11], s[20:21], s[20:21] op_sel_hi:[1,0,0]
	v_pk_mul_f32 v[10:11], v[134:135], v[130:131]
	v_rcp_f32_e32 v0, v0
	v_rcp_f32_e32 v1, v1
	v_pk_fma_f32 v[8:9], v[8:9], s[20:21], s[20:21] op_sel_hi:[1,0,0]
	v_mov_b32_e32 v5, v81
	v_rcp_f32_e32 v8, v8
	v_rcp_f32_e32 v9, v9
	v_pk_mul_f32 v[0:1], v[10:11], v[0:1]
	v_cvt_pk_fp8_f32 v4, v6, v7 op_sel:[0,0,1]
	v_cvt_pk_fp8_f32 v5, v0, v1
	v_pk_mul_f32 v[0:1], v[136:137], v[132:133]
	s_or_b32 s0, s0, s38
	v_pk_mul_f32 v[0:1], v[0:1], v[8:9]
	v_pk_mul_f32 v[8:9], v[126:127], s[22:23] op_sel_hi:[1,0]
	v_cvt_pk_fp8_f32 v5, v0, v1 op_sel:[0,0,1]
	v_exp_f32_e32 v8, v8
	v_exp_f32_e32 v9, v9
	v_mov_b64_e32 v[0:1], s[68:69]
	s_movk_i32 s13, 0xe00
	s_ashr_i32 s1, s0, 31
	v_permlane16_swap_b32_e32 v2, v3
	v_permlane16_swap_b32_e32 v4, v5
	v_mad_i64_i32 v[6:7], s[24:25], v16, s13, v[0:1]
	s_nop 0
	v_permlane32_swap_b32_e32 v2, v4
	v_permlane32_swap_b32_e32 v3, v5
	v_pk_mul_f32 v[10:11], v[128:129], s[22:23] op_sel_hi:[1,0]
	v_lshl_add_u64 v[6:7], v[6:7], 0, s[0:1]
	v_exp_f32_e32 v10, v10
	v_exp_f32_e32 v11, v11
	global_store_dwordx4 v[6:7], v[2:5], off
	v_pk_mul_f32 v[12:13], v[120:121], s[22:23] op_sel_hi:[1,0]
	s_andn2_b64 vcc, exec, s[4:5]
	v_pk_fma_f32 v[2:3], v[8:9], s[20:21], s[20:21] op_sel_hi:[1,0,0]
	v_pk_fma_f32 v[4:5], v[10:11], s[20:21], s[20:21] op_sel_hi:[1,0,0]
	v_rcp_f32_e32 v2, v2
	v_rcp_f32_e32 v3, v3
	v_pk_mul_f32 v[10:11], v[126:127], v[122:123]
	v_rcp_f32_e32 v4, v4
	v_rcp_f32_e32 v5, v5
	v_pk_mul_f32 v[10:11], v[10:11], v[2:3]
	v_mov_b32_e32 v2, v81
	v_cvt_pk_fp8_f32 v2, v10, v11
	v_pk_mul_f32 v[10:11], v[118:119], s[22:23] op_sel_hi:[1,0]
	v_pk_mul_f32 v[8:9], v[128:129], v[124:125]
	v_exp_f32_e32 v10, v10
	v_exp_f32_e32 v11, v11
	v_pk_mul_f32 v[4:5], v[8:9], v[4:5]
	v_exp_f32_e32 v12, v12
	v_exp_f32_e32 v13, v13
	v_cvt_pk_fp8_f32 v2, v4, v5 op_sel:[0,0,1]
	v_pk_fma_f32 v[4:5], v[10:11], s[20:21], s[20:21] op_sel_hi:[1,0,0]
	v_mov_b32_e32 v3, v81
	v_rcp_f32_e32 v4, v4
	v_rcp_f32_e32 v5, v5
	v_pk_fma_f32 v[8:9], v[12:13], s[20:21], s[20:21] op_sel_hi:[1,0,0]
	v_pk_mul_f32 v[12:13], v[118:119], v[114:115]
	v_rcp_f32_e32 v8, v8
	v_pk_mul_f32 v[4:5], v[12:13], v[4:5]
	v_rcp_f32_e32 v9, v9
	v_cvt_pk_fp8_f32 v3, v4, v5
	v_pk_mul_f32 v[4:5], v[110:111], s[22:23] op_sel_hi:[1,0]
	v_pk_mul_f32 v[12:13], v[112:113], s[22:23] op_sel_hi:[1,0]
	v_exp_f32_e32 v4, v4
	v_exp_f32_e32 v5, v5
	v_exp_f32_e32 v12, v12
	v_exp_f32_e32 v13, v13
	v_pk_mul_f32 v[10:11], v[120:121], v[116:117]
	v_pk_fma_f32 v[4:5], v[4:5], s[20:21], s[20:21] op_sel_hi:[1,0,0]
	v_pk_mul_f32 v[8:9], v[10:11], v[8:9]
	v_rcp_f32_e32 v4, v4
	v_rcp_f32_e32 v5, v5
	v_cvt_pk_fp8_f32 v3, v8, v9 op_sel:[0,0,1]
	v_pk_fma_f32 v[8:9], v[12:13], s[20:21], s[20:21] op_sel_hi:[1,0,0]
	v_pk_mul_f32 v[12:13], v[110:111], v[106:107]
	v_rcp_f32_e32 v8, v8
	v_rcp_f32_e32 v9, v9
	v_pk_mul_f32 v[12:13], v[12:13], v[4:5]
	v_pk_mul_f32 v[4:5], v[102:103], s[22:23] op_sel_hi:[1,0]
	v_pk_mul_f32 v[10:11], v[112:113], v[108:109]
	v_exp_f32_e32 v14, v4
	v_exp_f32_e32 v15, v5
	v_pk_mul_f32 v[8:9], v[10:11], v[8:9]
	v_pk_mul_f32 v[10:11], v[104:105], s[22:23] op_sel_hi:[1,0]
; __device__ __forceinline__ unsigned pk4_fp8(float a, float b, float c, float d) { int w = 0; w = __builtin_amdgcn_cvt_pk_fp8_f32(a, b, w, false); w = __builtin_amdgcn_cvt_pk_fp8_f32(c, d, w, true); return (unsigned)w; }
; __device__ __forceinline__ f32x4 swiglu4(f32x4 a, f32x4 b, float k1, float k3) {
;     const f32x2v a0 = {a[0], a[1]}, a1 = {a[2], a[3]}, b0 = {b[0], b[1]}, b1 = {b[2], b[3]};
;     const f32x2v t0 = a0 * k1, t1 = a1 * k1;
;     const f32x2v e0 = {__builtin_amdgcn_exp2f(t0[0]), __builtin_amdgcn_exp2f(t0[1])}, e1 = {__builtin_amdgcn_exp2f(t1[0]), __builtin_amdgcn_exp2f(t1[1])};
;     const f32x2v d0 = e0 * k3 + k3, d1 = e1 * k3 + k3;
;     const f32x2v r0 = {__builtin_amdgcn_rcpf(d0[0]), __builtin_amdgcn_rcpf(d0[1])}, r1 = {__builtin_amdgcn_rcpf(d1[0]), __builtin_amdgcn_rcpf(d1[1])};
;     const f32x2v y0 = (a0 * b0) * r0, y1 = (a1 * b1) * r1;
;     return (f32x4){y0[0], y0[1], y1[0], y1[1]};
;     __device__ __forceinline__ void operator()(const f32x4 (&acc)[2][2][4][2], const Unit& u, int wr, int wc, int fr, int fq) const {
;     ...
;             for (int bj = 0; bj < 2; ++bj) { unsigned d[4];
; #pragma unroll
;                 for (int m = 0; m < 4; ++m) { const f32x4 y = swiglu4(acc[ai][bj][m][0], acc[ai][bj][m][1], k1, k3);
;                     d[m] = pk4_fp8(y[0], y[1], y[2], y[3]); }
;                 const u32x4 q = xpose4(d[0], d[1], d[2], d[3]);
;                 *(u32x4*)(O + (size_t)(row0 + ai * HALF + 16 * fq) * ldc + hc0 + bj * 64) = q; }
	v_mov_b32_e32 v4, v81
	v_exp_f32_e32 v10, v10
	v_exp_f32_e32 v11, v11
	v_cvt_pk_fp8_f32 v4, v12, v13
	v_pk_fma_f32 v[12:13], v[14:15], s[20:21], s[20:21] op_sel_hi:[1,0,0]
	v_pk_mul_f32 v[14:15], v[102:103], v[98:99]
	v_rcp_f32_e32 v12, v12
	v_rcp_f32_e32 v13, v13
	v_pk_fma_f32 v[10:11], v[10:11], s[20:21], s[20:21] op_sel_hi:[1,0,0]
	v_mov_b32_e32 v5, v81
	v_rcp_f32_e32 v10, v10
	v_rcp_f32_e32 v11, v11
	v_pk_mul_f32 v[12:13], v[14:15], v[12:13]
	v_cvt_pk_fp8_f32 v4, v8, v9 op_sel:[0,0,1]
	v_cvt_pk_fp8_f32 v5, v12, v13
	v_pk_mul_f32 v[8:9], v[104:105], v[100:101]
	v_permlane16_swap_b32_e32 v2, v3
	v_pk_mul_f32 v[8:9], v[8:9], v[10:11]
	v_pk_mul_f32 v[10:11], v[96:97], s[22:23] op_sel_hi:[1,0]
	v_cvt_pk_fp8_f32 v5, v8, v9 op_sel:[0,0,1]
	v_pk_mul_f32 v[8:9], v[94:95], s[22:23] op_sel_hi:[1,0]
	v_exp_f32_e32 v10, v10
	v_exp_f32_e32 v8, v8
	v_exp_f32_e32 v9, v9
	v_permlane16_swap_b32_e32 v4, v5
	s_nop 1
	v_permlane32_swap_b32_e32 v2, v4
	v_permlane32_swap_b32_e32 v3, v5
	global_store_dwordx4 v[6:7], v[2:5], off offset:64
	v_exp_f32_e32 v11, v11
	v_pk_mul_f32 v[6:7], v[96:97], v[92:93]
	v_pk_fma_f32 v[2:3], v[8:9], s[20:21], s[20:21] op_sel_hi:[1,0,0]
	v_pk_mul_f32 v[8:9], v[94:95], v[90:91]
	v_rcp_f32_e32 v2, v2
	v_rcp_f32_e32 v3, v3
	v_pk_fma_f32 v[4:5], v[10:11], s[20:21], s[20:21] op_sel_hi:[1,0,0]
	v_pk_mul_f32 v[10:11], v[88:89], s[22:23] op_sel_hi:[1,0]
	v_rcp_f32_e32 v4, v4
	v_pk_mul_f32 v[8:9], v[8:9], v[2:3]
	v_mov_b32_e32 v2, v81
	v_rcp_f32_e32 v5, v5
	v_cvt_pk_fp8_f32 v2, v8, v9
	v_pk_mul_f32 v[8:9], v[86:87], s[22:23] op_sel_hi:[1,0]
	v_exp_f32_e32 v10, v10
	v_exp_f32_e32 v8, v8
	v_exp_f32_e32 v9, v9
	v_pk_mul_f32 v[4:5], v[6:7], v[4:5]
	v_exp_f32_e32 v11, v11
	v_cvt_pk_fp8_f32 v2, v4, v5 op_sel:[0,0,1]
	v_pk_fma_f32 v[4:5], v[8:9], s[20:21], s[20:21] op_sel_hi:[1,0,0]
	v_mov_b32_e32 v3, v81
	v_rcp_f32_e32 v4, v4
	v_rcp_f32_e32 v5, v5
	v_pk_fma_f32 v[6:7], v[10:11], s[20:21], s[20:21] op_sel_hi:[1,0,0]
	v_pk_mul_f32 v[10:11], v[86:87], v[82:83]
	v_rcp_f32_e32 v6, v6
	v_pk_mul_f32 v[4:5], v[10:11], v[4:5]
	v_rcp_f32_e32 v7, v7
	v_cvt_pk_fp8_f32 v3, v4, v5
	v_pk_mul_f32 v[4:5], v[76:77], s[22:23] op_sel_hi:[1,0]
	v_pk_mul_f32 v[10:11], v[78:79], s[22:23] op_sel_hi:[1,0]
	v_exp_f32_e32 v4, v4
	v_exp_f32_e32 v5, v5
	v_exp_f32_e32 v10, v10
	v_exp_f32_e32 v11, v11
	v_pk_mul_f32 v[8:9], v[88:89], v[84:85]
	v_pk_fma_f32 v[4:5], v[4:5], s[20:21], s[20:21] op_sel_hi:[1,0,0]
	v_pk_mul_f32 v[6:7], v[8:9], v[6:7]
	v_rcp_f32_e32 v4, v4
	v_rcp_f32_e32 v5, v5
	v_cvt_pk_fp8_f32 v3, v6, v7 op_sel:[0,0,1]
	v_pk_fma_f32 v[6:7], v[10:11], s[20:21], s[20:21] op_sel_hi:[1,0,0]
	v_pk_mul_f32 v[10:11], v[76:77], v[72:73]
	v_rcp_f32_e32 v6, v6
	v_rcp_f32_e32 v7, v7
	v_pk_mul_f32 v[10:11], v[10:11], v[4:5]
	v_pk_mul_f32 v[4:5], v[68:69], s[22:23] op_sel_hi:[1,0]
	v_pk_mul_f32 v[8:9], v[78:79], v[74:75]
	v_exp_f32_e32 v12, v4
	v_exp_f32_e32 v13, v5
	v_pk_mul_f32 v[6:7], v[8:9], v[6:7]
	v_pk_mul_f32 v[8:9], v[70:71], s[22:23] op_sel_hi:[1,0]
	v_mov_b32_e32 v4, v81
	v_exp_f32_e32 v8, v8
	v_exp_f32_e32 v9, v9
	v_cvt_pk_fp8_f32 v4, v10, v11
	v_pk_fma_f32 v[10:11], v[12:13], s[20:21], s[20:21] op_sel_hi:[1,0,0]
	v_pk_mul_f32 v[12:13], v[68:69], v[64:65]
	v_rcp_f32_e32 v10, v10
	v_rcp_f32_e32 v11, v11
	v_pk_fma_f32 v[8:9], v[8:9], s[20:21], s[20:21] op_sel_hi:[1,0,0]
	v_mov_b32_e32 v5, v81
	v_rcp_f32_e32 v8, v8
	v_rcp_f32_e32 v9, v9
	v_pk_mul_f32 v[10:11], v[12:13], v[10:11]
	v_cvt_pk_fp8_f32 v4, v6, v7 op_sel:[0,0,1]
	v_cvt_pk_fp8_f32 v5, v10, v11
	v_pk_mul_f32 v[6:7], v[70:71], v[66:67]
	v_add_u32_e32 v14, 0x80, v16
	v_pk_mul_f32 v[6:7], v[6:7], v[8:9]
	v_mad_i64_i32 v[0:1], s[24:25], v14, s13, v[0:1]
	v_cvt_pk_fp8_f32 v5, v6, v7 op_sel:[0,0,1]
	v_pk_mul_f32 v[6:7], v[60:61], s[22:23] op_sel_hi:[1,0]
	v_pk_mul_f32 v[8:9], v[62:63], s[22:23] op_sel_hi:[1,0]
	v_exp_f32_e32 v6, v6
	v_exp_f32_e32 v7, v7
	v_lshl_add_u64 v[10:11], v[0:1], 0, s[0:1]
	v_exp_f32_e32 v8, v8
	v_exp_f32_e32 v9, v9
	v_pk_fma_f32 v[0:1], v[6:7], s[20:21], s[20:21] op_sel_hi:[1,0,0]
	v_permlane16_swap_b32_e32 v2, v3
	v_rcp_f32_e32 v0, v0
	v_rcp_f32_e32 v1, v1
	v_permlane16_swap_b32_e32 v4, v5
	s_nop 1
	v_permlane32_swap_b32_e32 v2, v4
	v_permlane32_swap_b32_e32 v3, v5
	v_pk_mul_f32 v[6:7], v[60:61], v[56:57]
	global_store_dwordx4 v[10:11], v[2:5], off
	v_pk_mul_f32 v[6:7], v[6:7], v[0:1]
	v_mov_b32_e32 v0, v81
	v_pk_fma_f32 v[2:3], v[8:9], s[20:21], s[20:21] op_sel_hi:[1,0,0]
	v_cvt_pk_fp8_f32 v0, v6, v7
	v_rcp_f32_e32 v2, v2
	v_rcp_f32_e32 v3, v3
	v_pk_mul_f32 v[6:7], v[52:53], s[22:23] op_sel_hi:[1,0]
	v_pk_mul_f32 v[4:5], v[62:63], v[58:59]
	v_exp_f32_e32 v6, v6
	v_exp_f32_e32 v7, v7
	v_pk_mul_f32 v[8:9], v[54:55], s[22:23] op_sel_hi:[1,0]
	v_pk_mul_f32 v[2:3], v[4:5], v[2:3]
	v_exp_f32_e32 v8, v8
	v_exp_f32_e32 v9, v9
	v_cvt_pk_fp8_f32 v0, v2, v3 op_sel:[0,0,1]
	v_pk_fma_f32 v[2:3], v[6:7], s[20:21], s[20:21] op_sel_hi:[1,0,0]
	v_mov_b32_e32 v1, v81
	v_rcp_f32_e32 v2, v2
	v_rcp_f32_e32 v3, v3
	v_pk_fma_f32 v[4:5], v[8:9], s[20:21], s[20:21] op_sel_hi:[1,0,0]
	v_pk_mul_f32 v[8:9], v[52:53], v[48:49]
	v_rcp_f32_e32 v4, v4
	v_pk_mul_f32 v[2:3], v[8:9], v[2:3]
	v_rcp_f32_e32 v5, v5
	v_cvt_pk_fp8_f32 v1, v2, v3
	v_pk_mul_f32 v[2:3], v[44:45], s[22:23] op_sel_hi:[1,0]
	v_pk_mul_f32 v[8:9], v[46:47], s[22:23] op_sel_hi:[1,0]
	v_exp_f32_e32 v2, v2
	v_exp_f32_e32 v3, v3
	v_exp_f32_e32 v8, v8
	v_exp_f32_e32 v9, v9
	v_pk_mul_f32 v[6:7], v[54:55], v[50:51]
	v_pk_fma_f32 v[2:3], v[2:3], s[20:21], s[20:21] op_sel_hi:[1,0,0]
	v_pk_mul_f32 v[4:5], v[6:7], v[4:5]
	v_rcp_f32_e32 v2, v2
	v_rcp_f32_e32 v3, v3
	v_cvt_pk_fp8_f32 v1, v4, v5 op_sel:[0,0,1]
	v_pk_fma_f32 v[4:5], v[8:9], s[20:21], s[20:21] op_sel_hi:[1,0,0]
	v_pk_mul_f32 v[8:9], v[44:45], v[40:41]
	v_rcp_f32_e32 v4, v4
	v_rcp_f32_e32 v5, v5
	v_pk_mul_f32 v[8:9], v[8:9], v[2:3]
	v_pk_mul_f32 v[2:3], v[36:37], s[22:23] op_sel_hi:[1,0]
	v_pk_mul_f32 v[6:7], v[46:47], v[42:43]
	v_exp_f32_e32 v12, v2
	v_exp_f32_e32 v13, v3
	v_pk_mul_f32 v[4:5], v[6:7], v[4:5]
	v_pk_mul_f32 v[6:7], v[38:39], s[22:23] op_sel_hi:[1,0]
	v_mov_b32_e32 v2, v81
	v_exp_f32_e32 v6, v6
	v_exp_f32_e32 v7, v7
	v_cvt_pk_fp8_f32 v2, v8, v9
	v_pk_fma_f32 v[8:9], v[12:13], s[20:21], s[20:21] op_sel_hi:[1,0,0]
	v_pk_mul_f32 v[12:13], v[36:37], v[32:33]
	v_rcp_f32_e32 v8, v8
	v_rcp_f32_e32 v9, v9
	v_pk_fma_f32 v[6:7], v[6:7], s[20:21], s[20:21] op_sel_hi:[1,0,0]
	v_mov_b32_e32 v3, v81
	v_rcp_f32_e32 v6, v6
	v_rcp_f32_e32 v7, v7
	v_pk_mul_f32 v[8:9], v[12:13], v[8:9]
	v_cvt_pk_fp8_f32 v2, v4, v5 op_sel:[0,0,1]
	v_cvt_pk_fp8_f32 v3, v8, v9
	v_pk_mul_f32 v[4:5], v[38:39], v[34:35]
	v_permlane16_swap_b32_e32 v0, v1
	v_pk_mul_f32 v[4:5], v[4:5], v[6:7]
	s_mov_b64 s[0:1], -1
	v_cvt_pk_fp8_f32 v3, v4, v5 op_sel:[0,0,1]
	s_nop 1
	v_permlane16_swap_b32_e32 v2, v3
	s_nop 1
	v_permlane32_swap_b32_e32 v0, v2
	v_permlane32_swap_b32_e32 v1, v3
	global_store_dwordx4 v[10:11], v[0:3], off offset:64
	s_cbranch_vccnz .LBB0_914
	s_andn2_b64 vcc, exec, s[6:7]
	s_cbranch_vccnz .LBB0_913
	s_barrier
	s_branch .LBB0_913

; __device__ __forceinline__ unsigned pk4_fp8(float a, float b, float c, float d) { int w = 0; w = __builtin_amdgcn_cvt_pk_fp8_f32(a, b, w, false); w = __builtin_amdgcn_cvt_pk_fp8_f32(c, d, w, true); return (unsigned)w; }
; template <int MODE, int KL>
; __device__ __forceinline__ void p0_cvt_item(const float* W, int K, int N, unsigned char* WT, int il, int which, int item, int lane, const float* gk, float scale, int ldk, int koff) {
;     const int nblk = N >> 6, kb = item / nblk, nb = item - kb * nblk, nq = lane & 15, kr = lane >> 4, k0 = 4 * KL * kb + KL * kr, n0 = 64 * nb + 4 * nq;
;     const GAS f32x4* src = (const GAS f32x4*)(W + (size_t)k0 * N + n0);
;     f32x4 v[KL];
; #pragma unroll
;     for (int i = 0; i < KL; ++i) v[i] = src[(size_t)i * (N >> 2)];
;     if (MODE == 1) {
; #pragma unroll
;         for (int q = 0; q < KL / 4; ++q) { const f32x4 g = *(const GAS f32x4*)(gk + k0 + 4 * q); v[4 * q] *= g.x; v[4 * q + 1] *= g.y; v[4 * q + 2] *= g.z; v[4 * q + 3] *= g.w; } }
;     if (MODE == 2) {
; #pragma unroll
;         for (int i = 0; i < KL; ++i) v[i] *= scale; }
; #pragma unroll
;     for (int c = 0; c < 4; ++c) { const int n = n0 + c, row = il ? ((n >> 4) * 32 + which * 16 + (n & 15)) : n;
;         if (MODE == 2) { GAS v4u* dst = (GAS v4u*)(WT + (size_t)row * ldk + koff + k0);
; #pragma unroll
;             for (int q = 0; q < KL / 16; ++q) { v4u o;
;                 o.x = pg8::pk4_fp8(v[16 * q][c], v[16 * q + 1][c], v[16 * q + 2][c], v[16 * q + 3][c]);     o.y = pg8::pk4_fp8(v[16 * q + 4][c], v[16 * q + 5][c], v[16 * q + 6][c], v[16 * q + 7][c]);
;                 o.z = pg8::pk4_fp8(v[16 * q + 8][c], v[16 * q + 9][c], v[16 * q + 10][c], v[16 * q + 11][c]); o.w = pg8::pk4_fp8(v[16 * q + 12][c], v[16 * q + 13][c], v[16 * q + 14][c], v[16 * q + 15][c]);
;                 dst[q] = o; } }
; __device__ __forceinline__ void moe_cvt_tile(const Args& a, int set, int id, int lane) {
;     const int j = id / MT_PER, item = id - j * MT_PER;
;     if (j < 16) { const int e = set * 8 + (j & 7), wh = j >> 3;
;         p0_cvt_item<2, 32>(a.in[17 + wh] + (size_t)e * D * FE, D, FE, a.ws + W_13M + (size_t)e * 2 * FE * D, 1, wh, item, lane, nullptr, 32.f, D, 0); }
;     else { const int e = set * 8 + (j - 16); p0_cvt_item<2, 32>(a.in[19] + (size_t)e * FE * D, FE, D, a.ws + W_2M + (size_t)e * D * FE, 0, 0, item, lane, nullptr, 64.f, FE, 0); }
.LBB0_930:
	s_mul_hi_i32 s0, s7, 0x92492493
	s_add_i32 s0, s0, s7
	s_lshr_b32 s1, s0, 31
	s_ashr_i32 s10, s0, 8
	s_add_i32 s10, s10, s1
	s_mul_i32 s0, s10, 0xfffffe40
	s_add_i32 s11, s7, s0
	s_cmpk_gt_i32 s7, 0x1bff
	s_mov_b64 s[0:1], -1
	s_cbranch_scc0 .LBB0_932
	v_mov_b64_e32 v[0:1], s[66:67]
	global_load_dwordx2 v[2:3], v[0:1], off offset:152
	s_add_i32 s4, s9, s10
	global_load_dwordx2 v[0:1], v[0:1], off offset:192
	s_waitcnt vmcnt(0) lgkmcnt(0)
	v_mad_i64_i32 v[2:3], s[0:1], s4, v192, v[2:3]
	v_mad_i64_i32 v[78:79], s[0:1], s4, v193, v[0:1]
	s_ashr_i32 s0, s11, 31
	s_lshr_b32 s0, s0, 28
	s_add_i32 s0, s11, s0
	s_ashr_i32 s0, s0, 4
	v_lshl_add_u32 v122, s0, 7, v80
	s_lshl_b32 s0, s0, 10
	s_mul_i32 s1, s10, 0x7000
	s_add_i32 s0, s0, s1
	s_sub_i32 s0, s6, s0
	v_add_u32_e32 v157, s0, v156
	v_ashrrev_i32_e32 v123, 31, v122
	v_add_u32_e32 v124, 0xffff0000, v157
	v_lshlrev_b64 v[0:1], 12, v[122:123]
	v_lshl_add_u64 v[0:1], v[2:3], 0, v[0:1]
	v_ashrrev_i32_e32 v125, 31, v124
	v_lshl_add_u64 v[8:9], v[124:125], 2, v[0:1]
	s_movk_i32 s0, 0x2000
	v_add_co_u32_e32 v10, vcc, s0, v8
	s_movk_i32 s0, 0x4000
	s_nop 0
	v_addc_co_u32_e32 v11, vcc, 0, v9, vcc
	v_add_co_u32_e32 v14, vcc, s0, v8
	s_movk_i32 s0, 0x6000
	s_nop 0
	v_addc_co_u32_e32 v15, vcc, 0, v9, vcc
	v_add_co_u32_e32 v18, vcc, s0, v8
	s_mov_b32 s0, 0xc000
	s_nop 0
	v_addc_co_u32_e32 v19, vcc, 0, v9, vcc
	v_add_co_u32_e32 v26, vcc, s33, v8
	global_load_dwordx4 v[0:3], v[8:9], off
	s_nop 0
	v_addc_co_u32_e32 v27, vcc, 0, v9, vcc
	v_add_co_u32_e32 v34, vcc, s97, v8
	global_load_dwordx4 v[4:7], v[10:11], off offset:-4096
	s_nop 0
	global_load_dwordx4 v[10:13], v[10:11], off
	v_addc_co_u32_e32 v35, vcc, 0, v9, vcc
	v_add_co_u32_e32 v42, vcc, s0, v8
	s_mov_b32 s0, 0xe000
	s_nop 0
	v_addc_co_u32_e32 v43, vcc, 0, v9, vcc
	v_add_co_u32_e32 v50, vcc, s0, v8
	s_mov_b32 s0, 0x10000
	s_nop 0
	v_addc_co_u32_e32 v51, vcc, 0, v9, vcc
	v_add_co_u32_e32 v58, vcc, s0, v8
	s_mov_b32 s0, 0x12000
	s_nop 0
	v_addc_co_u32_e32 v59, vcc, 0, v9, vcc
	v_add_co_u32_e32 v70, vcc, s0, v8
	s_mov_b32 s0, 0x14000
	s_nop 0
	v_addc_co_u32_e32 v71, vcc, 0, v9, vcc
	v_add_co_u32_e32 v82, vcc, s0, v8
	s_mov_b32 s0, 0x16000
	s_nop 0
	v_addc_co_u32_e32 v83, vcc, 0, v9, vcc
	global_load_dwordx4 v[22:25], v[14:15], off offset:-4096
	s_nop 0
	global_load_dwordx4 v[14:17], v[14:15], off
	s_nop 0
	global_load_dwordx4 v[30:33], v[18:19], off offset:-4096
	s_nop 0
	global_load_dwordx4 v[18:21], v[18:19], off
	s_nop 0
	global_load_dwordx4 v[38:41], v[26:27], off offset:-4096
	s_nop 0
	global_load_dwordx4 v[26:29], v[26:27], off
	s_nop 0
	global_load_dwordx4 v[46:49], v[34:35], off offset:-4096
	s_nop 0
	global_load_dwordx4 v[34:37], v[34:35], off
	s_nop 0
	global_load_dwordx4 v[54:57], v[42:43], off offset:-4096
	s_nop 0
	global_load_dwordx4 v[42:45], v[42:43], off
	s_nop 0
	global_load_dwordx4 v[62:65], v[50:51], off offset:-4096
	s_nop 0
	global_load_dwordx4 v[50:53], v[50:51], off
	s_nop 0
	global_load_dwordx4 v[66:69], v[58:59], off offset:-4096
	s_nop 0
	global_load_dwordx4 v[58:61], v[58:59], off
	s_nop 0
	global_load_dwordx4 v[74:77], v[70:71], off offset:-4096
	s_nop 0
	global_load_dwordx4 v[70:73], v[70:71], off
	v_add_co_u32_e32 v90, vcc, s0, v8
	s_mov_b32 s0, 0x18000
	s_nop 0
	v_addc_co_u32_e32 v91, vcc, 0, v9, vcc
	v_add_co_u32_e32 v98, vcc, s0, v8
	s_mov_b32 s0, 0x1a000
	s_nop 0
	v_addc_co_u32_e32 v99, vcc, 0, v9, vcc
	v_add_co_u32_e32 v106, vcc, s0, v8
	s_mov_b32 s0, 0x1c000
	s_nop 0
	v_addc_co_u32_e32 v107, vcc, 0, v9, vcc
	v_add_co_u32_e32 v114, vcc, s0, v8
	s_mov_b32 s0, 0x1e000
	s_nop 0
	v_addc_co_u32_e32 v115, vcc, 0, v9, vcc
	v_add_co_u32_e32 v126, vcc, s0, v8
	global_load_dwordx4 v[86:89], v[82:83], off offset:-4096
	s_nop 0
	global_load_dwordx4 v[82:85], v[82:83], off
	s_nop 0
	global_load_dwordx4 v[94:97], v[90:91], off offset:-4096
	s_nop 0
	global_load_dwordx4 v[90:93], v[90:91], off
	s_nop 0
	global_load_dwordx4 v[102:105], v[98:99], off offset:-4096
	s_nop 0
	global_load_dwordx4 v[98:101], v[98:99], off
	s_nop 0
	global_load_dwordx4 v[110:113], v[106:107], off offset:-4096
	s_nop 0
	global_load_dwordx4 v[106:109], v[106:107], off
	s_nop 0
	global_load_dwordx4 v[118:121], v[114:115], off offset:-4096
	s_nop 0
	global_load_dwordx4 v[114:117], v[114:115], off
	v_addc_co_u32_e32 v127, vcc, 0, v9, vcc
	global_load_dwordx4 v[158:161], v[126:127], off offset:-4096
	global_load_dwordx4 v[174:177], v[126:127], off
	s_mov_b32 s0, 0x1f000
	v_add_co_u32_e32 v8, vcc, s0, v8
	s_mov_b64 s[0:1], 0x33f00000
	s_nop 0
	v_addc_co_u32_e32 v9, vcc, 0, v9, vcc
	global_load_dwordx4 v[178:181], v[8:9], off
	s_movk_i32 s4, 0xe00
	s_waitcnt vmcnt(31)
	v_pk_mul_f32 v[126:127], v[0:1], s[82:83] op_sel_hi:[1,0]
	v_lshl_add_u64 v[0:1], v[78:79], 0, v[122:123]
	v_lshl_add_u64 v[0:1], v[0:1], 0, s[0:1]
	v_mad_i64_i32 v[78:79], s[0:1], v124, s4, v[0:1]
	s_waitcnt vmcnt(30)
	v_pk_mul_f32 v[8:9], v[6:7], s[82:83] op_sel_hi:[1,0]
	v_pk_mul_f32 v[6:7], v[4:5], s[82:83] op_sel_hi:[1,0]
	s_waitcnt vmcnt(29)
	v_pk_mul_f32 v[128:129], v[10:11], s[82:83] op_sel_hi:[1,0]
	v_pk_mul_f32 v[4:5], v[12:13], s[82:83] op_sel_hi:[1,0]
	v_pk_mul_f32 v[2:3], v[2:3], s[82:83] op_sel_hi:[1,0]
	s_waitcnt vmcnt(28)
	v_pk_mul_f32 v[132:133], v[22:23], s[82:83] op_sel_hi:[1,0]
	s_waitcnt vmcnt(27)
	v_pk_mul_f32 v[130:131], v[14:15], s[82:83] op_sel_hi:[1,0]
	s_waitcnt vmcnt(26)
	v_pk_mul_f32 v[134:135], v[30:31], s[82:83] op_sel_hi:[1,0]
	s_waitcnt vmcnt(25)
	v_pk_mul_f32 v[136:137], v[18:19], s[82:83] op_sel_hi:[1,0]
	s_waitcnt vmcnt(24)
	v_pk_mul_f32 v[18:19], v[40:41], s[82:83] op_sel_hi:[1,0]
	v_pk_mul_f32 v[138:139], v[38:39], s[82:83] op_sel_hi:[1,0]
	s_waitcnt vmcnt(23)
; __device__ __forceinline__ unsigned pk4_fp8(float a, float b, float c, float d) { int w = 0; w = __builtin_amdgcn_cvt_pk_fp8_f32(a, b, w, false); w = __builtin_amdgcn_cvt_pk_fp8_f32(c, d, w, true); return (unsigned)w; }
; #define GAS __attribute__((address_space(1)))
; template <int MODE, int KL>
; __device__ __forceinline__ void p0_cvt_item(const float* W, int K, int N, unsigned char* WT, int il, int which, int item, int lane, const float* gk, float scale, int ldk, int koff) {
;     const int nblk = N >> 6, kb = item / nblk, nb = item - kb * nblk, nq = lane & 15, kr = lane >> 4, k0 = 4 * KL * kb + KL * kr, n0 = 64 * nb + 4 * nq;
;     const GAS f32x4* src = (const GAS f32x4*)(W + (size_t)k0 * N + n0);
;     f32x4 v[KL];
; #pragma unroll
;     for (int i = 0; i < KL; ++i) v[i] = src[(size_t)i * (N >> 2)];
;     if (MODE == 1) {
; #pragma unroll
;         for (int q = 0; q < KL / 4; ++q) { const f32x4 g = *(const GAS f32x4*)(gk + k0 + 4 * q); v[4 * q] *= g.x; v[4 * q + 1] *= g.y; v[4 * q + 2] *= g.z; v[4 * q + 3] *= g.w; } }
;     if (MODE == 2) {
; #pragma unroll
;         for (int i = 0; i < KL; ++i) v[i] *= scale; }
; #pragma unroll
;     for (int c = 0; c < 4; ++c) { const int n = n0 + c, row = il ? ((n >> 4) * 32 + which * 16 + (n & 15)) : n;
;         if (MODE == 2) { GAS v4u* dst = (GAS v4u*)(WT + (size_t)row * ldk + koff + k0);
; #pragma unroll
;             for (int q = 0; q < KL / 16; ++q) { v4u o;
;                 o.x = pg8::pk4_fp8(v[16 * q][c], v[16 * q + 1][c], v[16 * q + 2][c], v[16 * q + 3][c]);     o.y = pg8::pk4_fp8(v[16 * q + 4][c], v[16 * q + 5][c], v[16 * q + 6][c], v[16 * q + 7][c]);
;                 o.z = pg8::pk4_fp8(v[16 * q + 8][c], v[16 * q + 9][c], v[16 * q + 10][c], v[16 * q + 11][c]); o.w = pg8::pk4_fp8(v[16 * q + 12][c], v[16 * q + 13][c], v[16 * q + 14][c], v[16 * q + 15][c]);
;                 dst[q] = o; } }
	v_pk_mul_f32 v[40:41], v[26:27], s[82:83] op_sel_hi:[1,0]
	s_waitcnt vmcnt(22)
	v_pk_mul_f32 v[140:141], v[46:47], s[82:83] op_sel_hi:[1,0]
	s_waitcnt vmcnt(19)
	v_pk_mul_f32 v[148:149], v[42:43], s[82:83] op_sel_hi:[1,0]
	s_waitcnt vmcnt(18)
	v_pk_mul_f32 v[182:183], v[62:63], s[82:83] op_sel_hi:[1,0]
	s_waitcnt vmcnt(14)
	v_pk_mul_f32 v[42:43], v[76:77], s[82:83] op_sel_hi:[1,0]
	s_waitcnt vmcnt(13)
	v_pk_mul_f32 v[38:39], v[72:73], s[82:83] op_sel_hi:[1,0]
	v_pk_mul_f32 v[76:77], v[70:71], s[82:83] op_sel_hi:[1,0]
	v_mov_b32_e32 v70, v81
	v_mov_b32_e32 v71, v81
	v_mov_b32_e32 v72, v81
	v_mov_b32_e32 v73, v81
	v_cvt_pk_fp8_f32 v70, v126, v6
	v_cvt_pk_fp8_f32 v71, v130, v134
	v_cvt_pk_fp8_f32 v72, v40, v140
	v_cvt_pk_fp8_f32 v73, v148, v182
	v_pk_mul_f32 v[142:143], v[34:35], s[82:83] op_sel_hi:[1,0]
	v_pk_mul_f32 v[150:151], v[54:55], s[82:83] op_sel_hi:[1,0]
	v_pk_mul_f32 v[144:145], v[50:51], s[82:83] op_sel_hi:[1,0]
	v_pk_mul_f32 v[152:153], v[66:67], s[82:83] op_sel_hi:[1,0]
	v_cvt_pk_fp8_f32 v70, v128, v132 op_sel:[0,0,1]
	v_cvt_pk_fp8_f32 v71, v136, v138 op_sel:[0,0,1]
	v_cvt_pk_fp8_f32 v72, v142, v150 op_sel:[0,0,1]
	v_cvt_pk_fp8_f32 v73, v144, v152 op_sel:[0,0,1]
	v_pk_mul_f32 v[12:13], v[16:17], s[82:83] op_sel_hi:[1,0]
	v_pk_mul_f32 v[16:17], v[20:21], s[82:83] op_sel_hi:[1,0]
	v_pk_mul_f32 v[20:21], v[28:29], s[82:83] op_sel_hi:[1,0]
	v_pk_mul_f32 v[28:29], v[44:45], s[82:83] op_sel_hi:[1,0]
	v_pk_mul_f32 v[146:147], v[58:59], s[82:83] op_sel_hi:[1,0]
	v_pk_mul_f32 v[74:75], v[74:75], s[82:83] op_sel_hi:[1,0]
	s_waitcnt vmcnt(12)
	v_pk_mul_f32 v[44:45], v[88:89], s[82:83] op_sel_hi:[1,0]
	s_waitcnt vmcnt(11)
	v_pk_mul_f32 v[46:47], v[84:85], s[82:83] op_sel_hi:[1,0]
	v_pk_mul_f32 v[82:83], v[82:83], s[82:83] op_sel_hi:[1,0]
	s_waitcnt vmcnt(10)
	v_pk_mul_f32 v[84:85], v[94:95], s[82:83] op_sel_hi:[1,0]
	s_waitcnt vmcnt(9)
	v_pk_mul_f32 v[50:51], v[92:93], s[82:83] op_sel_hi:[1,0]
	v_pk_mul_f32 v[88:89], v[90:91], s[82:83] op_sel_hi:[1,0]
	s_waitcnt vmcnt(8)
	v_pk_mul_f32 v[90:91], v[102:103], s[82:83] op_sel_hi:[1,0]
	s_waitcnt vmcnt(7)
	v_pk_mul_f32 v[54:55], v[100:101], s[82:83] op_sel_hi:[1,0]
	v_pk_mul_f32 v[92:93], v[98:99], s[82:83] op_sel_hi:[1,0]
	s_waitcnt vmcnt(6)
	v_pk_mul_f32 v[94:95], v[110:111], s[82:83] op_sel_hi:[1,0]
	s_waitcnt vmcnt(3)
	v_pk_mul_f32 v[100:101], v[114:115], s[82:83] op_sel_hi:[1,0]
	s_waitcnt vmcnt(2)
	v_pk_mul_f32 v[102:103], v[158:159], s[82:83] op_sel_hi:[1,0]
	global_store_dwordx4 v[78:79], v[70:73], off
	v_pk_mul_f32 v[14:15], v[32:33], s[82:83] op_sel_hi:[1,0]
	v_pk_mul_f32 v[22:23], v[48:49], s[82:83] op_sel_hi:[1,0]
	v_mov_b32_e32 v70, v81
	v_mov_b32_e32 v71, v81
	v_mov_b32_e32 v72, v81
	v_mov_b32_e32 v73, v81
	v_cvt_pk_fp8_f32 v70, v146, v74
	v_cvt_pk_fp8_f32 v71, v82, v84
	v_cvt_pk_fp8_f32 v72, v92, v94
	v_cvt_pk_fp8_f32 v73, v100, v102
	v_pk_mul_f32 v[32:33], v[52:53], s[82:83] op_sel_hi:[1,0]
	v_pk_mul_f32 v[86:87], v[86:87], s[82:83] op_sel_hi:[1,0]
	v_pk_mul_f32 v[48:49], v[96:97], s[82:83] op_sel_hi:[1,0]
	v_pk_mul_f32 v[52:53], v[104:105], s[82:83] op_sel_hi:[1,0]
	v_pk_mul_f32 v[96:97], v[106:107], s[82:83] op_sel_hi:[1,0]
	v_pk_mul_f32 v[98:99], v[118:119], s[82:83] op_sel_hi:[1,0]
	s_waitcnt vmcnt(2)
	v_pk_mul_f32 v[104:105], v[174:175], s[82:83] op_sel_hi:[1,0]
	s_waitcnt vmcnt(1)
	v_pk_mul_f32 v[106:107], v[178:179], s[82:83] op_sel_hi:[1,0]
	v_cvt_pk_fp8_f32 v70, v76, v86 op_sel:[0,0,1]
	v_cvt_pk_fp8_f32 v71, v88, v90 op_sel:[0,0,1]
	v_cvt_pk_fp8_f32 v72, v96, v98 op_sel:[0,0,1]
	v_cvt_pk_fp8_f32 v73, v104, v106 op_sel:[0,0,1]
	v_add_u32_e32 v6, 0xffff0001, v157
	v_pk_mul_f32 v[30:31], v[64:65], s[82:83] op_sel_hi:[1,0]
	v_pk_mul_f32 v[10:11], v[24:25], s[82:83] op_sel_hi:[1,0]
	global_store_dwordx4 v[78:79], v[70:73], off offset:16
	v_mad_i64_i32 v[78:79], s[0:1], v6, s4, v[0:1]
	s_nop 0
	v_mov_b32_e32 v70, v81
	v_mov_b32_e32 v71, v81
	v_mov_b32_e32 v72, v81
	v_mov_b32_e32 v73, v81
	v_cvt_pk_fp8_f32 v70, v127, v7
	v_cvt_pk_fp8_f32 v71, v131, v135
	v_cvt_pk_fp8_f32 v72, v41, v141
	v_cvt_pk_fp8_f32 v73, v149, v183
	v_cvt_pk_fp8_f32 v70, v129, v133 op_sel:[0,0,1]
	v_cvt_pk_fp8_f32 v71, v137, v139 op_sel:[0,0,1]
	v_cvt_pk_fp8_f32 v72, v143, v151 op_sel:[0,0,1]
	v_cvt_pk_fp8_f32 v73, v145, v153 op_sel:[0,0,1]
	v_pk_mul_f32 v[24:25], v[36:37], s[82:83] op_sel_hi:[1,0]
	v_pk_mul_f32 v[26:27], v[56:57], s[82:83] op_sel_hi:[1,0]
	v_pk_mul_f32 v[34:35], v[68:69], s[82:83] op_sel_hi:[1,0]
	global_store_dwordx4 v[78:79], v[70:73], off
	v_add_u32_e32 v6, 0xffff0002, v157
	v_mad_i64_i32 v[6:7], s[0:1], v6, s4, v[0:1]
	v_mov_b32_e32 v70, v81
	v_mov_b32_e32 v71, v81
	v_mov_b32_e32 v72, v81
	v_mov_b32_e32 v73, v81
	v_cvt_pk_fp8_f32 v70, v147, v75
	v_cvt_pk_fp8_f32 v71, v83, v85
	v_cvt_pk_fp8_f32 v72, v93, v95
	v_cvt_pk_fp8_f32 v73, v101, v103
	v_cvt_pk_fp8_f32 v70, v77, v87 op_sel:[0,0,1]
	v_cvt_pk_fp8_f32 v71, v89, v91 op_sel:[0,0,1]
	v_cvt_pk_fp8_f32 v72, v97, v99 op_sel:[0,0,1]
	v_cvt_pk_fp8_f32 v73, v105, v107 op_sel:[0,0,1]
	v_pk_mul_f32 v[36:37], v[60:61], s[82:83] op_sel_hi:[1,0]
	v_pk_mul_f32 v[56:57], v[112:113], s[82:83] op_sel_hi:[1,0]
	v_pk_mul_f32 v[62:63], v[116:117], s[82:83] op_sel_hi:[1,0]
	global_store_dwordx4 v[78:79], v[70:73], off offset:16
	v_pk_mul_f32 v[64:65], v[160:161], s[82:83] op_sel_hi:[1,0]
	v_pk_mul_f32 v[58:59], v[108:109], s[82:83] op_sel_hi:[1,0]
	v_mov_b32_e32 v70, v81
	v_mov_b32_e32 v71, v81
	v_mov_b32_e32 v72, v81
	v_mov_b32_e32 v73, v81
	v_cvt_pk_fp8_f32 v70, v2, v8
	v_cvt_pk_fp8_f32 v71, v12, v14
	v_cvt_pk_fp8_f32 v72, v20, v22
	v_cvt_pk_fp8_f32 v73, v28, v30
	v_cvt_pk_fp8_f32 v70, v4, v10 op_sel:[0,0,1]
	v_cvt_pk_fp8_f32 v71, v16, v18 op_sel:[0,0,1]
	v_cvt_pk_fp8_f32 v72, v24, v26 op_sel:[0,0,1]
	v_cvt_pk_fp8_f32 v73, v32, v34 op_sel:[0,0,1]
	v_pk_mul_f32 v[60:61], v[120:121], s[82:83] op_sel_hi:[1,0]
	v_pk_mul_f32 v[66:67], v[176:177], s[82:83] op_sel_hi:[1,0]
	v_pk_mul_f32 v[68:69], v[180:181], s[82:83] op_sel_hi:[1,0]
	global_store_dwordx4 v[6:7], v[70:73], off
	v_add_u32_e32 v2, 0xffff0003, v157
	v_mad_i64_i32 v[0:1], s[0:1], v2, s4, v[0:1]
	v_mov_b32_e32 v70, v81
	v_mov_b32_e32 v71, v81
	v_mov_b32_e32 v72, v81
	v_mov_b32_e32 v73, v81
	v_cvt_pk_fp8_f32 v70, v36, v42
	v_cvt_pk_fp8_f32 v71, v46, v48
	v_cvt_pk_fp8_f32 v72, v54, v56
	v_cvt_pk_fp8_f32 v73, v62, v64
	v_cvt_pk_fp8_f32 v70, v38, v44 op_sel:[0,0,1]
	v_cvt_pk_fp8_f32 v71, v50, v52 op_sel:[0,0,1]
	v_cvt_pk_fp8_f32 v72, v58, v60 op_sel:[0,0,1]
	v_cvt_pk_fp8_f32 v73, v66, v68 op_sel:[0,0,1]
	s_mov_b64 s[0:1], 0
	global_store_dwordx4 v[6:7], v[70:73], off offset:16
; __device__ __forceinline__ unsigned pk4_fp8(float a, float b, float c, float d) { int w = 0; w = __builtin_amdgcn_cvt_pk_fp8_f32(a, b, w, false); w = __builtin_amdgcn_cvt_pk_fp8_f32(c, d, w, true); return (unsigned)w; }
; #define GAS __attribute__((address_space(1)))
; template <int MODE, int KL>
; __device__ __forceinline__ void p0_cvt_item(const float* W, int K, int N, unsigned char* WT, int il, int which, int item, int lane, const float* gk, float scale, int ldk, int koff) {
;     const int nblk = N >> 6, kb = item / nblk, nb = item - kb * nblk, nq = lane & 15, kr = lane >> 4, k0 = 4 * KL * kb + KL * kr, n0 = 64 * nb + 4 * nq;
;     const GAS f32x4* src = (const GAS f32x4*)(W + (size_t)k0 * N + n0);
;     f32x4 v[KL];
; #pragma unroll
;     for (int i = 0; i < KL; ++i) v[i] = src[(size_t)i * (N >> 2)];
;     if (MODE == 1) {
; #pragma unroll
;         for (int q = 0; q < KL / 4; ++q) { const f32x4 g = *(const GAS f32x4*)(gk + k0 + 4 * q); v[4 * q] *= g.x; v[4 * q + 1] *= g.y; v[4 * q + 2] *= g.z; v[4 * q + 3] *= g.w; } }
;     if (MODE == 2) {
; #pragma unroll
;         for (int i = 0; i < KL; ++i) v[i] *= scale; }
; #pragma unroll
;     for (int c = 0; c < 4; ++c) { const int n = n0 + c, row = il ? ((n >> 4) * 32 + which * 16 + (n & 15)) : n;
;         if (MODE == 2) { GAS v4u* dst = (GAS v4u*)(WT + (size_t)row * ldk + koff + k0);
; #pragma unroll
;             for (int q = 0; q < KL / 16; ++q) { v4u o;
;                 o.x = pg8::pk4_fp8(v[16 * q][c], v[16 * q + 1][c], v[16 * q + 2][c], v[16 * q + 3][c]);     o.y = pg8::pk4_fp8(v[16 * q + 4][c], v[16 * q + 5][c], v[16 * q + 6][c], v[16 * q + 7][c]);
;                 o.z = pg8::pk4_fp8(v[16 * q + 8][c], v[16 * q + 9][c], v[16 * q + 10][c], v[16 * q + 11][c]); o.w = pg8::pk4_fp8(v[16 * q + 12][c], v[16 * q + 13][c], v[16 * q + 14][c], v[16 * q + 15][c]);
;                 dst[q] = o; } }
; __device__ __forceinline__ void moe_cvt_tile(const Args& a, int set, int id, int lane) {
;     const int j = id / MT_PER, item = id - j * MT_PER;
;     if (j < 16) { const int e = set * 8 + (j & 7), wh = j >> 3;
;         p0_cvt_item<2, 32>(a.in[17 + wh] + (size_t)e * D * FE, D, FE, a.ws + W_13M + (size_t)e * 2 * FE * D, 1, wh, item, lane, nullptr, 32.f, D, 0); }
.LBB0_932:
	s_andn2_b64 vcc, exec, s[0:1]
	s_cbranch_vccnz .LBB0_929
	s_ashr_i32 s4, s10, 3
	s_and_b32 s0, s10, 7
	s_ashr_i32 s5, s4, 31
	s_or_b32 s12, s0, s8
	s_lshl_b64 s[0:1], s[4:5], 3
	s_add_u32 s0, s66, s0
	s_addc_u32 s1, s67, s1
	v_mov_b64_e32 v[0:1], s[0:1]
	v_mov_b64_e32 v[2:3], s[66:67]
	global_load_dwordx2 v[0:1], v[0:1], off offset:136
	v_mov_b32_e32 v4, 0x700000
	global_load_dwordx2 v[2:3], v[2:3], off offset:192
	s_mulk_i32 s10, 0x1c0
	s_waitcnt vmcnt(0) lgkmcnt(0)
	v_mad_u64_u32 v[0:1], s[0:1], s12, v192, v[0:1]
	v_mad_u64_u32 v[70:71], s[0:1], s12, v4, v[2:3]
	s_mul_hi_i32 s0, s11, 0x92492493
	s_add_i32 s0, s0, s11
	s_lshr_b32 s1, s0, 31
	s_ashr_i32 s0, s0, 5
	s_add_i32 s0, s0, s1
	s_mul_i32 s1, s0, 0xffffffc8
	s_sub_i32 s1, s1, s10
	s_add_i32 s1, s7, s1
	v_lshl_add_u32 v72, s0, 7, v80
	v_lshl_or_b32 v74, s1, 6, v154
	s_movk_i32 s0, 0x3800
	v_mad_i64_i32 v[0:1], s[0:1], v72, s0, v[0:1]
	v_ashrrev_i32_e32 v75, 31, v74
	v_lshl_add_u64 v[8:9], v[74:75], 2, v[0:1]
	s_movk_i32 s0, 0x3000
	v_add_co_u32_e32 v4, vcc, s0, v8
	s_movk_i32 s0, 0x7000
	s_nop 0
	v_addc_co_u32_e32 v5, vcc, 0, v9, vcc
	v_add_co_u32_e32 v10, vcc, s0, v8
	s_mov_b32 s0, 0xe000
	s_nop 0
	v_addc_co_u32_e32 v11, vcc, 0, v9, vcc
	v_add_co_u32_e32 v14, vcc, s97, v8
	global_load_dwordx4 v[0:3], v[8:9], off
	s_nop 0
	v_addc_co_u32_e32 v15, vcc, 0, v9, vcc
	v_add_co_u32_e32 v18, vcc, s0, v8
	s_mov_b32 s0, 0x11000
	s_nop 0
	v_addc_co_u32_e32 v19, vcc, 0, v9, vcc
	v_add_co_u32_e32 v22, vcc, s0, v8
	s_mov_b32 s0, 0x15000
	s_nop 0
	v_addc_co_u32_e32 v23, vcc, 0, v9, vcc
	v_add_co_u32_e32 v26, vcc, s0, v8
	s_mov_b32 s0, 0x18000
	s_nop 0
	v_addc_co_u32_e32 v27, vcc, 0, v9, vcc
	v_add_co_u32_e32 v30, vcc, s0, v8
	s_mov_b32 s0, 0x1c000
	s_nop 0
	v_addc_co_u32_e32 v31, vcc, 0, v9, vcc
	v_add_co_u32_e32 v34, vcc, s0, v8
	s_mov_b32 s0, 0x1f000
	s_nop 0
	v_addc_co_u32_e32 v35, vcc, 0, v9, vcc
	v_add_co_u32_e32 v38, vcc, s0, v8
	s_mov_b32 s0, 0x23000
	s_nop 0
	v_addc_co_u32_e32 v39, vcc, 0, v9, vcc
	v_add_co_u32_e32 v42, vcc, s0, v8
	s_mov_b32 s0, 0x26000
	s_nop 0
	v_addc_co_u32_e32 v43, vcc, 0, v9, vcc
	v_add_co_u32_e32 v46, vcc, s0, v8
	s_mov_b32 s0, 0x2a000
	s_nop 0
	v_addc_co_u32_e32 v47, vcc, 0, v9, vcc
	v_add_co_u32_e32 v50, vcc, s0, v8
	s_mov_b32 s0, 0x2d000
	s_nop 0
	v_addc_co_u32_e32 v51, vcc, 0, v9, vcc
	v_add_co_u32_e32 v54, vcc, s0, v8
	s_mov_b32 s0, 0x31000
	s_nop 0
	v_addc_co_u32_e32 v55, vcc, 0, v9, vcc
	v_add_co_u32_e32 v58, vcc, s0, v8
	s_mov_b32 s0, 0x34000
	s_nop 0
	v_addc_co_u32_e32 v59, vcc, 0, v9, vcc
	v_add_co_u32_e32 v62, vcc, s0, v8
	s_mov_b32 s0, 0x38000
	s_nop 0
	v_addc_co_u32_e32 v63, vcc, 0, v9, vcc
	v_add_co_u32_e32 v66, vcc, s0, v8
	s_mov_b32 s0, 0x3b000
	s_nop 0
	v_addc_co_u32_e32 v67, vcc, 0, v9, vcc
	v_add_co_u32_e32 v76, vcc, s0, v8
	s_mov_b32 s0, 0x3f000
	s_nop 0
	v_addc_co_u32_e32 v77, vcc, 0, v9, vcc
	global_load_dwordx4 v[112:115], v[76:77], off offset:2048
	v_add_co_u32_e32 v76, vcc, s0, v8
	s_mov_b32 s0, 0x42000
	s_nop 0
	v_addc_co_u32_e32 v77, vcc, 0, v9, vcc
	global_load_dwordx4 v[116:119], v[76:77], off
	v_add_co_u32_e32 v76, vcc, s0, v8
	s_mov_b32 s0, 0x46000
	s_nop 0
	v_addc_co_u32_e32 v77, vcc, 0, v9, vcc
	global_load_dwordx4 v[120:123], v[76:77], off offset:2048
	v_add_co_u32_e32 v76, vcc, s0, v8
	s_mov_b32 s0, 0x49000
	s_nop 0
	v_addc_co_u32_e32 v77, vcc, 0, v9, vcc
	global_load_dwordx4 v[124:127], v[76:77], off
	v_add_co_u32_e32 v76, vcc, s0, v8
	s_mov_b32 s0, 0x4d000
	s_nop 0
	v_addc_co_u32_e32 v77, vcc, 0, v9, vcc
	global_load_dwordx4 v[128:131], v[76:77], off offset:2048
	v_add_co_u32_e32 v76, vcc, s0, v8
	s_mov_b32 s0, 0x50000
	s_nop 0
	v_addc_co_u32_e32 v77, vcc, 0, v9, vcc
	global_load_dwordx4 v[132:135], v[76:77], off
	v_add_co_u32_e32 v76, vcc, s0, v8
	global_load_dwordx4 v[4:7], v[4:5], off offset:2048
	s_nop 0
	v_addc_co_u32_e32 v77, vcc, 0, v9, vcc
	s_mov_b32 s0, 0x54000
	global_load_dwordx4 v[136:139], v[76:77], off offset:2048
	v_add_co_u32_e32 v76, vcc, s0, v8
	s_mov_b32 s0, 0x57000
	s_nop 0
	v_addc_co_u32_e32 v77, vcc, 0, v9, vcc
	global_load_dwordx4 v[140:143], v[76:77], off
	v_add_co_u32_e32 v76, vcc, s0, v8
	global_load_dwordx4 v[14:17], v[14:15], off offset:2048
	s_nop 0
	v_addc_co_u32_e32 v77, vcc, 0, v9, vcc
	global_load_dwordx4 v[18:21], v[18:19], off
	s_mov_b32 s0, 0x5b000
	global_load_dwordx4 v[22:25], v[22:23], off offset:2048
	v_ashrrev_i32_e32 v73, 31, v72
	global_load_dwordx4 v[30:33], v[30:31], off offset:2048
	s_waitcnt vmcnt(13)
	v_pk_mul_f32 v[2:3], v[2:3], s[96:97] op_sel_hi:[1,0]
	global_load_dwordx4 v[34:37], v[34:35], off
	s_waitcnt vmcnt(13)
	v_pk_mul_f32 v[108:109], v[112:113], s[96:97] op_sel_hi:[1,0]
	global_load_dwordx4 v[38:41], v[38:39], off offset:2048
	s_waitcnt vmcnt(13)
	v_pk_mul_f32 v[112:113], v[116:117], s[96:97] op_sel_hi:[1,0]
	global_load_dwordx4 v[46:49], v[46:47], off offset:2048
	s_waitcnt vmcnt(13)
	v_pk_mul_f32 v[116:117], v[120:121], s[96:97] op_sel_hi:[1,0]
	global_load_dwordx4 v[50:53], v[50:51], off
	s_waitcnt vmcnt(11)
	v_pk_mul_f32 v[120:121], v[132:133], s[96:97] op_sel_hi:[1,0]
	global_load_dwordx4 v[54:57], v[54:55], off offset:2048
	s_waitcnt vmcnt(11)
	v_pk_mul_f32 v[78:79], v[4:5], s[96:97] op_sel_hi:[1,0]
	global_load_dwordx4 v[144:147], v[76:77], off offset:2048
	v_add_co_u32_e32 v76, vcc, s0, v8
	s_mov_b32 s0, 0x5e000
	s_nop 0
	v_addc_co_u32_e32 v77, vcc, 0, v9, vcc
	global_load_dwordx4 v[148:151], v[76:77], off
	v_add_co_u32_e32 v76, vcc, s0, v8
	global_load_dwordx4 v[10:13], v[10:11], off
	s_nop 0
	v_addc_co_u32_e32 v77, vcc, 0, v9, vcc
	global_load_dwordx4 v[26:29], v[26:27], off
	s_mov_b32 s0, 0x62000
	global_load_dwordx4 v[42:45], v[42:43], off
	s_waitcnt vmcnt(12)
; __device__ __forceinline__ unsigned pk4_fp8(float a, float b, float c, float d) { int w = 0; w = __builtin_amdgcn_cvt_pk_fp8_f32(a, b, w, false); w = __builtin_amdgcn_cvt_pk_fp8_f32(c, d, w, true); return (unsigned)w; }
; #define GAS __attribute__((address_space(1)))
; template <int MODE, int KL>
; __device__ __forceinline__ void p0_cvt_item(const float* W, int K, int N, unsigned char* WT, int il, int which, int item, int lane, const float* gk, float scale, int ldk, int koff) {
;     const int nblk = N >> 6, kb = item / nblk, nb = item - kb * nblk, nq = lane & 15, kr = lane >> 4, k0 = 4 * KL * kb + KL * kr, n0 = 64 * nb + 4 * nq;
;     const GAS f32x4* src = (const GAS f32x4*)(W + (size_t)k0 * N + n0);
;     f32x4 v[KL];
; #pragma unroll
;     for (int i = 0; i < KL; ++i) v[i] = src[(size_t)i * (N >> 2)];
;     if (MODE == 1) {
; #pragma unroll
;         for (int q = 0; q < KL / 4; ++q) { const f32x4 g = *(const GAS f32x4*)(gk + k0 + 4 * q); v[4 * q] *= g.x; v[4 * q + 1] *= g.y; v[4 * q + 2] *= g.z; v[4 * q + 3] *= g.w; } }
;     if (MODE == 2) {
; #pragma unroll
;         for (int i = 0; i < KL; ++i) v[i] *= scale; }
; #pragma unroll
;     for (int c = 0; c < 4; ++c) { const int n = n0 + c, row = il ? ((n >> 4) * 32 + which * 16 + (n & 15)) : n;
;         if (MODE == 2) { GAS v4u* dst = (GAS v4u*)(WT + (size_t)row * ldk + koff + k0);
; #pragma unroll
;             for (int q = 0; q < KL / 16; ++q) { v4u o;
;                 o.x = pg8::pk4_fp8(v[16 * q][c], v[16 * q + 1][c], v[16 * q + 2][c], v[16 * q + 3][c]);     o.y = pg8::pk4_fp8(v[16 * q + 4][c], v[16 * q + 5][c], v[16 * q + 6][c], v[16 * q + 7][c]);
;                 o.z = pg8::pk4_fp8(v[16 * q + 8][c], v[16 * q + 9][c], v[16 * q + 10][c], v[16 * q + 11][c]); o.w = pg8::pk4_fp8(v[16 * q + 12][c], v[16 * q + 13][c], v[16 * q + 14][c], v[16 * q + 15][c]);
;                 dst[q] = o; } }
	v_pk_mul_f32 v[84:85], v[18:19], s[96:97] op_sel_hi:[1,0]
	global_load_dwordx4 v[58:61], v[58:59], off
	s_waitcnt vmcnt(12)
	v_pk_mul_f32 v[88:89], v[22:23], s[96:97] op_sel_hi:[1,0]
	global_load_dwordx4 v[62:65], v[62:63], off offset:2048
	v_pk_mul_f32 v[86:87], v[14:15], s[96:97] op_sel_hi:[1,0]
	global_load_dwordx4 v[158:161], v[76:77], off offset:2048
	v_add_co_u32_e32 v76, vcc, s0, v8
	s_mov_b32 s0, 0x65000
	s_nop 0
	v_addc_co_u32_e32 v77, vcc, 0, v9, vcc
	global_load_dwordx4 v[174:177], v[76:77], off
	v_add_co_u32_e32 v76, vcc, s0, v8
	s_mov_b32 s0, 0x69000
	s_nop 0
	v_addc_co_u32_e32 v77, vcc, 0, v9, vcc
	global_load_dwordx4 v[66:69], v[66:67], off
	s_waitcnt vmcnt(14)
	v_pk_mul_f32 v[92:93], v[34:35], s[96:97] op_sel_hi:[1,0]
	global_load_dwordx4 v[178:181], v[76:77], off offset:2048
	v_add_co_u32_e32 v76, vcc, s0, v8
	s_mov_b32 s0, 0x6c000
	s_nop 0
	v_addc_co_u32_e32 v77, vcc, 0, v9, vcc
	v_add_co_u32_e32 v8, vcc, s0, v8
	global_load_dwordx4 v[182:185], v[76:77], off
	s_nop 0
	v_addc_co_u32_e32 v9, vcc, 0, v9, vcc
	global_load_dwordx4 v[186:189], v[8:9], off offset:2048
	v_pk_mul_f32 v[76:77], v[0:1], s[96:97] op_sel_hi:[1,0]
	v_lshlrev_b32_e32 v0, 1, v74
	v_and_b32_e32 v0, 0xffffffe0, v0
	v_pk_mul_f32 v[8:9], v[6:7], s[96:97] op_sel_hi:[1,0]
	v_lshl_add_u32 v6, s4, 4, v0
	v_or_b32_e32 v6, v6, v155
	v_lshl_add_u64 v[0:1], v[70:71], 0, v[72:73]
	s_mov_b64 s[0:1], 0x25f00000
	v_ashrrev_i32_e32 v7, 31, v6
	v_lshl_add_u64 v[0:1], v[0:1], 0, s[0:1]
	v_lshlrev_b64 v[70:71], 10, v[6:7]
	s_waitcnt vmcnt(16)
	v_pk_mul_f32 v[22:23], v[40:41], s[96:97] op_sel_hi:[1,0]
	v_pk_mul_f32 v[40:41], v[38:39], s[96:97] op_sel_hi:[1,0]
	s_waitcnt vmcnt(14)
	v_pk_mul_f32 v[102:103], v[50:51], s[96:97] op_sel_hi:[1,0]
	v_lshl_add_u64 v[74:75], v[0:1], 0, v[70:71]
	v_mov_b32_e32 v70, v81
	v_mov_b32_e32 v71, v81
	v_mov_b32_e32 v72, v81
	v_mov_b32_e32 v73, v81
	v_cvt_pk_fp8_f32 v70, v76, v78
	v_cvt_pk_fp8_f32 v71, v84, v88
	v_cvt_pk_fp8_f32 v72, v92, v40
	v_pk_mul_f32 v[94:95], v[30:31], s[96:97] op_sel_hi:[1,0]
	v_pk_mul_f32 v[104:105], v[46:47], s[96:97] op_sel_hi:[1,0]
	v_pk_mul_f32 v[38:39], v[118:119], s[96:97] op_sel_hi:[1,0]
	v_pk_mul_f32 v[46:47], v[126:127], s[96:97] op_sel_hi:[1,0]
	v_pk_mul_f32 v[118:119], v[128:129], s[96:97] op_sel_hi:[1,0]
	v_pk_mul_f32 v[50:51], v[134:135], s[96:97] op_sel_hi:[1,0]
	v_pk_mul_f32 v[14:15], v[24:25], s[96:97] op_sel_hi:[1,0]
	v_pk_mul_f32 v[18:19], v[32:33], s[96:97] op_sel_hi:[1,0]
	v_or_b32_e32 v40, 2, v6
	s_waitcnt vmcnt(13)
	v_pk_mul_f32 v[110:111], v[54:55], s[96:97] op_sel_hi:[1,0]
	v_pk_mul_f32 v[30:31], v[56:57], s[96:97] op_sel_hi:[1,0]
	v_cvt_pk_fp8_f32 v73, v102, v110
	s_waitcnt vmcnt(12)
	v_pk_mul_f32 v[126:127], v[144:145], s[96:97] op_sel_hi:[1,0]
	v_pk_mul_f32 v[54:55], v[142:143], s[96:97] op_sel_hi:[1,0]
	v_pk_mul_f32 v[56:57], v[146:147], s[96:97] op_sel_hi:[1,0]
	s_waitcnt vmcnt(11)
	v_pk_mul_f32 v[128:129], v[148:149], s[96:97] op_sel_hi:[1,0]
	s_waitcnt vmcnt(10)
	v_pk_mul_f32 v[82:83], v[10:11], s[96:97] op_sel_hi:[1,0]
	s_nop 0
	v_cvt_pk_fp8_f32 v70, v82, v86 op_sel:[0,0,1]
	v_pk_mul_f32 v[10:11], v[16:17], s[96:97] op_sel_hi:[1,0]
	s_waitcnt vmcnt(9)
	v_pk_mul_f32 v[90:91], v[26:27], s[96:97] op_sel_hi:[1,0]
	v_pk_mul_f32 v[16:17], v[28:29], s[96:97] op_sel_hi:[1,0]
	s_waitcnt vmcnt(8)
	v_pk_mul_f32 v[96:97], v[42:43], s[96:97] op_sel_hi:[1,0]
	v_cvt_pk_fp8_f32 v71, v90, v94 op_sel:[0,0,1]
	s_waitcnt vmcnt(7)
	v_pk_mul_f32 v[98:99], v[58:59], s[96:97] op_sel_hi:[1,0]
	v_cvt_pk_fp8_f32 v72, v96, v104 op_sel:[0,0,1]
	s_waitcnt vmcnt(6)
	v_pk_mul_f32 v[106:107], v[62:63], s[96:97] op_sel_hi:[1,0]
	v_pk_mul_f32 v[42:43], v[114:115], s[96:97] op_sel_hi:[1,0]
	v_cvt_pk_fp8_f32 v73, v98, v106 op_sel:[0,0,1]
	v_pk_mul_f32 v[114:115], v[124:125], s[96:97] op_sel_hi:[1,0]
	v_pk_mul_f32 v[124:125], v[140:141], s[96:97] op_sel_hi:[1,0]
	v_pk_mul_f32 v[24:25], v[44:45], s[96:97] op_sel_hi:[1,0]
	global_store_dwordx4 v[74:75], v[70:73], off
	v_pk_mul_f32 v[26:27], v[48:49], s[96:97] op_sel_hi:[1,0]
	s_waitcnt vmcnt(5)
	v_pk_mul_f32 v[132:133], v[174:175], s[96:97] op_sel_hi:[1,0]
	v_mov_b32_e32 v70, v81
	v_mov_b32_e32 v71, v81
	v_mov_b32_e32 v72, v81
	v_mov_b32_e32 v73, v81
	v_cvt_pk_fp8_f32 v71, v114, v118
	s_waitcnt vmcnt(4)
	v_pk_mul_f32 v[100:101], v[66:67], s[96:97] op_sel_hi:[1,0]
	v_cvt_pk_fp8_f32 v72, v124, v126
	s_waitcnt vmcnt(3)
	v_pk_mul_f32 v[134:135], v[178:179], s[96:97] op_sel_hi:[1,0]
	v_cvt_pk_fp8_f32 v70, v100, v108
	v_cvt_pk_fp8_f32 v73, v132, v134
	v_pk_mul_f32 v[28:29], v[52:53], s[96:97] op_sel_hi:[1,0]
	v_pk_mul_f32 v[44:45], v[122:123], s[96:97] op_sel_hi:[1,0]
	v_pk_mul_f32 v[48:49], v[130:131], s[96:97] op_sel_hi:[1,0]
	v_pk_mul_f32 v[52:53], v[138:139], s[96:97] op_sel_hi:[1,0]
	v_pk_mul_f32 v[122:123], v[136:137], s[96:97] op_sel_hi:[1,0]
	v_pk_mul_f32 v[130:131], v[158:159], s[96:97] op_sel_hi:[1,0]
	s_waitcnt vmcnt(2)
	v_pk_mul_f32 v[136:137], v[182:183], s[96:97] op_sel_hi:[1,0]
	v_cvt_pk_fp8_f32 v70, v112, v116 op_sel:[0,0,1]
	s_waitcnt vmcnt(1)
; __device__ __forceinline__ unsigned pk4_fp8(float a, float b, float c, float d) { int w = 0; w = __builtin_amdgcn_cvt_pk_fp8_f32(a, b, w, false); w = __builtin_amdgcn_cvt_pk_fp8_f32(c, d, w, true); return (unsigned)w; }
; #define GAS __attribute__((address_space(1)))
; template <int MODE, int KL>
; __device__ __forceinline__ void p0_cvt_item(const float* W, int K, int N, unsigned char* WT, int il, int which, int item, int lane, const float* gk, float scale, int ldk, int koff) {
;     const int nblk = N >> 6, kb = item / nblk, nb = item - kb * nblk, nq = lane & 15, kr = lane >> 4, k0 = 4 * KL * kb + KL * kr, n0 = 64 * nb + 4 * nq;
;     const GAS f32x4* src = (const GAS f32x4*)(W + (size_t)k0 * N + n0);
;     f32x4 v[KL];
; #pragma unroll
;     for (int i = 0; i < KL; ++i) v[i] = src[(size_t)i * (N >> 2)];
;     if (MODE == 1) {
; #pragma unroll
;         for (int q = 0; q < KL / 4; ++q) { const f32x4 g = *(const GAS f32x4*)(gk + k0 + 4 * q); v[4 * q] *= g.x; v[4 * q + 1] *= g.y; v[4 * q + 2] *= g.z; v[4 * q + 3] *= g.w; } }
;     if (MODE == 2) {
; #pragma unroll
;         for (int i = 0; i < KL; ++i) v[i] *= scale; }
; #pragma unroll
;     for (int c = 0; c < 4; ++c) { const int n = n0 + c, row = il ? ((n >> 4) * 32 + which * 16 + (n & 15)) : n;
;         if (MODE == 2) { GAS v4u* dst = (GAS v4u*)(WT + (size_t)row * ldk + koff + k0);
; #pragma unroll
;             for (int q = 0; q < KL / 16; ++q) { v4u o;
;                 o.x = pg8::pk4_fp8(v[16 * q][c], v[16 * q + 1][c], v[16 * q + 2][c], v[16 * q + 3][c]);     o.y = pg8::pk4_fp8(v[16 * q + 4][c], v[16 * q + 5][c], v[16 * q + 6][c], v[16 * q + 7][c]);
;                 o.z = pg8::pk4_fp8(v[16 * q + 8][c], v[16 * q + 9][c], v[16 * q + 10][c], v[16 * q + 11][c]); o.w = pg8::pk4_fp8(v[16 * q + 12][c], v[16 * q + 13][c], v[16 * q + 14][c], v[16 * q + 15][c]);
;                 dst[q] = o; } }
	v_pk_mul_f32 v[138:139], v[186:187], s[96:97] op_sel_hi:[1,0]
	v_cvt_pk_fp8_f32 v71, v120, v122 op_sel:[0,0,1]
	v_cvt_pk_fp8_f32 v72, v128, v130 op_sel:[0,0,1]
	v_cvt_pk_fp8_f32 v73, v136, v138 op_sel:[0,0,1]
	v_pk_mul_f32 v[4:5], v[12:13], s[96:97] op_sel_hi:[1,0]
	v_pk_mul_f32 v[12:13], v[20:21], s[96:97] op_sel_hi:[1,0]
	v_pk_mul_f32 v[20:21], v[36:37], s[96:97] op_sel_hi:[1,0]
	global_store_dwordx4 v[74:75], v[70:73], off offset:16
	v_pk_mul_f32 v[32:33], v[60:61], s[96:97] op_sel_hi:[1,0]
	v_pk_mul_f32 v[34:35], v[64:65], s[96:97] op_sel_hi:[1,0]
	v_or_b32_e32 v70, 1, v6
	v_ashrrev_i32_e32 v71, 31, v70
	v_lshlrev_b64 v[70:71], 10, v[70:71]
	v_lshl_add_u64 v[74:75], v[0:1], 0, v[70:71]
	v_mov_b32_e32 v70, v81
	v_mov_b32_e32 v71, v81
	v_mov_b32_e32 v72, v81
	v_mov_b32_e32 v73, v81
	v_cvt_pk_fp8_f32 v70, v77, v79
	v_cvt_pk_fp8_f32 v71, v85, v89
	v_cvt_pk_fp8_f32 v72, v93, v41
	v_cvt_pk_fp8_f32 v73, v103, v111
	v_cvt_pk_fp8_f32 v70, v83, v87 op_sel:[0,0,1]
	v_cvt_pk_fp8_f32 v71, v91, v95 op_sel:[0,0,1]
	v_cvt_pk_fp8_f32 v72, v97, v105 op_sel:[0,0,1]
	v_cvt_pk_fp8_f32 v73, v99, v107 op_sel:[0,0,1]
	v_ashrrev_i32_e32 v41, 31, v40
	v_lshlrev_b64 v[40:41], 10, v[40:41]
	v_lshl_add_u64 v[40:41], v[0:1], 0, v[40:41]
	global_store_dwordx4 v[74:75], v[70:73], off
	v_pk_mul_f32 v[36:37], v[68:69], s[96:97] op_sel_hi:[1,0]
	v_pk_mul_f32 v[62:63], v[176:177], s[96:97] op_sel_hi:[1,0]
	v_mov_b32_e32 v70, v81
	v_mov_b32_e32 v71, v81
	v_mov_b32_e32 v72, v81
	v_mov_b32_e32 v73, v81
	v_cvt_pk_fp8_f32 v70, v101, v109
	v_cvt_pk_fp8_f32 v71, v115, v119
	v_cvt_pk_fp8_f32 v72, v125, v127
	v_cvt_pk_fp8_f32 v73, v133, v135
	v_cvt_pk_fp8_f32 v70, v113, v117 op_sel:[0,0,1]
	v_cvt_pk_fp8_f32 v71, v121, v123 op_sel:[0,0,1]
	v_cvt_pk_fp8_f32 v72, v129, v131 op_sel:[0,0,1]
	v_cvt_pk_fp8_f32 v73, v137, v139 op_sel:[0,0,1]
	v_pk_mul_f32 v[64:65], v[180:181], s[96:97] op_sel_hi:[1,0]
	v_pk_mul_f32 v[58:59], v[150:151], s[96:97] op_sel_hi:[1,0]
	v_pk_mul_f32 v[60:61], v[160:161], s[96:97] op_sel_hi:[1,0]
	global_store_dwordx4 v[74:75], v[70:73], off offset:16
	v_pk_mul_f32 v[66:67], v[184:185], s[96:97] op_sel_hi:[1,0]
	v_pk_mul_f32 v[68:69], v[188:189], s[96:97] op_sel_hi:[1,0]
	v_mov_b32_e32 v70, v81
	v_mov_b32_e32 v71, v81
	v_mov_b32_e32 v72, v81
	v_mov_b32_e32 v73, v81
	v_cvt_pk_fp8_f32 v70, v2, v8
	v_cvt_pk_fp8_f32 v71, v12, v14
	v_cvt_pk_fp8_f32 v72, v20, v22
	v_cvt_pk_fp8_f32 v73, v28, v30
	v_cvt_pk_fp8_f32 v70, v4, v10 op_sel:[0,0,1]
	v_cvt_pk_fp8_f32 v71, v16, v18 op_sel:[0,0,1]
	v_cvt_pk_fp8_f32 v72, v24, v26 op_sel:[0,0,1]
	v_cvt_pk_fp8_f32 v73, v32, v34 op_sel:[0,0,1]
	v_or_b32_e32 v6, 3, v6
	v_ashrrev_i32_e32 v7, 31, v6
	v_lshlrev_b64 v[6:7], 10, v[6:7]
	global_store_dwordx4 v[40:41], v[70:73], off
	v_lshl_add_u64 v[0:1], v[0:1], 0, v[6:7]
	s_nop 0
	v_mov_b32_e32 v70, v81
	v_mov_b32_e32 v71, v81
	v_mov_b32_e32 v72, v81
	v_mov_b32_e32 v73, v81
	v_cvt_pk_fp8_f32 v70, v36, v42
	v_cvt_pk_fp8_f32 v71, v46, v48
	v_cvt_pk_fp8_f32 v72, v54, v56
	v_cvt_pk_fp8_f32 v73, v62, v64
	v_cvt_pk_fp8_f32 v70, v38, v44 op_sel:[0,0,1]
	v_cvt_pk_fp8_f32 v71, v50, v52 op_sel:[0,0,1]
	v_cvt_pk_fp8_f32 v72, v58, v60 op_sel:[0,0,1]
	v_cvt_pk_fp8_f32 v73, v66, v68 op_sel:[0,0,1]
	global_store_dwordx4 v[40:41], v[70:73], off offset:16
	s_branch .LBB0_929
; #define PG8_WAIT_V(n) asm volatile("s_waitcnt vmcnt(" #n ")" ::: "memory")
; #define PG8_BAR __builtin_amdgcn_s_barrier()
;     ...
;     for (int i = 0; i < 2; ++i) { int R, C; stage_rc(tid * 16 + i * 8192, R, C); const int Rb = Epi::PERM ? ((R & ~31) + perm32(R & 31)) : R;
;         voffA[i] = (unsigned)(R * K + C) * 2u; voffB[i] = (unsigned)(Rb * K + C) * 2u; }
;     const size_t kstep = (size_t)(BK * 2);
;     const size_t hstep = (size_t)HALF * K * 2;
;     const size_t tstep = 2 * hstep;
;     const unsigned ldsw = (unsigned)wid * 1024u;
;     const int aoff = lds_byte(wr * 64 + fr, fq * 8), boff = lds_byte(wc * 32 + fr, fq * 8);
;     ...
;     Unit cur, nxt; int ui = 0;
;     if (!S.next(0, cur)) return;
;     f32x4 acc[2][2][4][2];
; #pragma unroll
;     for (int a = 0; a < 2; ++a)
; #pragma unroll
;         for (int b = 0; b < 2; ++b)
; #pragma unroll
;             for (int m = 0; m < 4; ++m)
; #pragma unroll
;                 for (int n = 0; n < 2; ++n) acc[a][b][m][n] = (f32x4){0.f, 0.f, 0.f, 0.f};
;     bf16x8 At[4][2], B0[2][2], B1[2][2];
;     int sc7f = 0x7F7F7F7F; asm volatile("" : "+v"(sc7f));
;     pg8_v8i At8[4], B08[2], B18[2];
;     const char* cA = (const char*)g.A + (size_t)cur.pm * tstep; const char* cB = (const char*)g.Bt + (size_t)cur.pn * tstep;
;     S.a_ready(cur);
;     if constexpr (SP2) {
;         PG8_STAGE(PG8_SB(0, 0), cB, voffB); PG8_STAGE(PG8_SB(0, 1), cB + hstep, voffB); PG8_STAGE(PG8_SA(0, 0), cA, voffA); PG8_STAGE(PG8_SA(0, 1), cA + hstep, voffA);
;         if (wr == 1) PG8_BAR;
;         PG8_WAIT_V(2); PG8_BAR;
; __global__ void __launch_bounds__(NWAVES * 64, 2) mk_fwd(Args args) {
;     ...
;                   const int nun = (M / 256) * (2 * FD / 256), nfull = nun / F.G, nbusy = nun - nfull * F.G, nsub = F.G - nbusy;
;                   pg8::SubOrder Sp{nsub > 0 ? (bix >= nbusy ? bix - nbusy : -1) : bix, nsub > 0 ? nsub : F.G, (M / 256) * (D / 256)};
;                   int kple = PLE; asm volatile("" : "+s"(kple));
;                   pg8::Gemm gp{(const bf16*)(ws + WS_PB) + (size_t)l * M * PLE, (const bf16*)(ws + W_PP) + (size_t)l * D * PLE, M, D, kple};
;                   pg8::EpiBfPlain Ep{mg, D};
;                   pg8::gemm_phase<pg8::EpiBfPlain, pg8::SubOrder, true, true>(F.lds + RING_OFF, gp, Sp, Ep, tidv); }
.LBB0_934:
	v_mov_b32_e32 v0, v81
	v_readlane_b32 s0, v254, 25
	v_mbcnt_lo_u32_b32 v0, -1, v0
	v_mbcnt_hi_u32_b32 v0, -1, v0
	v_readlane_b32 s4, v254, 2
	v_readlane_b32 s1, v255, 18
	v_add_u32_e32 v6, s0, v0
	s_sub_i32 s0, s4, s1
	s_cmp_ge_i32 s4, s1
	s_cselect_b32 s5, s0, -1
	v_readlane_b32 s0, v255, 19
	v_readlane_b32 s1, v255, 20
	s_and_b64 s[0:1], s[0:1], exec
	s_mov_b32 s22, s4
	s_movk_i32 s4, 0x100
	s_cmpk_gt_u32 s22, 0xff
	v_readfirstlane_b32 s14, v6
	s_cbranch_scc1 .LBB0_953
	v_lshlrev_b32_e32 v3, 4, v6
	v_add_u32_e32 v0, 0x2000, v3
	s_waitcnt lgkmcnt(0)
	v_ashrrev_i32_e32 v1, 31, v0
	v_lshrrev_b32_e32 v1, 22, v1
	v_readlane_b32 s6, v255, 40
	v_add_u32_e32 v1, v0, v1
	v_readlane_b32 s7, v255, 41
	v_ashrrev_i32_e32 v1, 10, v1
	s_mov_b32 s7, s63
	v_mul_i32_i24_e32 v2, 0x400, v1
	s_lshl_b64 s[0:1], s[6:7], 23
	v_sub_u32_e32 v0, v0, v2
	s_add_u32 s0, s80, s0
	v_lshrrev_b32_e32 v2, 4, v0
	s_addc_u32 s1, s81, s1
	v_bitop3_b32 v2, v2, v0, 32 bitop3:0x6c
	s_add_u32 s23, s0, 0x1de00000
	s_mov_b32 s0, s6
	v_ashrrev_i32_e32 v0, 31, v2
	s_addc_u32 s24, s1, 0
	v_writelane_b32 v255, s0, 40
	v_lshrrev_b32_e32 v0, 26, v0
	v_add_u32_e32 v4, v2, v0
	v_writelane_b32 v255, s1, 41
	s_lshl_b64 s[0:1], s[6:7], 19
	v_lshlrev_b32_e32 v5, 3, v1
	s_add_u32 s0, s80, s0
	v_ashrrev_i32_e32 v0, 6, v4
	v_and_b32_e32 v5, -16, v5
	s_addc_u32 s1, s81, s1
	v_add_u32_e32 v5, v0, v5
	s_add_u32 s25, s0, 0x23c00000
	v_and_b32_e32 v0, 3, v0
	s_mov_b32 s0, 0x7fffffe0
	v_lshrrev_b32_e32 v7, 2, v5
	v_lshlrev_b32_e32 v8, 1, v5
	v_and_or_b32 v0, v5, s0, v0
	v_and_b32_e32 v7, 4, v7
	v_and_b32_e32 v8, 24, v8
	v_or3_b32 v0, v0, v7, v8
	v_mul_lo_u32 v7, v0, s4
	v_lshlrev_b32_e32 v0, 5, v1
	v_and_b32_e32 v1, 0xc0, v4
	v_sub_u32_e32 v1, v2, v1
	v_ashrrev_i16_sdwa v1, v163, sext(v1) dst_sel:DWORD dst_unused:UNUSED_PAD src0_sel:DWORD src1_sel:BYTE_0
	v_and_b32_e32 v0, 32, v0
	v_bfe_i32 v1, v1, 0, 16
	v_add_u32_e32 v4, v0, v1
	v_mul_lo_u32 v2, v5, s4
	v_add_lshl_u32 v130, v7, v4, 1
	v_add_lshl_u32 v132, v4, v2, 1
	v_bfe_i32 v4, v6, 27, 1
	v_lshrrev_b32_e32 v4, 22, v4
	v_add_u32_e32 v4, v3, v4
	v_and_b32_e32 v4, 0xfffffc00, v4
	v_sub_u32_e32 v3, v3, v4
	v_lshrrev_b32_e32 v4, 4, v3
	v_ashrrev_i32_e32 v7, 31, v6
	v_bitop3_b32 v4, v4, v3, 32 bitop3:0x6c
	v_lshrrev_b32_e32 v7, 26, v7
	v_ashrrev_i32_e32 v3, 31, v4
	v_add_u32_e32 v7, v6, v7
	v_lshrrev_b32_e32 v3, 26, v3
	v_ashrrev_i32_e32 v7, 6, v7
	v_add_u32_e32 v5, v4, v3
	v_lshlrev_b32_e32 v8, 3, v7
	v_ashrrev_i32_e32 v3, 6, v5
	v_and_b32_e32 v8, -16, v8
	s_addc_u32 s26, s1, 0
	s_ashr_i32 s5, s4, 31
	v_add_u32_e32 v8, v3, v8
	v_and_b32_e32 v3, 3, v3
	s_lshl_b64 s[8:9], s[4:5], 9
	s_lshr_b32 s37, s22, 2
	v_and_or_b32 v3, v8, s0, v3
	v_lshrrev_b32_e32 v9, 2, v8
	v_lshlrev_b32_e32 v10, 1, v8
	s_lshr_b64 s[0:1], s[4:5], 23
	s_and_b32 s38, s22, 3
	v_and_b32_e32 v9, 4, v9
	v_and_b32_e32 v10, 24, v10
	v_and_b32_e32 v5, 0xc0, v5
	s_mul_i32 s1, s0, s37
	s_mul_hi_u32 s10, s8, s37
	s_ashr_i32 s15, s14, 6
	v_or3_b32 v3, v3, v9, v10
	v_sub_u32_e32 v4, v4, v5
	s_add_i32 s10, s10, s1
	s_mul_i32 s0, s0, s38
	s_mul_hi_u32 s1, s8, s38
	s_ashr_i32 s16, s14, 8
	s_lshl_b64 s[6:7], s[4:5], 8
	s_lshl_b32 s27, s15, 10
	v_mul_lo_u32 v9, v3, s4
	v_lshlrev_b32_e32 v3, 5, v7
	v_ashrrev_i16_sdwa v4, v163, sext(v4) dst_sel:DWORD dst_unused:UNUSED_PAD src0_sel:DWORD src1_sel:BYTE_0
	s_add_i32 s1, s1, s0
	s_mul_i32 s0, s8, s38
	v_and_b32_e32 v3, 32, v3
	v_bfe_i32 v4, v4, 0, 16
	s_add_u32 s0, s25, s0
	v_add_u32_e32 v7, v3, v4
	v_mul_lo_u32 v5, v8, s4
	s_addc_u32 s1, s26, s1
	s_add_i32 s28, s27, 0
	v_add_lshl_u32 v80, v9, v7, 1
	v_add_lshl_u32 v134, v7, v5, 1
	v_mov_b32_e32 v7, 0x7f7f7f7f
	s_add_i32 m0, s28, 0x10000
	s_mul_i32 s11, s8, s37
	global_load_lds_dwordx4 v80, s[0:1]
	s_add_i32 m0, s28, 0x12000
	s_add_u32 s12, s0, s6
	global_load_lds_dwordx4 v130, s[0:1]
	s_addc_u32 s13, s1, s7
	s_add_i32 m0, s28, 0x14000
	s_nop 0
	global_load_lds_dwordx4 v80, s[12:13]
	s_add_i32 m0, s28, 0x16000
	s_add_u32 s20, s23, s11
	s_addc_u32 s21, s24, s10
	s_add_i32 s29, s28, 0x2000
	global_load_lds_dwordx4 v130, s[12:13]
	s_mov_b32 m0, s28
	s_add_u32 s10, s20, s6
	global_load_lds_dwordx4 v134, s[20:21]
	s_mov_b32 m0, s29
	s_addc_u32 s11, s21, s7
	s_add_i32 s30, s28, 0x4000
	global_load_lds_dwordx4 v132, s[20:21]
	s_mov_b32 m0, s30
	s_add_i32 s31, s28, 0x6000
	global_load_lds_dwordx4 v134, s[10:11]
	s_mov_b32 m0, s31
	s_cmp_eq_u32 s16, 1
	global_load_lds_dwordx4 v132, s[10:11]
	s_cselect_b64 s[10:11], -1, 0
	s_cmp_lg_u32 s16, 1
	s_cbranch_scc1 .LBB0_937
	s_barrier

;     ...
;         const bool has_next = S.next(ui + 1, nxt);
;         const char* nA = has_next ? (const char*)g.A + (size_t)nxt.pm * tstep : cA; const char* nB = has_next ? (const char*)g.Bt + (size_t)nxt.pn * tstep : cB;
;         for (int t = 0; t < nt; t += 2) {
;             if constexpr (MID) { if (t == (nt >> 1)) E.mid(acc, cur, wr, wc); }
;             const bool last = (t == nt - 2);
;             const char* a1 = cA + (size_t)(t + 1) * kstep;
;             const char* a2 = last ? nA : cA + (size_t)(t + 2) * kstep; const char* b2 = last ? nB : cB + (size_t)(t + 2) * kstep;
;     __device__ __forceinline__ bool next(int i, Unit& u) const { if (j < 0) return false; const int L = i * nsub + j; if (L >= n) return false; u.pm = L >> 2; u.pn = L & 3; return true; }
.LBB0_940:
	s_add_i32 s42, s42, 1
	v_readlane_b32 s4, v255, 21
	s_lshl_b32 s4, s42, 8
	s_add_i32 s4, s4, s22
	s_cmpk_lt_i32 s4, 0x100
	s_cselect_b64 s[18:19], -1, 0
	s_ashr_i32 s43, s4, 2
	s_cmpk_gt_i32 s4, 0xff
	s_cbranch_scc1 .LBB0_942
	s_ashr_i32 s5, s43, 31
	s_mul_hi_u32 s16, s8, s43
	s_mul_i32 s5, s8, s5
	s_add_i32 s5, s16, s5
	s_mul_i32 s16, s9, s43
	s_add_i32 s5, s5, s16
	s_mul_i32 s16, s8, s43
	s_add_u32 s16, s23, s16
	s_addc_u32 s17, s24, s5

; __device__ __forceinline__ unsigned cvtpk(float lo, float hi) { f32x2_t v = {lo, hi}; bf16x2_t b = __builtin_convertvector(v, bf16x2_t); return __builtin_bit_cast(unsigned, b); }
;     __device__ __forceinline__ void operator()(const f32x4 (&acc)[2][2][4][2], const Unit& u, int wr, int wc, int fr, int fq) const {
;         { int z_ = 0; asm volatile("" : "+v"(z_)); const int l_ = (int)__builtin_amdgcn_mbcnt_hi(~0u, __builtin_amdgcn_mbcnt_lo(~0u, (unsigned)z_)); fr = l_ & 15; fq = l_ >> 4; }
;         const int row0 = u.pm * BM + wr * 64 + fr, col0 = u.pn * BM + wc * 32 + 8 * fq;
; #pragma unroll
;         for (int ai = 0; ai < 2; ++ai)
; #pragma unroll
;             for (int m = 0; m < 4; ++m) { bf16_t* rowp = O + (size_t)(row0 + ai * HALF + m * 16) * ldc + col0;
; #pragma unroll
;                 for (int bj = 0; bj < 2; ++bj) { const f32x4 v0 = acc[ai][bj][m][0], v1 = acc[ai][bj][m][1];
;                     u32x4 w; w.x = cvtpk(v0[0], v0[1]); w.y = cvtpk(v0[2], v0[3]); w.z = cvtpk(v1[0], v1[1]); w.w = cvtpk(v1[2], v1[3]);
;                     *(u32x4*)(rowp + bj * HALF) = w; } }
;     }
.LBB0_949:
	v_mov_b32_e32 v142, v81
	s_lshl_b32 s0, s38, 8
	v_mbcnt_lo_u32_b32 v142, -1, v142
	v_mbcnt_hi_u32_b32 v143, -1, v142
	v_ashrrev_i32_e32 v142, 1, v143
	v_and_or_b32 v143, v143, 15, s35
	v_and_b32_e32 v142, -8, v142
	s_or_b32 s0, s0, s36
	v_lshl_add_u32 v144, s37, 8, v143
	v_add_u32_e32 v142, s0, v142
	v_ashrrev_i32_e32 v145, 31, v144
	v_ashrrev_i32_e32 v143, 31, v142
	v_lshlrev_b64 v[146:147], 11, v[144:145]
	v_lshl_add_u64 v[146:147], s[70:71], 0, v[146:147]
	v_lshlrev_b64 v[142:143], 1, v[142:143]
	v_lshl_add_u64 v[146:147], v[146:147], 0, v[142:143]
	s_mov_b64 s[0:1], 0x40000
	v_cvt_pk_bf16_f32 v68, v68, v69
	v_cvt_pk_bf16_f32 v69, v70, v71
	v_cvt_pk_bf16_f32 v70, v64, v65
	v_lshl_add_u64 v[64:65], v[146:147], 0, s[0:1]
	s_mov_b32 s0, 0x40000
	v_cvt_pk_bf16_f32 v60, v60, v61
	v_cvt_pk_bf16_f32 v61, v62, v63
	v_cvt_pk_bf16_f32 v62, v56, v57
	v_add_co_u32_e32 v56, vcc, s0, v146
	s_mov_b64 s[0:1], 0x48000
	s_nop 0
	v_addc_co_u32_e32 v57, vcc, 0, v147, vcc
	v_cvt_pk_bf16_f32 v52, v52, v53
	v_cvt_pk_bf16_f32 v53, v54, v55
	v_cvt_pk_bf16_f32 v54, v48, v49
	v_lshl_add_u64 v[48:49], v[146:147], 0, s[0:1]
	s_mov_b32 s0, 0x48000
	v_cvt_pk_bf16_f32 v44, v44, v45
	v_cvt_pk_bf16_f32 v45, v46, v47
	v_cvt_pk_bf16_f32 v46, v40, v41
	v_add_co_u32_e32 v40, vcc, s0, v146
	s_mov_b64 s[0:1], 0x50000
	s_nop 0
	v_addc_co_u32_e32 v41, vcc, 0, v147, vcc
	v_cvt_pk_bf16_f32 v36, v36, v37
	v_cvt_pk_bf16_f32 v37, v38, v39
	v_cvt_pk_bf16_f32 v38, v32, v33
	v_lshl_add_u64 v[32:33], v[146:147], 0, s[0:1]
	s_mov_b32 s0, 0x50000
	v_cvt_pk_bf16_f32 v118, v118, v119
	v_cvt_pk_bf16_f32 v119, v120, v121
	v_cvt_pk_bf16_f32 v120, v114, v115
	v_or_b32_e32 v114, 16, v144
	v_cvt_pk_bf16_f32 v102, v102, v103
	v_cvt_pk_bf16_f32 v103, v104, v105
	v_cvt_pk_bf16_f32 v104, v98, v99
	v_or_b32_e32 v98, 32, v144
	v_cvt_pk_bf16_f32 v86, v86, v87
	v_cvt_pk_bf16_f32 v87, v88, v89
	v_cvt_pk_bf16_f32 v88, v82, v83
	v_or_b32_e32 v82, 48, v144
	v_cvt_pk_bf16_f32 v28, v28, v29
	v_cvt_pk_bf16_f32 v29, v30, v31
	v_cvt_pk_bf16_f32 v30, v24, v25
	v_add_co_u32_e32 v24, vcc, s0, v146
	s_mov_b64 s[0:1], 0x58000
	v_ashrrev_i32_e32 v115, 31, v114
	v_ashrrev_i32_e32 v99, 31, v98
	v_ashrrev_i32_e32 v83, 31, v82
	v_addc_co_u32_e32 v25, vcc, 0, v147, vcc
	v_cvt_pk_bf16_f32 v20, v20, v21
	v_cvt_pk_bf16_f32 v21, v22, v23
	v_cvt_pk_bf16_f32 v22, v16, v17
	v_lshl_add_u64 v[16:17], v[146:147], 0, s[0:1]
	s_mov_b32 s0, 0x58000
	v_lshlrev_b64 v[114:115], 11, v[114:115]
	v_lshlrev_b64 v[98:99], 11, v[98:99]
	v_lshlrev_b64 v[82:83], 11, v[82:83]
	v_cvt_pk_bf16_f32 v12, v12, v13
	v_cvt_pk_bf16_f32 v13, v14, v15
	v_cvt_pk_bf16_f32 v14, v8, v9
	v_add_co_u32_e32 v8, vcc, s0, v146
	v_lshl_add_u64 v[114:115], s[70:71], 0, v[114:115]
	v_lshl_add_u64 v[98:99], s[70:71], 0, v[98:99]
	v_lshl_add_u64 v[82:83], s[70:71], 0, v[82:83]
	v_addc_co_u32_e32 v9, vcc, 0, v147, vcc
	v_cvt_pk_bf16_f32 v122, v122, v123
	v_cvt_pk_bf16_f32 v123, v124, v125
	v_cvt_pk_bf16_f32 v124, v126, v127
	v_cvt_pk_bf16_f32 v125, v128, v129
	v_cvt_pk_bf16_f32 v121, v116, v117
	v_lshl_add_u64 v[114:115], v[114:115], 0, v[142:143]
	v_cvt_pk_bf16_f32 v110, v110, v111
	v_cvt_pk_bf16_f32 v111, v112, v113
	v_cvt_pk_bf16_f32 v112, v106, v107
	v_cvt_pk_bf16_f32 v113, v108, v109
	v_cvt_pk_bf16_f32 v105, v100, v101
	v_lshl_add_u64 v[98:99], v[98:99], 0, v[142:143]
	v_cvt_pk_bf16_f32 v94, v94, v95
	v_cvt_pk_bf16_f32 v95, v96, v97
	v_cvt_pk_bf16_f32 v96, v90, v91
	v_cvt_pk_bf16_f32 v97, v92, v93
	v_cvt_pk_bf16_f32 v89, v84, v85
	v_lshl_add_u64 v[82:83], v[82:83], 0, v[142:143]
	v_cvt_pk_bf16_f32 v76, v76, v77
	v_cvt_pk_bf16_f32 v77, v78, v79
	v_cvt_pk_bf16_f32 v78, v72, v73
	v_cvt_pk_bf16_f32 v79, v74, v75
	v_cvt_pk_bf16_f32 v71, v66, v67
	v_cvt_pk_bf16_f32 v63, v58, v59
	v_cvt_pk_bf16_f32 v55, v50, v51
	v_cvt_pk_bf16_f32 v47, v42, v43
	v_cvt_pk_bf16_f32 v39, v34, v35
	v_cvt_pk_bf16_f32 v31, v26, v27
	v_cvt_pk_bf16_f32 v23, v18, v19
	v_cvt_pk_bf16_f32 v15, v10, v11
	v_cvt_pk_bf16_f32 v4, v4, v5
	v_cvt_pk_bf16_f32 v5, v6, v7
	v_cvt_pk_bf16_f32 v6, v0, v1
	v_cvt_pk_bf16_f32 v7, v2, v3
	s_and_b64 vcc, exec, s[4:5]
	s_mov_b64 s[0:1], -1
	global_store_dwordx4 v[146:147], v[122:125], off
	global_store_dwordx4 v[146:147], v[118:121], off offset:256
	global_store_dwordx4 v[114:115], v[110:113], off
	global_store_dwordx4 v[114:115], v[102:105], off offset:256
	global_store_dwordx4 v[98:99], v[94:97], off
	global_store_dwordx4 v[98:99], v[86:89], off offset:256
	global_store_dwordx4 v[82:83], v[76:79], off
	global_store_dwordx4 v[82:83], v[68:71], off offset:256
	global_store_dwordx4 v[56:57], v[60:63], off
	global_store_dwordx4 v[64:65], v[52:55], off offset:256
	global_store_dwordx4 v[40:41], v[44:47], off
	global_store_dwordx4 v[48:49], v[36:39], off offset:256
	global_store_dwordx4 v[24:25], v[28:31], off
	global_store_dwordx4 v[32:33], v[20:23], off offset:256
	global_store_dwordx4 v[8:9], v[12:15], off
	global_store_dwordx4 v[16:17], v[4:7], off offset:256
	s_cbranch_vccnz .LBB0_939
	s_andn2_b64 vcc, exec, s[10:11]
	s_cbranch_vccnz .LBB0_938
	s_barrier
	s_branch .LBB0_938

; __device__ __forceinline__ float row_rstd(const float* ssp, size_t row) {
;     const f32x4* p = (const f32x4*)(ssp + row * 16); const f32x4 a = p[0], b = p[1], c = p[2], d = p[3];
;     const float s = (((a[0] + a[1]) + (a[2] + a[3])) + ((b[0] + b[1]) + (b[2] + b[3]))) + (((c[0] + c[1]) + (c[2] + c[3])) + ((d[0] + d[1]) + (d[2] + d[3])));
;     return rsqrtf(s * (1.f / 1024.f) + 1e-6f);
; }
.LBB0_955:
	v_mbcnt_lo_u32_b32 v0, -1, v0
	v_mbcnt_hi_u32_b32 v0, -1, v0
	v_readlane_b32 s4, v254, 25
	s_nop 1
	v_add_u32_e32 v0, s4, v0
	s_movk_i32 s4, 0x100
	v_cmp_gt_i32_e32 vcc, s4, v0
	s_and_saveexec_b64 s[4:5], vcc
	s_cbranch_execz .LBB0_957
	s_waitcnt lgkmcnt(0)
	v_ashrrev_i32_e32 v1, 31, v0
	v_lshl_add_u64 v[2:3], s[6:7], 0, v[0:1]
	v_lshlrev_b64 v[2:3], 6, v[2:3]
	v_lshl_add_u64 v[2:3], s[80:81], 0, v[2:3]
	s_mov_b64 s[6:7], 0x300000
	v_lshl_add_u64 v[14:15], v[2:3], 0, s[6:7]
	v_add_co_u32_e32 v2, vcc, 0x300000, v2
	s_nop 1
	v_addc_co_u32_e32 v3, vcc, 0, v3, vcc
	global_load_dwordx4 v[2:5], v[2:3], off
	s_nop 0
	global_load_dwordx4 v[6:9], v[14:15], off offset:16
	global_load_dwordx4 v[10:13], v[14:15], off offset:32
	s_nop 0
	global_load_dwordx4 v[14:17], v[14:15], off offset:48
	s_waitcnt vmcnt(0) lgkmcnt(0)
	v_mov_b32_e32 v18, v2
	v_mov_b32_e32 v19, v10
	v_mov_b32_e32 v10, v3
	v_pk_add_f32 v[2:3], v[18:19], v[10:11]
	v_mov_b32_e32 v10, v4
	v_mov_b32_e32 v11, v12
	v_mov_b32_e32 v12, v5
	v_pk_add_f32 v[4:5], v[10:11], v[12:13]
	s_nop 0
	v_pk_add_f32 v[2:3], v[2:3], v[4:5]
	v_mov_b32_e32 v4, v6
	v_mov_b32_e32 v5, v14
	v_mov_b32_e32 v14, v7
	v_mov_b32_e32 v6, v8
	v_mov_b32_e32 v7, v16
	v_mov_b32_e32 v16, v9
	v_pk_add_f32 v[4:5], v[4:5], v[14:15]
	v_pk_add_f32 v[6:7], v[6:7], v[16:17]
	s_nop 0
	v_pk_add_f32 v[4:5], v[4:5], v[6:7]
	s_nop 0
	v_pk_add_f32 v[2:3], v[2:3], v[4:5]
	s_nop 0
	v_add_f32_e32 v1, v2, v3
	v_fmamk_f32 v1, v1, 0x3a800000, v162
	v_cmp_gt_f32_e32 vcc, s85, v1
	v_mul_f32_e32 v2, 0x4b800000, v1
	s_nop 0
	v_cndmask_b32_e32 v1, v1, v2, vcc
	v_rsq_f32_e32 v1, v1
	s_nop 0
	v_mul_f32_e32 v2, 0x45800000, v1
	v_cndmask_b32_e32 v1, v1, v2, vcc
	v_lshl_add_u32 v2, v0, 2, 0
	v_add_u32_e32 v2, 0x20400, v2
	ds_write_b32 v2, v1

; __device__ __forceinline__ unsigned cvtpk(float lo, float hi) { f32x2_t v = {lo, hi}; bf16x2_t b = __builtin_convertvector(v, bf16x2_t); return __builtin_bit_cast(unsigned, b); }
; __device__ __forceinline__ f32x4 swiglu4(f32x4 a, f32x4 b, float k1, float k3) {
;     const f32x2v a0 = {a[0], a[1]}, a1 = {a[2], a[3]}, b0 = {b[0], b[1]}, b1 = {b[2], b[3]};
;     const f32x2v t0 = a0 * k1, t1 = a1 * k1;
;     const f32x2v e0 = {__builtin_amdgcn_exp2f(t0[0]), __builtin_amdgcn_exp2f(t0[1])}, e1 = {__builtin_amdgcn_exp2f(t1[0]), __builtin_amdgcn_exp2f(t1[1])};
;     const f32x2v d0 = e0 * k3 + k3, d1 = e1 * k3 + k3;
;     const f32x2v r0 = {__builtin_amdgcn_rcpf(d0[0]), __builtin_amdgcn_rcpf(d0[1])}, r1 = {__builtin_amdgcn_rcpf(d1[0]), __builtin_amdgcn_rcpf(d1[1])};
;     const f32x2v y0 = (a0 * b0) * r0, y1 = (a1 * b1) * r1;
;     return (f32x4){y0[0], y0[1], y1[0], y1[1]};
;     __device__ __forceinline__ void operator()(const f32x4 (&acc)[2][2][4][2], const Unit& u, int wr, int wc, int fr, int fq) const {
;         const int row0 = u.pm * BM + wr * 64 + fr, hc0 = u.pn * 128 + wc * 16 + 4 * fq;
; #pragma unroll
;         for (int ai = 0; ai < 2; ++ai)
; #pragma unroll
;             for (int m = 0; m < 4; ++m) { const size_t r = (size_t)(row0 + ai * HALF + m * 16); const float s = tbl[wr * 64 + fr + ai * HALF + m * 16];     bf16_t* rowp = O + r * ldc + hc0; const float k1 = s * -1.44269504f, k3 = __builtin_amdgcn_rcpf(s * s);
; #pragma unroll
;                 for (int bj = 0; bj < 2; ++bj) { const f32x4 y = swiglu4(acc[ai][bj][m][0], acc[ai][bj][m][1], k1, k3);
;                     u32x2 w; w.x = cvtpk(y[0], y[1]); w.y = cvtpk(y[2], y[3]);
;                     *(u32x2*)(rowp + bj * 64) = w; } }
;     }
.LBB0_969:
	ds_read_b32 v149, v143
	v_pk_mul_f32 v[124:125], v[128:129], v[124:125]
	v_pk_mul_f32 v[122:123], v[126:127], v[122:123]
	v_lshl_or_b32 v138, s37, 7, v142
	v_lshl_add_u32 v145, s18, 8, v140
	s_waitcnt lgkmcnt(0)
	v_mul_f32_e32 v148, 0xbfb8aa3b, v149
	v_mul_f32_e32 v149, v149, v149
	v_pk_mul_f32 v[152:153], v[126:127], v[148:149] op_sel_hi:[1,0]
	v_pk_mul_f32 v[154:155], v[128:129], v[148:149] op_sel_hi:[1,0]
	v_rcp_f32_e32 v150, v149
	v_exp_f32_e32 v152, v152
	v_exp_f32_e32 v153, v153
	v_exp_f32_e32 v154, v154
	v_exp_f32_e32 v155, v155
	v_pk_mul_f32 v[126:127], v[118:119], v[148:149] op_sel_hi:[1,0]
	v_pk_fma_f32 v[152:153], v[150:151], v[152:153], v[150:151] op_sel_hi:[0,1,0]
	v_rcp_f32_e32 v152, v152
	v_pk_fma_f32 v[154:155], v[150:151], v[154:155], v[150:151] op_sel_hi:[0,1,0]
	v_rcp_f32_e32 v153, v153
	v_rcp_f32_e32 v154, v154
	v_rcp_f32_e32 v155, v155
	v_pk_mul_f32 v[128:129], v[120:121], v[148:149] op_sel_hi:[1,0]
	v_exp_f32_e32 v126, v126
	v_exp_f32_e32 v127, v127
	v_exp_f32_e32 v128, v128
	v_exp_f32_e32 v129, v129
	v_ashrrev_i32_e32 v139, 31, v138
	v_mov_b64_e32 v[136:137], s[68:69]
	s_movk_i32 s11, 0x1600
	v_mad_i64_i32 v[146:147], s[0:1], v145, s11, v[136:137]
	v_lshlrev_b64 v[138:139], 1, v[138:139]
	v_pk_mul_f32 v[122:123], v[122:123], v[152:153]
	v_pk_mul_f32 v[124:125], v[124:125], v[154:155]
	v_lshl_add_u64 v[146:147], v[146:147], 0, v[138:139]
	v_cvt_pk_bf16_f32 v122, v122, v123
	v_cvt_pk_bf16_f32 v123, v124, v125
	global_store_dwordx2 v[146:147], v[122:123], off
	v_pk_fma_f32 v[122:123], v[150:151], v[126:127], v[150:151] op_sel_hi:[0,1,0]
	v_pk_fma_f32 v[124:125], v[150:151], v[128:129], v[150:151] op_sel_hi:[0,1,0]
	v_rcp_f32_e32 v122, v122
	v_rcp_f32_e32 v123, v123
	v_rcp_f32_e32 v124, v124
	v_rcp_f32_e32 v125, v125
	v_pk_mul_f32 v[116:117], v[120:121], v[116:117]
	v_pk_mul_f32 v[114:115], v[118:119], v[114:115]
	v_pk_mul_f32 v[108:109], v[112:113], v[108:109]
	v_pk_mul_f32 v[114:115], v[114:115], v[122:123]
	v_pk_mul_f32 v[116:117], v[116:117], v[124:125]
	v_cvt_pk_bf16_f32 v114, v114, v115
	v_cvt_pk_bf16_f32 v115, v116, v117
	global_store_dwordx2 v[146:147], v[114:115], off offset:128
	ds_read_b32 v115, v143 offset:64
	v_or_b32_e32 v117, 16, v145
	v_pk_mul_f32 v[106:107], v[110:111], v[106:107]
	v_mad_i64_i32 v[122:123], s[0:1], v117, s11, v[136:137]
	s_waitcnt lgkmcnt(0)
	v_mul_f32_e32 v114, 0xbfb8aa3b, v115
	v_mul_f32_e32 v115, v115, v115
	v_pk_mul_f32 v[118:119], v[110:111], v[114:115] op_sel_hi:[1,0]
	v_pk_mul_f32 v[120:121], v[112:113], v[114:115] op_sel_hi:[1,0]
	v_rcp_f32_e32 v116, v115
	v_exp_f32_e32 v118, v118
	v_exp_f32_e32 v119, v119
	v_exp_f32_e32 v120, v120
	v_exp_f32_e32 v121, v121
	v_pk_mul_f32 v[110:111], v[102:103], v[114:115] op_sel_hi:[1,0]
	v_pk_fma_f32 v[118:119], v[116:117], v[118:119], v[116:117] op_sel_hi:[0,1,0]
	v_rcp_f32_e32 v118, v118
	v_pk_fma_f32 v[120:121], v[116:117], v[120:121], v[116:117] op_sel_hi:[0,1,0]
	v_rcp_f32_e32 v119, v119
	v_rcp_f32_e32 v120, v120
	v_rcp_f32_e32 v121, v121
	v_pk_mul_f32 v[112:113], v[104:105], v[114:115] op_sel_hi:[1,0]
	v_exp_f32_e32 v110, v110
	v_exp_f32_e32 v111, v111
	v_exp_f32_e32 v112, v112
	v_exp_f32_e32 v113, v113
	v_pk_mul_f32 v[106:107], v[106:107], v[118:119]
	v_pk_mul_f32 v[108:109], v[108:109], v[120:121]
	v_lshl_add_u64 v[122:123], v[122:123], 0, v[138:139]
	v_cvt_pk_bf16_f32 v106, v106, v107
	v_cvt_pk_bf16_f32 v107, v108, v109
	global_store_dwordx2 v[122:123], v[106:107], off
	v_pk_fma_f32 v[106:107], v[116:117], v[110:111], v[116:117] op_sel_hi:[0,1,0]
	v_pk_fma_f32 v[108:109], v[116:117], v[112:113], v[116:117] op_sel_hi:[0,1,0]
	v_rcp_f32_e32 v106, v106
	v_rcp_f32_e32 v107, v107
	v_rcp_f32_e32 v108, v108
	v_rcp_f32_e32 v109, v109
	v_pk_mul_f32 v[100:101], v[104:105], v[100:101]
	v_pk_mul_f32 v[98:99], v[102:103], v[98:99]
	v_pk_mul_f32 v[92:93], v[96:97], v[92:93]
	v_pk_mul_f32 v[98:99], v[98:99], v[106:107]
	v_pk_mul_f32 v[100:101], v[100:101], v[108:109]
	v_cvt_pk_bf16_f32 v98, v98, v99
	v_cvt_pk_bf16_f32 v99, v100, v101
	global_store_dwordx2 v[122:123], v[98:99], off offset:128
	ds_read_b32 v99, v143 offset:128
	v_or_b32_e32 v101, 32, v145
	v_pk_mul_f32 v[90:91], v[94:95], v[90:91]
	v_mad_i64_i32 v[106:107], s[0:1], v101, s11, v[136:137]
	s_waitcnt lgkmcnt(0)
	v_mul_f32_e32 v98, 0xbfb8aa3b, v99
	v_mul_f32_e32 v99, v99, v99
	v_pk_mul_f32 v[102:103], v[94:95], v[98:99] op_sel_hi:[1,0]
	v_pk_mul_f32 v[104:105], v[96:97], v[98:99] op_sel_hi:[1,0]
	v_rcp_f32_e32 v100, v99
	v_exp_f32_e32 v102, v102
	v_exp_f32_e32 v103, v103
	v_exp_f32_e32 v104, v104
	v_exp_f32_e32 v105, v105
	v_pk_mul_f32 v[94:95], v[86:87], v[98:99] op_sel_hi:[1,0]
	v_pk_fma_f32 v[102:103], v[100:101], v[102:103], v[100:101] op_sel_hi:[0,1,0]
	v_rcp_f32_e32 v102, v102
	v_pk_fma_f32 v[104:105], v[100:101], v[104:105], v[100:101] op_sel_hi:[0,1,0]
	v_rcp_f32_e32 v103, v103
	v_rcp_f32_e32 v104, v104
	v_rcp_f32_e32 v105, v105
	v_pk_mul_f32 v[96:97], v[88:89], v[98:99] op_sel_hi:[1,0]
	v_exp_f32_e32 v94, v94
	v_exp_f32_e32 v95, v95
	v_exp_f32_e32 v96, v96
	v_exp_f32_e32 v97, v97
	v_pk_mul_f32 v[90:91], v[90:91], v[102:103]
	v_pk_mul_f32 v[92:93], v[92:93], v[104:105]
	v_lshl_add_u64 v[106:107], v[106:107], 0, v[138:139]
	v_cvt_pk_bf16_f32 v90, v90, v91
	v_cvt_pk_bf16_f32 v91, v92, v93
	global_store_dwordx2 v[106:107], v[90:91], off
	v_pk_fma_f32 v[90:91], v[100:101], v[94:95], v[100:101] op_sel_hi:[0,1,0]
	v_pk_fma_f32 v[92:93], v[100:101], v[96:97], v[100:101] op_sel_hi:[0,1,0]
	v_rcp_f32_e32 v90, v90
	v_rcp_f32_e32 v91, v91
	v_rcp_f32_e32 v92, v92
	v_rcp_f32_e32 v93, v93
	v_pk_mul_f32 v[84:85], v[88:89], v[84:85]
	v_pk_mul_f32 v[82:83], v[86:87], v[82:83]
	v_pk_mul_f32 v[74:75], v[78:79], v[74:75]
	v_pk_mul_f32 v[82:83], v[82:83], v[90:91]
	v_pk_mul_f32 v[84:85], v[84:85], v[92:93]
	v_cvt_pk_bf16_f32 v82, v82, v83
	v_cvt_pk_bf16_f32 v83, v84, v85
	global_store_dwordx2 v[106:107], v[82:83], off offset:128
	ds_read_b32 v83, v143 offset:192
	v_or_b32_e32 v85, 48, v145
	v_pk_mul_f32 v[72:73], v[76:77], v[72:73]
	v_mad_i64_i32 v[90:91], s[0:1], v85, s11, v[136:137]
	s_waitcnt lgkmcnt(0)
; __device__ __forceinline__ unsigned cvtpk(float lo, float hi) { f32x2_t v = {lo, hi}; bf16x2_t b = __builtin_convertvector(v, bf16x2_t); return __builtin_bit_cast(unsigned, b); }
; __device__ __forceinline__ f32x4 swiglu4(f32x4 a, f32x4 b, float k1, float k3) {
;     const f32x2v a0 = {a[0], a[1]}, a1 = {a[2], a[3]}, b0 = {b[0], b[1]}, b1 = {b[2], b[3]};
;     const f32x2v t0 = a0 * k1, t1 = a1 * k1;
;     const f32x2v e0 = {__builtin_amdgcn_exp2f(t0[0]), __builtin_amdgcn_exp2f(t0[1])}, e1 = {__builtin_amdgcn_exp2f(t1[0]), __builtin_amdgcn_exp2f(t1[1])};
;     const f32x2v d0 = e0 * k3 + k3, d1 = e1 * k3 + k3;
;     const f32x2v r0 = {__builtin_amdgcn_rcpf(d0[0]), __builtin_amdgcn_rcpf(d0[1])}, r1 = {__builtin_amdgcn_rcpf(d1[0]), __builtin_amdgcn_rcpf(d1[1])};
;     const f32x2v y0 = (a0 * b0) * r0, y1 = (a1 * b1) * r1;
;     return (f32x4){y0[0], y0[1], y1[0], y1[1]};
;     __device__ __forceinline__ void operator()(const f32x4 (&acc)[2][2][4][2], const Unit& u, int wr, int wc, int fr, int fq) const {
;         const int row0 = u.pm * BM + wr * 64 + fr, hc0 = u.pn * 128 + wc * 16 + 4 * fq;
; #pragma unroll
;         for (int ai = 0; ai < 2; ++ai)
; #pragma unroll
;             for (int m = 0; m < 4; ++m) { const size_t r = (size_t)(row0 + ai * HALF + m * 16); const float s = tbl[wr * 64 + fr + ai * HALF + m * 16];     bf16_t* rowp = O + r * ldc + hc0; const float k1 = s * -1.44269504f, k3 = __builtin_amdgcn_rcpf(s * s);
; #pragma unroll
;                 for (int bj = 0; bj < 2; ++bj) { const f32x4 y = swiglu4(acc[ai][bj][m][0], acc[ai][bj][m][1], k1, k3);
;                     u32x2 w; w.x = cvtpk(y[0], y[1]); w.y = cvtpk(y[2], y[3]);
;                     *(u32x2*)(rowp + bj * 64) = w; } }
;     }
	v_mul_f32_e32 v82, 0xbfb8aa3b, v83
	v_mul_f32_e32 v83, v83, v83
	v_pk_mul_f32 v[86:87], v[76:77], v[82:83] op_sel_hi:[1,0]
	v_pk_mul_f32 v[88:89], v[78:79], v[82:83] op_sel_hi:[1,0]
	v_rcp_f32_e32 v84, v83
	v_exp_f32_e32 v86, v86
	v_exp_f32_e32 v87, v87
	v_exp_f32_e32 v88, v88
	v_exp_f32_e32 v89, v89
	v_pk_mul_f32 v[76:77], v[68:69], v[82:83] op_sel_hi:[1,0]
	v_pk_fma_f32 v[86:87], v[84:85], v[86:87], v[84:85] op_sel_hi:[0,1,0]
	v_rcp_f32_e32 v86, v86
	v_pk_fma_f32 v[88:89], v[84:85], v[88:89], v[84:85] op_sel_hi:[0,1,0]
	v_rcp_f32_e32 v87, v87
	v_rcp_f32_e32 v88, v88
	v_rcp_f32_e32 v89, v89
	v_pk_mul_f32 v[78:79], v[70:71], v[82:83] op_sel_hi:[1,0]
	v_exp_f32_e32 v76, v76
	v_exp_f32_e32 v77, v77
	v_exp_f32_e32 v78, v78
	v_exp_f32_e32 v79, v79
	v_pk_mul_f32 v[72:73], v[72:73], v[86:87]
	v_pk_mul_f32 v[74:75], v[74:75], v[88:89]
	v_lshl_add_u64 v[90:91], v[90:91], 0, v[138:139]
	v_cvt_pk_bf16_f32 v72, v72, v73
	v_cvt_pk_bf16_f32 v73, v74, v75
	global_store_dwordx2 v[90:91], v[72:73], off
	v_pk_fma_f32 v[72:73], v[84:85], v[76:77], v[84:85] op_sel_hi:[0,1,0]
	v_pk_fma_f32 v[74:75], v[84:85], v[78:79], v[84:85] op_sel_hi:[0,1,0]
	v_rcp_f32_e32 v72, v72
	v_rcp_f32_e32 v73, v73
	v_rcp_f32_e32 v74, v74
	v_rcp_f32_e32 v75, v75
	v_pk_mul_f32 v[66:67], v[70:71], v[66:67]
	v_pk_mul_f32 v[64:65], v[68:69], v[64:65]
	v_pk_mul_f32 v[58:59], v[62:63], v[58:59]
	v_pk_mul_f32 v[64:65], v[64:65], v[72:73]
	v_pk_mul_f32 v[66:67], v[66:67], v[74:75]
	v_cvt_pk_bf16_f32 v64, v64, v65
	v_cvt_pk_bf16_f32 v65, v66, v67
	global_store_dwordx2 v[90:91], v[64:65], off offset:128
	ds_read_b32 v65, v143 offset:512
	v_add_u32_e32 v67, 0x80, v145
	v_pk_mul_f32 v[56:57], v[60:61], v[56:57]
	v_mad_i64_i32 v[72:73], s[0:1], v67, s11, v[136:137]
	s_waitcnt lgkmcnt(0)
	v_mul_f32_e32 v64, 0xbfb8aa3b, v65
	v_mul_f32_e32 v65, v65, v65
	v_pk_mul_f32 v[68:69], v[60:61], v[64:65] op_sel_hi:[1,0]
	v_pk_mul_f32 v[70:71], v[62:63], v[64:65] op_sel_hi:[1,0]
	v_rcp_f32_e32 v66, v65
	v_exp_f32_e32 v68, v68
	v_exp_f32_e32 v69, v69
	v_exp_f32_e32 v70, v70
	v_exp_f32_e32 v71, v71
	v_pk_mul_f32 v[60:61], v[52:53], v[64:65] op_sel_hi:[1,0]
	v_pk_fma_f32 v[68:69], v[66:67], v[68:69], v[66:67] op_sel_hi:[0,1,0]
	v_rcp_f32_e32 v68, v68
	v_pk_fma_f32 v[70:71], v[66:67], v[70:71], v[66:67] op_sel_hi:[0,1,0]
	v_rcp_f32_e32 v69, v69
	v_rcp_f32_e32 v70, v70
	v_rcp_f32_e32 v71, v71
	v_pk_mul_f32 v[62:63], v[54:55], v[64:65] op_sel_hi:[1,0]
	v_exp_f32_e32 v60, v60
	v_exp_f32_e32 v61, v61
	v_exp_f32_e32 v62, v62
	v_exp_f32_e32 v63, v63
	v_pk_mul_f32 v[56:57], v[56:57], v[68:69]
	v_pk_mul_f32 v[58:59], v[58:59], v[70:71]
	v_lshl_add_u64 v[72:73], v[72:73], 0, v[138:139]
	v_cvt_pk_bf16_f32 v56, v56, v57
	v_cvt_pk_bf16_f32 v57, v58, v59
	global_store_dwordx2 v[72:73], v[56:57], off
	v_pk_fma_f32 v[56:57], v[66:67], v[60:61], v[66:67] op_sel_hi:[0,1,0]
	v_pk_fma_f32 v[58:59], v[66:67], v[62:63], v[66:67] op_sel_hi:[0,1,0]
	v_rcp_f32_e32 v56, v56
	v_rcp_f32_e32 v57, v57
	v_rcp_f32_e32 v58, v58
	v_rcp_f32_e32 v59, v59
	v_pk_mul_f32 v[50:51], v[54:55], v[50:51]
	v_pk_mul_f32 v[48:49], v[52:53], v[48:49]
	v_pk_mul_f32 v[42:43], v[46:47], v[42:43]
	v_pk_mul_f32 v[48:49], v[48:49], v[56:57]
	v_pk_mul_f32 v[50:51], v[50:51], v[58:59]
	v_cvt_pk_bf16_f32 v48, v48, v49
	v_cvt_pk_bf16_f32 v49, v50, v51
	global_store_dwordx2 v[72:73], v[48:49], off offset:128
	ds_read_b32 v49, v143 offset:576
	v_add_u32_e32 v51, 0x90, v145
	v_pk_mul_f32 v[40:41], v[44:45], v[40:41]
	v_mad_i64_i32 v[56:57], s[0:1], v51, s11, v[136:137]
	s_waitcnt lgkmcnt(0)
; __device__ __forceinline__ unsigned cvtpk(float lo, float hi) { f32x2_t v = {lo, hi}; bf16x2_t b = __builtin_convertvector(v, bf16x2_t); return __builtin_bit_cast(unsigned, b); }
; __device__ __forceinline__ f32x4 swiglu4(f32x4 a, f32x4 b, float k1, float k3) {
;     const f32x2v a0 = {a[0], a[1]}, a1 = {a[2], a[3]}, b0 = {b[0], b[1]}, b1 = {b[2], b[3]};
;     const f32x2v t0 = a0 * k1, t1 = a1 * k1;
;     const f32x2v e0 = {__builtin_amdgcn_exp2f(t0[0]), __builtin_amdgcn_exp2f(t0[1])}, e1 = {__builtin_amdgcn_exp2f(t1[0]), __builtin_amdgcn_exp2f(t1[1])};
;     const f32x2v d0 = e0 * k3 + k3, d1 = e1 * k3 + k3;
;     const f32x2v r0 = {__builtin_amdgcn_rcpf(d0[0]), __builtin_amdgcn_rcpf(d0[1])}, r1 = {__builtin_amdgcn_rcpf(d1[0]), __builtin_amdgcn_rcpf(d1[1])};
;     const f32x2v y0 = (a0 * b0) * r0, y1 = (a1 * b1) * r1;
;     return (f32x4){y0[0], y0[1], y1[0], y1[1]};
;     __device__ __forceinline__ void operator()(const f32x4 (&acc)[2][2][4][2], const Unit& u, int wr, int wc, int fr, int fq) const {
;         const int row0 = u.pm * BM + wr * 64 + fr, hc0 = u.pn * 128 + wc * 16 + 4 * fq;
; #pragma unroll
;         for (int ai = 0; ai < 2; ++ai)
; #pragma unroll
;             for (int m = 0; m < 4; ++m) { const size_t r = (size_t)(row0 + ai * HALF + m * 16); const float s = tbl[wr * 64 + fr + ai * HALF + m * 16];     bf16_t* rowp = O + r * ldc + hc0; const float k1 = s * -1.44269504f, k3 = __builtin_amdgcn_rcpf(s * s);
; #pragma unroll
;                 for (int bj = 0; bj < 2; ++bj) { const f32x4 y = swiglu4(acc[ai][bj][m][0], acc[ai][bj][m][1], k1, k3);
;                     u32x2 w; w.x = cvtpk(y[0], y[1]); w.y = cvtpk(y[2], y[3]);
;                     *(u32x2*)(rowp + bj * 64) = w; } }
;     }
	v_mul_f32_e32 v48, 0xbfb8aa3b, v49
	v_mul_f32_e32 v49, v49, v49
	v_pk_mul_f32 v[52:53], v[44:45], v[48:49] op_sel_hi:[1,0]
	v_pk_mul_f32 v[54:55], v[46:47], v[48:49] op_sel_hi:[1,0]
	v_rcp_f32_e32 v50, v49
	v_exp_f32_e32 v52, v52
	v_exp_f32_e32 v53, v53
	v_exp_f32_e32 v54, v54
	v_exp_f32_e32 v55, v55
	v_pk_mul_f32 v[44:45], v[36:37], v[48:49] op_sel_hi:[1,0]
	v_pk_fma_f32 v[52:53], v[50:51], v[52:53], v[50:51] op_sel_hi:[0,1,0]
	v_rcp_f32_e32 v52, v52
	v_pk_fma_f32 v[54:55], v[50:51], v[54:55], v[50:51] op_sel_hi:[0,1,0]
	v_rcp_f32_e32 v53, v53
	v_rcp_f32_e32 v54, v54
	v_rcp_f32_e32 v55, v55
	v_pk_mul_f32 v[46:47], v[38:39], v[48:49] op_sel_hi:[1,0]
	v_exp_f32_e32 v44, v44
	v_exp_f32_e32 v45, v45
	v_exp_f32_e32 v46, v46
	v_exp_f32_e32 v47, v47
	v_pk_mul_f32 v[40:41], v[40:41], v[52:53]
	v_pk_mul_f32 v[42:43], v[42:43], v[54:55]
	v_lshl_add_u64 v[56:57], v[56:57], 0, v[138:139]
	v_cvt_pk_bf16_f32 v40, v40, v41
	v_cvt_pk_bf16_f32 v41, v42, v43
	global_store_dwordx2 v[56:57], v[40:41], off
	v_pk_fma_f32 v[40:41], v[50:51], v[44:45], v[50:51] op_sel_hi:[0,1,0]
	v_pk_fma_f32 v[42:43], v[50:51], v[46:47], v[50:51] op_sel_hi:[0,1,0]
	v_rcp_f32_e32 v40, v40
	v_rcp_f32_e32 v41, v41
	v_rcp_f32_e32 v42, v42
	v_rcp_f32_e32 v43, v43
	v_pk_mul_f32 v[34:35], v[38:39], v[34:35]
	v_pk_mul_f32 v[32:33], v[36:37], v[32:33]
	v_pk_mul_f32 v[26:27], v[30:31], v[26:27]
	v_pk_mul_f32 v[32:33], v[32:33], v[40:41]
	v_pk_mul_f32 v[34:35], v[34:35], v[42:43]
	v_cvt_pk_bf16_f32 v32, v32, v33
	v_cvt_pk_bf16_f32 v33, v34, v35
	global_store_dwordx2 v[56:57], v[32:33], off offset:128
	ds_read_b32 v33, v143 offset:640
	v_add_u32_e32 v35, 0xa0, v145
	v_pk_mul_f32 v[24:25], v[28:29], v[24:25]
	v_mad_i64_i32 v[40:41], s[0:1], v35, s11, v[136:137]
	s_waitcnt lgkmcnt(0)
	v_mul_f32_e32 v32, 0xbfb8aa3b, v33
	v_mul_f32_e32 v33, v33, v33
	v_pk_mul_f32 v[36:37], v[28:29], v[32:33] op_sel_hi:[1,0]
	v_pk_mul_f32 v[38:39], v[30:31], v[32:33] op_sel_hi:[1,0]
	v_rcp_f32_e32 v34, v33
	v_exp_f32_e32 v36, v36
	v_exp_f32_e32 v37, v37
	v_exp_f32_e32 v38, v38
	v_exp_f32_e32 v39, v39
	v_pk_mul_f32 v[28:29], v[20:21], v[32:33] op_sel_hi:[1,0]
	v_pk_fma_f32 v[36:37], v[34:35], v[36:37], v[34:35] op_sel_hi:[0,1,0]
	v_rcp_f32_e32 v36, v36
	v_pk_fma_f32 v[38:39], v[34:35], v[38:39], v[34:35] op_sel_hi:[0,1,0]
	v_rcp_f32_e32 v37, v37
	v_rcp_f32_e32 v38, v38
	v_rcp_f32_e32 v39, v39
	v_pk_mul_f32 v[30:31], v[22:23], v[32:33] op_sel_hi:[1,0]
	v_exp_f32_e32 v28, v28
	v_exp_f32_e32 v29, v29
	v_exp_f32_e32 v30, v30
	v_exp_f32_e32 v31, v31
	v_pk_mul_f32 v[24:25], v[24:25], v[36:37]
	v_pk_mul_f32 v[26:27], v[26:27], v[38:39]
	v_lshl_add_u64 v[40:41], v[40:41], 0, v[138:139]
	v_cvt_pk_bf16_f32 v24, v24, v25
	v_cvt_pk_bf16_f32 v25, v26, v27
	global_store_dwordx2 v[40:41], v[24:25], off
	v_pk_fma_f32 v[24:25], v[34:35], v[28:29], v[34:35] op_sel_hi:[0,1,0]
	v_pk_fma_f32 v[26:27], v[34:35], v[30:31], v[34:35] op_sel_hi:[0,1,0]
	v_rcp_f32_e32 v24, v24
	v_rcp_f32_e32 v25, v25
	v_rcp_f32_e32 v26, v26
	v_rcp_f32_e32 v27, v27
	v_pk_mul_f32 v[18:19], v[22:23], v[18:19]
	v_pk_mul_f32 v[16:17], v[20:21], v[16:17]
	v_pk_mul_f32 v[10:11], v[14:15], v[10:11]
	v_pk_mul_f32 v[16:17], v[16:17], v[24:25]
	v_pk_mul_f32 v[18:19], v[18:19], v[26:27]
	v_cvt_pk_bf16_f32 v16, v16, v17
	v_cvt_pk_bf16_f32 v17, v18, v19
	global_store_dwordx2 v[40:41], v[16:17], off offset:128
	ds_read_b32 v17, v143 offset:704
	v_add_u32_e32 v19, 0xb0, v145
	v_pk_mul_f32 v[8:9], v[12:13], v[8:9]
	v_mad_i64_i32 v[24:25], s[0:1], v19, s11, v[136:137]
	s_waitcnt lgkmcnt(0)
	v_mul_f32_e32 v16, 0xbfb8aa3b, v17
	v_mul_f32_e32 v17, v17, v17
	v_pk_mul_f32 v[20:21], v[12:13], v[16:17] op_sel_hi:[1,0]
	v_pk_mul_f32 v[22:23], v[14:15], v[16:17] op_sel_hi:[1,0]
	v_rcp_f32_e32 v18, v17
	v_exp_f32_e32 v20, v20
	v_exp_f32_e32 v21, v21
	v_exp_f32_e32 v22, v22
	v_exp_f32_e32 v23, v23
	v_pk_mul_f32 v[12:13], v[4:5], v[16:17] op_sel_hi:[1,0]
	v_pk_fma_f32 v[20:21], v[18:19], v[20:21], v[18:19] op_sel_hi:[0,1,0]
	v_rcp_f32_e32 v20, v20
	v_pk_fma_f32 v[22:23], v[18:19], v[22:23], v[18:19] op_sel_hi:[0,1,0]
	v_rcp_f32_e32 v21, v21
	v_rcp_f32_e32 v22, v22
	v_rcp_f32_e32 v23, v23
	v_pk_mul_f32 v[14:15], v[6:7], v[16:17] op_sel_hi:[1,0]
	v_exp_f32_e32 v12, v12
	v_exp_f32_e32 v13, v13
	v_exp_f32_e32 v14, v14
	v_exp_f32_e32 v15, v15
	v_pk_mul_f32 v[8:9], v[8:9], v[20:21]
	v_pk_mul_f32 v[10:11], v[10:11], v[22:23]
	v_lshl_add_u64 v[24:25], v[24:25], 0, v[138:139]
	v_cvt_pk_bf16_f32 v8, v8, v9
	v_cvt_pk_bf16_f32 v9, v10, v11
	global_store_dwordx2 v[24:25], v[8:9], off
	v_pk_fma_f32 v[8:9], v[18:19], v[12:13], v[18:19] op_sel_hi:[0,1,0]
	v_pk_fma_f32 v[10:11], v[18:19], v[14:15], v[18:19] op_sel_hi:[0,1,0]
	v_rcp_f32_e32 v8, v8
	v_rcp_f32_e32 v9, v9
	v_rcp_f32_e32 v10, v10
	v_rcp_f32_e32 v11, v11
	v_pk_mul_f32 v[2:3], v[6:7], v[2:3]
	v_pk_mul_f32 v[0:1], v[4:5], v[0:1]
	s_andn2_b64 vcc, exec, s[4:5]
	v_pk_mul_f32 v[0:1], v[0:1], v[8:9]
	v_pk_mul_f32 v[2:3], v[2:3], v[10:11]
	v_cvt_pk_bf16_f32 v0, v0, v1
	v_cvt_pk_bf16_f32 v1, v2, v3
	s_mov_b64 s[0:1], -1
	global_store_dwordx2 v[24:25], v[0:1], off offset:128
	s_cbranch_vccnz .LBB0_962
	s_andn2_b64 vcc, exec, s[6:7]
	s_cbranch_vccnz .LBB0_961
	s_barrier
	s_branch .LBB0_961

; __device__ __forceinline__ unsigned pk4_fp8(float a, float b, float c, float d) { int w = 0; w = __builtin_amdgcn_cvt_pk_fp8_f32(a, b, w, false); w = __builtin_amdgcn_cvt_pk_fp8_f32(c, d, w, true); return (unsigned)w; }
; template <int MODE, int KL>
; __device__ __forceinline__ void p0_cvt_item(const float* W, int K, int N, unsigned char* WT, int il, int which, int item, int lane, const float* gk, float scale, int ldk, int koff) {
;     const int nblk = N >> 6, kb = item / nblk, nb = item - kb * nblk, nq = lane & 15, kr = lane >> 4, k0 = 4 * KL * kb + KL * kr, n0 = 64 * nb + 4 * nq;
;     const GAS f32x4* src = (const GAS f32x4*)(W + (size_t)k0 * N + n0);
;     f32x4 v[KL];
; #pragma unroll
;     for (int i = 0; i < KL; ++i) v[i] = src[(size_t)i * (N >> 2)];
;     if (MODE == 1) {
; #pragma unroll
;         for (int q = 0; q < KL / 4; ++q) { const f32x4 g = *(const GAS f32x4*)(gk + k0 + 4 * q); v[4 * q] *= g.x; v[4 * q + 1] *= g.y; v[4 * q + 2] *= g.z; v[4 * q + 3] *= g.w; } }
;     if (MODE == 2) {
; #pragma unroll
;         for (int i = 0; i < KL; ++i) v[i] *= scale; }
; #pragma unroll
;     for (int c = 0; c < 4; ++c) { const int n = n0 + c, row = il ? ((n >> 4) * 32 + which * 16 + (n & 15)) : n;
;         if (MODE == 2) { GAS v4u* dst = (GAS v4u*)(WT + (size_t)row * ldk + koff + k0);
; #pragma unroll
;             for (int q = 0; q < KL / 16; ++q) { v4u o;
;                 o.x = pg8::pk4_fp8(v[16 * q][c], v[16 * q + 1][c], v[16 * q + 2][c], v[16 * q + 3][c]);     o.y = pg8::pk4_fp8(v[16 * q + 4][c], v[16 * q + 5][c], v[16 * q + 6][c], v[16 * q + 7][c]);
;                 o.z = pg8::pk4_fp8(v[16 * q + 8][c], v[16 * q + 9][c], v[16 * q + 10][c], v[16 * q + 11][c]); o.w = pg8::pk4_fp8(v[16 * q + 12][c], v[16 * q + 13][c], v[16 * q + 14][c], v[16 * q + 15][c]);
;                 dst[q] = o; } }
; __device__ __forceinline__ void moe_cvt_tile(const Args& a, int set, int id, int lane) {
;     const int j = id / MT_PER, item = id - j * MT_PER;
;     if (j < 16) { const int e = set * 8 + (j & 7), wh = j >> 3;
;         p0_cvt_item<2, 32>(a.in[17 + wh] + (size_t)e * D * FE, D, FE, a.ws + W_13M + (size_t)e * 2 * FE * D, 1, wh, item, lane, nullptr, 32.f, D, 0); }
;     else { const int e = set * 8 + (j - 16); p0_cvt_item<2, 32>(a.in[19] + (size_t)e * FE * D, FE, D, a.ws + W_2M + (size_t)e * D * FE, 0, 0, item, lane, nullptr, 64.f, FE, 0); }
.LBB0_1034:
	s_add_i32 s0, s6, s0
	s_mul_hi_i32 s1, s0, 0x92492493
	s_add_i32 s1, s1, s0
	s_lshr_b32 s4, s1, 31
	s_ashr_i32 s1, s1, 8
	s_add_i32 s4, s1, s4
	s_mul_i32 s7, s4, 0xfffffe40
	s_add_i32 s7, s7, s0
	s_cmpk_gt_i32 s0, 0x1bff
	s_mov_b64 s[0:1], -1
	s_cbranch_scc0 .LBB0_1036
	v_mov_b64_e32 v[0:1], s[66:67]
	global_load_dwordx2 v[2:3], v[0:1], off offset:152
	s_add_i32 s5, s4, -8
	global_load_dwordx2 v[0:1], v[0:1], off offset:192
	s_waitcnt vmcnt(0) lgkmcnt(0)
	v_mad_i64_i32 v[2:3], s[0:1], s5, v192, v[2:3]
	v_mad_i64_i32 v[122:123], s[0:1], s5, v193, v[0:1]
	s_ashr_i32 s0, s7, 31
	s_lshr_b32 s0, s0, 28
	s_add_i32 s0, s7, s0
	s_ashr_i32 s0, s0, 4
	v_lshl_add_u32 v124, s0, 7, v80
	s_lshl_b32 s0, s0, 10
	s_lshl_b32 s1, s7, 6
	s_sub_i32 s0, s1, s0
	v_ashrrev_i32_e32 v125, 31, v124
	v_or_b32_e32 v78, s0, v154
	v_lshlrev_b64 v[0:1], 12, v[124:125]
	v_lshl_add_u64 v[0:1], v[2:3], 0, v[0:1]
	v_ashrrev_i32_e32 v79, 31, v78
	v_lshl_add_u64 v[8:9], v[78:79], 2, v[0:1]
	s_movk_i32 s0, 0x2000
	v_add_co_u32_e32 v10, vcc, s0, v8
	s_movk_i32 s0, 0x4000
	s_nop 0
	v_addc_co_u32_e32 v11, vcc, 0, v9, vcc
	v_add_co_u32_e32 v14, vcc, s0, v8
	s_movk_i32 s0, 0x6000
	s_nop 0
	v_addc_co_u32_e32 v15, vcc, 0, v9, vcc
	v_add_co_u32_e32 v18, vcc, s0, v8
	s_mov_b32 s0, 0xc000
	s_nop 0
	v_addc_co_u32_e32 v19, vcc, 0, v9, vcc
	v_add_co_u32_e32 v26, vcc, s33, v8
	global_load_dwordx4 v[0:3], v[8:9], off
	s_nop 0
	v_addc_co_u32_e32 v27, vcc, 0, v9, vcc
	v_add_co_u32_e32 v34, vcc, s97, v8
	global_load_dwordx4 v[4:7], v[10:11], off offset:-4096
	s_nop 0
	global_load_dwordx4 v[10:13], v[10:11], off
	v_addc_co_u32_e32 v35, vcc, 0, v9, vcc
	v_add_co_u32_e32 v42, vcc, s0, v8
	s_mov_b32 s0, 0xe000
	s_nop 0
	v_addc_co_u32_e32 v43, vcc, 0, v9, vcc
	v_add_co_u32_e32 v50, vcc, s0, v8
	s_mov_b32 s0, 0x10000
	s_nop 0
	v_addc_co_u32_e32 v51, vcc, 0, v9, vcc
	v_add_co_u32_e32 v58, vcc, s0, v8
	s_mov_b32 s0, 0x12000
	s_nop 0
	v_addc_co_u32_e32 v59, vcc, 0, v9, vcc
	v_add_co_u32_e32 v70, vcc, s0, v8
	s_mov_b32 s0, 0x14000
	s_nop 0
	v_addc_co_u32_e32 v71, vcc, 0, v9, vcc
	v_add_co_u32_e32 v82, vcc, s0, v8
	s_mov_b32 s0, 0x16000
	s_nop 0
	v_addc_co_u32_e32 v83, vcc, 0, v9, vcc
	global_load_dwordx4 v[22:25], v[14:15], off offset:-4096
	s_nop 0
	global_load_dwordx4 v[14:17], v[14:15], off
	s_nop 0
	global_load_dwordx4 v[30:33], v[18:19], off offset:-4096
	s_nop 0
	global_load_dwordx4 v[18:21], v[18:19], off
	s_nop 0
	global_load_dwordx4 v[38:41], v[26:27], off offset:-4096
	s_nop 0
	global_load_dwordx4 v[26:29], v[26:27], off
	s_nop 0
	global_load_dwordx4 v[46:49], v[34:35], off offset:-4096
	s_nop 0
	global_load_dwordx4 v[34:37], v[34:35], off
	s_nop 0
	global_load_dwordx4 v[54:57], v[42:43], off offset:-4096
	s_nop 0
	global_load_dwordx4 v[42:45], v[42:43], off
	s_nop 0
	global_load_dwordx4 v[62:65], v[50:51], off offset:-4096
	s_nop 0
	global_load_dwordx4 v[50:53], v[50:51], off
	s_nop 0
	global_load_dwordx4 v[66:69], v[58:59], off offset:-4096
	s_nop 0
	global_load_dwordx4 v[58:61], v[58:59], off
	s_nop 0
	global_load_dwordx4 v[74:77], v[70:71], off offset:-4096
	s_nop 0
	global_load_dwordx4 v[70:73], v[70:71], off
	v_add_co_u32_e32 v90, vcc, s0, v8
	s_mov_b32 s0, 0x18000
	s_nop 0
	v_addc_co_u32_e32 v91, vcc, 0, v9, vcc
	v_add_co_u32_e32 v98, vcc, s0, v8
	s_mov_b32 s0, 0x1a000
	s_nop 0
	v_addc_co_u32_e32 v99, vcc, 0, v9, vcc
	v_add_co_u32_e32 v106, vcc, s0, v8
	s_mov_b32 s0, 0x1c000
	s_nop 0
	v_addc_co_u32_e32 v107, vcc, 0, v9, vcc
	v_add_co_u32_e32 v114, vcc, s0, v8
	s_mov_b32 s0, 0x1e000
	s_nop 0
	v_addc_co_u32_e32 v115, vcc, 0, v9, vcc
	global_load_dwordx4 v[86:89], v[82:83], off offset:-4096
	s_nop 0
	global_load_dwordx4 v[82:85], v[82:83], off
	s_nop 0
	global_load_dwordx4 v[94:97], v[90:91], off offset:-4096
	s_nop 0
	global_load_dwordx4 v[90:93], v[90:91], off
	s_nop 0
	global_load_dwordx4 v[102:105], v[98:99], off offset:-4096
	s_nop 0
	global_load_dwordx4 v[98:101], v[98:99], off
	s_nop 0
	global_load_dwordx4 v[110:113], v[106:107], off offset:-4096
	s_nop 0
	global_load_dwordx4 v[106:109], v[106:107], off
	v_add_co_u32_e32 v126, vcc, s0, v8
	global_load_dwordx4 v[118:121], v[114:115], off offset:-4096
	s_nop 0
	global_load_dwordx4 v[114:117], v[114:115], off
	v_addc_co_u32_e32 v127, vcc, 0, v9, vcc
	global_load_dwordx4 v[156:159], v[126:127], off offset:-4096
	global_load_dwordx4 v[174:177], v[126:127], off
	s_mov_b32 s0, 0x1f000
	v_add_co_u32_e32 v8, vcc, s0, v8
	s_mov_b64 s[0:1], 0x33f00000
	s_nop 0
	v_addc_co_u32_e32 v9, vcc, 0, v9, vcc
	global_load_dwordx4 v[178:181], v[8:9], off
	s_movk_i32 s5, 0xe00
	s_waitcnt vmcnt(31)
	v_pk_mul_f32 v[126:127], v[0:1], s[82:83] op_sel_hi:[1,0]
	v_lshl_add_u64 v[0:1], v[122:123], 0, v[124:125]
	v_lshl_add_u64 v[0:1], v[0:1], 0, s[0:1]
	v_pk_mul_f32 v[2:3], v[2:3], s[82:83] op_sel_hi:[1,0]
	s_waitcnt vmcnt(30)
	v_pk_mul_f32 v[8:9], v[6:7], s[82:83] op_sel_hi:[1,0]
	v_pk_mul_f32 v[6:7], v[4:5], s[82:83] op_sel_hi:[1,0]
	s_waitcnt vmcnt(29)
	v_pk_mul_f32 v[128:129], v[10:11], s[82:83] op_sel_hi:[1,0]
	v_pk_mul_f32 v[4:5], v[12:13], s[82:83] op_sel_hi:[1,0]
	s_waitcnt vmcnt(28)
	v_pk_mul_f32 v[132:133], v[22:23], s[82:83] op_sel_hi:[1,0]
	s_waitcnt vmcnt(27)
	v_pk_mul_f32 v[130:131], v[14:15], s[82:83] op_sel_hi:[1,0]
	s_waitcnt vmcnt(26)
	v_pk_mul_f32 v[134:135], v[30:31], s[82:83] op_sel_hi:[1,0]
	s_waitcnt vmcnt(25)
	v_pk_mul_f32 v[136:137], v[18:19], s[82:83] op_sel_hi:[1,0]
	s_waitcnt vmcnt(24)
	v_pk_mul_f32 v[18:19], v[40:41], s[82:83] op_sel_hi:[1,0]
	v_pk_mul_f32 v[138:139], v[38:39], s[82:83] op_sel_hi:[1,0]
	s_waitcnt vmcnt(23)
	v_pk_mul_f32 v[40:41], v[26:27], s[82:83] op_sel_hi:[1,0]
	s_waitcnt vmcnt(22)
; __device__ __forceinline__ unsigned pk4_fp8(float a, float b, float c, float d) { int w = 0; w = __builtin_amdgcn_cvt_pk_fp8_f32(a, b, w, false); w = __builtin_amdgcn_cvt_pk_fp8_f32(c, d, w, true); return (unsigned)w; }
; #define GAS __attribute__((address_space(1)))
; template <int MODE, int KL>
; __device__ __forceinline__ void p0_cvt_item(const float* W, int K, int N, unsigned char* WT, int il, int which, int item, int lane, const float* gk, float scale, int ldk, int koff) {
;     const int nblk = N >> 6, kb = item / nblk, nb = item - kb * nblk, nq = lane & 15, kr = lane >> 4, k0 = 4 * KL * kb + KL * kr, n0 = 64 * nb + 4 * nq;
;     const GAS f32x4* src = (const GAS f32x4*)(W + (size_t)k0 * N + n0);
;     f32x4 v[KL];
; #pragma unroll
;     for (int i = 0; i < KL; ++i) v[i] = src[(size_t)i * (N >> 2)];
;     if (MODE == 1) {
; #pragma unroll
;         for (int q = 0; q < KL / 4; ++q) { const f32x4 g = *(const GAS f32x4*)(gk + k0 + 4 * q); v[4 * q] *= g.x; v[4 * q + 1] *= g.y; v[4 * q + 2] *= g.z; v[4 * q + 3] *= g.w; } }
;     if (MODE == 2) {
; #pragma unroll
;         for (int i = 0; i < KL; ++i) v[i] *= scale; }
; #pragma unroll
;     for (int c = 0; c < 4; ++c) { const int n = n0 + c, row = il ? ((n >> 4) * 32 + which * 16 + (n & 15)) : n;
;         if (MODE == 2) { GAS v4u* dst = (GAS v4u*)(WT + (size_t)row * ldk + koff + k0);
; #pragma unroll
;             for (int q = 0; q < KL / 16; ++q) { v4u o;
;                 o.x = pg8::pk4_fp8(v[16 * q][c], v[16 * q + 1][c], v[16 * q + 2][c], v[16 * q + 3][c]);     o.y = pg8::pk4_fp8(v[16 * q + 4][c], v[16 * q + 5][c], v[16 * q + 6][c], v[16 * q + 7][c]);
;                 o.z = pg8::pk4_fp8(v[16 * q + 8][c], v[16 * q + 9][c], v[16 * q + 10][c], v[16 * q + 11][c]); o.w = pg8::pk4_fp8(v[16 * q + 12][c], v[16 * q + 13][c], v[16 * q + 14][c], v[16 * q + 15][c]);
;                 dst[q] = o; } }
	v_pk_mul_f32 v[140:141], v[46:47], s[82:83] op_sel_hi:[1,0]
	s_waitcnt vmcnt(19)
	v_pk_mul_f32 v[148:149], v[42:43], s[82:83] op_sel_hi:[1,0]
	s_waitcnt vmcnt(18)
	v_pk_mul_f32 v[160:161], v[62:63], s[82:83] op_sel_hi:[1,0]
	s_waitcnt vmcnt(14)
	v_pk_mul_f32 v[42:43], v[76:77], s[82:83] op_sel_hi:[1,0]
	s_waitcnt vmcnt(13)
	v_pk_mul_f32 v[38:39], v[72:73], s[82:83] op_sel_hi:[1,0]
	v_pk_mul_f32 v[76:77], v[70:71], s[82:83] op_sel_hi:[1,0]
	v_mov_b32_e32 v70, v81
	v_mov_b32_e32 v71, v81
	v_mov_b32_e32 v72, v81
	v_mov_b32_e32 v73, v81
	v_cvt_pk_fp8_f32 v70, v126, v6
	v_cvt_pk_fp8_f32 v71, v130, v134
	v_cvt_pk_fp8_f32 v72, v40, v140
	v_cvt_pk_fp8_f32 v73, v148, v160
	v_pk_mul_f32 v[142:143], v[34:35], s[82:83] op_sel_hi:[1,0]
	v_pk_mul_f32 v[150:151], v[54:55], s[82:83] op_sel_hi:[1,0]
	v_pk_mul_f32 v[144:145], v[50:51], s[82:83] op_sel_hi:[1,0]
	v_pk_mul_f32 v[152:153], v[66:67], s[82:83] op_sel_hi:[1,0]
	v_cvt_pk_fp8_f32 v70, v128, v132 op_sel:[0,0,1]
	v_cvt_pk_fp8_f32 v71, v136, v138 op_sel:[0,0,1]
	v_cvt_pk_fp8_f32 v72, v142, v150 op_sel:[0,0,1]
	v_cvt_pk_fp8_f32 v73, v144, v152 op_sel:[0,0,1]
	v_pk_mul_f32 v[146:147], v[58:59], s[82:83] op_sel_hi:[1,0]
	v_pk_mul_f32 v[12:13], v[16:17], s[82:83] op_sel_hi:[1,0]
	v_pk_mul_f32 v[16:17], v[20:21], s[82:83] op_sel_hi:[1,0]
	s_waitcnt vmcnt(5)
	v_pk_mul_f32 v[58:59], v[108:109], s[82:83] op_sel_hi:[1,0]
	v_mad_i64_i32 v[108:109], s[0:1], v78, s5, v[0:1]
	v_pk_mul_f32 v[20:21], v[28:29], s[82:83] op_sel_hi:[1,0]
	v_pk_mul_f32 v[28:29], v[44:45], s[82:83] op_sel_hi:[1,0]
	v_pk_mul_f32 v[74:75], v[74:75], s[82:83] op_sel_hi:[1,0]
	v_pk_mul_f32 v[44:45], v[88:89], s[82:83] op_sel_hi:[1,0]
	v_pk_mul_f32 v[46:47], v[84:85], s[82:83] op_sel_hi:[1,0]
	v_pk_mul_f32 v[82:83], v[82:83], s[82:83] op_sel_hi:[1,0]
	v_pk_mul_f32 v[84:85], v[94:95], s[82:83] op_sel_hi:[1,0]
	v_pk_mul_f32 v[50:51], v[92:93], s[82:83] op_sel_hi:[1,0]
	v_pk_mul_f32 v[88:89], v[90:91], s[82:83] op_sel_hi:[1,0]
	v_pk_mul_f32 v[90:91], v[102:103], s[82:83] op_sel_hi:[1,0]
	v_pk_mul_f32 v[54:55], v[100:101], s[82:83] op_sel_hi:[1,0]
	v_pk_mul_f32 v[92:93], v[98:99], s[82:83] op_sel_hi:[1,0]
	v_pk_mul_f32 v[94:95], v[110:111], s[82:83] op_sel_hi:[1,0]
	s_waitcnt vmcnt(3)
	v_pk_mul_f32 v[100:101], v[114:115], s[82:83] op_sel_hi:[1,0]
	s_waitcnt vmcnt(2)
	v_pk_mul_f32 v[102:103], v[156:157], s[82:83] op_sel_hi:[1,0]
	global_store_dwordx4 v[108:109], v[70:73], off
	v_pk_mul_f32 v[14:15], v[32:33], s[82:83] op_sel_hi:[1,0]
	v_pk_mul_f32 v[22:23], v[48:49], s[82:83] op_sel_hi:[1,0]
	v_mov_b32_e32 v70, v81
	v_mov_b32_e32 v71, v81
	v_mov_b32_e32 v72, v81
	v_mov_b32_e32 v73, v81
	v_cvt_pk_fp8_f32 v70, v146, v74
	v_cvt_pk_fp8_f32 v71, v82, v84
	v_cvt_pk_fp8_f32 v72, v92, v94
	v_cvt_pk_fp8_f32 v73, v100, v102
	v_pk_mul_f32 v[32:33], v[52:53], s[82:83] op_sel_hi:[1,0]
	v_pk_mul_f32 v[86:87], v[86:87], s[82:83] op_sel_hi:[1,0]
	v_pk_mul_f32 v[48:49], v[96:97], s[82:83] op_sel_hi:[1,0]
	v_pk_mul_f32 v[52:53], v[104:105], s[82:83] op_sel_hi:[1,0]
	v_pk_mul_f32 v[96:97], v[106:107], s[82:83] op_sel_hi:[1,0]
	v_pk_mul_f32 v[98:99], v[118:119], s[82:83] op_sel_hi:[1,0]
	s_waitcnt vmcnt(2)
	v_pk_mul_f32 v[104:105], v[174:175], s[82:83] op_sel_hi:[1,0]
	s_waitcnt vmcnt(1)
	v_pk_mul_f32 v[106:107], v[178:179], s[82:83] op_sel_hi:[1,0]
	v_cvt_pk_fp8_f32 v70, v76, v86 op_sel:[0,0,1]
	v_cvt_pk_fp8_f32 v71, v88, v90 op_sel:[0,0,1]
	v_cvt_pk_fp8_f32 v72, v96, v98 op_sel:[0,0,1]
	v_cvt_pk_fp8_f32 v73, v104, v106 op_sel:[0,0,1]
	v_or_b32_e32 v6, 1, v78
	v_pk_mul_f32 v[30:31], v[64:65], s[82:83] op_sel_hi:[1,0]
	v_pk_mul_f32 v[10:11], v[24:25], s[82:83] op_sel_hi:[1,0]
	global_store_dwordx4 v[108:109], v[70:73], off offset:16
	v_mad_i64_i32 v[108:109], s[0:1], v6, s5, v[0:1]
	s_nop 0
	v_mov_b32_e32 v70, v81
	v_mov_b32_e32 v71, v81
	v_mov_b32_e32 v72, v81
	v_mov_b32_e32 v73, v81
	v_cvt_pk_fp8_f32 v70, v127, v7
	v_cvt_pk_fp8_f32 v71, v131, v135
	v_cvt_pk_fp8_f32 v72, v41, v141
	v_cvt_pk_fp8_f32 v73, v149, v161
	v_cvt_pk_fp8_f32 v70, v129, v133 op_sel:[0,0,1]
	v_cvt_pk_fp8_f32 v71, v137, v139 op_sel:[0,0,1]
	v_cvt_pk_fp8_f32 v72, v143, v151 op_sel:[0,0,1]
	v_cvt_pk_fp8_f32 v73, v145, v153 op_sel:[0,0,1]
	v_pk_mul_f32 v[24:25], v[36:37], s[82:83] op_sel_hi:[1,0]
	v_pk_mul_f32 v[26:27], v[56:57], s[82:83] op_sel_hi:[1,0]
	v_pk_mul_f32 v[34:35], v[68:69], s[82:83] op_sel_hi:[1,0]
	global_store_dwordx4 v[108:109], v[70:73], off
	v_or_b32_e32 v6, 2, v78
	v_mad_i64_i32 v[6:7], s[0:1], v6, s5, v[0:1]
	v_mov_b32_e32 v70, v81
	v_mov_b32_e32 v71, v81
	v_mov_b32_e32 v72, v81
	v_mov_b32_e32 v73, v81
	v_cvt_pk_fp8_f32 v70, v147, v75
	v_cvt_pk_fp8_f32 v71, v83, v85
	v_cvt_pk_fp8_f32 v72, v93, v95
	v_cvt_pk_fp8_f32 v73, v101, v103
	v_cvt_pk_fp8_f32 v70, v77, v87 op_sel:[0,0,1]
	v_cvt_pk_fp8_f32 v71, v89, v91 op_sel:[0,0,1]
	v_cvt_pk_fp8_f32 v72, v97, v99 op_sel:[0,0,1]
	v_cvt_pk_fp8_f32 v73, v105, v107 op_sel:[0,0,1]
	v_pk_mul_f32 v[36:37], v[60:61], s[82:83] op_sel_hi:[1,0]
	v_pk_mul_f32 v[56:57], v[112:113], s[82:83] op_sel_hi:[1,0]
	v_pk_mul_f32 v[62:63], v[116:117], s[82:83] op_sel_hi:[1,0]
	global_store_dwordx4 v[108:109], v[70:73], off offset:16
	v_pk_mul_f32 v[64:65], v[158:159], s[82:83] op_sel_hi:[1,0]
	v_pk_mul_f32 v[60:61], v[120:121], s[82:83] op_sel_hi:[1,0]
	v_mov_b32_e32 v70, v81
	v_mov_b32_e32 v71, v81
	v_mov_b32_e32 v72, v81
	v_mov_b32_e32 v73, v81
	v_cvt_pk_fp8_f32 v70, v2, v8
	v_cvt_pk_fp8_f32 v71, v12, v14
	v_cvt_pk_fp8_f32 v72, v20, v22
	v_cvt_pk_fp8_f32 v73, v28, v30
	v_cvt_pk_fp8_f32 v70, v4, v10 op_sel:[0,0,1]
	v_cvt_pk_fp8_f32 v71, v16, v18 op_sel:[0,0,1]
	v_cvt_pk_fp8_f32 v72, v24, v26 op_sel:[0,0,1]
	v_cvt_pk_fp8_f32 v73, v32, v34 op_sel:[0,0,1]
	v_pk_mul_f32 v[66:67], v[176:177], s[82:83] op_sel_hi:[1,0]
	v_pk_mul_f32 v[68:69], v[180:181], s[82:83] op_sel_hi:[1,0]
	v_or_b32_e32 v2, 3, v78
	global_store_dwordx4 v[6:7], v[70:73], off
	v_mad_i64_i32 v[0:1], s[0:1], v2, s5, v[0:1]
	s_nop 0
	v_mov_b32_e32 v70, v81
	v_mov_b32_e32 v71, v81
	v_mov_b32_e32 v72, v81
	v_mov_b32_e32 v73, v81
	v_cvt_pk_fp8_f32 v70, v36, v42
	v_cvt_pk_fp8_f32 v71, v46, v48
	v_cvt_pk_fp8_f32 v72, v54, v56
	v_cvt_pk_fp8_f32 v73, v62, v64
	v_cvt_pk_fp8_f32 v70, v38, v44 op_sel:[0,0,1]
	v_cvt_pk_fp8_f32 v71, v50, v52 op_sel:[0,0,1]
	v_cvt_pk_fp8_f32 v72, v58, v60 op_sel:[0,0,1]
	v_cvt_pk_fp8_f32 v73, v66, v68 op_sel:[0,0,1]
	s_mov_b64 s[0:1], 0
	global_store_dwordx4 v[6:7], v[70:73], off offset:16
; __device__ __forceinline__ unsigned pk4_fp8(float a, float b, float c, float d) { int w = 0; w = __builtin_amdgcn_cvt_pk_fp8_f32(a, b, w, false); w = __builtin_amdgcn_cvt_pk_fp8_f32(c, d, w, true); return (unsigned)w; }
; #define GAS __attribute__((address_space(1)))
; template <int MODE, int KL>
; __device__ __forceinline__ void p0_cvt_item(const float* W, int K, int N, unsigned char* WT, int il, int which, int item, int lane, const float* gk, float scale, int ldk, int koff) {
;     const int nblk = N >> 6, kb = item / nblk, nb = item - kb * nblk, nq = lane & 15, kr = lane >> 4, k0 = 4 * KL * kb + KL * kr, n0 = 64 * nb + 4 * nq;
;     const GAS f32x4* src = (const GAS f32x4*)(W + (size_t)k0 * N + n0);
;     f32x4 v[KL];
; #pragma unroll
;     for (int i = 0; i < KL; ++i) v[i] = src[(size_t)i * (N >> 2)];
;     if (MODE == 1) {
; #pragma unroll
;         for (int q = 0; q < KL / 4; ++q) { const f32x4 g = *(const GAS f32x4*)(gk + k0 + 4 * q); v[4 * q] *= g.x; v[4 * q + 1] *= g.y; v[4 * q + 2] *= g.z; v[4 * q + 3] *= g.w; } }
;     if (MODE == 2) {
; #pragma unroll
;         for (int i = 0; i < KL; ++i) v[i] *= scale; }
; #pragma unroll
;     for (int c = 0; c < 4; ++c) { const int n = n0 + c, row = il ? ((n >> 4) * 32 + which * 16 + (n & 15)) : n;
;         if (MODE == 2) { GAS v4u* dst = (GAS v4u*)(WT + (size_t)row * ldk + koff + k0);
; #pragma unroll
;             for (int q = 0; q < KL / 16; ++q) { v4u o;
;                 o.x = pg8::pk4_fp8(v[16 * q][c], v[16 * q + 1][c], v[16 * q + 2][c], v[16 * q + 3][c]);     o.y = pg8::pk4_fp8(v[16 * q + 4][c], v[16 * q + 5][c], v[16 * q + 6][c], v[16 * q + 7][c]);
;                 o.z = pg8::pk4_fp8(v[16 * q + 8][c], v[16 * q + 9][c], v[16 * q + 10][c], v[16 * q + 11][c]); o.w = pg8::pk4_fp8(v[16 * q + 12][c], v[16 * q + 13][c], v[16 * q + 14][c], v[16 * q + 15][c]);
;                 dst[q] = o; } }
; __device__ __forceinline__ void moe_cvt_tile(const Args& a, int set, int id, int lane) {
;     ...
;     if (j < 16) { const int e = set * 8 + (j & 7), wh = j >> 3;
;         p0_cvt_item<2, 32>(a.in[17 + wh] + (size_t)e * D * FE, D, FE, a.ws + W_13M + (size_t)e * 2 * FE * D, 1, wh, item, lane, nullptr, 32.f, D, 0); }
.LBB0_1036:
	s_andn2_b64 vcc, exec, s[0:1]
	s_cbranch_vccnz .LBB0_1033
	s_and_b32 s0, s4, 7
	s_ashr_i32 s4, s4, 3
	s_ashr_i32 s5, s4, 31
	s_or_b32 s8, s0, 8
	s_lshl_b64 s[0:1], s[4:5], 3
	s_add_u32 s0, s66, s0
	s_addc_u32 s1, s67, s1
	v_mov_b64_e32 v[0:1], s[0:1]
	global_load_dwordx2 v[0:1], v[0:1], off offset:136
	v_mov_b64_e32 v[2:3], s[66:67]
	global_load_dwordx2 v[2:3], v[2:3], off offset:192
	s_mul_hi_i32 s0, s7, 0x92492493
	s_add_i32 s0, s0, s7
	s_lshr_b32 s1, s0, 31
	s_ashr_i32 s0, s0, 5
	s_add_i32 s0, s0, s1
	s_mul_i32 s1, s0, 0xffffffc8
	s_mul_i32 s62, s8, 0xe00000
	s_add_i32 s1, s1, s7
	v_lshl_add_u32 v72, s0, 7, v80
	v_lshl_or_b32 v74, s1, 6, v154
	s_movk_i32 s0, 0x3800
	v_ashrrev_i32_e32 v75, 31, v74
	v_ashrrev_i32_e32 v73, 31, v72
	s_waitcnt vmcnt(0) lgkmcnt(0)
	v_lshl_add_u64 v[0:1], v[0:1], 0, s[62:63]
	v_mad_i64_i32 v[0:1], s[0:1], v72, s0, v[0:1]
	v_lshl_add_u64 v[8:9], v[74:75], 2, v[0:1]
	s_movk_i32 s0, 0x3000
	v_add_co_u32_e32 v4, vcc, s0, v8
	s_movk_i32 s0, 0x7000
	s_nop 0
	v_addc_co_u32_e32 v5, vcc, 0, v9, vcc
	v_add_co_u32_e32 v10, vcc, s0, v8
	s_mov_b32 s0, 0xe000
	s_nop 0
	v_addc_co_u32_e32 v11, vcc, 0, v9, vcc
	v_add_co_u32_e32 v14, vcc, s97, v8
	s_mul_i32 s62, s8, 0x700000
	s_nop 0
	v_addc_co_u32_e32 v15, vcc, 0, v9, vcc
	v_add_co_u32_e32 v18, vcc, s0, v8
	s_mov_b32 s0, 0x11000
	s_nop 0
	v_addc_co_u32_e32 v19, vcc, 0, v9, vcc
	v_add_co_u32_e32 v22, vcc, s0, v8
	s_mov_b32 s0, 0x15000
	s_nop 0
	v_addc_co_u32_e32 v23, vcc, 0, v9, vcc
	v_add_co_u32_e32 v26, vcc, s0, v8
	s_mov_b32 s0, 0x18000
	s_nop 0
	v_addc_co_u32_e32 v27, vcc, 0, v9, vcc
	v_add_co_u32_e32 v30, vcc, s0, v8
	s_mov_b32 s0, 0x1c000
	s_nop 0
	v_addc_co_u32_e32 v31, vcc, 0, v9, vcc
	v_add_co_u32_e32 v34, vcc, s0, v8
	s_mov_b32 s0, 0x1f000
	s_nop 0
	v_addc_co_u32_e32 v35, vcc, 0, v9, vcc
	v_add_co_u32_e32 v38, vcc, s0, v8
	s_mov_b32 s0, 0x23000
	s_nop 0
	v_addc_co_u32_e32 v39, vcc, 0, v9, vcc
	v_add_co_u32_e32 v42, vcc, s0, v8
	s_mov_b32 s0, 0x26000
	s_nop 0
	v_addc_co_u32_e32 v43, vcc, 0, v9, vcc
	v_add_co_u32_e32 v46, vcc, s0, v8
	s_mov_b32 s0, 0x2a000
	s_nop 0
	v_addc_co_u32_e32 v47, vcc, 0, v9, vcc
	v_add_co_u32_e32 v50, vcc, s0, v8
	s_mov_b32 s0, 0x2d000
	s_nop 0
	v_addc_co_u32_e32 v51, vcc, 0, v9, vcc
	v_add_co_u32_e32 v54, vcc, s0, v8
	s_mov_b32 s0, 0x31000
	s_nop 0
	v_addc_co_u32_e32 v55, vcc, 0, v9, vcc
	global_load_dwordx4 v[58:61], v[54:55], off offset:2048
	v_add_co_u32_e32 v54, vcc, s0, v8
	s_mov_b32 s0, 0x34000
	s_nop 0
	v_addc_co_u32_e32 v55, vcc, 0, v9, vcc
	v_add_co_u32_e32 v62, vcc, s0, v8
	s_mov_b32 s0, 0x38000
	s_nop 0
	v_addc_co_u32_e32 v63, vcc, 0, v9, vcc
	v_add_co_u32_e32 v66, vcc, s0, v8
	s_mov_b32 s0, 0x3b000
	s_nop 0
	v_addc_co_u32_e32 v67, vcc, 0, v9, vcc
	v_add_co_u32_e32 v76, vcc, s0, v8
	s_mov_b32 s0, 0x3f000
	s_nop 0
	v_addc_co_u32_e32 v77, vcc, 0, v9, vcc
	global_load_dwordx4 v[112:115], v[76:77], off offset:2048
	v_add_co_u32_e32 v76, vcc, s0, v8
	s_mov_b32 s0, 0x42000
	s_nop 0
	v_addc_co_u32_e32 v77, vcc, 0, v9, vcc
	global_load_dwordx4 v[66:69], v[66:67], off
	v_lshl_add_u64 v[70:71], v[2:3], 0, s[62:63]
	global_load_dwordx4 v[116:119], v[76:77], off
	v_add_co_u32_e32 v76, vcc, s0, v8
	s_mov_b32 s0, 0x46000
	s_nop 0
	v_addc_co_u32_e32 v77, vcc, 0, v9, vcc
	global_load_dwordx4 v[120:123], v[76:77], off offset:2048
	v_add_co_u32_e32 v76, vcc, s0, v8
	s_mov_b32 s0, 0x49000
	s_nop 0
	v_addc_co_u32_e32 v77, vcc, 0, v9, vcc
	global_load_dwordx4 v[124:127], v[76:77], off
	v_add_co_u32_e32 v76, vcc, s0, v8
	s_mov_b32 s0, 0x4d000
	s_nop 0
	v_addc_co_u32_e32 v77, vcc, 0, v9, vcc
	global_load_dwordx4 v[128:131], v[76:77], off offset:2048
	v_add_co_u32_e32 v76, vcc, s0, v8
	global_load_dwordx4 v[0:3], v[8:9], off
	s_nop 0
	v_addc_co_u32_e32 v77, vcc, 0, v9, vcc
	s_mov_b32 s0, 0x50000
	global_load_dwordx4 v[132:135], v[76:77], off
	v_add_co_u32_e32 v76, vcc, s0, v8
	global_load_dwordx4 v[4:7], v[4:5], off offset:2048
	s_nop 0
	v_addc_co_u32_e32 v77, vcc, 0, v9, vcc
	s_mov_b32 s0, 0x54000
	global_load_dwordx4 v[136:139], v[76:77], off offset:2048
	v_add_co_u32_e32 v76, vcc, s0, v8
	s_mov_b32 s0, 0x57000
	s_nop 0
	v_addc_co_u32_e32 v77, vcc, 0, v9, vcc
	global_load_dwordx4 v[140:143], v[76:77], off
	v_add_co_u32_e32 v76, vcc, s0, v8
	global_load_dwordx4 v[14:17], v[14:15], off offset:2048
	s_nop 0
	v_addc_co_u32_e32 v77, vcc, 0, v9, vcc
	global_load_dwordx4 v[18:21], v[18:19], off
	s_mov_b32 s0, 0x5b000
	global_load_dwordx4 v[22:25], v[22:23], off offset:2048
	s_waitcnt vmcnt(14)
	v_pk_mul_f32 v[110:111], v[58:59], s[96:97] op_sel_hi:[1,0]
	global_load_dwordx4 v[30:33], v[30:31], off offset:2048
	s_waitcnt vmcnt(14)
	v_pk_mul_f32 v[108:109], v[112:113], s[96:97] op_sel_hi:[1,0]
	global_load_dwordx4 v[34:37], v[34:35], off
	s_waitcnt vmcnt(14)
	v_pk_mul_f32 v[100:101], v[66:67], s[96:97] op_sel_hi:[1,0]
	global_load_dwordx4 v[38:41], v[38:39], off offset:2048
	s_waitcnt vmcnt(14)
	v_pk_mul_f32 v[112:113], v[116:117], s[96:97] op_sel_hi:[1,0]
	global_load_dwordx4 v[46:49], v[46:47], off offset:2048
	s_waitcnt vmcnt(14)
	v_pk_mul_f32 v[116:117], v[120:121], s[96:97] op_sel_hi:[1,0]
	global_load_dwordx4 v[50:53], v[50:51], off
	s_waitcnt vmcnt(12)
	v_pk_mul_f32 v[2:3], v[2:3], s[96:97] op_sel_hi:[1,0]
	global_load_dwordx4 v[144:147], v[76:77], off offset:2048
	v_add_co_u32_e32 v76, vcc, s0, v8
	s_mov_b32 s0, 0x5e000
	s_nop 0
	v_addc_co_u32_e32 v77, vcc, 0, v9, vcc
	global_load_dwordx4 v[148:151], v[76:77], off
	v_add_co_u32_e32 v76, vcc, s0, v8
	global_load_dwordx4 v[10:13], v[10:11], off
	s_nop 0
	v_addc_co_u32_e32 v77, vcc, 0, v9, vcc
	global_load_dwordx4 v[26:29], v[26:27], off
	s_mov_b32 s0, 0x62000
	global_load_dwordx4 v[42:45], v[42:43], off
	s_waitcnt vmcnt(15)
; __device__ __forceinline__ unsigned pk4_fp8(float a, float b, float c, float d) { int w = 0; w = __builtin_amdgcn_cvt_pk_fp8_f32(a, b, w, false); w = __builtin_amdgcn_cvt_pk_fp8_f32(c, d, w, true); return (unsigned)w; }
; #define GAS __attribute__((address_space(1)))
; template <int MODE, int KL>
; __device__ __forceinline__ void p0_cvt_item(const float* W, int K, int N, unsigned char* WT, int il, int which, int item, int lane, const float* gk, float scale, int ldk, int koff) {
;     const int nblk = N >> 6, kb = item / nblk, nb = item - kb * nblk, nq = lane & 15, kr = lane >> 4, k0 = 4 * KL * kb + KL * kr, n0 = 64 * nb + 4 * nq;
;     const GAS f32x4* src = (const GAS f32x4*)(W + (size_t)k0 * N + n0);
;     f32x4 v[KL];
; #pragma unroll
;     for (int i = 0; i < KL; ++i) v[i] = src[(size_t)i * (N >> 2)];
;     if (MODE == 1) {
; #pragma unroll
;         for (int q = 0; q < KL / 4; ++q) { const f32x4 g = *(const GAS f32x4*)(gk + k0 + 4 * q); v[4 * q] *= g.x; v[4 * q + 1] *= g.y; v[4 * q + 2] *= g.z; v[4 * q + 3] *= g.w; } }
;     if (MODE == 2) {
; #pragma unroll
;         for (int i = 0; i < KL; ++i) v[i] *= scale; }
; #pragma unroll
;     for (int c = 0; c < 4; ++c) { const int n = n0 + c, row = il ? ((n >> 4) * 32 + which * 16 + (n & 15)) : n;
;         if (MODE == 2) { GAS v4u* dst = (GAS v4u*)(WT + (size_t)row * ldk + koff + k0);
; #pragma unroll
;             for (int q = 0; q < KL / 16; ++q) { v4u o;
;                 o.x = pg8::pk4_fp8(v[16 * q][c], v[16 * q + 1][c], v[16 * q + 2][c], v[16 * q + 3][c]);     o.y = pg8::pk4_fp8(v[16 * q + 4][c], v[16 * q + 5][c], v[16 * q + 6][c], v[16 * q + 7][c]);
;                 o.z = pg8::pk4_fp8(v[16 * q + 8][c], v[16 * q + 9][c], v[16 * q + 10][c], v[16 * q + 11][c]); o.w = pg8::pk4_fp8(v[16 * q + 12][c], v[16 * q + 13][c], v[16 * q + 14][c], v[16 * q + 15][c]);
;                 dst[q] = o; } }
	v_pk_mul_f32 v[78:79], v[4:5], s[96:97] op_sel_hi:[1,0]
	global_load_dwordx4 v[54:57], v[54:55], off
	v_pk_mul_f32 v[120:121], v[132:133], s[96:97] op_sel_hi:[1,0]
	global_load_dwordx4 v[62:65], v[62:63], off offset:2048
	s_waitcnt vmcnt(14)
	v_pk_mul_f32 v[86:87], v[14:15], s[96:97] op_sel_hi:[1,0]
	global_load_dwordx4 v[156:159], v[76:77], off offset:2048
	v_add_co_u32_e32 v76, vcc, s0, v8
	s_mov_b32 s0, 0x65000
	s_nop 0
	v_addc_co_u32_e32 v77, vcc, 0, v9, vcc
	global_load_dwordx4 v[174:177], v[76:77], off
	v_add_co_u32_e32 v76, vcc, s0, v8
	s_mov_b32 s0, 0x69000
	s_nop 0
	v_addc_co_u32_e32 v77, vcc, 0, v9, vcc
	global_load_dwordx4 v[178:181], v[76:77], off offset:2048
	v_add_co_u32_e32 v76, vcc, s0, v8
	s_mov_b32 s0, 0x6c000
	s_nop 0
	v_addc_co_u32_e32 v77, vcc, 0, v9, vcc
	v_add_co_u32_e32 v8, vcc, s0, v8
	global_load_dwordx4 v[182:185], v[76:77], off
	s_nop 0
	v_addc_co_u32_e32 v9, vcc, 0, v9, vcc
	global_load_dwordx4 v[186:189], v[8:9], off offset:2048
	v_pk_mul_f32 v[76:77], v[0:1], s[96:97] op_sel_hi:[1,0]
	v_lshlrev_b32_e32 v0, 1, v74
	v_and_b32_e32 v0, 0xffffffe0, v0
	v_pk_mul_f32 v[8:9], v[6:7], s[96:97] op_sel_hi:[1,0]
	v_lshl_add_u32 v6, s4, 4, v0
	v_or_b32_e32 v6, v6, v155
	v_lshl_add_u64 v[0:1], v[70:71], 0, v[72:73]
	s_mov_b64 s[0:1], 0x25f00000
	v_ashrrev_i32_e32 v7, 31, v6
	v_lshl_add_u64 v[0:1], v[0:1], 0, s[0:1]
	v_lshlrev_b64 v[70:71], 10, v[6:7]
	s_waitcnt vmcnt(18)
	v_pk_mul_f32 v[84:85], v[18:19], s[96:97] op_sel_hi:[1,0]
	s_waitcnt vmcnt(17)
	v_pk_mul_f32 v[88:89], v[22:23], s[96:97] op_sel_hi:[1,0]
	s_waitcnt vmcnt(15)
	v_pk_mul_f32 v[92:93], v[34:35], s[96:97] op_sel_hi:[1,0]
	s_waitcnt vmcnt(14)
	v_pk_mul_f32 v[22:23], v[40:41], s[96:97] op_sel_hi:[1,0]
	v_pk_mul_f32 v[40:41], v[38:39], s[96:97] op_sel_hi:[1,0]
	v_lshl_add_u64 v[74:75], v[0:1], 0, v[70:71]
	v_mov_b32_e32 v70, v81
	v_mov_b32_e32 v71, v81
	v_mov_b32_e32 v72, v81
	v_mov_b32_e32 v73, v81
	s_waitcnt vmcnt(12)
	v_pk_mul_f32 v[102:103], v[50:51], s[96:97] op_sel_hi:[1,0]
	v_cvt_pk_fp8_f32 v70, v76, v78
	v_cvt_pk_fp8_f32 v71, v84, v88
	v_cvt_pk_fp8_f32 v72, v92, v40
	v_cvt_pk_fp8_f32 v73, v102, v110
	v_pk_mul_f32 v[94:95], v[30:31], s[96:97] op_sel_hi:[1,0]
	v_pk_mul_f32 v[104:105], v[46:47], s[96:97] op_sel_hi:[1,0]
	v_pk_mul_f32 v[38:39], v[118:119], s[96:97] op_sel_hi:[1,0]
	v_pk_mul_f32 v[46:47], v[126:127], s[96:97] op_sel_hi:[1,0]
	v_pk_mul_f32 v[118:119], v[128:129], s[96:97] op_sel_hi:[1,0]
	v_pk_mul_f32 v[50:51], v[134:135], s[96:97] op_sel_hi:[1,0]
	v_pk_mul_f32 v[14:15], v[24:25], s[96:97] op_sel_hi:[1,0]
	v_pk_mul_f32 v[30:31], v[60:61], s[96:97] op_sel_hi:[1,0]
	v_pk_mul_f32 v[18:19], v[32:33], s[96:97] op_sel_hi:[1,0]
	v_or_b32_e32 v40, 2, v6
	s_waitcnt vmcnt(11)
	v_pk_mul_f32 v[126:127], v[144:145], s[96:97] op_sel_hi:[1,0]
	s_waitcnt vmcnt(10)
	v_pk_mul_f32 v[128:129], v[148:149], s[96:97] op_sel_hi:[1,0]
	v_pk_mul_f32 v[58:59], v[150:151], s[96:97] op_sel_hi:[1,0]
	s_waitcnt vmcnt(9)
	v_pk_mul_f32 v[82:83], v[10:11], s[96:97] op_sel_hi:[1,0]
	s_nop 0
	v_cvt_pk_fp8_f32 v70, v82, v86 op_sel:[0,0,1]
	v_pk_mul_f32 v[10:11], v[16:17], s[96:97] op_sel_hi:[1,0]
	s_waitcnt vmcnt(8)
	v_pk_mul_f32 v[90:91], v[26:27], s[96:97] op_sel_hi:[1,0]
	v_pk_mul_f32 v[16:17], v[28:29], s[96:97] op_sel_hi:[1,0]
	s_waitcnt vmcnt(7)
	v_pk_mul_f32 v[96:97], v[42:43], s[96:97] op_sel_hi:[1,0]
	v_cvt_pk_fp8_f32 v71, v90, v94 op_sel:[0,0,1]
	s_waitcnt vmcnt(6)
	v_pk_mul_f32 v[98:99], v[54:55], s[96:97] op_sel_hi:[1,0]
	v_cvt_pk_fp8_f32 v72, v96, v104 op_sel:[0,0,1]
	s_waitcnt vmcnt(5)
	v_pk_mul_f32 v[106:107], v[62:63], s[96:97] op_sel_hi:[1,0]
	v_pk_mul_f32 v[42:43], v[114:115], s[96:97] op_sel_hi:[1,0]
	v_cvt_pk_fp8_f32 v73, v98, v106 op_sel:[0,0,1]
	v_pk_mul_f32 v[114:115], v[124:125], s[96:97] op_sel_hi:[1,0]
	v_pk_mul_f32 v[124:125], v[140:141], s[96:97] op_sel_hi:[1,0]
	v_pk_mul_f32 v[24:25], v[44:45], s[96:97] op_sel_hi:[1,0]
	global_store_dwordx4 v[74:75], v[70:73], off
	v_pk_mul_f32 v[26:27], v[48:49], s[96:97] op_sel_hi:[1,0]
	s_waitcnt vmcnt(4)
	v_pk_mul_f32 v[132:133], v[174:175], s[96:97] op_sel_hi:[1,0]
	v_mov_b32_e32 v70, v81
	v_mov_b32_e32 v71, v81
	v_mov_b32_e32 v72, v81
	v_mov_b32_e32 v73, v81
	v_cvt_pk_fp8_f32 v70, v100, v108
	s_waitcnt vmcnt(3)
	v_pk_mul_f32 v[134:135], v[178:179], s[96:97] op_sel_hi:[1,0]
	v_cvt_pk_fp8_f32 v71, v114, v118
	v_cvt_pk_fp8_f32 v72, v124, v126
	v_cvt_pk_fp8_f32 v73, v132, v134
	v_pk_mul_f32 v[28:29], v[52:53], s[96:97] op_sel_hi:[1,0]
	v_pk_mul_f32 v[44:45], v[122:123], s[96:97] op_sel_hi:[1,0]
	v_pk_mul_f32 v[48:49], v[130:131], s[96:97] op_sel_hi:[1,0]
	v_pk_mul_f32 v[52:53], v[138:139], s[96:97] op_sel_hi:[1,0]
	v_pk_mul_f32 v[122:123], v[136:137], s[96:97] op_sel_hi:[1,0]
	v_pk_mul_f32 v[130:131], v[156:157], s[96:97] op_sel_hi:[1,0]
	s_waitcnt vmcnt(2)
	v_pk_mul_f32 v[136:137], v[182:183], s[96:97] op_sel_hi:[1,0]
	s_waitcnt vmcnt(1)
; __device__ __forceinline__ unsigned pk4_fp8(float a, float b, float c, float d) { int w = 0; w = __builtin_amdgcn_cvt_pk_fp8_f32(a, b, w, false); w = __builtin_amdgcn_cvt_pk_fp8_f32(c, d, w, true); return (unsigned)w; }
; #define GAS __attribute__((address_space(1)))
; template <int MODE, int KL>
; __device__ __forceinline__ void p0_cvt_item(const float* W, int K, int N, unsigned char* WT, int il, int which, int item, int lane, const float* gk, float scale, int ldk, int koff) {
;     ...
;     for (int c = 0; c < 4; ++c) { const int n = n0 + c, row = il ? ((n >> 4) * 32 + which * 16 + (n & 15)) : n;
;         if (MODE == 2) { GAS v4u* dst = (GAS v4u*)(WT + (size_t)row * ldk + koff + k0);
; #pragma unroll
;             for (int q = 0; q < KL / 16; ++q) { v4u o;
;                 o.x = pg8::pk4_fp8(v[16 * q][c], v[16 * q + 1][c], v[16 * q + 2][c], v[16 * q + 3][c]);     o.y = pg8::pk4_fp8(v[16 * q + 4][c], v[16 * q + 5][c], v[16 * q + 6][c], v[16 * q + 7][c]);
;                 o.z = pg8::pk4_fp8(v[16 * q + 8][c], v[16 * q + 9][c], v[16 * q + 10][c], v[16 * q + 11][c]); o.w = pg8::pk4_fp8(v[16 * q + 12][c], v[16 * q + 13][c], v[16 * q + 14][c], v[16 * q + 15][c]);
;                 dst[q] = o; } }
	v_pk_mul_f32 v[138:139], v[186:187], s[96:97] op_sel_hi:[1,0]
	v_cvt_pk_fp8_f32 v70, v112, v116 op_sel:[0,0,1]
	v_cvt_pk_fp8_f32 v71, v120, v122 op_sel:[0,0,1]
	v_cvt_pk_fp8_f32 v72, v128, v130 op_sel:[0,0,1]
	v_cvt_pk_fp8_f32 v73, v136, v138 op_sel:[0,0,1]
	v_pk_mul_f32 v[4:5], v[12:13], s[96:97] op_sel_hi:[1,0]
	v_pk_mul_f32 v[12:13], v[20:21], s[96:97] op_sel_hi:[1,0]
	v_pk_mul_f32 v[20:21], v[36:37], s[96:97] op_sel_hi:[1,0]
	global_store_dwordx4 v[74:75], v[70:73], off offset:16
	v_pk_mul_f32 v[32:33], v[56:57], s[96:97] op_sel_hi:[1,0]
	v_pk_mul_f32 v[34:35], v[64:65], s[96:97] op_sel_hi:[1,0]
	v_or_b32_e32 v70, 1, v6
	v_ashrrev_i32_e32 v71, 31, v70
	v_lshlrev_b64 v[70:71], 10, v[70:71]
	v_lshl_add_u64 v[74:75], v[0:1], 0, v[70:71]
	v_mov_b32_e32 v70, v81
	v_mov_b32_e32 v71, v81
	v_mov_b32_e32 v72, v81
	v_mov_b32_e32 v73, v81
	v_cvt_pk_fp8_f32 v70, v77, v79
	v_cvt_pk_fp8_f32 v71, v85, v89
	v_cvt_pk_fp8_f32 v72, v93, v41
	v_cvt_pk_fp8_f32 v73, v103, v111
	v_cvt_pk_fp8_f32 v70, v83, v87 op_sel:[0,0,1]
	v_cvt_pk_fp8_f32 v71, v91, v95 op_sel:[0,0,1]
	v_cvt_pk_fp8_f32 v72, v97, v105 op_sel:[0,0,1]
	v_cvt_pk_fp8_f32 v73, v99, v107 op_sel:[0,0,1]
	v_ashrrev_i32_e32 v41, 31, v40
	v_lshlrev_b64 v[40:41], 10, v[40:41]
	v_lshl_add_u64 v[40:41], v[0:1], 0, v[40:41]
	global_store_dwordx4 v[74:75], v[70:73], off
	v_pk_mul_f32 v[36:37], v[68:69], s[96:97] op_sel_hi:[1,0]
	v_pk_mul_f32 v[54:55], v[142:143], s[96:97] op_sel_hi:[1,0]
	v_mov_b32_e32 v70, v81
	v_mov_b32_e32 v71, v81
	v_mov_b32_e32 v72, v81
	v_mov_b32_e32 v73, v81
	v_cvt_pk_fp8_f32 v70, v101, v109
	v_cvt_pk_fp8_f32 v71, v115, v119
	v_cvt_pk_fp8_f32 v72, v125, v127
	v_cvt_pk_fp8_f32 v73, v133, v135
	v_cvt_pk_fp8_f32 v70, v113, v117 op_sel:[0,0,1]
	v_cvt_pk_fp8_f32 v71, v121, v123 op_sel:[0,0,1]
	v_cvt_pk_fp8_f32 v72, v129, v131 op_sel:[0,0,1]
	v_cvt_pk_fp8_f32 v73, v137, v139 op_sel:[0,0,1]
	v_pk_mul_f32 v[56:57], v[146:147], s[96:97] op_sel_hi:[1,0]
	v_pk_mul_f32 v[62:63], v[176:177], s[96:97] op_sel_hi:[1,0]
	v_pk_mul_f32 v[64:65], v[180:181], s[96:97] op_sel_hi:[1,0]
	global_store_dwordx4 v[74:75], v[70:73], off offset:16
	v_pk_mul_f32 v[60:61], v[158:159], s[96:97] op_sel_hi:[1,0]
	v_pk_mul_f32 v[66:67], v[184:185], s[96:97] op_sel_hi:[1,0]
	v_mov_b32_e32 v70, v81
	v_mov_b32_e32 v71, v81
	v_mov_b32_e32 v72, v81
	v_mov_b32_e32 v73, v81
	v_cvt_pk_fp8_f32 v70, v2, v8
	v_cvt_pk_fp8_f32 v71, v12, v14
	v_cvt_pk_fp8_f32 v72, v20, v22
	v_cvt_pk_fp8_f32 v73, v28, v30
	v_cvt_pk_fp8_f32 v70, v4, v10 op_sel:[0,0,1]
	v_cvt_pk_fp8_f32 v71, v16, v18 op_sel:[0,0,1]
	v_cvt_pk_fp8_f32 v72, v24, v26 op_sel:[0,0,1]
	v_cvt_pk_fp8_f32 v73, v32, v34 op_sel:[0,0,1]
	v_pk_mul_f32 v[68:69], v[188:189], s[96:97] op_sel_hi:[1,0]
	v_or_b32_e32 v6, 3, v6
	v_ashrrev_i32_e32 v7, 31, v6
	global_store_dwordx4 v[40:41], v[70:73], off
	v_lshlrev_b64 v[6:7], 10, v[6:7]
	v_lshl_add_u64 v[0:1], v[0:1], 0, v[6:7]
	v_mov_b32_e32 v70, v81
	v_mov_b32_e32 v71, v81
	v_mov_b32_e32 v72, v81
	v_mov_b32_e32 v73, v81
	v_cvt_pk_fp8_f32 v70, v36, v42
	v_cvt_pk_fp8_f32 v71, v46, v48
	v_cvt_pk_fp8_f32 v72, v54, v56
	v_cvt_pk_fp8_f32 v73, v62, v64
	v_cvt_pk_fp8_f32 v70, v38, v44 op_sel:[0,0,1]
	v_cvt_pk_fp8_f32 v71, v50, v52 op_sel:[0,0,1]
	v_cvt_pk_fp8_f32 v72, v58, v60 op_sel:[0,0,1]
	v_cvt_pk_fp8_f32 v73, v66, v68 op_sel:[0,0,1]
	global_store_dwordx4 v[40:41], v[70:73], off offset:16
	s_branch .LBB0_1033
; __device__ __forceinline__ int ld_agent_i(const int* p) { return (int)__hip_atomic_load((const unsigned*)p, RLX_AGENT); }
;     ...
;     const int tid = tid_o, wid = __builtin_amdgcn_readfirstlane(tid >> 6), lane = tid & 63, wr = wid >> 2, wc = wid & 3, fr = lane & 15, fq = lane >> 4;
;     const int K = g.K, nt = K / BK;
;     unsigned voffA[2], voffB[2];
; #pragma unroll
;     for (int i = 0; i < 2; ++i) { int R, C; stage_rc(tid * 16 + i * 8192, R, C); const int Rb = Epi::PERM ? ((R & ~31) + perm32(R & 31)) : R;
;         voffA[i] = (unsigned)(R * K + C) * 2u; voffB[i] = (unsigned)(Rb * K + C) * 2u; }
;     const size_t kstep = (size_t)(BK * 2);
;     const size_t hstep = (size_t)HALF * K * 2;
;     const size_t tstep = 2 * hstep;
;     const unsigned ldsw = (unsigned)wid * 1024u;
;     const int aoff = lds_byte(wr * 64 + fr, fq * 8), boff = lds_byte(wc * 32 + fr, fq * 8);
;     ...
;     Unit cur, nxt; int ui = 0;
;     if (!S.next(0, cur)) return;
;     f32x4 acc[2][2][4][2];
; #pragma unroll
;     for (int a = 0; a < 2; ++a)
; #pragma unroll
;         for (int b = 0; b < 2; ++b)
; #pragma unroll
;             for (int m = 0; m < 4; ++m)
; #pragma unroll
;                 for (int n = 0; n < 2; ++n) acc[a][b][m][n] = (f32x4){0.f, 0.f, 0.f, 0.f};
;     bf16x8 At[4][2], B0[2][2], B1[2][2];
;     int sc7f = 0x7F7F7F7F; asm volatile("" : "+v"(sc7f));
;     pg8_v8i At8[4], B08[2], B18[2];
;     const char* cA = (const char*)g.A + (size_t)cur.pm * tstep; const char* cB = (const char*)g.Bt + (size_t)cur.pn * tstep;
;     S.a_ready(cur);
;     if constexpr (SP2) {
; __global__ void __launch_bounds__(NWAVES * 64, 2) mk_fwd(Args args) {
;     ...
;                 { OPQ_LANE(); const int nd = __builtin_amdgcn_readfirstlane(ld_agent_i((const int*)(ws + WS_TBL + T_NUN) + 1));
;                   const int nfull = nd / F.G, nbusy = nd - nfull * F.G, nsub = F.G - nbusy;
;                   pg8::SubOrder Sp{nsub > 0 ? (bix >= nbusy ? bix - nbusy : -1) : bix, nsub > 0 ? nsub : F.G, (M / 256) * (D / 256)};
;                   int kple = PLE; asm volatile("" : "+s"(kple));
;                   pg8::Gemm gp{(const bf16*)(ws + WS_PB) + (size_t)l * M * PLE, (const bf16*)(ws + W_PP) + (size_t)l * D * PLE, M, D, kple};
;                   pg8::EpiBfPlain Ep{mg, D};
;                   pg8::gemm_phase<pg8::EpiBfPlain, pg8::SubOrder, true, true>(F.lds + RING_OFF, gp, Sp, Ep, tidv); }
.LBB0_1038:
	v_mov_b32_e32 v0, v81
	v_readlane_b32 s0, v254, 25
	v_mbcnt_lo_u32_b32 v0, -1, v0
	v_mbcnt_hi_u32_b32 v0, -1, v0
	v_add_u32_e32 v12, s0, v0
	v_mov_b32_e32 v0, s80
	v_add_co_u32_e32 v0, vcc, 0x28a000, v0
	s_waitcnt lgkmcnt(0)
	v_mov_b32_e32 v1, s81
	v_readlane_b32 s6, v254, 2
	v_addc_co_u32_e32 v1, vcc, 0, v1, vcc
	s_waitcnt vmcnt(0)
	global_load_dword v0, v[0:1], off offset:4 sc1
	s_add_u32 s4, s80, 0x28a004
	s_addc_u32 s5, s81, 0
	v_readlane_b32 s2, v255, 16
	v_readlane_b32 s3, v255, 17
	s_waitcnt vmcnt(0) lgkmcnt(0)
	v_readfirstlane_b32 s0, v0
	s_ashr_i32 s1, s0, 31
	s_abs_i32 s0, s0
	s_mul_hi_u32 s2, s0, s2
	s_mul_i32 s2, s2, s3
	s_sub_i32 s0, s0, s2
	s_sub_i32 s2, s0, s3
	s_cmp_ge_u32 s0, s3
	s_cselect_b32 s0, s2, s0
	s_sub_i32 s2, s0, s3
	s_cmp_ge_u32 s0, s3
	s_cselect_b32 s0, s2, s0
	s_xor_b32 s0, s0, s1
	s_sub_i32 s0, s0, s1
	s_sub_i32 s12, s59, s0
	s_sub_i32 s1, s6, s0
	s_cmp_ge_i32 s6, s0
	s_cselect_b32 s7, s1, -1
	s_cmp_gt_i32 s12, 0
	s_cselect_b64 s[2:3], -1, 0
	s_and_b64 s[0:1], s[2:3], exec
	s_cselect_b32 s24, s7, s6
	s_movk_i32 s0, 0x100
	s_cmpk_gt_u32 s24, 0xff
	v_readfirstlane_b32 s14, v12
	s_cbranch_scc1 .LBB0_1057
	v_lshlrev_b32_e32 v0, 4, v12
	v_add_u32_e32 v1, 0x2000, v0
	v_ashrrev_i32_e32 v2, 31, v1
	v_lshrrev_b32_e32 v2, 22, v2
	v_add_u32_e32 v2, v1, v2
	v_ashrrev_i32_e32 v2, 10, v2
	v_mul_i32_i24_e32 v3, 0x400, v2
	v_sub_u32_e32 v1, v1, v3
	v_lshrrev_b32_e32 v3, 4, v1
	v_bitop3_b32 v1, v3, v1, 32 bitop3:0x6c
	v_ashrrev_i32_e32 v3, 31, v1
	v_lshrrev_b32_e32 v3, 26, v3
	v_add_u32_e32 v3, v1, v3
	v_lshlrev_b32_e32 v5, 3, v2
	v_ashrrev_i32_e32 v4, 6, v3
	v_and_b32_e32 v5, -16, v5
	v_lshlrev_b32_e32 v2, 5, v2
	v_add_u32_e32 v5, v4, v5
	v_and_b32_e32 v13, 32, v2
	v_and_b32_e32 v2, 0xc0, v3
	v_and_b32_e32 v4, 3, v4
	s_mov_b32 s10, 0x7fffffe0
	v_lshrrev_b32_e32 v6, 2, v5
	v_lshlrev_b32_e32 v7, 1, v5
	v_sub_u32_e32 v1, v1, v2
	v_and_or_b32 v4, v5, s10, v4
	v_and_b32_e32 v6, 4, v6
	v_and_b32_e32 v7, 24, v7
	v_ashrrev_i16_sdwa v1, v163, sext(v1) dst_sel:DWORD dst_unused:UNUSED_PAD src0_sel:DWORD src1_sel:BYTE_0
	v_readlane_b32 s8, v255, 40
	v_or3_b32 v4, v4, v6, v7
	v_bfe_i32 v14, v1, 0, 16
	v_readlane_b32 s9, v255, 41
	v_mul_lo_u32 v4, v4, s0
	v_add_u32_e32 v1, v13, v14
	v_mul_lo_u32 v15, v5, s0
	s_mov_b32 s9, s63
	v_add_lshl_u32 v130, v4, v1, 1
	v_add_lshl_u32 v132, v1, v15, 1
	v_bfe_i32 v1, v12, 27, 1
	s_lshl_b64 s[6:7], s[8:9], 23
	v_lshrrev_b32_e32 v1, 22, v1
	s_add_u32 s1, s80, s6
	v_add_u32_e32 v1, v0, v1
	s_addc_u32 s6, s81, s7
	v_and_b32_e32 v1, 0xfffffc00, v1
	s_add_u32 s25, s1, 0x1de00000
	v_sub_u32_e32 v0, v0, v1
	s_addc_u32 s26, s6, 0
	s_mov_b32 s6, s8
	v_lshrrev_b32_e32 v1, 4, v0
	v_ashrrev_i32_e32 v3, 31, v12
	v_writelane_b32 v255, s6, 40
	v_bitop3_b32 v0, v1, v0, 32 bitop3:0x6c
	v_lshrrev_b32_e32 v3, 26, v3
	v_writelane_b32 v255, s7, 41
	s_lshl_b64 s[6:7], s[8:9], 19
	v_ashrrev_i32_e32 v1, 31, v0
	v_add_u32_e32 v3, v12, v3
	s_add_u32 s1, s80, s6
	v_lshrrev_b32_e32 v1, 26, v1
	v_ashrrev_i32_e32 v3, 6, v3
	s_addc_u32 s6, s81, s7
	v_add_u32_e32 v1, v0, v1
	v_lshlrev_b32_e32 v4, 3, v3
	s_add_u32 s27, s1, 0x23c00000
	v_ashrrev_i32_e32 v2, 6, v1
	v_and_b32_e32 v4, -16, v4
	s_addc_u32 s28, s6, 0
	s_ashr_i32 s1, s0, 31
	v_add_u32_e32 v4, v2, v4
	v_and_b32_e32 v2, 3, v2
	s_lshl_b64 s[8:9], s[0:1], 9
	s_lshr_b32 s38, s24, 2
	v_and_or_b32 v2, v4, s10, v2
	s_lshr_b64 s[10:11], s[0:1], 23
	s_and_b32 s40, s24, 3
	v_and_b32_e32 v1, 0xc0, v1
	s_mul_i32 s11, s10, s38
	s_mul_hi_u32 s16, s8, s38
	s_ashr_i32 s13, s14, 6
	v_lshrrev_b32_e32 v5, 2, v4
	v_lshlrev_b32_e32 v6, 1, v4
	v_sub_u32_e32 v0, v0, v1
	s_add_i32 s16, s16, s11
	s_mul_i32 s10, s10, s40
	s_mul_hi_u32 s11, s8, s40
	s_ashr_i32 s15, s14, 8
	s_lshl_b64 s[6:7], s[0:1], 8
	s_lshl_b32 s29, s13, 10
	v_and_b32_e32 v5, 4, v5
	v_and_b32_e32 v6, 24, v6
	v_lshlrev_b32_e32 v3, 5, v3
	v_ashrrev_i16_sdwa v0, v163, sext(v0) dst_sel:DWORD dst_unused:UNUSED_PAD src0_sel:DWORD src1_sel:BYTE_0
	s_add_i32 s11, s11, s10
	s_mul_i32 s10, s8, s40
	v_or3_b32 v2, v2, v5, v6
	v_and_b32_e32 v16, 32, v3
	v_bfe_i32 v17, v0, 0, 16
	s_add_u32 s20, s27, s10
	v_mul_lo_u32 v2, v2, s0
	v_add_u32_e32 v0, v16, v17
	v_mul_lo_u32 v18, v4, s0
	s_addc_u32 s21, s28, s11
	s_add_i32 s30, s29, 0
	v_add_lshl_u32 v80, v2, v0, 1
	v_add_lshl_u32 v134, v0, v18, 1
	v_mov_b32_e32 v0, 0x7f7f7f7f
	s_add_i32 m0, s30, 0x10000
	s_mul_i32 s17, s8, s38
	global_load_lds_dwordx4 v80, s[20:21]
	s_add_i32 m0, s30, 0x12000
	s_add_u32 s10, s20, s6
	global_load_lds_dwordx4 v130, s[20:21]
	s_addc_u32 s11, s21, s7
	s_add_i32 m0, s30, 0x14000
	v_mov_b32_e32 v131, v81
	global_load_lds_dwordx4 v80, s[10:11]
	s_add_i32 m0, s30, 0x16000
	s_add_u32 s22, s25, s17
	s_addc_u32 s23, s26, s16
	s_add_i32 s31, s30, 0x2000
	v_lshl_add_u64 v[4:5], s[10:11], 0, v[80:81]
	v_lshl_add_u64 v[6:7], s[10:11], 0, v[130:131]
	global_load_lds_dwordx4 v130, s[10:11]
	s_mov_b32 m0, s30
	s_add_u32 s10, s22, s6
	global_load_lds_dwordx4 v134, s[22:23]
	s_mov_b32 m0, s31
	s_addc_u32 s11, s23, s7
	s_add_i32 s34, s30, 0x4000
	global_load_lds_dwordx4 v132, s[22:23]
	s_mov_b32 m0, s34
	s_add_i32 s35, s30, 0x6000
	global_load_lds_dwordx4 v134, s[10:11]
	s_mov_b32 m0, s35
	v_mov_b32_e32 v135, v81
	global_load_lds_dwordx4 v132, s[10:11]
	v_mov_b32_e32 v133, v81
	s_cmp_eq_u32 s15, 1
	v_lshl_add_u64 v[0:1], s[20:21], 0, v[80:81]
	v_lshl_add_u64 v[2:3], s[20:21], 0, v[130:131]
	v_lshl_add_u64 v[8:9], s[22:23], 0, v[134:135]
	v_lshl_add_u64 v[10:11], s[22:23], 0, v[132:133]
	s_cselect_b64 s[10:11], -1, 0
	s_cmp_lg_u32 s15, 1
	s_cbranch_scc1 .LBB0_1041
	s_barrier

; __device__ __forceinline__ unsigned cvtpk(float lo, float hi) { f32x2_t v = {lo, hi}; bf16x2_t b = __builtin_convertvector(v, bf16x2_t); return __builtin_bit_cast(unsigned, b); }
;     __device__ __forceinline__ void operator()(const f32x4 (&acc)[2][2][4][2], const Unit& u, int wr, int wc, int fr, int fq) const {
;         { int z_ = 0; asm volatile("" : "+v"(z_)); const int l_ = (int)__builtin_amdgcn_mbcnt_hi(~0u, __builtin_amdgcn_mbcnt_lo(~0u, (unsigned)z_)); fr = l_ & 15; fq = l_ >> 4; }
;         const int row0 = u.pm * BM + wr * 64 + fr, col0 = u.pn * BM + wc * 32 + 8 * fq;
; #pragma unroll
;         for (int ai = 0; ai < 2; ++ai)
; #pragma unroll
;             for (int m = 0; m < 4; ++m) { bf16_t* rowp = O + (size_t)(row0 + ai * HALF + m * 16) * ldc + col0;
; #pragma unroll
;                 for (int bj = 0; bj < 2; ++bj) { const f32x4 v0 = acc[ai][bj][m][0], v1 = acc[ai][bj][m][1];
;                     u32x4 w; w.x = cvtpk(v0[0], v0[1]); w.y = cvtpk(v0[2], v0[3]); w.z = cvtpk(v1[0], v1[1]); w.w = cvtpk(v1[2], v1[3]);
;                     *(u32x4*)(rowp + bj * HALF) = w; } }
;     }
.LBB0_1053:
	v_mov_b32_e32 v142, v81
	s_lshl_b32 s0, s40, 8
	v_mbcnt_lo_u32_b32 v142, -1, v142
	v_mbcnt_hi_u32_b32 v143, -1, v142
	v_ashrrev_i32_e32 v142, 1, v143
	v_and_or_b32 v143, v143, 15, s39
	v_and_b32_e32 v142, -8, v142
	s_or_b32 s0, s0, s41
	v_lshl_add_u32 v144, s38, 8, v143
	v_add_u32_e32 v142, s0, v142
	v_ashrrev_i32_e32 v145, 31, v144
	v_ashrrev_i32_e32 v143, 31, v142
	v_lshlrev_b64 v[146:147], 11, v[144:145]
	v_lshl_add_u64 v[146:147], s[70:71], 0, v[146:147]
	v_lshlrev_b64 v[142:143], 1, v[142:143]
	v_lshl_add_u64 v[146:147], v[146:147], 0, v[142:143]
	s_mov_b64 s[0:1], 0x40000
	v_cvt_pk_bf16_f32 v68, v68, v69
	v_cvt_pk_bf16_f32 v69, v70, v71
	v_cvt_pk_bf16_f32 v70, v64, v65
	v_lshl_add_u64 v[64:65], v[146:147], 0, s[0:1]
	s_mov_b32 s0, 0x40000
	v_cvt_pk_bf16_f32 v60, v60, v61
	v_cvt_pk_bf16_f32 v61, v62, v63
	v_cvt_pk_bf16_f32 v62, v56, v57
	v_add_co_u32_e32 v56, vcc, s0, v146
	s_mov_b64 s[0:1], 0x48000
	s_nop 0
	v_addc_co_u32_e32 v57, vcc, 0, v147, vcc
	v_cvt_pk_bf16_f32 v52, v52, v53
	v_cvt_pk_bf16_f32 v53, v54, v55
	v_cvt_pk_bf16_f32 v54, v48, v49
	v_lshl_add_u64 v[48:49], v[146:147], 0, s[0:1]
	s_mov_b32 s0, 0x48000
	v_cvt_pk_bf16_f32 v44, v44, v45
	v_cvt_pk_bf16_f32 v45, v46, v47
	v_cvt_pk_bf16_f32 v46, v40, v41
	v_add_co_u32_e32 v40, vcc, s0, v146
	s_mov_b64 s[0:1], 0x50000
	s_nop 0
	v_addc_co_u32_e32 v41, vcc, 0, v147, vcc
	v_cvt_pk_bf16_f32 v36, v36, v37
	v_cvt_pk_bf16_f32 v37, v38, v39
	v_cvt_pk_bf16_f32 v38, v32, v33
	v_lshl_add_u64 v[32:33], v[146:147], 0, s[0:1]
	s_mov_b32 s0, 0x50000
	v_cvt_pk_bf16_f32 v118, v118, v119
	v_cvt_pk_bf16_f32 v119, v120, v121
	v_cvt_pk_bf16_f32 v120, v114, v115
	v_or_b32_e32 v114, 16, v144
	v_cvt_pk_bf16_f32 v102, v102, v103
	v_cvt_pk_bf16_f32 v103, v104, v105
	v_cvt_pk_bf16_f32 v104, v98, v99
	v_or_b32_e32 v98, 32, v144
	v_cvt_pk_bf16_f32 v86, v86, v87
	v_cvt_pk_bf16_f32 v87, v88, v89
	v_cvt_pk_bf16_f32 v88, v82, v83
	v_or_b32_e32 v82, 48, v144
	v_cvt_pk_bf16_f32 v28, v28, v29
	v_cvt_pk_bf16_f32 v29, v30, v31
	v_cvt_pk_bf16_f32 v30, v24, v25
	v_add_co_u32_e32 v24, vcc, s0, v146
	s_mov_b64 s[0:1], 0x58000
	v_ashrrev_i32_e32 v115, 31, v114
	v_ashrrev_i32_e32 v99, 31, v98
	v_ashrrev_i32_e32 v83, 31, v82
	v_addc_co_u32_e32 v25, vcc, 0, v147, vcc
	v_cvt_pk_bf16_f32 v20, v20, v21
	v_cvt_pk_bf16_f32 v21, v22, v23
	v_cvt_pk_bf16_f32 v22, v16, v17
	v_lshl_add_u64 v[16:17], v[146:147], 0, s[0:1]
	s_mov_b32 s0, 0x58000
	v_lshlrev_b64 v[114:115], 11, v[114:115]
	v_lshlrev_b64 v[98:99], 11, v[98:99]
	v_lshlrev_b64 v[82:83], 11, v[82:83]
	v_cvt_pk_bf16_f32 v12, v12, v13
	v_cvt_pk_bf16_f32 v13, v14, v15
	v_cvt_pk_bf16_f32 v14, v8, v9
	v_add_co_u32_e32 v8, vcc, s0, v146
	v_lshl_add_u64 v[114:115], s[70:71], 0, v[114:115]
	v_lshl_add_u64 v[98:99], s[70:71], 0, v[98:99]
	v_lshl_add_u64 v[82:83], s[70:71], 0, v[82:83]
	v_addc_co_u32_e32 v9, vcc, 0, v147, vcc
	v_cvt_pk_bf16_f32 v122, v122, v123
	v_cvt_pk_bf16_f32 v123, v124, v125
	v_cvt_pk_bf16_f32 v124, v126, v127
	v_cvt_pk_bf16_f32 v125, v128, v129
	v_cvt_pk_bf16_f32 v121, v116, v117
	v_lshl_add_u64 v[114:115], v[114:115], 0, v[142:143]
	v_cvt_pk_bf16_f32 v110, v110, v111
	v_cvt_pk_bf16_f32 v111, v112, v113
	v_cvt_pk_bf16_f32 v112, v106, v107
	v_cvt_pk_bf16_f32 v113, v108, v109
	v_cvt_pk_bf16_f32 v105, v100, v101
	v_lshl_add_u64 v[98:99], v[98:99], 0, v[142:143]
	v_cvt_pk_bf16_f32 v94, v94, v95
	v_cvt_pk_bf16_f32 v95, v96, v97
	v_cvt_pk_bf16_f32 v96, v90, v91
	v_cvt_pk_bf16_f32 v97, v92, v93
	v_cvt_pk_bf16_f32 v89, v84, v85
	v_lshl_add_u64 v[82:83], v[82:83], 0, v[142:143]
	v_cvt_pk_bf16_f32 v76, v76, v77
	v_cvt_pk_bf16_f32 v77, v78, v79
	v_cvt_pk_bf16_f32 v78, v72, v73
	v_cvt_pk_bf16_f32 v79, v74, v75
	v_cvt_pk_bf16_f32 v71, v66, v67
	v_cvt_pk_bf16_f32 v63, v58, v59
	v_cvt_pk_bf16_f32 v55, v50, v51
	v_cvt_pk_bf16_f32 v47, v42, v43
	v_cvt_pk_bf16_f32 v39, v34, v35
	v_cvt_pk_bf16_f32 v31, v26, v27
	v_cvt_pk_bf16_f32 v23, v18, v19
	v_cvt_pk_bf16_f32 v15, v10, v11
	v_cvt_pk_bf16_f32 v4, v4, v5
	v_cvt_pk_bf16_f32 v5, v6, v7
	v_cvt_pk_bf16_f32 v6, v0, v1
	v_cvt_pk_bf16_f32 v7, v2, v3
	s_and_b64 vcc, exec, s[2:3]
	s_mov_b64 s[0:1], -1
	global_store_dwordx4 v[146:147], v[122:125], off
	global_store_dwordx4 v[146:147], v[118:121], off offset:256
	global_store_dwordx4 v[114:115], v[110:113], off
	global_store_dwordx4 v[114:115], v[102:105], off offset:256
	global_store_dwordx4 v[98:99], v[94:97], off
	global_store_dwordx4 v[98:99], v[86:89], off offset:256
	global_store_dwordx4 v[82:83], v[76:79], off
	global_store_dwordx4 v[82:83], v[68:71], off offset:256
	global_store_dwordx4 v[56:57], v[60:63], off
	global_store_dwordx4 v[64:65], v[52:55], off offset:256
	global_store_dwordx4 v[40:41], v[44:47], off
	global_store_dwordx4 v[48:49], v[36:39], off offset:256
	global_store_dwordx4 v[24:25], v[28:31], off
	global_store_dwordx4 v[32:33], v[20:23], off offset:256
	global_store_dwordx4 v[8:9], v[12:15], off
	global_store_dwordx4 v[16:17], v[4:7], off offset:256
	s_cbranch_vccnz .LBB0_1043
	s_andn2_b64 vcc, exec, s[10:11]
	s_cbranch_vccnz .LBB0_1042
	s_barrier
	s_branch .LBB0_1042

; __device__ __forceinline__ int ld_agent_i(const int* p) { return (int)__hip_atomic_load((const unsigned*)p, RLX_AGENT); }
; #define OPQ_LANE() int z_ = 0; asm volatile("" : "+v"(z_)); const int ln = (int)__builtin_amdgcn_mbcnt_hi(~0u, __builtin_amdgcn_mbcnt_lo(~0u, (unsigned)z_)); const int tidv = F.wave * 64 + ln; (void)tidv; int bix = blockIdx.x; asm volatile("" : "+s"(bix)); (void)bix
; __global__ void __launch_bounds__(NWAVES * 64, 2) mk_fwd(Args args) {
;     ...
;                 { OPQ_LANE(); const int nd = __builtin_amdgcn_readfirstlane(ld_agent_i((const int*)(ws + WS_TBL + T_NUN) + 1));
;                   pg8::Gemm g{zb, (const bf16*)(ws + W_2M + (size_t)(l >> 1) * NE * D * FE), MOE_ROWS, NE * D, FE / 2};
;                   ULIST_FILL((const int*)(ws + WS_TBL + T_LISTD), nd);
;                   pg8::ListOrderL So{ulp, nd, F.G, bix};
.LBB0_1057:
	v_mov_b32_e32 v2, v81
	v_readlane_b32 s14, v254, 2
	v_mov_b64_e32 v[0:1], s[4:5]
	s_waitcnt vmcnt(0)
	global_load_dword v0, v[0:1], off sc1
	v_mbcnt_lo_u32_b32 v1, -1, v2
	v_mbcnt_hi_u32_b32 v1, -1, v1
	v_readlane_b32 s0, v254, 25
	s_nop 1
	v_add_u32_e32 v8, s0, v1
	v_cmp_gt_i32_e32 vcc, 32, v8
	s_waitcnt vmcnt(0) lgkmcnt(0)
	v_readfirstlane_b32 s0, v0
	s_and_saveexec_b64 s[2:3], vcc
	s_cbranch_execz .LBB0_1064
	s_ashr_i32 s1, s14, 31
	v_mov_b32_e32 v0, s14
	v_mov_b32_e32 v1, s1
	v_mad_i64_i32 v[0:1], s[4:5], v8, s59, v[0:1]
	s_ashr_i32 s1, s0, 31
	v_cmp_gt_i64_e32 vcc, s[0:1], v[0:1]
	s_and_b64 exec, exec, vcc
	s_cbranch_execz .LBB0_1064
	v_ashrrev_i32_e32 v1, 31, v0
	s_lshr_b32 s1, s1, 29
	v_lshrrev_b32_e32 v1, 29, v1
	s_add_i32 s1, s0, s1
	v_add_u32_e32 v1, v0, v1
	s_ashr_i32 s6, s1, 3
	s_and_b32 s1, s1, -8
	v_and_b32_e32 v2, -8, v1
	s_sub_i32 s7, s0, s1
	v_sub_u32_e32 v2, v0, v2
	v_cmp_le_i32_e32 vcc, s7, v2
	s_add_i32 s1, s6, 1
	s_and_saveexec_b64 s[4:5], vcc
	s_xor_b64 s[4:5], exec, s[4:5]
	v_subrev_u32_e32 v0, s7, v2
	s_mul_i32 s8, s1, s7
	v_mul_lo_u32 v0, v0, s6
	v_add_u32_e32 v0, s8, v0
	s_andn2_saveexec_b64 s[4:5], s[4:5]
	v_mul_lo_u32 v0, v2, s1
	s_or_b64 exec, exec, s[4:5]
	v_ashrrev_i32_e32 v1, 3, v1
	v_add_lshl_u32 v0, v0, v1, 1
	v_ashrrev_i32_e32 v1, 31, v0
	v_lshl_add_u64 v[0:1], v[0:1], 2, s[80:81]
	v_add_co_u32_e32 v2, vcc, 0x288000, v0
	s_mov_b64 s[4:5], 0x288000
	s_nop 0
	v_addc_co_u32_e32 v3, vcc, 0, v1, vcc
	global_load_dword v2, v[2:3], off sc1
	v_lshl_add_u32 v3, v8, 3, 0
	v_add_u32_e32 v3, 0x21000, v3
	v_lshl_add_u64 v[0:1], v[0:1], 0, s[4:5]
	s_waitcnt vmcnt(0) lgkmcnt(0)
	ds_write_b32 v3, v2
	global_load_dword v0, v[0:1], off offset:4 sc1
	s_waitcnt vmcnt(0) lgkmcnt(0)
	ds_write_b32 v3, v0 offset:4

; __device__ __forceinline__ unsigned cvtpk(float lo, float hi) { f32x2_t v = {lo, hi}; bf16x2_t b = __builtin_convertvector(v, bf16x2_t); return __builtin_bit_cast(unsigned, b); }
;     __device__ __forceinline__ void operator()(const f32x4 (&acc)[2][2][4][2], const Unit& u, int wr, int wc, int fr, int fq) const {
;         const int row0 = u.pm * BM + wr * 64 + fr, col0 = (u.pn % nmod) * BM + wc * 32 + 8 * fq;
; #pragma unroll
;         for (int ai = 0; ai < 2; ++ai)
; #pragma unroll
;             for (int m = 0; m < 4; ++m) { const size_t r = (size_t)(row0 + ai * HALF + m * 16); const float s = gw[r] * sc; bf16_t* rowp = Y + r * ldc + col0;
; #pragma unroll
;                 for (int bj = 0; bj < 2; ++bj) { const f32x4 v0 = acc[ai][bj][m][0] * s, v1 = acc[ai][bj][m][1] * s;
;                     u32x4 w; w.x = cvtpk(v0[0], v0[1]); w.y = cvtpk(v0[2], v0[3]); w.z = cvtpk(v1[0], v1[1]); w.w = cvtpk(v1[2], v1[3]);
;                     *(u32x4*)(rowp + bj * HALF) = w; } }
;     }
.LBB0_1080:
	v_lshl_add_u32 v6, s39, 8, v206
	v_ashrrev_i32_e32 v7, 31, v6
	v_lshl_add_u64 v[2:3], v[6:7], 2, s[10:11]
	global_load_dword v4, v[2:3], off
	s_ashr_i32 s0, s38, 31
	s_lshr_b32 s0, s0, 30
	s_add_i32 s0, s38, s0
	s_and_b32 s0, s0, 0xfffffc
	s_sub_i32 s0, s38, s0
	v_lshl_or_b32 v0, s0, 8, v208
	v_ashrrev_i32_e32 v1, 31, v0
	s_mov_b64 s[0:1], 0x40000
	s_waitcnt vmcnt(0) lgkmcnt(0)
	v_mul_f32_e32 v12, 0x3b800000, v4
	v_lshlrev_b64 v[4:5], 11, v[6:7]
	v_lshl_add_u64 v[8:9], s[8:9], 0, v[4:5]
	v_lshlrev_b64 v[4:5], 1, v[0:1]
	v_lshl_add_u64 v[0:1], v[8:9], 0, v[4:5]
	v_pk_mul_f32 v[10:11], v[160:161], v[12:13] op_sel_hi:[1,0]
	v_pk_mul_f32 v[8:9], v[158:159], v[12:13] op_sel_hi:[1,0]
	v_pk_mul_f32 v[14:15], v[156:157], v[12:13] op_sel_hi:[1,0]
	v_pk_mul_f32 v[16:17], v[154:155], v[12:13] op_sel_hi:[1,0]
	v_cvt_pk_bf16_f32 v8, v8, v9
	v_cvt_pk_bf16_f32 v9, v10, v11
	v_cvt_pk_bf16_f32 v10, v16, v17
	v_cvt_pk_bf16_f32 v11, v14, v15
	global_store_dwordx4 v[0:1], v[8:11], off
	v_pk_mul_f32 v[14:15], v[148:149], v[12:13] op_sel_hi:[1,0]
	s_nop 0
	v_pk_mul_f32 v[10:11], v[152:153], v[12:13] op_sel_hi:[1,0]
	v_pk_mul_f32 v[8:9], v[150:151], v[12:13] op_sel_hi:[1,0]
	v_pk_mul_f32 v[12:13], v[146:147], v[12:13] op_sel_hi:[1,0]
	v_cvt_pk_bf16_f32 v8, v8, v9
	v_cvt_pk_bf16_f32 v9, v10, v11
	v_cvt_pk_bf16_f32 v10, v12, v13
	v_cvt_pk_bf16_f32 v11, v14, v15
	global_store_dwordx4 v[0:1], v[8:11], off offset:256
	s_nop 1
	v_or_b32_e32 v8, 16, v6
	v_ashrrev_i32_e32 v9, 31, v8
	v_lshl_add_u64 v[10:11], v[8:9], 2, s[10:11]
	global_load_dword v7, v[10:11], off
	v_lshlrev_b64 v[8:9], 11, v[8:9]
	v_lshl_add_u64 v[8:9], s[8:9], 0, v[8:9]
	v_lshl_add_u64 v[14:15], v[8:9], 0, v[4:5]
	s_waitcnt vmcnt(0) lgkmcnt(0)
	v_mul_f32_e32 v12, 0x3b800000, v7
	v_pk_mul_f32 v[10:11], v[144:145], v[12:13] op_sel_hi:[1,0]
	v_pk_mul_f32 v[8:9], v[142:143], v[12:13] op_sel_hi:[1,0]
	v_pk_mul_f32 v[16:17], v[140:141], v[12:13] op_sel_hi:[1,0]
	v_pk_mul_f32 v[18:19], v[138:139], v[12:13] op_sel_hi:[1,0]
	v_cvt_pk_bf16_f32 v8, v8, v9
	v_cvt_pk_bf16_f32 v9, v10, v11
	v_cvt_pk_bf16_f32 v10, v18, v19
	v_cvt_pk_bf16_f32 v11, v16, v17
	global_store_dwordx4 v[14:15], v[8:11], off
	v_pk_mul_f32 v[16:17], v[132:133], v[12:13] op_sel_hi:[1,0]
	s_nop 0
	v_pk_mul_f32 v[10:11], v[136:137], v[12:13] op_sel_hi:[1,0]
	v_pk_mul_f32 v[8:9], v[134:135], v[12:13] op_sel_hi:[1,0]
	v_pk_mul_f32 v[12:13], v[130:131], v[12:13] op_sel_hi:[1,0]
	v_cvt_pk_bf16_f32 v8, v8, v9
	v_cvt_pk_bf16_f32 v9, v10, v11
	v_cvt_pk_bf16_f32 v10, v12, v13
	v_cvt_pk_bf16_f32 v11, v16, v17
	global_store_dwordx4 v[14:15], v[8:11], off offset:256
	s_nop 1
	v_or_b32_e32 v8, 32, v6
	v_ashrrev_i32_e32 v9, 31, v8
	v_lshl_add_u64 v[10:11], v[8:9], 2, s[10:11]
	global_load_dword v7, v[10:11], off
	v_lshlrev_b64 v[8:9], 11, v[8:9]
	v_lshl_add_u64 v[8:9], s[8:9], 0, v[8:9]
	v_lshl_add_u64 v[14:15], v[8:9], 0, v[4:5]
	v_or_b32_e32 v6, 48, v6
	s_waitcnt vmcnt(0) lgkmcnt(0)
	v_mul_f32_e32 v12, 0x3b800000, v7
	v_pk_mul_f32 v[10:11], v[128:129], v[12:13] op_sel_hi:[1,0]
	v_pk_mul_f32 v[8:9], v[126:127], v[12:13] op_sel_hi:[1,0]
	v_pk_mul_f32 v[16:17], v[124:125], v[12:13] op_sel_hi:[1,0]
	v_pk_mul_f32 v[18:19], v[122:123], v[12:13] op_sel_hi:[1,0]
	v_cvt_pk_bf16_f32 v8, v8, v9
	v_cvt_pk_bf16_f32 v9, v10, v11
	v_cvt_pk_bf16_f32 v10, v18, v19
	v_cvt_pk_bf16_f32 v11, v16, v17
	global_store_dwordx4 v[14:15], v[8:11], off
	v_pk_mul_f32 v[16:17], v[116:117], v[12:13] op_sel_hi:[1,0]
	v_ashrrev_i32_e32 v7, 31, v6
	v_pk_mul_f32 v[10:11], v[120:121], v[12:13] op_sel_hi:[1,0]
	v_pk_mul_f32 v[8:9], v[118:119], v[12:13] op_sel_hi:[1,0]
	v_pk_mul_f32 v[12:13], v[114:115], v[12:13] op_sel_hi:[1,0]
	v_cvt_pk_bf16_f32 v8, v8, v9
	v_cvt_pk_bf16_f32 v9, v10, v11
	v_cvt_pk_bf16_f32 v10, v12, v13
	v_cvt_pk_bf16_f32 v11, v16, v17
	global_store_dwordx4 v[14:15], v[8:11], off offset:256
	s_nop 1
	v_lshl_add_u64 v[8:9], v[6:7], 2, s[10:11]
	global_load_dword v8, v[8:9], off
	v_lshlrev_b64 v[6:7], 11, v[6:7]
	v_lshl_add_u64 v[6:7], s[8:9], 0, v[6:7]
	v_lshl_add_u64 v[10:11], v[6:7], 0, v[4:5]
	s_waitcnt vmcnt(0) lgkmcnt(0)
	v_mul_f32_e32 v8, 0x3b800000, v8
	v_pk_mul_f32 v[6:7], v[112:113], v[8:9] op_sel_hi:[1,0]
	v_pk_mul_f32 v[4:5], v[110:111], v[8:9] op_sel_hi:[1,0]
	v_pk_mul_f32 v[12:13], v[108:109], v[8:9] op_sel_hi:[1,0]
	v_pk_mul_f32 v[14:15], v[106:107], v[8:9] op_sel_hi:[1,0]
	v_cvt_pk_bf16_f32 v4, v4, v5
	v_cvt_pk_bf16_f32 v5, v6, v7
	v_cvt_pk_bf16_f32 v6, v14, v15
	v_cvt_pk_bf16_f32 v7, v12, v13
	global_store_dwordx4 v[10:11], v[4:7], off
	v_pk_mul_f32 v[12:13], v[100:101], v[8:9] op_sel_hi:[1,0]
	s_nop 0
	v_pk_mul_f32 v[6:7], v[104:105], v[8:9] op_sel_hi:[1,0]
	v_pk_mul_f32 v[4:5], v[102:103], v[8:9] op_sel_hi:[1,0]
	v_pk_mul_f32 v[8:9], v[98:99], v[8:9] op_sel_hi:[1,0]
	v_cvt_pk_bf16_f32 v4, v4, v5
	v_cvt_pk_bf16_f32 v5, v6, v7
	v_cvt_pk_bf16_f32 v6, v8, v9
	v_cvt_pk_bf16_f32 v7, v12, v13
	global_store_dwordx4 v[10:11], v[4:7], off offset:256
	global_load_dword v4, v[2:3], off offset:512
	v_lshl_add_u64 v[10:11], v[0:1], 0, s[0:1]
	s_mov_b32 s0, 0x40000
	s_waitcnt vmcnt(0) lgkmcnt(0)
; __device__ __forceinline__ unsigned cvtpk(float lo, float hi) { f32x2_t v = {lo, hi}; bf16x2_t b = __builtin_convertvector(v, bf16x2_t); return __builtin_bit_cast(unsigned, b); }
;     __device__ __forceinline__ void operator()(const f32x4 (&acc)[2][2][4][2], const Unit& u, int wr, int wc, int fr, int fq) const {
;         const int row0 = u.pm * BM + wr * 64 + fr, col0 = (u.pn % nmod) * BM + wc * 32 + 8 * fq;
; #pragma unroll
;         for (int ai = 0; ai < 2; ++ai)
; #pragma unroll
;             for (int m = 0; m < 4; ++m) { const size_t r = (size_t)(row0 + ai * HALF + m * 16); const float s = gw[r] * sc; bf16_t* rowp = Y + r * ldc + col0;
; #pragma unroll
;                 for (int bj = 0; bj < 2; ++bj) { const f32x4 v0 = acc[ai][bj][m][0] * s, v1 = acc[ai][bj][m][1] * s;
;                     u32x4 w; w.x = cvtpk(v0[0], v0[1]); w.y = cvtpk(v0[2], v0[3]); w.z = cvtpk(v1[0], v1[1]); w.w = cvtpk(v1[2], v1[3]);
;                     *(u32x4*)(rowp + bj * HALF) = w; } }
;     }
	v_mul_f32_e32 v8, 0x3b800000, v4
	v_pk_mul_f32 v[6:7], v[96:97], v[8:9] op_sel_hi:[1,0]
	v_pk_mul_f32 v[4:5], v[94:95], v[8:9] op_sel_hi:[1,0]
	v_pk_mul_f32 v[12:13], v[92:93], v[8:9] op_sel_hi:[1,0]
	v_pk_mul_f32 v[14:15], v[90:91], v[8:9] op_sel_hi:[1,0]
	v_cvt_pk_bf16_f32 v4, v4, v5
	v_cvt_pk_bf16_f32 v5, v6, v7
	v_cvt_pk_bf16_f32 v7, v12, v13
	v_add_co_u32_e32 v12, vcc, s0, v0
	v_cvt_pk_bf16_f32 v6, v14, v15
	s_nop 0
	v_addc_co_u32_e32 v13, vcc, 0, v1, vcc
	global_store_dwordx4 v[12:13], v[4:7], off
	v_pk_mul_f32 v[12:13], v[84:85], v[8:9] op_sel_hi:[1,0]
	s_mov_b64 s[0:1], 0x48000
	v_pk_mul_f32 v[6:7], v[88:89], v[8:9] op_sel_hi:[1,0]
	v_pk_mul_f32 v[4:5], v[86:87], v[8:9] op_sel_hi:[1,0]
	v_pk_mul_f32 v[8:9], v[82:83], v[8:9] op_sel_hi:[1,0]
	v_cvt_pk_bf16_f32 v4, v4, v5
	v_cvt_pk_bf16_f32 v5, v6, v7
	v_cvt_pk_bf16_f32 v6, v8, v9
	v_cvt_pk_bf16_f32 v7, v12, v13
	global_store_dwordx4 v[10:11], v[4:7], off offset:256
	global_load_dword v4, v[2:3], off offset:576
	v_lshl_add_u64 v[10:11], v[0:1], 0, s[0:1]
	s_mov_b32 s0, 0x48000
	s_waitcnt vmcnt(0) lgkmcnt(0)
	v_mul_f32_e32 v8, 0x3b800000, v4
	v_pk_mul_f32 v[6:7], v[78:79], v[8:9] op_sel_hi:[1,0]
	v_pk_mul_f32 v[4:5], v[76:77], v[8:9] op_sel_hi:[1,0]
	v_pk_mul_f32 v[12:13], v[74:75], v[8:9] op_sel_hi:[1,0]
	v_pk_mul_f32 v[14:15], v[72:73], v[8:9] op_sel_hi:[1,0]
	v_cvt_pk_bf16_f32 v4, v4, v5
	v_cvt_pk_bf16_f32 v5, v6, v7
	v_cvt_pk_bf16_f32 v7, v12, v13
	v_add_co_u32_e32 v12, vcc, s0, v0
	v_cvt_pk_bf16_f32 v6, v14, v15
	s_nop 0
	v_addc_co_u32_e32 v13, vcc, 0, v1, vcc
	global_store_dwordx4 v[12:13], v[4:7], off
	v_pk_mul_f32 v[12:13], v[66:67], v[8:9] op_sel_hi:[1,0]
	s_mov_b64 s[0:1], 0x50000
	v_pk_mul_f32 v[6:7], v[70:71], v[8:9] op_sel_hi:[1,0]
	v_pk_mul_f32 v[4:5], v[68:69], v[8:9] op_sel_hi:[1,0]
	v_pk_mul_f32 v[8:9], v[64:65], v[8:9] op_sel_hi:[1,0]
	v_cvt_pk_bf16_f32 v4, v4, v5
	v_cvt_pk_bf16_f32 v5, v6, v7
	v_cvt_pk_bf16_f32 v6, v8, v9
	v_cvt_pk_bf16_f32 v7, v12, v13
	global_store_dwordx4 v[10:11], v[4:7], off offset:256
	global_load_dword v4, v[2:3], off offset:640
	v_lshl_add_u64 v[10:11], v[0:1], 0, s[0:1]
	s_mov_b32 s0, 0x50000
	s_waitcnt vmcnt(0) lgkmcnt(0)
	v_mul_f32_e32 v8, 0x3b800000, v4
	v_pk_mul_f32 v[6:7], v[62:63], v[8:9] op_sel_hi:[1,0]
	v_pk_mul_f32 v[4:5], v[60:61], v[8:9] op_sel_hi:[1,0]
	v_pk_mul_f32 v[12:13], v[58:59], v[8:9] op_sel_hi:[1,0]
	v_pk_mul_f32 v[14:15], v[56:57], v[8:9] op_sel_hi:[1,0]
	v_cvt_pk_bf16_f32 v4, v4, v5
	v_cvt_pk_bf16_f32 v5, v6, v7
	v_cvt_pk_bf16_f32 v7, v12, v13
	v_add_co_u32_e32 v12, vcc, s0, v0
	v_cvt_pk_bf16_f32 v6, v14, v15
	s_nop 0
	v_addc_co_u32_e32 v13, vcc, 0, v1, vcc
	global_store_dwordx4 v[12:13], v[4:7], off
	v_pk_mul_f32 v[12:13], v[50:51], v[8:9] op_sel_hi:[1,0]
	s_mov_b64 s[0:1], 0x58000
	v_pk_mul_f32 v[6:7], v[54:55], v[8:9] op_sel_hi:[1,0]
	v_pk_mul_f32 v[4:5], v[52:53], v[8:9] op_sel_hi:[1,0]
	v_pk_mul_f32 v[8:9], v[48:49], v[8:9] op_sel_hi:[1,0]
	v_cvt_pk_bf16_f32 v4, v4, v5
	v_cvt_pk_bf16_f32 v5, v6, v7
	v_cvt_pk_bf16_f32 v6, v8, v9
	v_cvt_pk_bf16_f32 v7, v12, v13
	global_store_dwordx4 v[10:11], v[4:7], off offset:256
	global_load_dword v2, v[2:3], off offset:704
	v_lshl_add_u64 v[8:9], v[0:1], 0, s[0:1]
	s_mov_b32 s0, 0x58000
	v_add_co_u32_e32 v0, vcc, s0, v0
	s_mov_b64 s[0:1], -1
	s_nop 0
	v_addc_co_u32_e32 v1, vcc, 0, v1, vcc
	s_and_b64 vcc, exec, s[2:3]
	s_waitcnt vmcnt(0) lgkmcnt(0)
	v_mul_f32_e32 v6, 0x3b800000, v2
	v_pk_mul_f32 v[4:5], v[46:47], v[6:7] op_sel_hi:[1,0]
	v_pk_mul_f32 v[2:3], v[44:45], v[6:7] op_sel_hi:[1,0]
	v_pk_mul_f32 v[10:11], v[42:43], v[6:7] op_sel_hi:[1,0]
	v_pk_mul_f32 v[12:13], v[40:41], v[6:7] op_sel_hi:[1,0]
	v_cvt_pk_bf16_f32 v2, v2, v3
	v_cvt_pk_bf16_f32 v3, v4, v5
	v_cvt_pk_bf16_f32 v4, v12, v13
	v_cvt_pk_bf16_f32 v5, v10, v11
	global_store_dwordx4 v[0:1], v[2:5], off
	v_pk_mul_f32 v[0:1], v[36:37], v[6:7] op_sel_hi:[1,0]
	s_nop 0
	v_pk_mul_f32 v[2:3], v[38:39], v[6:7] op_sel_hi:[1,0]
	v_pk_mul_f32 v[4:5], v[34:35], v[6:7] op_sel_hi:[1,0]
	v_pk_mul_f32 v[6:7], v[32:33], v[6:7] op_sel_hi:[1,0]
	v_cvt_pk_bf16_f32 v0, v0, v1
	v_cvt_pk_bf16_f32 v1, v2, v3
	v_cvt_pk_bf16_f32 v2, v6, v7
	v_cvt_pk_bf16_f32 v3, v4, v5
	global_store_dwordx4 v[8:9], v[0:3], off offset:256
	s_cbranch_vccnz .LBB0_1069
	s_andn2_b64 vcc, exec, s[6:7]
	s_cbranch_vccnz .LBB0_1068
	s_barrier
	s_branch .LBB0_1068

; __device__ __forceinline__ float xor_add(float v, int lane, int o) { return v + __builtin_bit_cast(float, __builtin_amdgcn_ds_bpermute((lane ^ o) << 2, __builtin_bit_cast(int, v))); }
; __device__ __forceinline__ float f16_lo(unsigned u) { return (float)__builtin_bit_cast(h16x2, u)[0]; }
;     __device__ __forceinline__ void operator()(const f32x4 (&acc)[2][2][4][2], const Unit& u, int wr, int wc, int fr, int fq) const {
;         { int z_ = 0; asm volatile("" : "+v"(z_)); const int l_ = (int)__builtin_amdgcn_mbcnt_hi(~0u, __builtin_amdgcn_mbcnt_lo(~0u, (unsigned)z_)); fr = l_ & 15; fq = l_ >> 4; }
;         const int row0 = u.pm * BM + wr * 64 + fr, col0 = u.pn * BM + wc * 32 + 8 * fq, lane = fq * 16 + fr;
; #pragma unroll
;         for (int ai = 0; ai < 2; ++ai)
; #pragma unroll
;             for (int mp = 0; mp < 2; ++mp) {
;                 u32x4 bsv[2][2];
; #pragma unroll
;                 for (int mm = 0; mm < 2; ++mm)
; #pragma unroll
;                     for (int bj = 0; bj < 2; ++bj) bsv[mm][bj] = *(const u32x4*)(base + (size_t)(row0 + ai * HALF + (2 * mp + mm) * 16) * ldc + col0 + bj * HALF);
; #pragma unroll
;                 for (int mm = 0; mm < 2; ++mm) { const int m = 2 * mp + mm; const size_t r = (size_t)(row0 + ai * HALF + m * 16), off = r * ldc + col0; float ss = 0.f;
; #pragma unroll
;                     for (int bj = 0; bj < 2; ++bj) { const u32x4 b = bsv[mm][bj]; const f32x4 a0 = acc[ai][bj][m][0] * sc, a1 = acc[ai][bj][m][1] * sc;
;                         f32x4 v0, v1; v0[0] = f16_lo(b.x) + a0[0]; v0[1] = f16_hi(b.x) + a0[1]; v0[2] = f16_lo(b.y) + a0[2]; v0[3] = f16_hi(b.y) + a0[3];
;                         v1[0] = f16_lo(b.z) + a1[0]; v1[1] = f16_hi(b.z) + a1[1]; v1[2] = f16_lo(b.w) + a1[2]; v1[3] = f16_hi(b.w) + a1[3];
;                         u32x4 w; w.x = pk_f16(v0[0], v0[1]); w.y = pk_f16(v0[2], v0[3]); w.z = pk_f16(v1[0], v1[1]); w.w = pk_f16(v1[2], v1[3]); *(u32x4*)(out + off + bj * HALF) = w;
;                         ss += ((v0[0] * v0[0] + v0[1] * v0[1]) + (v0[2] * v0[2] + v0[3] * v0[3])) + ((v1[0] * v1[0] + v1[1] * v1[1]) + (v1[2] * v1[2] + v1[3] * v1[3])); }
;                     ss = xor_add(ss, lane, 16); ss = xor_add(ss, lane, 32);
;                     if (fq == 0) ssp[r * 16 + (u.pn & 3) * 4 + wc] = ss; }
;                 asm volatile("" ::: "memory");
;             }
;     }
.LBB0_1112:
	v_mov_b32_e32 v130, v81
	s_lshl_b32 s0, s40, 8
	v_mbcnt_lo_u32_b32 v130, -1, v130
	v_mbcnt_hi_u32_b32 v158, -1, v130
	s_add_i32 s0, s0, s29
	v_and_or_b32 v150, v158, 15, s0
	s_lshl_b32 s0, s39, 8
	v_ashrrev_i32_e32 v130, 1, v158
	s_or_b32 s0, s0, s30
	v_and_b32_e32 v130, -8, v130
	v_add_u32_e32 v148, s0, v130
	v_ashrrev_i32_e32 v149, 31, v148
	v_lshlrev_b64 v[160:161], 1, v[148:149]
	v_ashrrev_i32_e32 v151, 31, v150
	v_lshl_add_u64 v[152:153], s[72:73], 0, v[160:161]
	v_lshlrev_b64 v[182:183], 11, v[150:151]
	v_lshl_add_u64 v[130:131], v[152:153], 0, v[182:183]
	global_load_dwordx4 v[174:177], v[130:131], off
	global_load_dwordx4 v[178:181], v[130:131], off offset:256
	v_or_b32_e32 v154, 16, v150
	v_ashrrev_i32_e32 v155, 31, v154
	v_lshlrev_b64 v[130:131], 11, v[154:155]
	v_lshl_add_u64 v[130:131], v[152:153], 0, v[130:131]
	global_load_dwordx4 v[134:137], v[130:131], off
	s_nop 0
	global_load_dwordx4 v[130:133], v[130:131], off offset:256
	v_lshlrev_b32_e32 v170, 2, v158
	v_cmp_gt_u32_e32 vcc, 16, v158
	v_xor_b32_e32 v159, 64, v170
	v_xor_b32_e32 v158, 0x80, v170
	s_lshl_b32 s0, s39, 2
	s_and_b32 s14, s0, 12
	s_waitcnt vmcnt(0) lgkmcnt(0)
	v_cvt_f32_f16_e32 v184, v174
	v_cvt_f32_f16_sdwa v185, v174 dst_sel:DWORD dst_unused:UNUSED_PAD src0_sel:WORD_1
	v_cvt_f32_f16_e32 v174, v175
	v_cvt_f32_f16_sdwa v175, v175 dst_sel:DWORD dst_unused:UNUSED_PAD src0_sel:WORD_1
	v_cvt_f32_f16_e32 v186, v176
	v_cvt_f32_f16_sdwa v187, v176 dst_sel:DWORD dst_unused:UNUSED_PAD src0_sel:WORD_1
	v_cvt_f32_f16_e32 v176, v177
	v_cvt_f32_f16_sdwa v177, v177 dst_sel:DWORD dst_unused:UNUSED_PAD src0_sel:WORD_1
	v_cvt_f32_f16_e32 v188, v178
	v_cvt_f32_f16_sdwa v189, v178 dst_sel:DWORD dst_unused:UNUSED_PAD src0_sel:WORD_1
	v_cvt_f32_f16_e32 v178, v179
	v_cvt_f32_f16_sdwa v179, v179 dst_sel:DWORD dst_unused:UNUSED_PAD src0_sel:WORD_1
	v_cvt_f32_f16_e32 v190, v180
	v_cvt_f32_f16_sdwa v191, v180 dst_sel:DWORD dst_unused:UNUSED_PAD src0_sel:WORD_1
	v_cvt_f32_f16_e32 v180, v181
	v_cvt_f32_f16_sdwa v181, v181 dst_sel:DWORD dst_unused:UNUSED_PAD src0_sel:WORD_1
	v_pk_add_f32 v[126:127], v[126:127], v[184:185]
	v_pk_add_f32 v[128:129], v[128:129], v[174:175]
	v_pk_add_f32 v[122:123], v[122:123], v[186:187]
	v_pk_add_f32 v[124:125], v[124:125], v[176:177]
	v_pk_add_f32 v[118:119], v[118:119], v[188:189]
	v_pk_add_f32 v[120:121], v[120:121], v[178:179]
	v_pk_add_f32 v[174:175], v[114:115], v[190:191]
	v_pk_add_f32 v[176:177], v[116:117], v[180:181]
	v_cvt_pk_f16_f32 v114, v126, v127
	v_cvt_pk_f16_f32 v115, v128, v129
	v_cvt_pk_f16_f32 v116, v122, v123
	v_cvt_pk_f16_f32 v117, v124, v125
	v_pk_mul_f32 v[126:127], v[126:127], v[126:127]
	v_pk_mul_f32 v[128:129], v[128:129], v[128:129]
	v_pk_mul_f32 v[122:123], v[122:123], v[122:123]
	v_pk_mul_f32 v[124:125], v[124:125], v[124:125]
	v_pk_mul_f32 v[178:179], v[118:119], v[118:119]
	v_pk_mul_f32 v[180:181], v[120:121], v[120:121]
	v_pk_mul_f32 v[184:185], v[174:175], v[174:175]
	v_pk_mul_f32 v[186:187], v[176:177], v[176:177]
	v_add_f32_e32 v171, v184, v185
	v_add_f32_e32 v170, v186, v187
	v_add_f32_e32 v172, v180, v181
	v_add_f32_e32 v173, v178, v179
	v_add_f32_e32 v124, v124, v125
	v_add_f32_e32 v122, v122, v123
	v_add_f32_e32 v123, v128, v129
	v_add_f32_e32 v125, v126, v127
	v_add_f32_e32 v126, v171, v170
	v_add_f32_e32 v127, v173, v172
	v_add_f32_e32 v122, v122, v124
	v_add_f32_e32 v123, v125, v123
	v_add_f32_e32 v124, v127, v126
	v_add_f32_e32 v122, v123, v122
	v_add_f32_e32 v124, v122, v124
	ds_bpermute_b32 v125, v159, v124
	v_lshl_add_u64 v[122:123], s[72:73], 0, v[182:183]
	v_lshl_add_u64 v[122:123], v[122:123], 0, v[160:161]
	global_store_dwordx4 v[122:123], v[114:117], off
	s_waitcnt lgkmcnt(0)
	s_nop 0
	v_add_f32_e32 v114, v124, v125
	ds_bpermute_b32 v115, v158, v114
	v_cvt_pk_f16_f32 v116, v118, v119
	v_cvt_pk_f16_f32 v117, v120, v121
	v_cvt_pk_f16_f32 v118, v174, v175
	v_cvt_pk_f16_f32 v119, v176, v177
	global_store_dwordx4 v[122:123], v[116:119], off offset:256
	s_and_saveexec_b64 s[0:1], vcc
	s_cbranch_execz .LBB0_1114
	v_lshlrev_b64 v[116:117], 6, v[150:151]
	v_lshl_add_u64 v[116:117], s[8:9], 0, v[116:117]
	s_lshl_b32 s62, s14, 2
	v_lshl_add_u64 v[116:117], v[116:117], 0, s[62:63]
	s_lshl_b32 s62, s28, 2
	v_lshl_add_u64 v[116:117], v[116:117], 0, s[62:63]
	s_waitcnt lgkmcnt(0)
	v_add_f32_e32 v114, v114, v115
	global_store_dword v[116:117], v114, off
; __device__ __forceinline__ float xor_add(float v, int lane, int o) { return v + __builtin_bit_cast(float, __builtin_amdgcn_ds_bpermute((lane ^ o) << 2, __builtin_bit_cast(int, v))); }
; __device__ __forceinline__ float f16_lo(unsigned u) { return (float)__builtin_bit_cast(h16x2, u)[0]; }
;     __device__ __forceinline__ void operator()(const f32x4 (&acc)[2][2][4][2], const Unit& u, int wr, int wc, int fr, int fq) const {
;         { int z_ = 0; asm volatile("" : "+v"(z_)); const int l_ = (int)__builtin_amdgcn_mbcnt_hi(~0u, __builtin_amdgcn_mbcnt_lo(~0u, (unsigned)z_)); fr = l_ & 15; fq = l_ >> 4; }
;         const int row0 = u.pm * BM + wr * 64 + fr, col0 = u.pn * BM + wc * 32 + 8 * fq, lane = fq * 16 + fr;
; #pragma unroll
;         for (int ai = 0; ai < 2; ++ai)
; #pragma unroll
;             for (int mp = 0; mp < 2; ++mp) {
;                 u32x4 bsv[2][2];
; #pragma unroll
;                 for (int mm = 0; mm < 2; ++mm)
; #pragma unroll
;                     for (int bj = 0; bj < 2; ++bj) bsv[mm][bj] = *(const u32x4*)(base + (size_t)(row0 + ai * HALF + (2 * mp + mm) * 16) * ldc + col0 + bj * HALF);
; #pragma unroll
;                 for (int mm = 0; mm < 2; ++mm) { const int m = 2 * mp + mm; const size_t r = (size_t)(row0 + ai * HALF + m * 16), off = r * ldc + col0; float ss = 0.f;
; #pragma unroll
;                     for (int bj = 0; bj < 2; ++bj) { const u32x4 b = bsv[mm][bj]; const f32x4 a0 = acc[ai][bj][m][0] * sc, a1 = acc[ai][bj][m][1] * sc;
;                         f32x4 v0, v1; v0[0] = f16_lo(b.x) + a0[0]; v0[1] = f16_hi(b.x) + a0[1]; v0[2] = f16_lo(b.y) + a0[2]; v0[3] = f16_hi(b.y) + a0[3];
;                         v1[0] = f16_lo(b.z) + a1[0]; v1[1] = f16_hi(b.z) + a1[1]; v1[2] = f16_lo(b.w) + a1[2]; v1[3] = f16_hi(b.w) + a1[3];
;                         u32x4 w; w.x = pk_f16(v0[0], v0[1]); w.y = pk_f16(v0[2], v0[3]); w.z = pk_f16(v1[0], v1[1]); w.w = pk_f16(v1[2], v1[3]); *(u32x4*)(out + off + bj * HALF) = w;
;                         ss += ((v0[0] * v0[0] + v0[1] * v0[1]) + (v0[2] * v0[2] + v0[3] * v0[3])) + ((v1[0] * v1[0] + v1[1] * v1[1]) + (v1[2] * v1[2] + v1[3] * v1[3])); }
;                     ss = xor_add(ss, lane, 16); ss = xor_add(ss, lane, 32);
;                     if (fq == 0) ssp[r * 16 + (u.pn & 3) * 4 + wc] = ss; }
;                 asm volatile("" ::: "memory");
;             }
;     }
.LBB0_1114:
	s_or_b64 exec, exec, s[0:1]
	v_cvt_f32_f16_sdwa v119, v135 dst_sel:DWORD dst_unused:UNUSED_PAD src0_sel:WORD_1
	v_cvt_f32_f16_e32 v118, v135
	v_cvt_f32_f16_sdwa v117, v134 dst_sel:DWORD dst_unused:UNUSED_PAD src0_sel:WORD_1
	v_cvt_f32_f16_e32 v116, v134
	v_cvt_f32_f16_sdwa v121, v137 dst_sel:DWORD dst_unused:UNUSED_PAD src0_sel:WORD_1
	v_pk_add_f32 v[118:119], v[112:113], v[118:119]
	v_cvt_f32_f16_sdwa v113, v136 dst_sel:DWORD dst_unused:UNUSED_PAD src0_sel:WORD_1
	v_cvt_f32_f16_e32 v112, v136
	v_cvt_f32_f16_e32 v120, v137
	s_waitcnt lgkmcnt(0)
	v_lshlrev_b64 v[114:115], 10, v[154:155]
	v_pk_add_f32 v[116:117], v[110:111], v[116:117]
	v_pk_add_f32 v[106:107], v[106:107], v[112:113]
	v_pk_add_f32 v[108:109], v[108:109], v[120:121]
	v_lshl_add_u64 v[114:115], v[114:115], 1, s[72:73]
	v_cvt_pk_f16_f32 v110, v116, v117
	v_cvt_pk_f16_f32 v111, v118, v119
	v_cvt_pk_f16_f32 v112, v106, v107
	v_cvt_pk_f16_f32 v113, v108, v109
	v_lshl_add_u64 v[114:115], v[148:149], 1, v[114:115]
	global_store_dwordx4 v[114:115], v[110:113], off
	v_cvt_f32_f16_sdwa v121, v133 dst_sel:DWORD dst_unused:UNUSED_PAD src0_sel:WORD_1
	v_cvt_f32_f16_e32 v120, v133
	v_pk_mul_f32 v[112:113], v[118:119], v[118:119]
	v_cvt_f32_f16_sdwa v119, v131 dst_sel:DWORD dst_unused:UNUSED_PAD src0_sel:WORD_1
	v_cvt_f32_f16_e32 v118, v131
	v_pk_mul_f32 v[110:111], v[116:117], v[116:117]
	v_cvt_f32_f16_sdwa v117, v130 dst_sel:DWORD dst_unused:UNUSED_PAD src0_sel:WORD_1
	v_cvt_f32_f16_e32 v116, v130
	v_pk_add_f32 v[118:119], v[104:105], v[118:119]
	v_cvt_f32_f16_sdwa v105, v132 dst_sel:DWORD dst_unused:UNUSED_PAD src0_sel:WORD_1
	v_cvt_f32_f16_e32 v104, v132
	v_pk_add_f32 v[116:117], v[102:103], v[116:117]
	v_pk_add_f32 v[100:101], v[100:101], v[120:121]
	v_cvt_pk_f16_f32 v102, v116, v117
	v_pk_add_f32 v[98:99], v[98:99], v[104:105]
	v_cvt_pk_f16_f32 v103, v118, v119
	v_cvt_pk_f16_f32 v104, v98, v99
	v_cvt_pk_f16_f32 v105, v100, v101
	v_pk_mul_f32 v[98:99], v[98:99], v[98:99]
	v_pk_mul_f32 v[100:101], v[100:101], v[100:101]
	global_store_dwordx4 v[114:115], v[102:105], off offset:256
	v_add_f32_e32 v100, v100, v101
	v_add_f32_e32 v98, v98, v99
	v_pk_mul_f32 v[102:103], v[116:117], v[116:117]
	v_pk_mul_f32 v[104:105], v[118:119], v[118:119]
	v_add_f32_e32 v98, v98, v100
	v_add_f32_e32 v99, v104, v105
	v_add_f32_e32 v100, v102, v103
	v_pk_mul_f32 v[106:107], v[106:107], v[106:107]
	v_pk_mul_f32 v[108:109], v[108:109], v[108:109]
	v_add_f32_e32 v99, v100, v99
	v_add_f32_e32 v98, v99, v98
	v_add_f32_e32 v99, v108, v109
	v_add_f32_e32 v100, v106, v107
	v_add_f32_e32 v99, v100, v99
	v_add_f32_e32 v100, v112, v113
	v_add_f32_e32 v101, v110, v111
	v_add_f32_e32 v100, v101, v100
	v_add_f32_e32 v99, v100, v99
	v_add_f32_e32 v98, v99, v98
	ds_bpermute_b32 v99, v159, v98
	s_waitcnt lgkmcnt(0)
	v_add_f32_e32 v98, v98, v99
	ds_bpermute_b32 v99, v158, v98
	s_and_saveexec_b64 s[0:1], vcc
	s_cbranch_execz .LBB0_1116
	v_lshlrev_b64 v[100:101], 6, v[154:155]
	v_lshl_add_u64 v[100:101], s[8:9], 0, v[100:101]
	s_lshl_b32 s62, s14, 2
	v_lshl_add_u64 v[100:101], v[100:101], 0, s[62:63]
	s_lshl_b32 s62, s28, 2
	v_lshl_add_u64 v[100:101], v[100:101], 0, s[62:63]
	s_waitcnt lgkmcnt(0)
	v_add_f32_e32 v98, v98, v99
	global_store_dword v[100:101], v98, off
.LBB0_1116:
	s_or_b64 exec, exec, s[0:1]
	v_or_b32_e32 v108, 32, v150
	v_ashrrev_i32_e32 v109, 31, v108
	v_lshlrev_b64 v[118:119], 11, v[108:109]
	s_waitcnt lgkmcnt(0)
	v_lshl_add_u64 v[98:99], v[152:153], 0, v[118:119]
	global_load_dwordx4 v[110:113], v[98:99], off
	global_load_dwordx4 v[114:117], v[98:99], off offset:256
	v_or_b32_e32 v106, 48, v150
	v_ashrrev_i32_e32 v107, 31, v106
	v_lshlrev_b64 v[98:99], 11, v[106:107]
	v_lshl_add_u64 v[98:99], v[152:153], 0, v[98:99]
	global_load_dwordx4 v[102:105], v[98:99], off
	s_nop 0
	global_load_dwordx4 v[98:101], v[98:99], off offset:256
	s_waitcnt vmcnt(0) lgkmcnt(0)
	v_cvt_f32_f16_e32 v120, v110
	v_cvt_f32_f16_sdwa v121, v110 dst_sel:DWORD dst_unused:UNUSED_PAD src0_sel:WORD_1
	v_cvt_f32_f16_e32 v110, v111
	v_cvt_f32_f16_sdwa v111, v111 dst_sel:DWORD dst_unused:UNUSED_PAD src0_sel:WORD_1
	v_pk_add_f32 v[120:121], v[94:95], v[120:121]
	s_nop 0
	v_cvt_pk_f16_f32 v94, v120, v121
	v_pk_add_f32 v[110:111], v[96:97], v[110:111]
	v_cvt_f32_f16_e32 v96, v112
	v_cvt_f32_f16_sdwa v97, v112 dst_sel:DWORD dst_unused:UNUSED_PAD src0_sel:WORD_1
	v_cvt_f32_f16_e32 v112, v113
	v_cvt_f32_f16_sdwa v113, v113 dst_sel:DWORD dst_unused:UNUSED_PAD src0_sel:WORD_1
	v_cvt_pk_f16_f32 v95, v110, v111
	v_pk_add_f32 v[90:91], v[90:91], v[96:97]
	v_pk_add_f32 v[92:93], v[92:93], v[112:113]
	v_lshl_add_u64 v[112:113], s[72:73], 0, v[118:119]
	v_cvt_pk_f16_f32 v96, v90, v91
	v_cvt_pk_f16_f32 v97, v92, v93
	v_lshl_add_u64 v[112:113], v[148:149], 1, v[112:113]
	global_store_dwordx4 v[112:113], v[94:97], off
	v_pk_mul_f32 v[90:91], v[90:91], v[90:91]
	v_pk_mul_f32 v[92:93], v[92:93], v[92:93]
	v_pk_mul_f32 v[96:97], v[110:111], v[110:111]
	v_cvt_f32_f16_e32 v110, v114
	v_cvt_f32_f16_sdwa v111, v114 dst_sel:DWORD dst_unused:UNUSED_PAD src0_sel:WORD_1
	v_cvt_f32_f16_e32 v114, v115
	v_cvt_f32_f16_sdwa v115, v115 dst_sel:DWORD dst_unused:UNUSED_PAD src0_sel:WORD_1
	v_pk_mul_f32 v[94:95], v[120:121], v[120:121]
	v_pk_add_f32 v[110:111], v[86:87], v[110:111]
	v_pk_add_f32 v[114:115], v[88:89], v[114:115]
	v_cvt_f32_f16_e32 v88, v116
	v_cvt_f32_f16_sdwa v89, v116 dst_sel:DWORD dst_unused:UNUSED_PAD src0_sel:WORD_1
	v_cvt_f32_f16_e32 v116, v117
	v_cvt_f32_f16_sdwa v117, v117 dst_sel:DWORD dst_unused:UNUSED_PAD src0_sel:WORD_1
	v_cvt_pk_f16_f32 v86, v110, v111
	v_pk_add_f32 v[82:83], v[82:83], v[88:89]
	v_cvt_pk_f16_f32 v87, v114, v115
	v_pk_add_f32 v[84:85], v[84:85], v[116:117]
	v_cvt_pk_f16_f32 v88, v82, v83
	v_cvt_pk_f16_f32 v89, v84, v85
	v_pk_mul_f32 v[82:83], v[82:83], v[82:83]
	v_pk_mul_f32 v[84:85], v[84:85], v[84:85]
	global_store_dwordx4 v[112:113], v[86:89], off offset:256
	v_add_f32_e32 v84, v84, v85
	v_add_f32_e32 v82, v82, v83
	v_pk_mul_f32 v[86:87], v[110:111], v[110:111]
	v_pk_mul_f32 v[88:89], v[114:115], v[114:115]
	v_add_f32_e32 v82, v82, v84
	v_add_f32_e32 v83, v88, v89
	v_add_f32_e32 v84, v86, v87
	v_add_f32_e32 v83, v84, v83
	v_add_f32_e32 v82, v83, v82
	v_add_f32_e32 v83, v92, v93
	v_add_f32_e32 v84, v90, v91
	v_add_f32_e32 v83, v84, v83
	v_add_f32_e32 v84, v96, v97
	v_add_f32_e32 v85, v94, v95
	v_add_f32_e32 v84, v85, v84
	v_add_f32_e32 v83, v84, v83
	v_add_f32_e32 v82, v83, v82
	ds_bpermute_b32 v83, v159, v82
	s_waitcnt lgkmcnt(0)
	v_add_f32_e32 v82, v82, v83
	ds_bpermute_b32 v83, v158, v82
	s_and_saveexec_b64 s[0:1], vcc
	s_cbranch_execz .LBB0_1118
	v_lshlrev_b64 v[84:85], 6, v[108:109]
	v_lshl_add_u64 v[84:85], s[8:9], 0, v[84:85]
	s_lshl_b32 s62, s14, 2
	v_lshl_add_u64 v[84:85], v[84:85], 0, s[62:63]
	s_lshl_b32 s62, s28, 2
	v_lshl_add_u64 v[84:85], v[84:85], 0, s[62:63]
	s_waitcnt lgkmcnt(0)
	v_add_f32_e32 v82, v82, v83
	global_store_dword v[84:85], v82, off
; __device__ __forceinline__ float xor_add(float v, int lane, int o) { return v + __builtin_bit_cast(float, __builtin_amdgcn_ds_bpermute((lane ^ o) << 2, __builtin_bit_cast(int, v))); }
; __device__ __forceinline__ float f16_lo(unsigned u) { return (float)__builtin_bit_cast(h16x2, u)[0]; }
;     __device__ __forceinline__ void operator()(const f32x4 (&acc)[2][2][4][2], const Unit& u, int wr, int wc, int fr, int fq) const {
;         { int z_ = 0; asm volatile("" : "+v"(z_)); const int l_ = (int)__builtin_amdgcn_mbcnt_hi(~0u, __builtin_amdgcn_mbcnt_lo(~0u, (unsigned)z_)); fr = l_ & 15; fq = l_ >> 4; }
;         const int row0 = u.pm * BM + wr * 64 + fr, col0 = u.pn * BM + wc * 32 + 8 * fq, lane = fq * 16 + fr;
; #pragma unroll
;         for (int ai = 0; ai < 2; ++ai)
; #pragma unroll
;             for (int mp = 0; mp < 2; ++mp) {
;                 u32x4 bsv[2][2];
; #pragma unroll
;                 for (int mm = 0; mm < 2; ++mm)
; #pragma unroll
;                     for (int bj = 0; bj < 2; ++bj) bsv[mm][bj] = *(const u32x4*)(base + (size_t)(row0 + ai * HALF + (2 * mp + mm) * 16) * ldc + col0 + bj * HALF);
; #pragma unroll
;                 for (int mm = 0; mm < 2; ++mm) { const int m = 2 * mp + mm; const size_t r = (size_t)(row0 + ai * HALF + m * 16), off = r * ldc + col0; float ss = 0.f;
; #pragma unroll
;                     for (int bj = 0; bj < 2; ++bj) { const u32x4 b = bsv[mm][bj]; const f32x4 a0 = acc[ai][bj][m][0] * sc, a1 = acc[ai][bj][m][1] * sc;
;                         f32x4 v0, v1; v0[0] = f16_lo(b.x) + a0[0]; v0[1] = f16_hi(b.x) + a0[1]; v0[2] = f16_lo(b.y) + a0[2]; v0[3] = f16_hi(b.y) + a0[3];
;                         v1[0] = f16_lo(b.z) + a1[0]; v1[1] = f16_hi(b.z) + a1[1]; v1[2] = f16_lo(b.w) + a1[2]; v1[3] = f16_hi(b.w) + a1[3];
;                         u32x4 w; w.x = pk_f16(v0[0], v0[1]); w.y = pk_f16(v0[2], v0[3]); w.z = pk_f16(v1[0], v1[1]); w.w = pk_f16(v1[2], v1[3]); *(u32x4*)(out + off + bj * HALF) = w;
;                         ss += ((v0[0] * v0[0] + v0[1] * v0[1]) + (v0[2] * v0[2] + v0[3] * v0[3])) + ((v1[0] * v1[0] + v1[1] * v1[1]) + (v1[2] * v1[2] + v1[3] * v1[3])); }
;                     ss = xor_add(ss, lane, 16); ss = xor_add(ss, lane, 32);
;                     if (fq == 0) ssp[r * 16 + (u.pn & 3) * 4 + wc] = ss; }
;                 asm volatile("" ::: "memory");
;             }
;     }
.LBB0_1118:
	s_or_b64 exec, exec, s[0:1]
	v_cvt_f32_f16_sdwa v87, v103 dst_sel:DWORD dst_unused:UNUSED_PAD src0_sel:WORD_1
	v_cvt_f32_f16_e32 v86, v103
	v_cvt_f32_f16_sdwa v85, v102 dst_sel:DWORD dst_unused:UNUSED_PAD src0_sel:WORD_1
	v_cvt_f32_f16_e32 v84, v102
	v_cvt_f32_f16_sdwa v89, v105 dst_sel:DWORD dst_unused:UNUSED_PAD src0_sel:WORD_1
	v_pk_add_f32 v[86:87], v[78:79], v[86:87]
	v_cvt_f32_f16_sdwa v79, v104 dst_sel:DWORD dst_unused:UNUSED_PAD src0_sel:WORD_1
	v_cvt_f32_f16_e32 v78, v104
	v_cvt_f32_f16_e32 v88, v105
	s_waitcnt lgkmcnt(0)
	v_lshlrev_b64 v[82:83], 10, v[106:107]
	v_pk_add_f32 v[84:85], v[76:77], v[84:85]
	v_pk_add_f32 v[72:73], v[72:73], v[78:79]
	v_pk_add_f32 v[74:75], v[74:75], v[88:89]
	v_lshl_add_u64 v[82:83], v[82:83], 1, s[72:73]
	v_cvt_pk_f16_f32 v76, v84, v85
	v_cvt_pk_f16_f32 v77, v86, v87
	v_cvt_pk_f16_f32 v78, v72, v73
	v_cvt_pk_f16_f32 v79, v74, v75
	v_lshl_add_u64 v[82:83], v[148:149], 1, v[82:83]
	global_store_dwordx4 v[82:83], v[76:79], off
	v_cvt_f32_f16_sdwa v89, v101 dst_sel:DWORD dst_unused:UNUSED_PAD src0_sel:WORD_1
	v_cvt_f32_f16_e32 v88, v101
	v_pk_mul_f32 v[78:79], v[86:87], v[86:87]
	v_cvt_f32_f16_sdwa v87, v99 dst_sel:DWORD dst_unused:UNUSED_PAD src0_sel:WORD_1
	v_cvt_f32_f16_e32 v86, v99
	v_pk_mul_f32 v[76:77], v[84:85], v[84:85]
	v_cvt_f32_f16_sdwa v85, v98 dst_sel:DWORD dst_unused:UNUSED_PAD src0_sel:WORD_1
	v_cvt_f32_f16_e32 v84, v98
	v_pk_add_f32 v[86:87], v[70:71], v[86:87]
	v_cvt_f32_f16_sdwa v71, v100 dst_sel:DWORD dst_unused:UNUSED_PAD src0_sel:WORD_1
	v_cvt_f32_f16_e32 v70, v100
	v_pk_add_f32 v[84:85], v[68:69], v[84:85]
	v_pk_add_f32 v[66:67], v[66:67], v[88:89]
	v_cvt_pk_f16_f32 v68, v84, v85
	v_pk_add_f32 v[64:65], v[64:65], v[70:71]
	v_cvt_pk_f16_f32 v69, v86, v87
	v_cvt_pk_f16_f32 v70, v64, v65
	v_cvt_pk_f16_f32 v71, v66, v67
	v_pk_mul_f32 v[64:65], v[64:65], v[64:65]
	v_pk_mul_f32 v[66:67], v[66:67], v[66:67]
	global_store_dwordx4 v[82:83], v[68:71], off offset:256
	v_add_f32_e32 v66, v66, v67
	v_add_f32_e32 v64, v64, v65
	v_pk_mul_f32 v[68:69], v[84:85], v[84:85]
	v_pk_mul_f32 v[70:71], v[86:87], v[86:87]
	v_add_f32_e32 v64, v64, v66
	v_add_f32_e32 v65, v70, v71
	v_add_f32_e32 v66, v68, v69
	v_pk_mul_f32 v[72:73], v[72:73], v[72:73]
	v_pk_mul_f32 v[74:75], v[74:75], v[74:75]
	v_add_f32_e32 v65, v66, v65
	v_add_f32_e32 v64, v65, v64
	v_add_f32_e32 v65, v74, v75
	v_add_f32_e32 v66, v72, v73
	v_add_f32_e32 v65, v66, v65
	v_add_f32_e32 v66, v78, v79
	v_add_f32_e32 v67, v76, v77
	v_add_f32_e32 v66, v67, v66
	v_add_f32_e32 v65, v66, v65
	v_add_f32_e32 v64, v65, v64
	ds_bpermute_b32 v65, v159, v64
	s_waitcnt lgkmcnt(0)
	v_add_f32_e32 v64, v64, v65
	ds_bpermute_b32 v65, v158, v64
	s_and_saveexec_b64 s[0:1], vcc
	s_cbranch_execz .LBB0_1120
	v_lshlrev_b64 v[66:67], 6, v[106:107]
	v_lshl_add_u64 v[66:67], s[8:9], 0, v[66:67]
	s_lshl_b32 s62, s14, 2
	v_lshl_add_u64 v[66:67], v[66:67], 0, s[62:63]
	s_lshl_b32 s62, s28, 2
	v_lshl_add_u64 v[66:67], v[66:67], 0, s[62:63]
	s_waitcnt lgkmcnt(0)
	v_add_f32_e32 v64, v64, v65
	global_store_dword v[66:67], v64, off
.LBB0_1120:
	s_or_b64 exec, exec, s[0:1]
	v_add_u32_e32 v74, 0x80, v150
	v_ashrrev_i32_e32 v75, 31, v74
	v_lshlrev_b64 v[86:87], 11, v[74:75]
	s_waitcnt lgkmcnt(0)
	v_lshl_add_u64 v[64:65], v[152:153], 0, v[86:87]
	global_load_dwordx4 v[76:79], v[64:65], off
	global_load_dwordx4 v[82:85], v[64:65], off offset:256
	v_add_u32_e32 v72, 0x90, v150
	v_ashrrev_i32_e32 v73, 31, v72
	v_lshlrev_b64 v[64:65], 11, v[72:73]
	v_lshl_add_u64 v[64:65], v[152:153], 0, v[64:65]
	global_load_dwordx4 v[68:71], v[64:65], off
	s_nop 0
	global_load_dwordx4 v[64:67], v[64:65], off offset:256
	s_waitcnt vmcnt(0) lgkmcnt(0)
	v_cvt_f32_f16_e32 v88, v76
	v_cvt_f32_f16_sdwa v89, v76 dst_sel:DWORD dst_unused:UNUSED_PAD src0_sel:WORD_1
	v_cvt_f32_f16_e32 v76, v77
	v_cvt_f32_f16_sdwa v77, v77 dst_sel:DWORD dst_unused:UNUSED_PAD src0_sel:WORD_1
	v_pk_add_f32 v[88:89], v[60:61], v[88:89]
	s_nop 0
	v_cvt_pk_f16_f32 v60, v88, v89
	v_pk_add_f32 v[76:77], v[62:63], v[76:77]
	v_cvt_f32_f16_e32 v62, v78
	v_cvt_f32_f16_sdwa v63, v78 dst_sel:DWORD dst_unused:UNUSED_PAD src0_sel:WORD_1
	v_cvt_f32_f16_e32 v78, v79
	v_cvt_f32_f16_sdwa v79, v79 dst_sel:DWORD dst_unused:UNUSED_PAD src0_sel:WORD_1
	v_cvt_pk_f16_f32 v61, v76, v77
	v_pk_add_f32 v[56:57], v[56:57], v[62:63]
	v_pk_add_f32 v[58:59], v[58:59], v[78:79]
	v_lshl_add_u64 v[78:79], s[72:73], 0, v[86:87]
	v_cvt_pk_f16_f32 v62, v56, v57
	v_cvt_pk_f16_f32 v63, v58, v59
	v_lshl_add_u64 v[78:79], v[148:149], 1, v[78:79]
	global_store_dwordx4 v[78:79], v[60:63], off
	v_pk_mul_f32 v[56:57], v[56:57], v[56:57]
	v_pk_mul_f32 v[58:59], v[58:59], v[58:59]
	v_pk_mul_f32 v[62:63], v[76:77], v[76:77]
	v_cvt_f32_f16_e32 v76, v82
	v_cvt_f32_f16_sdwa v77, v82 dst_sel:DWORD dst_unused:UNUSED_PAD src0_sel:WORD_1
	v_cvt_f32_f16_e32 v82, v83
	v_cvt_f32_f16_sdwa v83, v83 dst_sel:DWORD dst_unused:UNUSED_PAD src0_sel:WORD_1
	v_pk_mul_f32 v[60:61], v[88:89], v[88:89]
	v_pk_add_f32 v[76:77], v[52:53], v[76:77]
	v_pk_add_f32 v[82:83], v[54:55], v[82:83]
	v_cvt_f32_f16_e32 v54, v84
	v_cvt_f32_f16_sdwa v55, v84 dst_sel:DWORD dst_unused:UNUSED_PAD src0_sel:WORD_1
	v_cvt_f32_f16_e32 v84, v85
	v_cvt_f32_f16_sdwa v85, v85 dst_sel:DWORD dst_unused:UNUSED_PAD src0_sel:WORD_1
	v_cvt_pk_f16_f32 v52, v76, v77
	v_pk_add_f32 v[48:49], v[48:49], v[54:55]
	v_cvt_pk_f16_f32 v53, v82, v83
	v_pk_add_f32 v[50:51], v[50:51], v[84:85]
	v_cvt_pk_f16_f32 v54, v48, v49
	v_cvt_pk_f16_f32 v55, v50, v51
	v_pk_mul_f32 v[48:49], v[48:49], v[48:49]
	v_pk_mul_f32 v[50:51], v[50:51], v[50:51]
	global_store_dwordx4 v[78:79], v[52:55], off offset:256
	v_add_f32_e32 v50, v50, v51
	v_add_f32_e32 v48, v48, v49
	v_pk_mul_f32 v[52:53], v[76:77], v[76:77]
	v_pk_mul_f32 v[54:55], v[82:83], v[82:83]
	v_add_f32_e32 v48, v48, v50
	v_add_f32_e32 v49, v54, v55
	v_add_f32_e32 v50, v52, v53
	v_add_f32_e32 v49, v50, v49
	v_add_f32_e32 v48, v49, v48
	v_add_f32_e32 v49, v58, v59
	v_add_f32_e32 v50, v56, v57
	v_add_f32_e32 v49, v50, v49
	v_add_f32_e32 v50, v62, v63
	v_add_f32_e32 v51, v60, v61
	v_add_f32_e32 v50, v51, v50
	v_add_f32_e32 v49, v50, v49
	v_add_f32_e32 v48, v49, v48
	ds_bpermute_b32 v49, v159, v48
	s_waitcnt lgkmcnt(0)
	v_add_f32_e32 v48, v48, v49
	ds_bpermute_b32 v49, v158, v48
	s_and_saveexec_b64 s[0:1], vcc
	s_cbranch_execz .LBB0_1122
	v_lshlrev_b64 v[50:51], 6, v[74:75]
	v_lshl_add_u64 v[50:51], s[8:9], 0, v[50:51]
	s_lshl_b32 s62, s14, 2
	v_lshl_add_u64 v[50:51], v[50:51], 0, s[62:63]
	s_lshl_b32 s62, s28, 2
	v_lshl_add_u64 v[50:51], v[50:51], 0, s[62:63]
	s_waitcnt lgkmcnt(0)
	v_add_f32_e32 v48, v48, v49
	global_store_dword v[50:51], v48, off
; __device__ __forceinline__ float xor_add(float v, int lane, int o) { return v + __builtin_bit_cast(float, __builtin_amdgcn_ds_bpermute((lane ^ o) << 2, __builtin_bit_cast(int, v))); }
; __device__ __forceinline__ float f16_lo(unsigned u) { return (float)__builtin_bit_cast(h16x2, u)[0]; }
;     __device__ __forceinline__ void operator()(const f32x4 (&acc)[2][2][4][2], const Unit& u, int wr, int wc, int fr, int fq) const {
;         { int z_ = 0; asm volatile("" : "+v"(z_)); const int l_ = (int)__builtin_amdgcn_mbcnt_hi(~0u, __builtin_amdgcn_mbcnt_lo(~0u, (unsigned)z_)); fr = l_ & 15; fq = l_ >> 4; }
;         const int row0 = u.pm * BM + wr * 64 + fr, col0 = u.pn * BM + wc * 32 + 8 * fq, lane = fq * 16 + fr;
; #pragma unroll
;         for (int ai = 0; ai < 2; ++ai)
; #pragma unroll
;             for (int mp = 0; mp < 2; ++mp) {
;                 u32x4 bsv[2][2];
; #pragma unroll
;                 for (int mm = 0; mm < 2; ++mm)
; #pragma unroll
;                     for (int bj = 0; bj < 2; ++bj) bsv[mm][bj] = *(const u32x4*)(base + (size_t)(row0 + ai * HALF + (2 * mp + mm) * 16) * ldc + col0 + bj * HALF);
; #pragma unroll
;                 for (int mm = 0; mm < 2; ++mm) { const int m = 2 * mp + mm; const size_t r = (size_t)(row0 + ai * HALF + m * 16), off = r * ldc + col0; float ss = 0.f;
; #pragma unroll
;                     for (int bj = 0; bj < 2; ++bj) { const u32x4 b = bsv[mm][bj]; const f32x4 a0 = acc[ai][bj][m][0] * sc, a1 = acc[ai][bj][m][1] * sc;
;                         f32x4 v0, v1; v0[0] = f16_lo(b.x) + a0[0]; v0[1] = f16_hi(b.x) + a0[1]; v0[2] = f16_lo(b.y) + a0[2]; v0[3] = f16_hi(b.y) + a0[3];
;                         v1[0] = f16_lo(b.z) + a1[0]; v1[1] = f16_hi(b.z) + a1[1]; v1[2] = f16_lo(b.w) + a1[2]; v1[3] = f16_hi(b.w) + a1[3];
;                         u32x4 w; w.x = pk_f16(v0[0], v0[1]); w.y = pk_f16(v0[2], v0[3]); w.z = pk_f16(v1[0], v1[1]); w.w = pk_f16(v1[2], v1[3]); *(u32x4*)(out + off + bj * HALF) = w;
;                         ss += ((v0[0] * v0[0] + v0[1] * v0[1]) + (v0[2] * v0[2] + v0[3] * v0[3])) + ((v1[0] * v1[0] + v1[1] * v1[1]) + (v1[2] * v1[2] + v1[3] * v1[3])); }
;                     ss = xor_add(ss, lane, 16); ss = xor_add(ss, lane, 32);
;                     if (fq == 0) ssp[r * 16 + (u.pn & 3) * 4 + wc] = ss; }
;                 asm volatile("" ::: "memory");
;             }
;     }
.LBB0_1122:
	s_or_b64 exec, exec, s[0:1]
	v_cvt_f32_f16_sdwa v53, v69 dst_sel:DWORD dst_unused:UNUSED_PAD src0_sel:WORD_1
	v_cvt_f32_f16_e32 v52, v69
	v_cvt_f32_f16_sdwa v51, v68 dst_sel:DWORD dst_unused:UNUSED_PAD src0_sel:WORD_1
	v_cvt_f32_f16_e32 v50, v68
	v_cvt_f32_f16_sdwa v55, v71 dst_sel:DWORD dst_unused:UNUSED_PAD src0_sel:WORD_1
	v_pk_add_f32 v[52:53], v[46:47], v[52:53]
	v_cvt_f32_f16_sdwa v47, v70 dst_sel:DWORD dst_unused:UNUSED_PAD src0_sel:WORD_1
	v_cvt_f32_f16_e32 v46, v70
	v_cvt_f32_f16_e32 v54, v71
	s_waitcnt lgkmcnt(0)
	v_lshlrev_b64 v[48:49], 10, v[72:73]
	v_pk_add_f32 v[50:51], v[44:45], v[50:51]
	v_pk_add_f32 v[40:41], v[40:41], v[46:47]
	v_pk_add_f32 v[42:43], v[42:43], v[54:55]
	v_lshl_add_u64 v[48:49], v[48:49], 1, s[72:73]
	v_cvt_pk_f16_f32 v44, v50, v51
	v_cvt_pk_f16_f32 v45, v52, v53
	v_cvt_pk_f16_f32 v46, v40, v41
	v_cvt_pk_f16_f32 v47, v42, v43
	v_lshl_add_u64 v[48:49], v[148:149], 1, v[48:49]
	global_store_dwordx4 v[48:49], v[44:47], off
	v_cvt_f32_f16_sdwa v55, v67 dst_sel:DWORD dst_unused:UNUSED_PAD src0_sel:WORD_1
	v_cvt_f32_f16_e32 v54, v67
	v_pk_mul_f32 v[46:47], v[52:53], v[52:53]
	v_cvt_f32_f16_sdwa v53, v65 dst_sel:DWORD dst_unused:UNUSED_PAD src0_sel:WORD_1
	v_cvt_f32_f16_e32 v52, v65
	v_pk_mul_f32 v[44:45], v[50:51], v[50:51]
	v_cvt_f32_f16_sdwa v51, v64 dst_sel:DWORD dst_unused:UNUSED_PAD src0_sel:WORD_1
	v_cvt_f32_f16_e32 v50, v64
	v_pk_add_f32 v[52:53], v[38:39], v[52:53]
	v_cvt_f32_f16_sdwa v39, v66 dst_sel:DWORD dst_unused:UNUSED_PAD src0_sel:WORD_1
	v_cvt_f32_f16_e32 v38, v66
	v_pk_add_f32 v[50:51], v[36:37], v[50:51]
	v_pk_add_f32 v[34:35], v[34:35], v[54:55]
	v_cvt_pk_f16_f32 v36, v50, v51
	v_pk_add_f32 v[32:33], v[32:33], v[38:39]
	v_cvt_pk_f16_f32 v37, v52, v53
	v_cvt_pk_f16_f32 v38, v32, v33
	v_cvt_pk_f16_f32 v39, v34, v35
	v_pk_mul_f32 v[32:33], v[32:33], v[32:33]
	v_pk_mul_f32 v[34:35], v[34:35], v[34:35]
	global_store_dwordx4 v[48:49], v[36:39], off offset:256
	v_add_f32_e32 v34, v34, v35
	v_add_f32_e32 v32, v32, v33
	v_pk_mul_f32 v[36:37], v[50:51], v[50:51]
	v_pk_mul_f32 v[38:39], v[52:53], v[52:53]
	v_add_f32_e32 v32, v32, v34
	v_add_f32_e32 v33, v38, v39
	v_add_f32_e32 v34, v36, v37
	v_pk_mul_f32 v[40:41], v[40:41], v[40:41]
	v_pk_mul_f32 v[42:43], v[42:43], v[42:43]
	v_add_f32_e32 v33, v34, v33
	v_add_f32_e32 v32, v33, v32
	v_add_f32_e32 v33, v42, v43
	v_add_f32_e32 v34, v40, v41
	v_add_f32_e32 v33, v34, v33
	v_add_f32_e32 v34, v46, v47
	v_add_f32_e32 v35, v44, v45
	v_add_f32_e32 v34, v35, v34
	v_add_f32_e32 v33, v34, v33
	v_add_f32_e32 v32, v33, v32
	ds_bpermute_b32 v33, v159, v32
	s_waitcnt lgkmcnt(0)
	v_add_f32_e32 v32, v32, v33
	ds_bpermute_b32 v33, v158, v32
	s_and_saveexec_b64 s[0:1], vcc
	s_cbranch_execz .LBB0_1124
	v_lshlrev_b64 v[34:35], 6, v[72:73]
	v_lshl_add_u64 v[34:35], s[8:9], 0, v[34:35]
	s_lshl_b32 s62, s14, 2
	v_lshl_add_u64 v[34:35], v[34:35], 0, s[62:63]
	s_lshl_b32 s62, s28, 2
	v_lshl_add_u64 v[34:35], v[34:35], 0, s[62:63]
	s_waitcnt lgkmcnt(0)
	v_add_f32_e32 v32, v32, v33
	global_store_dword v[34:35], v32, off
; __device__ __forceinline__ float xor_add(float v, int lane, int o) { return v + __builtin_bit_cast(float, __builtin_amdgcn_ds_bpermute((lane ^ o) << 2, __builtin_bit_cast(int, v))); }
; __device__ __forceinline__ float f16_lo(unsigned u) { return (float)__builtin_bit_cast(h16x2, u)[0]; }
;     __device__ __forceinline__ void operator()(const f32x4 (&acc)[2][2][4][2], const Unit& u, int wr, int wc, int fr, int fq) const {
;         { int z_ = 0; asm volatile("" : "+v"(z_)); const int l_ = (int)__builtin_amdgcn_mbcnt_hi(~0u, __builtin_amdgcn_mbcnt_lo(~0u, (unsigned)z_)); fr = l_ & 15; fq = l_ >> 4; }
;         const int row0 = u.pm * BM + wr * 64 + fr, col0 = u.pn * BM + wc * 32 + 8 * fq, lane = fq * 16 + fr;
; #pragma unroll
;         for (int ai = 0; ai < 2; ++ai)
; #pragma unroll
;             for (int mp = 0; mp < 2; ++mp) {
;                 u32x4 bsv[2][2];
; #pragma unroll
;                 for (int mm = 0; mm < 2; ++mm)
; #pragma unroll
;                     for (int bj = 0; bj < 2; ++bj) bsv[mm][bj] = *(const u32x4*)(base + (size_t)(row0 + ai * HALF + (2 * mp + mm) * 16) * ldc + col0 + bj * HALF);
; #pragma unroll
;                 for (int mm = 0; mm < 2; ++mm) { const int m = 2 * mp + mm; const size_t r = (size_t)(row0 + ai * HALF + m * 16), off = r * ldc + col0; float ss = 0.f;
; #pragma unroll
;                     for (int bj = 0; bj < 2; ++bj) { const u32x4 b = bsv[mm][bj]; const f32x4 a0 = acc[ai][bj][m][0] * sc, a1 = acc[ai][bj][m][1] * sc;
;                         f32x4 v0, v1; v0[0] = f16_lo(b.x) + a0[0]; v0[1] = f16_hi(b.x) + a0[1]; v0[2] = f16_lo(b.y) + a0[2]; v0[3] = f16_hi(b.y) + a0[3];
;                         v1[0] = f16_lo(b.z) + a1[0]; v1[1] = f16_hi(b.z) + a1[1]; v1[2] = f16_lo(b.w) + a1[2]; v1[3] = f16_hi(b.w) + a1[3];
;                         u32x4 w; w.x = pk_f16(v0[0], v0[1]); w.y = pk_f16(v0[2], v0[3]); w.z = pk_f16(v1[0], v1[1]); w.w = pk_f16(v1[2], v1[3]); *(u32x4*)(out + off + bj * HALF) = w;
;                         ss += ((v0[0] * v0[0] + v0[1] * v0[1]) + (v0[2] * v0[2] + v0[3] * v0[3])) + ((v1[0] * v1[0] + v1[1] * v1[1]) + (v1[2] * v1[2] + v1[3] * v1[3])); }
;                     ss = xor_add(ss, lane, 16); ss = xor_add(ss, lane, 32);
;                     if (fq == 0) ssp[r * 16 + (u.pn & 3) * 4 + wc] = ss; }
;                 asm volatile("" ::: "memory");
;             }
;     }
.LBB0_1124:
	s_or_b64 exec, exec, s[0:1]
	v_add_u32_e32 v42, 0xa0, v150
	v_ashrrev_i32_e32 v43, 31, v42
	v_lshlrev_b64 v[52:53], 11, v[42:43]
	s_waitcnt lgkmcnt(0)
	v_lshl_add_u64 v[32:33], v[152:153], 0, v[52:53]
	global_load_dwordx4 v[44:47], v[32:33], off
	global_load_dwordx4 v[48:51], v[32:33], off offset:256
	v_add_u32_e32 v40, 0xb0, v150
	v_ashrrev_i32_e32 v41, 31, v40
	v_lshlrev_b64 v[32:33], 11, v[40:41]
	v_lshl_add_u64 v[32:33], v[152:153], 0, v[32:33]
	global_load_dwordx4 v[36:39], v[32:33], off
	s_nop 0
	global_load_dwordx4 v[32:35], v[32:33], off offset:256
	s_waitcnt vmcnt(0) lgkmcnt(0)
	v_cvt_f32_f16_e32 v54, v44
	v_cvt_f32_f16_sdwa v55, v44 dst_sel:DWORD dst_unused:UNUSED_PAD src0_sel:WORD_1
	v_cvt_f32_f16_e32 v44, v45
	v_cvt_f32_f16_sdwa v45, v45 dst_sel:DWORD dst_unused:UNUSED_PAD src0_sel:WORD_1
	v_pk_add_f32 v[54:55], v[28:29], v[54:55]
	s_nop 0
	v_cvt_pk_f16_f32 v28, v54, v55
	v_pk_add_f32 v[44:45], v[30:31], v[44:45]
	v_cvt_f32_f16_e32 v30, v46
	v_cvt_f32_f16_sdwa v31, v46 dst_sel:DWORD dst_unused:UNUSED_PAD src0_sel:WORD_1
	v_cvt_f32_f16_e32 v46, v47
	v_cvt_f32_f16_sdwa v47, v47 dst_sel:DWORD dst_unused:UNUSED_PAD src0_sel:WORD_1
	v_cvt_pk_f16_f32 v29, v44, v45
	v_pk_add_f32 v[24:25], v[24:25], v[30:31]
	v_pk_add_f32 v[26:27], v[26:27], v[46:47]
	v_lshl_add_u64 v[46:47], s[72:73], 0, v[52:53]
	v_cvt_pk_f16_f32 v30, v24, v25
	v_cvt_pk_f16_f32 v31, v26, v27
	v_lshl_add_u64 v[46:47], v[148:149], 1, v[46:47]
	global_store_dwordx4 v[46:47], v[28:31], off
	v_pk_mul_f32 v[24:25], v[24:25], v[24:25]
	v_pk_mul_f32 v[26:27], v[26:27], v[26:27]
	v_pk_mul_f32 v[30:31], v[44:45], v[44:45]
	v_cvt_f32_f16_e32 v44, v48
	v_cvt_f32_f16_sdwa v45, v48 dst_sel:DWORD dst_unused:UNUSED_PAD src0_sel:WORD_1
	v_cvt_f32_f16_e32 v48, v49
	v_cvt_f32_f16_sdwa v49, v49 dst_sel:DWORD dst_unused:UNUSED_PAD src0_sel:WORD_1
	v_pk_mul_f32 v[28:29], v[54:55], v[54:55]
	v_pk_add_f32 v[44:45], v[20:21], v[44:45]
	v_pk_add_f32 v[48:49], v[22:23], v[48:49]
	v_cvt_f32_f16_e32 v22, v50
	v_cvt_f32_f16_sdwa v23, v50 dst_sel:DWORD dst_unused:UNUSED_PAD src0_sel:WORD_1
	v_cvt_f32_f16_e32 v50, v51
	v_cvt_f32_f16_sdwa v51, v51 dst_sel:DWORD dst_unused:UNUSED_PAD src0_sel:WORD_1
	v_cvt_pk_f16_f32 v20, v44, v45
	v_pk_add_f32 v[16:17], v[16:17], v[22:23]
	v_cvt_pk_f16_f32 v21, v48, v49
	v_pk_add_f32 v[18:19], v[18:19], v[50:51]
	v_cvt_pk_f16_f32 v22, v16, v17
	v_cvt_pk_f16_f32 v23, v18, v19
	v_pk_mul_f32 v[16:17], v[16:17], v[16:17]
	v_pk_mul_f32 v[18:19], v[18:19], v[18:19]
	global_store_dwordx4 v[46:47], v[20:23], off offset:256
	v_add_f32_e32 v18, v18, v19
	v_add_f32_e32 v16, v16, v17
	v_pk_mul_f32 v[20:21], v[44:45], v[44:45]
	v_pk_mul_f32 v[22:23], v[48:49], v[48:49]
	v_add_f32_e32 v16, v16, v18
	v_add_f32_e32 v17, v22, v23
	v_add_f32_e32 v18, v20, v21
	v_add_f32_e32 v17, v18, v17
	v_add_f32_e32 v16, v17, v16
	v_add_f32_e32 v17, v26, v27
	v_add_f32_e32 v18, v24, v25
	v_add_f32_e32 v17, v18, v17
	v_add_f32_e32 v18, v30, v31
	v_add_f32_e32 v19, v28, v29
	v_add_f32_e32 v18, v19, v18
	v_add_f32_e32 v17, v18, v17
	v_add_f32_e32 v16, v17, v16
	ds_bpermute_b32 v17, v159, v16
	s_waitcnt lgkmcnt(0)
	v_add_f32_e32 v16, v16, v17
	ds_bpermute_b32 v17, v158, v16
	s_and_saveexec_b64 s[0:1], vcc
	s_cbranch_execz .LBB0_1126
	v_lshlrev_b64 v[18:19], 6, v[42:43]
	v_lshl_add_u64 v[18:19], s[8:9], 0, v[18:19]
	s_lshl_b32 s62, s14, 2
	v_lshl_add_u64 v[18:19], v[18:19], 0, s[62:63]
	s_lshl_b32 s62, s28, 2
	v_lshl_add_u64 v[18:19], v[18:19], 0, s[62:63]
	s_waitcnt lgkmcnt(0)
	v_add_f32_e32 v16, v16, v17
	global_store_dword v[18:19], v16, off
.LBB0_1126:
	s_or_b64 exec, exec, s[0:1]
	v_cvt_f32_f16_sdwa v21, v37 dst_sel:DWORD dst_unused:UNUSED_PAD src0_sel:WORD_1
	v_cvt_f32_f16_e32 v20, v37
	v_cvt_f32_f16_sdwa v19, v36 dst_sel:DWORD dst_unused:UNUSED_PAD src0_sel:WORD_1
	v_cvt_f32_f16_e32 v18, v36
	v_cvt_f32_f16_sdwa v23, v39 dst_sel:DWORD dst_unused:UNUSED_PAD src0_sel:WORD_1
	v_pk_add_f32 v[20:21], v[14:15], v[20:21]
	v_cvt_f32_f16_sdwa v15, v38 dst_sel:DWORD dst_unused:UNUSED_PAD src0_sel:WORD_1
	v_cvt_f32_f16_e32 v14, v38
	v_cvt_f32_f16_e32 v22, v39
	s_waitcnt lgkmcnt(0)
	v_lshlrev_b64 v[16:17], 10, v[40:41]
	v_pk_add_f32 v[18:19], v[12:13], v[18:19]
	v_pk_add_f32 v[8:9], v[8:9], v[14:15]
	v_pk_add_f32 v[10:11], v[10:11], v[22:23]
	v_lshl_add_u64 v[16:17], v[16:17], 1, s[72:73]
	v_cvt_pk_f16_f32 v12, v18, v19
	v_cvt_pk_f16_f32 v13, v20, v21
	v_cvt_pk_f16_f32 v14, v8, v9
	v_cvt_pk_f16_f32 v15, v10, v11
	v_lshl_add_u64 v[16:17], v[148:149], 1, v[16:17]
	global_store_dwordx4 v[16:17], v[12:15], off
	v_cvt_f32_f16_sdwa v23, v35 dst_sel:DWORD dst_unused:UNUSED_PAD src0_sel:WORD_1
	v_cvt_f32_f16_e32 v22, v35
	v_pk_mul_f32 v[14:15], v[20:21], v[20:21]
	v_cvt_f32_f16_sdwa v21, v33 dst_sel:DWORD dst_unused:UNUSED_PAD src0_sel:WORD_1
	v_cvt_f32_f16_e32 v20, v33
	v_pk_mul_f32 v[12:13], v[18:19], v[18:19]
	v_cvt_f32_f16_sdwa v19, v32 dst_sel:DWORD dst_unused:UNUSED_PAD src0_sel:WORD_1
	v_cvt_f32_f16_e32 v18, v32
	v_pk_add_f32 v[20:21], v[6:7], v[20:21]
	v_cvt_f32_f16_sdwa v7, v34 dst_sel:DWORD dst_unused:UNUSED_PAD src0_sel:WORD_1
	v_cvt_f32_f16_e32 v6, v34
	v_pk_add_f32 v[18:19], v[4:5], v[18:19]
	v_pk_add_f32 v[2:3], v[2:3], v[22:23]
	v_cvt_pk_f16_f32 v4, v18, v19
	v_pk_add_f32 v[0:1], v[0:1], v[6:7]
	v_cvt_pk_f16_f32 v5, v20, v21
	v_cvt_pk_f16_f32 v6, v0, v1
	v_cvt_pk_f16_f32 v7, v2, v3
	v_pk_mul_f32 v[0:1], v[0:1], v[0:1]
	v_pk_mul_f32 v[2:3], v[2:3], v[2:3]
	global_store_dwordx4 v[16:17], v[4:7], off offset:256
	v_add_f32_e32 v2, v2, v3
	v_add_f32_e32 v0, v0, v1
	v_pk_mul_f32 v[4:5], v[18:19], v[18:19]
	v_pk_mul_f32 v[6:7], v[20:21], v[20:21]
	v_add_f32_e32 v0, v0, v2
	v_add_f32_e32 v1, v6, v7
	v_add_f32_e32 v2, v4, v5
	v_pk_mul_f32 v[8:9], v[8:9], v[8:9]
	v_pk_mul_f32 v[10:11], v[10:11], v[10:11]
	v_add_f32_e32 v1, v2, v1
	v_add_f32_e32 v0, v1, v0
	v_add_f32_e32 v1, v10, v11
	v_add_f32_e32 v2, v8, v9
	v_add_f32_e32 v1, v2, v1
	v_add_f32_e32 v2, v14, v15
	v_add_f32_e32 v3, v12, v13
	v_add_f32_e32 v2, v3, v2
	v_add_f32_e32 v1, v2, v1
	v_add_f32_e32 v0, v1, v0
	ds_bpermute_b32 v1, v159, v0
	s_waitcnt lgkmcnt(0)
	v_add_f32_e32 v0, v0, v1
	ds_bpermute_b32 v1, v158, v0
	s_and_saveexec_b64 s[0:1], vcc
	s_cbranch_execz .LBB0_1128
	v_lshlrev_b64 v[2:3], 6, v[40:41]
	v_lshl_add_u64 v[2:3], s[8:9], 0, v[2:3]
	s_lshl_b32 s62, s14, 2
	v_lshl_add_u64 v[2:3], v[2:3], 0, s[62:63]
	s_lshl_b32 s62, s28, 2
	v_lshl_add_u64 v[2:3], v[2:3], 0, s[62:63]
	s_waitcnt lgkmcnt(0)
	v_add_f32_e32 v0, v0, v1
	global_store_dword v[2:3], v0, off

; __device__ __forceinline__ float row_rstd(const float* ssp, size_t row) {
;     const f32x4* p = (const f32x4*)(ssp + row * 16); const f32x4 a = p[0], b = p[1], c = p[2], d = p[3];
;     const float s = (((a[0] + a[1]) + (a[2] + a[3])) + ((b[0] + b[1]) + (b[2] + b[3]))) + (((c[0] + c[1]) + (c[2] + c[3])) + ((d[0] + d[1]) + (d[2] + d[3])));
;     return rsqrtf(s * (1.f / 1024.f) + 1e-6f);
; }
.LBB0_1259:
	v_mbcnt_lo_u32_b32 v0, -1, v0
	v_mbcnt_hi_u32_b32 v0, -1, v0
	v_readlane_b32 s2, v254, 25
	s_nop 1
	v_add_u32_e32 v0, s2, v0
	s_movk_i32 s2, 0x100
	v_cmp_gt_i32_e32 vcc, s2, v0
	s_and_saveexec_b64 s[2:3], vcc
	s_cbranch_execz .LBB0_1261
	s_waitcnt lgkmcnt(0)
	v_ashrrev_i32_e32 v1, 31, v0
	v_lshl_add_u64 v[2:3], s[4:5], 0, v[0:1]
	v_lshlrev_b64 v[2:3], 6, v[2:3]
	v_lshl_add_u64 v[2:3], s[80:81], 0, v[2:3]
	s_mov_b64 s[4:5], 0x300000
	v_lshl_add_u64 v[14:15], v[2:3], 0, s[4:5]
	v_add_co_u32_e32 v2, vcc, 0x300000, v2
	s_nop 1
	v_addc_co_u32_e32 v3, vcc, 0, v3, vcc
	global_load_dwordx4 v[2:5], v[2:3], off
	s_nop 0
	global_load_dwordx4 v[6:9], v[14:15], off offset:16
	global_load_dwordx4 v[10:13], v[14:15], off offset:32
	s_nop 0
	global_load_dwordx4 v[14:17], v[14:15], off offset:48
	s_waitcnt vmcnt(0) lgkmcnt(0)
	v_mov_b32_e32 v18, v2
	v_mov_b32_e32 v19, v10
	v_mov_b32_e32 v10, v3
	v_pk_add_f32 v[2:3], v[18:19], v[10:11]
	v_mov_b32_e32 v10, v4
	v_mov_b32_e32 v11, v12
	v_mov_b32_e32 v12, v5
	v_pk_add_f32 v[4:5], v[10:11], v[12:13]
	s_nop 0
	v_pk_add_f32 v[2:3], v[2:3], v[4:5]
	v_mov_b32_e32 v4, v6
	v_mov_b32_e32 v5, v14
	v_mov_b32_e32 v14, v7
	v_mov_b32_e32 v6, v8
	v_mov_b32_e32 v7, v16
	v_mov_b32_e32 v16, v9
	v_pk_add_f32 v[4:5], v[4:5], v[14:15]
	v_pk_add_f32 v[6:7], v[6:7], v[16:17]
	s_nop 0
	v_pk_add_f32 v[4:5], v[4:5], v[6:7]
	s_nop 0
	v_pk_add_f32 v[2:3], v[2:3], v[4:5]
	s_nop 0
	v_add_f32_e32 v1, v2, v3
	v_fmamk_f32 v1, v1, 0x3a800000, v162
	v_cmp_gt_f32_e32 vcc, s85, v1
	v_mul_f32_e32 v2, 0x4b800000, v1
	s_nop 0
	v_cndmask_b32_e32 v1, v1, v2, vcc
	v_rsq_f32_e32 v1, v1
	s_nop 0
	v_mul_f32_e32 v2, 0x45800000, v1
	v_cndmask_b32_e32 v1, v1, v2, vcc
	v_lshl_add_u32 v2, v0, 2, 0
	v_add_u32_e32 v2, 0x20400, v2
	ds_write_b32 v2, v1

;     __device__ __forceinline__ void operator()(const f32x4 (&acc)[2][2][4][2], const Unit& u, int wr, int wc, int fr, int fq) const {
;         { int z_ = 0; asm volatile("" : "+v"(z_)); const int l_ = (int)__builtin_amdgcn_mbcnt_hi(~0u, __builtin_amdgcn_mbcnt_lo(~0u, (unsigned)z_)); fr = l_ & 15; fq = l_ >> 4; }
;         const int row0 = u.pm * BM + wr * 64 + fr, col0 = u.pn * BM + wc * 32 + 8 * fq, lane = fq * 16 + fr;
; #pragma unroll
;         for (int ai = 0; ai < 2; ++ai)
; #pragma unroll
;             for (int mp = 0; mp < 2; ++mp) {
;                 u32x4 bsv[2][2], tv[2][2];
; #pragma unroll
;                 for (int mm = 0; mm < 2; ++mm)
; #pragma unroll
;                     for (int bj = 0; bj < 2; ++bj) { const size_t o = (size_t)(row0 + ai * HALF + (2 * mp + mm) * 16) * ldc + col0 + bj * HALF; bsv[mm][bj] = *(const u32x4*)(base + o); tv[mm][bj] = *(const u32x4*)(PP + o); }
; #pragma unroll
;                 for (int mm = 0; mm < 2; ++mm) { const int m = 2 * mp + mm; const size_t r = (size_t)(row0 + ai * HALF + m * 16), off = r * ldc + col0; float ss = 0.f;
;                     const float rs = tbl[wr * 64 + fr + ai * HALF + m * 16];
; #pragma unroll
;                     for (int bj = 0; bj < 2; ++bj) { const u32x4 t = tv[mm][bj], b = bsv[mm][bj]; const f32x4 a0 = acc[ai][bj][m][0] * rs, a1 = acc[ai][bj][m][1] * rs;
;                         f32x4 v0, v1; v0[0] = f16_lo(b.x) + bf_lo(t.x) * sigm(a0[0]); v0[1] = f16_hi(b.x) + bf_hi(t.x) * sigm(a0[1]); v0[2] = f16_lo(b.y) + bf_lo(t.y) * sigm(a0[2]); v0[3] = f16_hi(b.y) + bf_hi(t.y) * sigm(a0[3]);
;                         v1[0] = f16_lo(b.z) + bf_lo(t.z) * sigm(a1[0]); v1[1] = f16_hi(b.z) + bf_hi(t.z) * sigm(a1[1]); v1[2] = f16_lo(b.w) + bf_lo(t.w) * sigm(a1[2]); v1[3] = f16_hi(b.w) + bf_hi(t.w) * sigm(a1[3]);
;                         u32x4 w; w.x = pk_f16(v0[0], v0[1]); w.y = pk_f16(v0[2], v0[3]); w.z = pk_f16(v1[0], v1[1]); w.w = pk_f16(v1[2], v1[3]); *(u32x4*)(out + off + bj * HALF) = w;
;                         ss += ((v0[0] * v0[0] + v0[1] * v0[1]) + (v0[2] * v0[2] + v0[3] * v0[3])) + ((v1[0] * v1[0] + v1[1] * v1[1]) + (v1[2] * v1[2] + v1[3] * v1[3])); }
;                     ss = xor_add(ss, lane, 16); ss = xor_add(ss, lane, 32);
;                     if (fq == 0) ssp[r * 16 + (u.pn & 3) * 4 + wc] = ss; }
;                 asm volatile("" ::: "memory");
;             }
;     }
.LBB0_1283:
	v_mov_b32_e32 v130, v81
	s_lshl_b32 s0, s20, 8
	v_mbcnt_lo_u32_b32 v130, -1, v130
	v_mbcnt_hi_u32_b32 v134, -1, v130
	v_and_b32_e32 v135, 15, v134
	s_add_i32 s0, s0, s36
	v_or_b32_e32 v150, s0, v135
	s_lshl_b32 s0, s18, 8
	v_ashrrev_i32_e32 v130, 1, v134
	s_or_b32 s0, s0, s37
	v_and_b32_e32 v130, -8, v130
	v_add_u32_e32 v148, s0, v130
	v_ashrrev_i32_e32 v151, 31, v150
	v_ashrrev_i32_e32 v149, 31, v148
	v_lshlrev_b64 v[130:131], 10, v[150:151]
	v_lshl_add_u64 v[130:131], v[130:131], 0, v[148:149]
	v_lshlrev_b64 v[130:131], 1, v[130:131]
	v_lshl_add_u64 v[132:133], s[72:73], 0, v[130:131]
	global_load_dwordx4 v[174:177], v[132:133], off
	v_lshl_add_u64 v[130:131], s[70:71], 0, v[130:131]
	v_lshl_add_u32 v160, v135, 2, s40
	global_load_dwordx4 v[178:181], v[130:131], off
	ds_read_b32 v190, v160
	global_load_dwordx4 v[182:185], v[132:133], off offset:256
	global_load_dwordx4 v[186:189], v[130:131], off offset:256
	v_or_b32_e32 v152, 16, v150
	v_ashrrev_i32_e32 v153, 31, v152
	v_lshlrev_b64 v[154:155], 10, v[152:153]
	v_lshlrev_b32_e32 v136, 2, v134
	v_cmp_gt_u32_e32 vcc, 16, v134
	v_lshl_add_u64 v[134:135], v[154:155], 0, v[148:149]
	v_lshlrev_b64 v[134:135], 1, v[134:135]
	v_lshl_add_u64 v[130:131], s[72:73], 0, v[134:135]
	v_xor_b32_e32 v159, 64, v136
	v_xor_b32_e32 v158, 0x80, v136
	v_lshl_add_u64 v[206:207], s[70:71], 0, v[134:135]
	s_waitcnt lgkmcnt(0)
	v_pk_mul_f32 v[208:209], v[128:129], v[190:191] op_sel_hi:[1,0]
	v_pk_mul_f32 v[210:211], v[126:127], v[190:191] op_sel_hi:[1,0]
	v_pk_mul_f32 v[212:213], v[124:125], v[190:191] op_sel_hi:[1,0]
	v_pk_mul_f32 v[214:215], v[122:123], v[190:191] op_sel_hi:[1,0]
	global_load_dwordx4 v[134:137], v[130:131], off
	global_load_dwordx4 v[126:129], v[130:131], off offset:256
	s_nop 0
	global_load_dwordx4 v[130:133], v[206:207], off
	global_load_dwordx4 v[122:125], v[206:207], off offset:256
	v_mul_f32_e32 v191, 0xbfb8aa3b, v215
	v_exp_f32_e32 v191, v191
	v_mul_f32_e32 v196, 0xbfb8aa3b, v212
	v_mul_f32_e32 v204, 0xbfb8aa3b, v213
	v_exp_f32_e32 v196, v196
	v_add_f32_e32 v191, 1.0, v191
	v_pk_mul_f32 v[120:121], v[120:121], v[190:191] op_sel_hi:[1,0]
	v_exp_f32_e32 v204, v204
	v_mul_f32_e32 v120, 0xbfb8aa3b, v120
	v_mul_f32_e32 v121, 0xbfb8aa3b, v121
	v_exp_f32_e32 v120, v120
	v_exp_f32_e32 v121, v121
	v_pk_mul_f32 v[118:119], v[118:119], v[190:191] op_sel_hi:[1,0]
	v_pk_mul_f32 v[114:115], v[114:115], v[190:191] op_sel_hi:[1,0]
	v_add_f32_e32 v196, 1.0, v196
	v_add_f32_e32 v204, 1.0, v204
	v_pk_mul_f32 v[116:117], v[116:117], v[190:191] op_sel_hi:[1,0]
	v_mul_f32_e32 v118, 0xbfb8aa3b, v118
	v_mul_f32_e32 v119, 0xbfb8aa3b, v119
	v_mul_f32_e32 v114, 0xbfb8aa3b, v114
	v_mul_f32_e32 v115, 0xbfb8aa3b, v115
	v_mul_f32_e32 v171, 0xbfb8aa3b, v208
	v_mul_f32_e32 v172, 0xbfb8aa3b, v209
	v_mul_f32_e32 v173, 0xbfb8aa3b, v214
	v_rcp_f32_e32 v212, v196
	v_rcp_f32_e32 v213, v204
	v_exp_f32_e32 v118, v118
	v_exp_f32_e32 v119, v119
	v_add_f32_e32 v120, 1.0, v120
	v_add_f32_e32 v121, 1.0, v121
	v_exp_f32_e32 v114, v114
	v_exp_f32_e32 v115, v115
	v_mul_f32_e32 v116, 0xbfb8aa3b, v116
	v_mul_f32_e32 v117, 0xbfb8aa3b, v117
	v_mul_f32_e32 v161, 0xbfb8aa3b, v210
	v_mul_f32_e32 v170, 0xbfb8aa3b, v211
	v_exp_f32_e32 v171, v171
	v_exp_f32_e32 v172, v172
	v_exp_f32_e32 v173, v173
	v_rcp_f32_e32 v211, v191
	v_rcp_f32_e32 v120, v120
	v_rcp_f32_e32 v121, v121
	v_exp_f32_e32 v116, v116
	v_exp_f32_e32 v117, v117
	v_exp_f32_e32 v161, v161
	v_exp_f32_e32 v170, v170
	v_add_f32_e32 v118, 1.0, v118
	v_add_f32_e32 v119, 1.0, v119
	v_add_f32_e32 v114, 1.0, v114
	v_add_f32_e32 v115, 1.0, v115
	v_add_f32_e32 v171, 1.0, v171
	v_add_f32_e32 v172, 1.0, v172
	v_add_f32_e32 v173, 1.0, v173
	v_rcp_f32_e32 v118, v118
	v_rcp_f32_e32 v119, v119
	v_rcp_f32_e32 v114, v114
	v_rcp_f32_e32 v115, v115
	v_add_f32_e32 v116, 1.0, v116
	s_waitcnt vmcnt(0)
	v_cvt_f32_f16_e32 v222, v177
	v_cvt_f32_f16_sdwa v223, v177 dst_sel:DWORD dst_unused:UNUSED_PAD src0_sel:WORD_1
	v_add_f32_e32 v117, 1.0, v117
	v_lshlrev_b32_e32 v220, 16, v180
	v_cvt_f32_f16_e32 v190, v182
	v_cvt_f32_f16_sdwa v191, v182 dst_sel:DWORD dst_unused:UNUSED_PAD src0_sel:WORD_1
	v_cvt_f32_f16_e32 v182, v183
	v_cvt_f32_f16_sdwa v183, v183 dst_sel:DWORD dst_unused:UNUSED_PAD src0_sel:WORD_1
	v_and_b32_e32 v221, 0xffff0000, v180
	v_lshlrev_b32_e32 v180, 16, v181
	v_and_b32_e32 v181, 0xffff0000, v181
	v_pk_fma_f32 v[180:181], v[212:213], v[180:181], v[222:223]
	v_lshlrev_b32_e32 v212, 16, v186
	v_and_b32_e32 v213, 0xffff0000, v186
	v_lshlrev_b32_e32 v186, 16, v187
	v_and_b32_e32 v187, 0xffff0000, v187
	v_pk_fma_f32 v[120:121], v[120:121], v[186:187], v[182:183]
	v_cvt_f32_f16_e32 v182, v184
	v_cvt_f32_f16_sdwa v183, v184 dst_sel:DWORD dst_unused:UNUSED_PAD src0_sel:WORD_1
	v_add_f32_e32 v161, 1.0, v161
	v_add_f32_e32 v170, 1.0, v170
	v_rcp_f32_e32 v208, v171
	v_rcp_f32_e32 v209, v172
	v_rcp_f32_e32 v210, v173
	v_cvt_f32_f16_e32 v214, v174
	v_cvt_f32_f16_sdwa v215, v174 dst_sel:DWORD dst_unused:UNUSED_PAD src0_sel:WORD_1
	v_cvt_f32_f16_e32 v174, v175
	v_cvt_f32_f16_sdwa v175, v175 dst_sel:DWORD dst_unused:UNUSED_PAD src0_sel:WORD_1
	v_cvt_f32_f16_e32 v218, v176
	v_cvt_f32_f16_sdwa v219, v176 dst_sel:DWORD dst_unused:UNUSED_PAD src0_sel:WORD_1
	v_rcp_f32_e32 v116, v116
	v_rcp_f32_e32 v117, v117
	v_cvt_f32_f16_e32 v184, v185
	v_cvt_f32_f16_sdwa v185, v185 dst_sel:DWORD dst_unused:UNUSED_PAD src0_sel:WORD_1
	v_rcp_f32_e32 v206, v161
	v_rcp_f32_e32 v207, v170
	v_lshlrev_b32_e32 v186, 16, v188
	v_and_b32_e32 v187, 0xffff0000, v188
	v_lshlrev_b32_e32 v216, 16, v178
	v_and_b32_e32 v217, 0xffff0000, v178
	v_lshlrev_b32_e32 v178, 16, v179
	v_and_b32_e32 v179, 0xffff0000, v179
;     __device__ __forceinline__ void operator()(const f32x4 (&acc)[2][2][4][2], const Unit& u, int wr, int wc, int fr, int fq) const {
;         { int z_ = 0; asm volatile("" : "+v"(z_)); const int l_ = (int)__builtin_amdgcn_mbcnt_hi(~0u, __builtin_amdgcn_mbcnt_lo(~0u, (unsigned)z_)); fr = l_ & 15; fq = l_ >> 4; }
;         const int row0 = u.pm * BM + wr * 64 + fr, col0 = u.pn * BM + wc * 32 + 8 * fq, lane = fq * 16 + fr;
; #pragma unroll
;         for (int ai = 0; ai < 2; ++ai)
; #pragma unroll
;             for (int mp = 0; mp < 2; ++mp) {
;                 u32x4 bsv[2][2], tv[2][2];
; #pragma unroll
;                 for (int mm = 0; mm < 2; ++mm)
; #pragma unroll
;                     for (int bj = 0; bj < 2; ++bj) { const size_t o = (size_t)(row0 + ai * HALF + (2 * mp + mm) * 16) * ldc + col0 + bj * HALF; bsv[mm][bj] = *(const u32x4*)(base + o); tv[mm][bj] = *(const u32x4*)(PP + o); }
; #pragma unroll
;                 for (int mm = 0; mm < 2; ++mm) { const int m = 2 * mp + mm; const size_t r = (size_t)(row0 + ai * HALF + m * 16), off = r * ldc + col0; float ss = 0.f;
;                     const float rs = tbl[wr * 64 + fr + ai * HALF + m * 16];
; #pragma unroll
;                     for (int bj = 0; bj < 2; ++bj) { const u32x4 t = tv[mm][bj], b = bsv[mm][bj]; const f32x4 a0 = acc[ai][bj][m][0] * rs, a1 = acc[ai][bj][m][1] * rs;
;                         f32x4 v0, v1; v0[0] = f16_lo(b.x) + bf_lo(t.x) * sigm(a0[0]); v0[1] = f16_hi(b.x) + bf_hi(t.x) * sigm(a0[1]); v0[2] = f16_lo(b.y) + bf_lo(t.y) * sigm(a0[2]); v0[3] = f16_hi(b.y) + bf_hi(t.y) * sigm(a0[3]);
;                         v1[0] = f16_lo(b.z) + bf_lo(t.z) * sigm(a1[0]); v1[1] = f16_hi(b.z) + bf_hi(t.z) * sigm(a1[1]); v1[2] = f16_lo(b.w) + bf_lo(t.w) * sigm(a1[2]); v1[3] = f16_hi(b.w) + bf_hi(t.w) * sigm(a1[3]);
;                         u32x4 w; w.x = pk_f16(v0[0], v0[1]); w.y = pk_f16(v0[2], v0[3]); w.z = pk_f16(v1[0], v1[1]); w.w = pk_f16(v1[2], v1[3]); *(u32x4*)(out + off + bj * HALF) = w;
;                         ss += ((v0[0] * v0[0] + v0[1] * v0[1]) + (v0[2] * v0[2] + v0[3] * v0[3])) + ((v1[0] * v1[0] + v1[1] * v1[1]) + (v1[2] * v1[2] + v1[3] * v1[3])); }
;                     ss = xor_add(ss, lane, 16); ss = xor_add(ss, lane, 32);
;                     if (fq == 0) ssp[r * 16 + (u.pn & 3) * 4 + wc] = ss; }
;                 asm volatile("" ::: "memory");
;             }
;     }
	v_pk_fma_f32 v[118:119], v[118:119], v[212:213], v[190:191]
	v_pk_fma_f32 v[182:183], v[114:115], v[186:187], v[182:183]
	v_lshlrev_b32_e32 v114, 16, v189
	v_and_b32_e32 v115, 0xffff0000, v189
	v_pk_fma_f32 v[178:179], v[208:209], v[178:179], v[174:175]
	v_pk_fma_f32 v[208:209], v[210:211], v[220:221], v[218:219]
	v_pk_fma_f32 v[184:185], v[116:117], v[114:115], v[184:185]
	v_pk_mul_f32 v[114:115], v[118:119], v[118:119]
	v_pk_mul_f32 v[116:117], v[120:121], v[120:121]
	v_pk_fma_f32 v[206:207], v[206:207], v[216:217], v[214:215]
	v_cvt_pk_f16_f32 v176, v208, v209
	v_cvt_pk_f16_f32 v177, v180, v181
	v_pk_mul_f32 v[208:209], v[208:209], v[208:209]
	v_pk_mul_f32 v[180:181], v[180:181], v[180:181]
	v_add_f32_e32 v116, v116, v117
	v_add_f32_e32 v114, v114, v115
	v_cvt_pk_f16_f32 v174, v206, v207
	v_cvt_pk_f16_f32 v175, v178, v179
	v_pk_mul_f32 v[206:207], v[206:207], v[206:207]
	v_pk_mul_f32 v[178:179], v[178:179], v[178:179]
	v_pk_mul_f32 v[186:187], v[182:183], v[182:183]
	v_pk_mul_f32 v[188:189], v[184:185], v[184:185]
	v_add_f32_e32 v114, v114, v116
	v_add_f32_e32 v115, v180, v181
	v_add_f32_e32 v116, v208, v209
	v_add_f32_e32 v161, v188, v189
	v_add_f32_e32 v170, v186, v187
	v_add_f32_e32 v115, v116, v115
	v_add_f32_e32 v116, v178, v179
	v_add_f32_e32 v117, v206, v207
	v_add_f32_e32 v161, v170, v161
	v_add_f32_e32 v116, v117, v116
	v_add_f32_e32 v114, v114, v161
	v_add_f32_e32 v115, v116, v115
	v_add_f32_e32 v117, v115, v114
	ds_bpermute_b32 v161, v159, v117
	v_lshlrev_b64 v[210:211], 11, v[150:151]
	v_lshl_add_u64 v[114:115], s[56:57], 0, v[210:211]
	v_lshl_add_u64 v[178:179], v[148:149], 1, v[114:115]
	s_lshl_b32 s0, s18, 2
	s_waitcnt lgkmcnt(0)
	v_add_f32_e32 v114, v117, v161
	ds_bpermute_b32 v115, v158, v114
	s_and_b32 s11, s0, 12
	v_cvt_pk_f16_f32 v116, v118, v119
	v_cvt_pk_f16_f32 v117, v120, v121
	v_cvt_pk_f16_f32 v118, v182, v183
	v_cvt_pk_f16_f32 v119, v184, v185
	global_store_dwordx4 v[178:179], v[174:177], off
	global_store_dwordx4 v[178:179], v[116:119], off offset:256
	s_and_saveexec_b64 s[0:1], vcc
	s_cbranch_execz .LBB0_1285
	v_lshlrev_b64 v[116:117], 6, v[150:151]
	v_lshl_add_u64 v[116:117], s[6:7], 0, v[116:117]
	s_lshl_b32 s62, s11, 2
	v_lshl_add_u64 v[116:117], v[116:117], 0, s[62:63]
	s_lshl_b32 s62, s35, 2
	v_lshl_add_u64 v[116:117], v[116:117], 0, s[62:63]
	s_waitcnt lgkmcnt(0)
	v_add_f32_e32 v114, v114, v115
	global_store_dword v[116:117], v114, off
.LBB0_1285:
	s_or_b64 exec, exec, s[0:1]
	ds_read_b32 v114, v160 offset:64
	v_lshlrev_b32_e32 v120, 16, v131
	v_and_b32_e32 v121, 0xffff0000, v131
	v_and_b32_e32 v131, 0xffff0000, v133
	s_waitcnt lgkmcnt(0)
	v_pk_mul_f32 v[106:107], v[106:107], v[114:115] op_sel_hi:[1,0]
	s_nop 0
	v_mul_f32_e32 v106, 0xbfb8aa3b, v106
	v_exp_f32_e32 v106, v106
	v_mul_f32_e32 v107, 0xbfb8aa3b, v107
	v_exp_f32_e32 v107, v107
	v_pk_mul_f32 v[110:111], v[110:111], v[114:115] op_sel_hi:[1,0]
	v_pk_mul_f32 v[108:109], v[108:109], v[114:115] op_sel_hi:[1,0]
	v_add_f32_e32 v106, 1.0, v106
	v_mul_f32_e32 v110, 0xbfb8aa3b, v110
	v_mul_f32_e32 v111, 0xbfb8aa3b, v111
	v_rcp_f32_e32 v116, v106
	v_add_f32_e32 v106, 1.0, v107
	v_mul_f32_e32 v107, 0xbfb8aa3b, v108
	v_exp_f32_e32 v110, v110
	v_exp_f32_e32 v111, v111
	v_exp_f32_e32 v107, v107
	v_pk_mul_f32 v[112:113], v[112:113], v[114:115] op_sel_hi:[1,0]
	v_mul_f32_e32 v108, 0xbfb8aa3b, v109
	v_mul_f32_e32 v112, 0xbfb8aa3b, v112
	v_mul_f32_e32 v113, 0xbfb8aa3b, v113
	v_exp_f32_e32 v108, v108
	v_add_f32_e32 v110, 1.0, v110
	v_add_f32_e32 v111, 1.0, v111
	v_exp_f32_e32 v112, v112
	v_exp_f32_e32 v113, v113
	v_rcp_f32_e32 v117, v106
	v_add_f32_e32 v106, 1.0, v107
	v_rcp_f32_e32 v110, v110
	v_rcp_f32_e32 v111, v111
	v_rcp_f32_e32 v118, v106
	v_cvt_f32_f16_sdwa v107, v134 dst_sel:DWORD dst_unused:UNUSED_PAD src0_sel:WORD_1
	v_cvt_f32_f16_e32 v106, v134
	v_add_f32_e32 v108, 1.0, v108
	v_add_f32_e32 v112, 1.0, v112
	v_add_f32_e32 v113, 1.0, v113
	v_rcp_f32_e32 v119, v108
	v_lshlrev_b32_e32 v108, 16, v130
	v_and_b32_e32 v109, 0xffff0000, v130
	v_rcp_f32_e32 v112, v112
	v_rcp_f32_e32 v113, v113
	v_pk_fma_f32 v[110:111], v[110:111], v[108:109], v[106:107]
	v_cvt_f32_f16_sdwa v109, v135 dst_sel:DWORD dst_unused:UNUSED_PAD src0_sel:WORD_1
	v_cvt_f32_f16_e32 v108, v135
	v_pk_mul_f32 v[102:103], v[102:103], v[114:115] op_sel_hi:[1,0]
	v_pk_mul_f32 v[104:105], v[104:105], v[114:115] op_sel_hi:[1,0]
	v_mul_f32_e32 v102, 0xbfb8aa3b, v102
	v_pk_fma_f32 v[112:113], v[112:113], v[120:121], v[108:109]
	v_cvt_f32_f16_sdwa v109, v136 dst_sel:DWORD dst_unused:UNUSED_PAD src0_sel:WORD_1
	v_cvt_f32_f16_e32 v108, v136
	v_mul_f32_e32 v103, 0xbfb8aa3b, v103
	v_exp_f32_e32 v102, v102
	v_exp_f32_e32 v103, v103
	v_mul_f32_e32 v104, 0xbfb8aa3b, v104
	v_mul_f32_e32 v105, 0xbfb8aa3b, v105
	v_lshlrev_b32_e32 v120, 16, v132
	v_and_b32_e32 v121, 0xffff0000, v132
	v_exp_f32_e32 v104, v104
	v_exp_f32_e32 v105, v105
	v_pk_fma_f32 v[116:117], v[116:117], v[120:121], v[108:109]
	v_cvt_f32_f16_sdwa v121, v137 dst_sel:DWORD dst_unused:UNUSED_PAD src0_sel:WORD_1
	v_cvt_f32_f16_e32 v120, v137
	v_pk_mul_f32 v[98:99], v[98:99], v[114:115] op_sel_hi:[1,0]
	v_pk_mul_f32 v[100:101], v[100:101], v[114:115] op_sel_hi:[1,0]
	v_add_f32_e32 v102, 1.0, v102
	v_add_f32_e32 v103, 1.0, v103
	v_mul_f32_e32 v98, 0xbfb8aa3b, v98
	v_mul_f32_e32 v99, 0xbfb8aa3b, v99
	v_lshlrev_b32_e32 v130, 16, v133
	v_rcp_f32_e32 v102, v102
	v_rcp_f32_e32 v103, v103
	v_add_f32_e32 v104, 1.0, v104
	v_add_f32_e32 v105, 1.0, v105
	v_exp_f32_e32 v98, v98
	v_exp_f32_e32 v99, v99
	v_mul_f32_e32 v100, 0xbfb8aa3b, v100
	v_mul_f32_e32 v101, 0xbfb8aa3b, v101
	v_cvt_f32_f16_sdwa v115, v126 dst_sel:DWORD dst_unused:UNUSED_PAD src0_sel:WORD_1
;     __device__ __forceinline__ void operator()(const f32x4 (&acc)[2][2][4][2], const Unit& u, int wr, int wc, int fr, int fq) const {
;         { int z_ = 0; asm volatile("" : "+v"(z_)); const int l_ = (int)__builtin_amdgcn_mbcnt_hi(~0u, __builtin_amdgcn_mbcnt_lo(~0u, (unsigned)z_)); fr = l_ & 15; fq = l_ >> 4; }
;         const int row0 = u.pm * BM + wr * 64 + fr, col0 = u.pn * BM + wc * 32 + 8 * fq, lane = fq * 16 + fr;
; #pragma unroll
;         for (int ai = 0; ai < 2; ++ai)
; #pragma unroll
;             for (int mp = 0; mp < 2; ++mp) {
;                 u32x4 bsv[2][2], tv[2][2];
; #pragma unroll
;                 for (int mm = 0; mm < 2; ++mm)
; #pragma unroll
;                     for (int bj = 0; bj < 2; ++bj) { const size_t o = (size_t)(row0 + ai * HALF + (2 * mp + mm) * 16) * ldc + col0 + bj * HALF; bsv[mm][bj] = *(const u32x4*)(base + o); tv[mm][bj] = *(const u32x4*)(PP + o); }
; #pragma unroll
;                 for (int mm = 0; mm < 2; ++mm) { const int m = 2 * mp + mm; const size_t r = (size_t)(row0 + ai * HALF + m * 16), off = r * ldc + col0; float ss = 0.f;
;                     const float rs = tbl[wr * 64 + fr + ai * HALF + m * 16];
; #pragma unroll
;                     for (int bj = 0; bj < 2; ++bj) { const u32x4 t = tv[mm][bj], b = bsv[mm][bj]; const f32x4 a0 = acc[ai][bj][m][0] * rs, a1 = acc[ai][bj][m][1] * rs;
;                         f32x4 v0, v1; v0[0] = f16_lo(b.x) + bf_lo(t.x) * sigm(a0[0]); v0[1] = f16_hi(b.x) + bf_hi(t.x) * sigm(a0[1]); v0[2] = f16_lo(b.y) + bf_lo(t.y) * sigm(a0[2]); v0[3] = f16_hi(b.y) + bf_hi(t.y) * sigm(a0[3]);
;                         v1[0] = f16_lo(b.z) + bf_lo(t.z) * sigm(a1[0]); v1[1] = f16_hi(b.z) + bf_hi(t.z) * sigm(a1[1]); v1[2] = f16_lo(b.w) + bf_lo(t.w) * sigm(a1[2]); v1[3] = f16_hi(b.w) + bf_hi(t.w) * sigm(a1[3]);
;                         u32x4 w; w.x = pk_f16(v0[0], v0[1]); w.y = pk_f16(v0[2], v0[3]); w.z = pk_f16(v1[0], v1[1]); w.w = pk_f16(v1[2], v1[3]); *(u32x4*)(out + off + bj * HALF) = w;
;                         ss += ((v0[0] * v0[0] + v0[1] * v0[1]) + (v0[2] * v0[2] + v0[3] * v0[3])) + ((v1[0] * v1[0] + v1[1] * v1[1]) + (v1[2] * v1[2] + v1[3] * v1[3])); }
;                     ss = xor_add(ss, lane, 16); ss = xor_add(ss, lane, 32);
;                     if (fq == 0) ssp[r * 16 + (u.pn & 3) * 4 + wc] = ss; }
;                 asm volatile("" ::: "memory");
;             }
;     }
	v_cvt_f32_f16_e32 v114, v126
	v_pk_fma_f32 v[118:119], v[118:119], v[130:131], v[120:121]
	v_rcp_f32_e32 v104, v104
	v_rcp_f32_e32 v105, v105
	v_exp_f32_e32 v100, v100
	v_exp_f32_e32 v101, v101
	v_cvt_f32_f16_sdwa v131, v127 dst_sel:DWORD dst_unused:UNUSED_PAD src0_sel:WORD_1
	v_cvt_f32_f16_e32 v130, v127
	v_lshlrev_b32_e32 v120, 16, v122
	v_and_b32_e32 v121, 0xffff0000, v122
	v_add_f32_e32 v98, 1.0, v98
	v_add_f32_e32 v99, 1.0, v99
	v_pk_fma_f32 v[102:103], v[102:103], v[120:121], v[114:115]
	v_lshlrev_b32_e32 v114, 16, v123
	v_and_b32_e32 v115, 0xffff0000, v123
	v_rcp_f32_e32 v98, v98
	v_rcp_f32_e32 v99, v99
	v_add_f32_e32 v100, 1.0, v100
	v_add_f32_e32 v101, 1.0, v101
	v_pk_fma_f32 v[104:105], v[104:105], v[114:115], v[130:131]
	v_cvt_f32_f16_sdwa v115, v128 dst_sel:DWORD dst_unused:UNUSED_PAD src0_sel:WORD_1
	v_cvt_f32_f16_e32 v114, v128
	v_rcp_f32_e32 v100, v100
	v_rcp_f32_e32 v101, v101
	v_cvt_f32_f16_sdwa v123, v129 dst_sel:DWORD dst_unused:UNUSED_PAD src0_sel:WORD_1
	v_cvt_f32_f16_e32 v122, v129
	v_lshlrev_b32_e32 v120, 16, v124
	v_and_b32_e32 v121, 0xffff0000, v124
	v_pk_fma_f32 v[114:115], v[98:99], v[120:121], v[114:115]
	v_lshlrev_b32_e32 v98, 16, v125
	v_and_b32_e32 v99, 0xffff0000, v125
	v_pk_fma_f32 v[120:121], v[100:101], v[98:99], v[122:123]
	v_pk_mul_f32 v[98:99], v[102:103], v[102:103]
	v_pk_mul_f32 v[100:101], v[104:105], v[104:105]
	v_cvt_pk_f16_f32 v108, v116, v117
	v_cvt_pk_f16_f32 v109, v118, v119
	v_pk_mul_f32 v[116:117], v[116:117], v[116:117]
	v_pk_mul_f32 v[118:119], v[118:119], v[118:119]
	v_add_f32_e32 v100, v100, v101
	v_add_f32_e32 v98, v98, v99
	v_cvt_pk_f16_f32 v106, v110, v111
	v_cvt_pk_f16_f32 v107, v112, v113
	v_pk_mul_f32 v[110:111], v[110:111], v[110:111]
	v_pk_mul_f32 v[112:113], v[112:113], v[112:113]
	v_pk_mul_f32 v[122:123], v[114:115], v[114:115]
	v_pk_mul_f32 v[124:125], v[120:121], v[120:121]
	v_add_f32_e32 v98, v98, v100
	v_add_f32_e32 v99, v118, v119
	v_add_f32_e32 v100, v116, v117
	v_add_f32_e32 v124, v124, v125
	v_add_f32_e32 v122, v122, v123
	v_add_f32_e32 v99, v100, v99
	v_add_f32_e32 v100, v112, v113
	v_add_f32_e32 v101, v110, v111
	v_add_f32_e32 v122, v122, v124
	v_add_f32_e32 v100, v101, v100
	v_add_f32_e32 v98, v98, v122
	v_add_f32_e32 v99, v100, v99
	v_add_f32_e32 v101, v99, v98
	ds_bpermute_b32 v112, v159, v101
	v_lshl_add_u64 v[98:99], v[154:155], 1, s[56:57]
	v_lshl_add_u64 v[110:111], v[148:149], 1, v[98:99]
	v_cvt_pk_f16_f32 v100, v102, v103
	v_cvt_pk_f16_f32 v102, v114, v115
	s_waitcnt lgkmcnt(0)
	v_add_f32_e32 v98, v101, v112
	ds_bpermute_b32 v99, v158, v98
	v_cvt_pk_f16_f32 v101, v104, v105
	v_cvt_pk_f16_f32 v103, v120, v121
	global_store_dwordx4 v[110:111], v[106:109], off
	global_store_dwordx4 v[110:111], v[100:103], off offset:256
	s_and_saveexec_b64 s[0:1], vcc
	s_cbranch_execz .LBB0_1287
	v_lshlrev_b64 v[100:101], 6, v[152:153]
	v_lshl_add_u64 v[100:101], s[6:7], 0, v[100:101]
	s_lshl_b32 s62, s11, 2
	v_lshl_add_u64 v[100:101], v[100:101], 0, s[62:63]
	s_lshl_b32 s62, s35, 2
	v_lshl_add_u64 v[100:101], v[100:101], 0, s[62:63]
	s_waitcnt lgkmcnt(0)
	v_add_f32_e32 v98, v98, v99
	global_store_dword v[100:101], v98, off
.LBB0_1287:
	s_or_b64 exec, exec, s[0:1]
	v_or_b32_e32 v126, 32, v150
	v_ashrrev_i32_e32 v127, 31, v126
	s_waitcnt lgkmcnt(0)
	v_lshlrev_b64 v[98:99], 10, v[126:127]
	v_lshl_add_u64 v[98:99], v[98:99], 0, v[148:149]
	v_lshlrev_b64 v[98:99], 1, v[98:99]
	v_lshl_add_u64 v[100:101], s[72:73], 0, v[98:99]
	global_load_dwordx4 v[132:135], v[100:101], off
	v_lshl_add_u64 v[98:99], s[70:71], 0, v[98:99]
	global_load_dwordx4 v[152:155], v[98:99], off
	global_load_dwordx4 v[118:121], v[100:101], off offset:256
	global_load_dwordx4 v[114:117], v[98:99], off offset:256
	v_or_b32_e32 v122, 48, v150
	v_ashrrev_i32_e32 v123, 31, v122
	v_lshlrev_b64 v[124:125], 10, v[122:123]
	v_lshl_add_u64 v[98:99], v[124:125], 0, v[148:149]
	v_lshlrev_b64 v[98:99], 1, v[98:99]
	v_lshl_add_u64 v[100:101], s[72:73], 0, v[98:99]
	v_lshl_add_u64 v[98:99], s[70:71], 0, v[98:99]
	global_load_dwordx4 v[110:113], v[100:101], off
	global_load_dwordx4 v[106:109], v[98:99], off
	global_load_dwordx4 v[102:105], v[100:101], off offset:256
	s_nop 0
	global_load_dwordx4 v[98:101], v[98:99], off offset:256
	ds_read_b32 v130, v160 offset:128
	s_waitcnt lgkmcnt(0)
	v_pk_mul_f32 v[90:91], v[90:91], v[130:131] op_sel_hi:[1,0]
	s_nop 0
	v_mul_f32_e32 v90, 0xbfb8aa3b, v90
	v_exp_f32_e32 v90, v90
	v_pk_mul_f32 v[92:93], v[92:93], v[130:131] op_sel_hi:[1,0]
	v_pk_mul_f32 v[94:95], v[94:95], v[130:131] op_sel_hi:[1,0]
	v_pk_mul_f32 v[96:97], v[96:97], v[130:131] op_sel_hi:[1,0]
	v_add_f32_e32 v90, 1.0, v90
	v_rcp_f32_e32 v128, v90
	v_mul_f32_e32 v90, 0xbfb8aa3b, v91
	v_exp_f32_e32 v90, v90
	v_mul_f32_e32 v94, 0xbfb8aa3b, v94
	v_mul_f32_e32 v95, 0xbfb8aa3b, v95
	v_exp_f32_e32 v94, v94
	v_add_f32_e32 v90, 1.0, v90
	v_rcp_f32_e32 v129, v90
	v_mul_f32_e32 v90, 0xbfb8aa3b, v92
	v_exp_f32_e32 v90, v90
	v_exp_f32_e32 v95, v95
	v_mul_f32_e32 v96, 0xbfb8aa3b, v96
	v_mul_f32_e32 v97, 0xbfb8aa3b, v97
	v_add_f32_e32 v90, 1.0, v90
	v_rcp_f32_e32 v136, v90
	v_mul_f32_e32 v90, 0xbfb8aa3b, v93
	v_exp_f32_e32 v90, v90
	v_add_f32_e32 v94, 1.0, v94
	v_add_f32_e32 v95, 1.0, v95
	v_exp_f32_e32 v96, v96
	v_exp_f32_e32 v97, v97
	v_add_f32_e32 v90, 1.0, v90
	v_rcp_f32_e32 v94, v94
	v_rcp_f32_e32 v95, v95
	v_rcp_f32_e32 v137, v90
	v_pk_mul_f32 v[82:83], v[82:83], v[130:131] op_sel_hi:[1,0]
	v_add_f32_e32 v96, 1.0, v96
	v_mul_f32_e32 v82, 0xbfb8aa3b, v82
	v_exp_f32_e32 v82, v82
	v_add_f32_e32 v97, 1.0, v97
	v_rcp_f32_e32 v96, v96
	v_rcp_f32_e32 v97, v97
	v_add_f32_e32 v82, 1.0, v82
	v_pk_mul_f32 v[88:89], v[88:89], v[130:131] op_sel_hi:[1,0]
	v_pk_mul_f32 v[86:87], v[86:87], v[130:131] op_sel_hi:[1,0]
	v_pk_mul_f32 v[84:85], v[84:85], v[130:131] op_sel_hi:[1,0]
	v_rcp_f32_e32 v130, v82
	v_mul_f32_e32 v82, 0xbfb8aa3b, v83
	v_exp_f32_e32 v82, v82
	v_mul_f32_e32 v86, 0xbfb8aa3b, v86
	v_mul_f32_e32 v87, 0xbfb8aa3b, v87
	v_exp_f32_e32 v86, v86
	v_add_f32_e32 v82, 1.0, v82
	v_rcp_f32_e32 v131, v82
	v_mul_f32_e32 v82, 0xbfb8aa3b, v84
	v_exp_f32_e32 v82, v82
	v_exp_f32_e32 v87, v87
	v_mul_f32_e32 v88, 0xbfb8aa3b, v88
	v_mul_f32_e32 v89, 0xbfb8aa3b, v89
	v_add_f32_e32 v82, 1.0, v82
	v_add_f32_e32 v86, 1.0, v86
	v_add_f32_e32 v87, 1.0, v87
	v_exp_f32_e32 v88, v88
	v_exp_f32_e32 v89, v89
	v_rcp_f32_e32 v86, v86
	v_rcp_f32_e32 v87, v87
	s_waitcnt vmcnt(0)
;     __device__ __forceinline__ void operator()(const f32x4 (&acc)[2][2][4][2], const Unit& u, int wr, int wc, int fr, int fq) const {
;         { int z_ = 0; asm volatile("" : "+v"(z_)); const int l_ = (int)__builtin_amdgcn_mbcnt_hi(~0u, __builtin_amdgcn_mbcnt_lo(~0u, (unsigned)z_)); fr = l_ & 15; fq = l_ >> 4; }
;         const int row0 = u.pm * BM + wr * 64 + fr, col0 = u.pn * BM + wc * 32 + 8 * fq, lane = fq * 16 + fr;
; #pragma unroll
;         for (int ai = 0; ai < 2; ++ai)
; #pragma unroll
;             for (int mp = 0; mp < 2; ++mp) {
;                 u32x4 bsv[2][2], tv[2][2];
; #pragma unroll
;                 for (int mm = 0; mm < 2; ++mm)
; #pragma unroll
;                     for (int bj = 0; bj < 2; ++bj) { const size_t o = (size_t)(row0 + ai * HALF + (2 * mp + mm) * 16) * ldc + col0 + bj * HALF; bsv[mm][bj] = *(const u32x4*)(base + o); tv[mm][bj] = *(const u32x4*)(PP + o); }
; #pragma unroll
;                 for (int mm = 0; mm < 2; ++mm) { const int m = 2 * mp + mm; const size_t r = (size_t)(row0 + ai * HALF + m * 16), off = r * ldc + col0; float ss = 0.f;
;                     const float rs = tbl[wr * 64 + fr + ai * HALF + m * 16];
; #pragma unroll
;                     for (int bj = 0; bj < 2; ++bj) { const u32x4 t = tv[mm][bj], b = bsv[mm][bj]; const f32x4 a0 = acc[ai][bj][m][0] * rs, a1 = acc[ai][bj][m][1] * rs;
;                         f32x4 v0, v1; v0[0] = f16_lo(b.x) + bf_lo(t.x) * sigm(a0[0]); v0[1] = f16_hi(b.x) + bf_hi(t.x) * sigm(a0[1]); v0[2] = f16_lo(b.y) + bf_lo(t.y) * sigm(a0[2]); v0[3] = f16_hi(b.y) + bf_hi(t.y) * sigm(a0[3]);
;                         v1[0] = f16_lo(b.z) + bf_lo(t.z) * sigm(a1[0]); v1[1] = f16_hi(b.z) + bf_hi(t.z) * sigm(a1[1]); v1[2] = f16_lo(b.w) + bf_lo(t.w) * sigm(a1[2]); v1[3] = f16_hi(b.w) + bf_hi(t.w) * sigm(a1[3]);
;                         u32x4 w; w.x = pk_f16(v0[0], v0[1]); w.y = pk_f16(v0[2], v0[3]); w.z = pk_f16(v1[0], v1[1]); w.w = pk_f16(v1[2], v1[3]); *(u32x4*)(out + off + bj * HALF) = w;
;                         ss += ((v0[0] * v0[0] + v0[1] * v0[1]) + (v0[2] * v0[2] + v0[3] * v0[3])) + ((v1[0] * v1[0] + v1[1] * v1[1]) + (v1[2] * v1[2] + v1[3] * v1[3])); }
;                     ss = xor_add(ss, lane, 16); ss = xor_add(ss, lane, 32);
;                     if (fq == 0) ssp[r * 16 + (u.pn & 3) * 4 + wc] = ss; }
;                 asm volatile("" ::: "memory");
;             }
;     }
	v_cvt_f32_f16_e32 v90, v132
	v_cvt_f32_f16_sdwa v91, v132 dst_sel:DWORD dst_unused:UNUSED_PAD src0_sel:WORD_1
	v_lshlrev_b32_e32 v92, 16, v152
	v_and_b32_e32 v93, 0xffff0000, v152
	v_lshlrev_b32_e32 v132, 16, v153
	v_pk_fma_f32 v[94:95], v[94:95], v[92:93], v[90:91]
	v_cvt_f32_f16_e32 v92, v133
	v_cvt_f32_f16_sdwa v93, v133 dst_sel:DWORD dst_unused:UNUSED_PAD src0_sel:WORD_1
	v_and_b32_e32 v133, 0xffff0000, v153
	v_cvt_pk_f16_f32 v90, v94, v95
	v_cvt_f32_f16_sdwa v83, v118 dst_sel:DWORD dst_unused:UNUSED_PAD src0_sel:WORD_1
	v_pk_fma_f32 v[96:97], v[96:97], v[132:133], v[92:93]
	v_cvt_f32_f16_e32 v92, v134
	v_cvt_f32_f16_sdwa v93, v134 dst_sel:DWORD dst_unused:UNUSED_PAD src0_sel:WORD_1
	v_lshlrev_b32_e32 v132, 16, v154
	v_and_b32_e32 v133, 0xffff0000, v154
	v_lshlrev_b32_e32 v134, 16, v155
	v_pk_fma_f32 v[132:133], v[128:129], v[132:133], v[92:93]
	v_cvt_f32_f16_e32 v128, v135
	v_cvt_f32_f16_sdwa v129, v135 dst_sel:DWORD dst_unused:UNUSED_PAD src0_sel:WORD_1
	v_and_b32_e32 v135, 0xffff0000, v155
	v_cvt_pk_f16_f32 v91, v96, v97
	v_cvt_pk_f16_f32 v92, v132, v133
	v_pk_fma_f32 v[134:135], v[136:137], v[134:135], v[128:129]
	v_lshlrev_b64 v[128:129], 11, v[126:127]
	v_lshl_add_u64 v[128:129], s[56:57], 0, v[128:129]
	v_cvt_pk_f16_f32 v93, v134, v135
	v_lshl_add_u64 v[128:129], v[148:149], 1, v[128:129]
	global_store_dwordx4 v[128:129], v[90:93], off
	v_add_f32_e32 v88, 1.0, v88
	v_add_f32_e32 v89, 1.0, v89
	v_pk_mul_f32 v[90:91], v[94:95], v[94:95]
	v_pk_mul_f32 v[94:95], v[132:133], v[132:133]
	v_rcp_f32_e32 v132, v82
	v_mul_f32_e32 v82, 0xbfb8aa3b, v85
	v_exp_f32_e32 v82, v82
	v_lshlrev_b32_e32 v84, 16, v114
	v_and_b32_e32 v85, 0xffff0000, v114
	v_rcp_f32_e32 v88, v88
	v_add_f32_e32 v82, 1.0, v82
	v_rcp_f32_e32 v133, v82
	v_cvt_f32_f16_e32 v82, v118
	v_rcp_f32_e32 v89, v89
	v_lshlrev_b32_e32 v114, 16, v115
	v_and_b32_e32 v115, 0xffff0000, v115
	v_pk_fma_f32 v[86:87], v[86:87], v[84:85], v[82:83]
	v_cvt_f32_f16_e32 v84, v119
	v_cvt_f32_f16_sdwa v85, v119 dst_sel:DWORD dst_unused:UNUSED_PAD src0_sel:WORD_1
	v_cvt_f32_f16_e32 v118, v121
	v_cvt_f32_f16_sdwa v119, v121 dst_sel:DWORD dst_unused:UNUSED_PAD src0_sel:WORD_1
	v_cvt_pk_f16_f32 v82, v86, v87
	v_pk_fma_f32 v[88:89], v[88:89], v[114:115], v[84:85]
	v_cvt_f32_f16_e32 v84, v120
	v_cvt_f32_f16_sdwa v85, v120 dst_sel:DWORD dst_unused:UNUSED_PAD src0_sel:WORD_1
	v_lshlrev_b32_e32 v114, 16, v116
	v_and_b32_e32 v115, 0xffff0000, v116
	v_lshlrev_b32_e32 v116, 16, v117
	v_and_b32_e32 v117, 0xffff0000, v117
	v_pk_fma_f32 v[114:115], v[130:131], v[114:115], v[84:85]
	v_pk_fma_f32 v[116:117], v[132:133], v[116:117], v[118:119]
	v_cvt_pk_f16_f32 v83, v88, v89
	v_cvt_pk_f16_f32 v84, v114, v115
	v_cvt_pk_f16_f32 v85, v116, v117
	global_store_dwordx4 v[128:129], v[82:85], off offset:256
	v_pk_mul_f32 v[92:93], v[96:97], v[96:97]
	v_pk_mul_f32 v[96:97], v[134:135], v[134:135]
	v_pk_mul_f32 v[82:83], v[86:87], v[86:87]
	v_pk_mul_f32 v[84:85], v[88:89], v[88:89]
	v_add_f32_e32 v82, v82, v83
	v_add_f32_e32 v84, v84, v85
	v_pk_mul_f32 v[86:87], v[114:115], v[114:115]
	v_pk_mul_f32 v[88:89], v[116:117], v[116:117]
	v_add_f32_e32 v82, v82, v84
	v_add_f32_e32 v83, v96, v97
	v_add_f32_e32 v84, v94, v95
	v_add_f32_e32 v88, v88, v89
	v_add_f32_e32 v86, v86, v87
	v_add_f32_e32 v83, v84, v83
	v_add_f32_e32 v84, v92, v93
	v_add_f32_e32 v85, v90, v91
	v_add_f32_e32 v86, v86, v88
	v_add_f32_e32 v84, v85, v84
	v_add_f32_e32 v82, v82, v86
	v_add_f32_e32 v83, v84, v83
	v_add_f32_e32 v82, v83, v82
	ds_bpermute_b32 v83, v159, v82
	s_waitcnt lgkmcnt(0)
	v_add_f32_e32 v82, v82, v83
	ds_bpermute_b32 v83, v158, v82
	s_and_saveexec_b64 s[0:1], vcc
	s_cbranch_execz .LBB0_1289
	v_lshlrev_b64 v[84:85], 6, v[126:127]
	v_lshl_add_u64 v[84:85], s[6:7], 0, v[84:85]
	s_lshl_b32 s62, s11, 2
	v_lshl_add_u64 v[84:85], v[84:85], 0, s[62:63]
	s_lshl_b32 s62, s35, 2
	v_lshl_add_u64 v[84:85], v[84:85], 0, s[62:63]
	s_waitcnt lgkmcnt(0)
	v_add_f32_e32 v82, v82, v83
	global_store_dword v[84:85], v82, off
.LBB0_1289:
	s_or_b64 exec, exec, s[0:1]
	ds_read_b32 v82, v160 offset:192
	v_lshlrev_b32_e32 v88, 16, v107
	v_and_b32_e32 v89, 0xffff0000, v107
	v_lshlrev_b32_e32 v90, 16, v109
	v_and_b32_e32 v91, 0xffff0000, v109
	s_waitcnt lgkmcnt(0)
	v_pk_mul_f32 v[72:73], v[72:73], v[82:83] op_sel_hi:[1,0]
	v_pk_mul_f32 v[76:77], v[76:77], v[82:83] op_sel_hi:[1,0]
	v_mul_f32_e32 v72, 0xbfb8aa3b, v72
	v_exp_f32_e32 v72, v72
	v_mul_f32_e32 v73, 0xbfb8aa3b, v73
	v_exp_f32_e32 v73, v73
	v_pk_mul_f32 v[74:75], v[74:75], v[82:83] op_sel_hi:[1,0]
	v_add_f32_e32 v72, 1.0, v72
	v_mul_f32_e32 v76, 0xbfb8aa3b, v76
	v_mul_f32_e32 v77, 0xbfb8aa3b, v77
	v_rcp_f32_e32 v84, v72
	v_add_f32_e32 v72, 1.0, v73
	v_mul_f32_e32 v73, 0xbfb8aa3b, v74
	v_exp_f32_e32 v76, v76
	v_exp_f32_e32 v77, v77
	v_exp_f32_e32 v73, v73
	v_pk_mul_f32 v[78:79], v[78:79], v[82:83] op_sel_hi:[1,0]
	v_mul_f32_e32 v74, 0xbfb8aa3b, v75
	v_mul_f32_e32 v78, 0xbfb8aa3b, v78
	v_mul_f32_e32 v79, 0xbfb8aa3b, v79
	v_exp_f32_e32 v74, v74
	v_add_f32_e32 v76, 1.0, v76
	v_add_f32_e32 v77, 1.0, v77
	v_exp_f32_e32 v78, v78
	v_exp_f32_e32 v79, v79
	v_rcp_f32_e32 v85, v72
	v_add_f32_e32 v72, 1.0, v73
	v_rcp_f32_e32 v76, v76
	v_rcp_f32_e32 v77, v77
	v_rcp_f32_e32 v86, v72
	v_cvt_f32_f16_sdwa v73, v110 dst_sel:DWORD dst_unused:UNUSED_PAD src0_sel:WORD_1
	v_cvt_f32_f16_e32 v72, v110
	v_add_f32_e32 v74, 1.0, v74
	v_add_f32_e32 v78, 1.0, v78
	v_add_f32_e32 v79, 1.0, v79
	v_rcp_f32_e32 v87, v74
	v_lshlrev_b32_e32 v74, 16, v106
	v_and_b32_e32 v75, 0xffff0000, v106
	v_rcp_f32_e32 v78, v78
	v_rcp_f32_e32 v79, v79
	v_pk_fma_f32 v[76:77], v[76:77], v[74:75], v[72:73]
	v_cvt_f32_f16_sdwa v75, v111 dst_sel:DWORD dst_unused:UNUSED_PAD src0_sel:WORD_1
;     __device__ __forceinline__ void operator()(const f32x4 (&acc)[2][2][4][2], const Unit& u, int wr, int wc, int fr, int fq) const {
;         { int z_ = 0; asm volatile("" : "+v"(z_)); const int l_ = (int)__builtin_amdgcn_mbcnt_hi(~0u, __builtin_amdgcn_mbcnt_lo(~0u, (unsigned)z_)); fr = l_ & 15; fq = l_ >> 4; }
;         const int row0 = u.pm * BM + wr * 64 + fr, col0 = u.pn * BM + wc * 32 + 8 * fq, lane = fq * 16 + fr;
; #pragma unroll
;         for (int ai = 0; ai < 2; ++ai)
; #pragma unroll
;             for (int mp = 0; mp < 2; ++mp) {
;                 u32x4 bsv[2][2], tv[2][2];
; #pragma unroll
;                 for (int mm = 0; mm < 2; ++mm)
; #pragma unroll
;                     for (int bj = 0; bj < 2; ++bj) { const size_t o = (size_t)(row0 + ai * HALF + (2 * mp + mm) * 16) * ldc + col0 + bj * HALF; bsv[mm][bj] = *(const u32x4*)(base + o); tv[mm][bj] = *(const u32x4*)(PP + o); }
; #pragma unroll
;                 for (int mm = 0; mm < 2; ++mm) { const int m = 2 * mp + mm; const size_t r = (size_t)(row0 + ai * HALF + m * 16), off = r * ldc + col0; float ss = 0.f;
;                     const float rs = tbl[wr * 64 + fr + ai * HALF + m * 16];
; #pragma unroll
;                     for (int bj = 0; bj < 2; ++bj) { const u32x4 t = tv[mm][bj], b = bsv[mm][bj]; const f32x4 a0 = acc[ai][bj][m][0] * rs, a1 = acc[ai][bj][m][1] * rs;
;                         f32x4 v0, v1; v0[0] = f16_lo(b.x) + bf_lo(t.x) * sigm(a0[0]); v0[1] = f16_hi(b.x) + bf_hi(t.x) * sigm(a0[1]); v0[2] = f16_lo(b.y) + bf_lo(t.y) * sigm(a0[2]); v0[3] = f16_hi(b.y) + bf_hi(t.y) * sigm(a0[3]);
;                         v1[0] = f16_lo(b.z) + bf_lo(t.z) * sigm(a1[0]); v1[1] = f16_hi(b.z) + bf_hi(t.z) * sigm(a1[1]); v1[2] = f16_lo(b.w) + bf_lo(t.w) * sigm(a1[2]); v1[3] = f16_hi(b.w) + bf_hi(t.w) * sigm(a1[3]);
;                         u32x4 w; w.x = pk_f16(v0[0], v0[1]); w.y = pk_f16(v0[2], v0[3]); w.z = pk_f16(v1[0], v1[1]); w.w = pk_f16(v1[2], v1[3]); *(u32x4*)(out + off + bj * HALF) = w;
;                         ss += ((v0[0] * v0[0] + v0[1] * v0[1]) + (v0[2] * v0[2] + v0[3] * v0[3])) + ((v1[0] * v1[0] + v1[1] * v1[1]) + (v1[2] * v1[2] + v1[3] * v1[3])); }
;                     ss = xor_add(ss, lane, 16); ss = xor_add(ss, lane, 32);
;                     if (fq == 0) ssp[r * 16 + (u.pn & 3) * 4 + wc] = ss; }
;                 asm volatile("" ::: "memory");
;             }
;     }
	v_cvt_f32_f16_e32 v74, v111
	v_pk_mul_f32 v[68:69], v[68:69], v[82:83] op_sel_hi:[1,0]
	v_pk_mul_f32 v[70:71], v[70:71], v[82:83] op_sel_hi:[1,0]
	v_mul_f32_e32 v68, 0xbfb8aa3b, v68
	v_pk_fma_f32 v[78:79], v[78:79], v[88:89], v[74:75]
	v_cvt_f32_f16_sdwa v75, v112 dst_sel:DWORD dst_unused:UNUSED_PAD src0_sel:WORD_1
	v_cvt_f32_f16_e32 v74, v112
	v_mul_f32_e32 v69, 0xbfb8aa3b, v69
	v_exp_f32_e32 v68, v68
	v_exp_f32_e32 v69, v69
	v_mul_f32_e32 v70, 0xbfb8aa3b, v70
	v_mul_f32_e32 v71, 0xbfb8aa3b, v71
	v_lshlrev_b32_e32 v88, 16, v108
	v_and_b32_e32 v89, 0xffff0000, v108
	v_exp_f32_e32 v70, v70
	v_exp_f32_e32 v71, v71
	v_pk_fma_f32 v[84:85], v[84:85], v[88:89], v[74:75]
	v_cvt_f32_f16_sdwa v89, v113 dst_sel:DWORD dst_unused:UNUSED_PAD src0_sel:WORD_1
	v_cvt_f32_f16_e32 v88, v113
	v_pk_mul_f32 v[64:65], v[64:65], v[82:83] op_sel_hi:[1,0]
	v_pk_mul_f32 v[66:67], v[66:67], v[82:83] op_sel_hi:[1,0]
	v_add_f32_e32 v68, 1.0, v68
	v_add_f32_e32 v69, 1.0, v69
	v_mul_f32_e32 v64, 0xbfb8aa3b, v64
	v_mul_f32_e32 v65, 0xbfb8aa3b, v65
	v_rcp_f32_e32 v68, v68
	v_rcp_f32_e32 v69, v69
	v_add_f32_e32 v70, 1.0, v70
	v_add_f32_e32 v71, 1.0, v71
	v_exp_f32_e32 v64, v64
	v_exp_f32_e32 v65, v65
	v_mul_f32_e32 v66, 0xbfb8aa3b, v66
	v_mul_f32_e32 v67, 0xbfb8aa3b, v67
	v_cvt_f32_f16_sdwa v83, v102 dst_sel:DWORD dst_unused:UNUSED_PAD src0_sel:WORD_1
	v_cvt_f32_f16_e32 v82, v102
	v_pk_fma_f32 v[86:87], v[86:87], v[90:91], v[88:89]
	v_rcp_f32_e32 v70, v70
	v_rcp_f32_e32 v71, v71
	v_exp_f32_e32 v66, v66
	v_exp_f32_e32 v67, v67
	v_cvt_f32_f16_sdwa v91, v103 dst_sel:DWORD dst_unused:UNUSED_PAD src0_sel:WORD_1
	v_cvt_f32_f16_e32 v90, v103
	v_lshlrev_b32_e32 v88, 16, v98
	v_and_b32_e32 v89, 0xffff0000, v98
	v_add_f32_e32 v64, 1.0, v64
	v_add_f32_e32 v65, 1.0, v65
	v_pk_fma_f32 v[68:69], v[68:69], v[88:89], v[82:83]
	v_lshlrev_b32_e32 v82, 16, v99
	v_and_b32_e32 v83, 0xffff0000, v99
	v_rcp_f32_e32 v64, v64
	v_rcp_f32_e32 v65, v65
	v_add_f32_e32 v66, 1.0, v66
	v_add_f32_e32 v67, 1.0, v67
	v_pk_fma_f32 v[70:71], v[70:71], v[82:83], v[90:91]
	v_cvt_f32_f16_sdwa v83, v104 dst_sel:DWORD dst_unused:UNUSED_PAD src0_sel:WORD_1
	v_cvt_f32_f16_e32 v82, v104
	v_rcp_f32_e32 v66, v66
	v_rcp_f32_e32 v67, v67
	v_cvt_f32_f16_sdwa v91, v105 dst_sel:DWORD dst_unused:UNUSED_PAD src0_sel:WORD_1
	v_cvt_f32_f16_e32 v90, v105
	v_lshlrev_b32_e32 v88, 16, v100
	v_and_b32_e32 v89, 0xffff0000, v100
	v_pk_fma_f32 v[82:83], v[64:65], v[88:89], v[82:83]
	v_lshlrev_b32_e32 v64, 16, v101
	v_and_b32_e32 v65, 0xffff0000, v101
	v_pk_fma_f32 v[88:89], v[66:67], v[64:65], v[90:91]
	v_pk_mul_f32 v[64:65], v[68:69], v[68:69]
	v_pk_mul_f32 v[66:67], v[70:71], v[70:71]
	v_cvt_pk_f16_f32 v74, v84, v85
	v_cvt_pk_f16_f32 v75, v86, v87
	v_pk_mul_f32 v[84:85], v[84:85], v[84:85]
	v_pk_mul_f32 v[86:87], v[86:87], v[86:87]
	v_add_f32_e32 v66, v66, v67
	v_add_f32_e32 v64, v64, v65
	v_cvt_pk_f16_f32 v72, v76, v77
	v_cvt_pk_f16_f32 v73, v78, v79
	v_pk_mul_f32 v[76:77], v[76:77], v[76:77]
	v_pk_mul_f32 v[78:79], v[78:79], v[78:79]
	v_pk_mul_f32 v[90:91], v[82:83], v[82:83]
	v_pk_mul_f32 v[92:93], v[88:89], v[88:89]
	v_add_f32_e32 v64, v64, v66
	v_add_f32_e32 v65, v86, v87
	v_add_f32_e32 v66, v84, v85
	v_add_f32_e32 v92, v92, v93
	v_add_f32_e32 v90, v90, v91
	v_add_f32_e32 v65, v66, v65
	v_add_f32_e32 v66, v78, v79
	v_add_f32_e32 v67, v76, v77
	v_add_f32_e32 v90, v90, v92
	v_add_f32_e32 v66, v67, v66
	v_add_f32_e32 v64, v64, v90
	v_add_f32_e32 v65, v66, v65
	v_add_f32_e32 v67, v65, v64
	ds_bpermute_b32 v78, v159, v67
	v_lshl_add_u64 v[64:65], v[124:125], 1, s[56:57]
	v_lshl_add_u64 v[76:77], v[148:149], 1, v[64:65]
	v_cvt_pk_f16_f32 v66, v68, v69
	v_cvt_pk_f16_f32 v68, v82, v83
	s_waitcnt lgkmcnt(0)
	v_add_f32_e32 v64, v67, v78
	ds_bpermute_b32 v65, v158, v64
	v_cvt_pk_f16_f32 v67, v70, v71
	v_cvt_pk_f16_f32 v69, v88, v89
	global_store_dwordx4 v[76:77], v[72:75], off
	global_store_dwordx4 v[76:77], v[66:69], off offset:256
	s_and_saveexec_b64 s[0:1], vcc
	s_cbranch_execz .LBB0_1291
	v_lshlrev_b64 v[66:67], 6, v[122:123]
	v_lshl_add_u64 v[66:67], s[6:7], 0, v[66:67]
	s_lshl_b32 s62, s11, 2
	v_lshl_add_u64 v[66:67], v[66:67], 0, s[62:63]
	s_lshl_b32 s62, s35, 2
	v_lshl_add_u64 v[66:67], v[66:67], 0, s[62:63]
	s_waitcnt lgkmcnt(0)
	v_add_f32_e32 v64, v64, v65
	global_store_dword v[66:67], v64, off
;     __device__ __forceinline__ void operator()(const f32x4 (&acc)[2][2][4][2], const Unit& u, int wr, int wc, int fr, int fq) const {
;         { int z_ = 0; asm volatile("" : "+v"(z_)); const int l_ = (int)__builtin_amdgcn_mbcnt_hi(~0u, __builtin_amdgcn_mbcnt_lo(~0u, (unsigned)z_)); fr = l_ & 15; fq = l_ >> 4; }
;         const int row0 = u.pm * BM + wr * 64 + fr, col0 = u.pn * BM + wc * 32 + 8 * fq, lane = fq * 16 + fr;
; #pragma unroll
;         for (int ai = 0; ai < 2; ++ai)
; #pragma unroll
;             for (int mp = 0; mp < 2; ++mp) {
;                 u32x4 bsv[2][2], tv[2][2];
; #pragma unroll
;                 for (int mm = 0; mm < 2; ++mm)
; #pragma unroll
;                     for (int bj = 0; bj < 2; ++bj) { const size_t o = (size_t)(row0 + ai * HALF + (2 * mp + mm) * 16) * ldc + col0 + bj * HALF; bsv[mm][bj] = *(const u32x4*)(base + o); tv[mm][bj] = *(const u32x4*)(PP + o); }
; #pragma unroll
;                 for (int mm = 0; mm < 2; ++mm) { const int m = 2 * mp + mm; const size_t r = (size_t)(row0 + ai * HALF + m * 16), off = r * ldc + col0; float ss = 0.f;
;                     const float rs = tbl[wr * 64 + fr + ai * HALF + m * 16];
; #pragma unroll
;                     for (int bj = 0; bj < 2; ++bj) { const u32x4 t = tv[mm][bj], b = bsv[mm][bj]; const f32x4 a0 = acc[ai][bj][m][0] * rs, a1 = acc[ai][bj][m][1] * rs;
;                         f32x4 v0, v1; v0[0] = f16_lo(b.x) + bf_lo(t.x) * sigm(a0[0]); v0[1] = f16_hi(b.x) + bf_hi(t.x) * sigm(a0[1]); v0[2] = f16_lo(b.y) + bf_lo(t.y) * sigm(a0[2]); v0[3] = f16_hi(b.y) + bf_hi(t.y) * sigm(a0[3]);
;                         v1[0] = f16_lo(b.z) + bf_lo(t.z) * sigm(a1[0]); v1[1] = f16_hi(b.z) + bf_hi(t.z) * sigm(a1[1]); v1[2] = f16_lo(b.w) + bf_lo(t.w) * sigm(a1[2]); v1[3] = f16_hi(b.w) + bf_hi(t.w) * sigm(a1[3]);
;                         u32x4 w; w.x = pk_f16(v0[0], v0[1]); w.y = pk_f16(v0[2], v0[3]); w.z = pk_f16(v1[0], v1[1]); w.w = pk_f16(v1[2], v1[3]); *(u32x4*)(out + off + bj * HALF) = w;
;                         ss += ((v0[0] * v0[0] + v0[1] * v0[1]) + (v0[2] * v0[2] + v0[3] * v0[3])) + ((v1[0] * v1[0] + v1[1] * v1[1]) + (v1[2] * v1[2] + v1[3] * v1[3])); }
;                     ss = xor_add(ss, lane, 16); ss = xor_add(ss, lane, 32);
;                     if (fq == 0) ssp[r * 16 + (u.pn & 3) * 4 + wc] = ss; }
;                 asm volatile("" ::: "memory");
;             }
;     }
.LBB0_1291:
	s_or_b64 exec, exec, s[0:1]
	v_add_u32_e32 v94, 0x80, v150
	v_ashrrev_i32_e32 v95, 31, v94
	s_waitcnt lgkmcnt(0)
	v_lshlrev_b64 v[64:65], 10, v[94:95]
	v_lshl_add_u64 v[64:65], v[64:65], 0, v[148:149]
	v_lshlrev_b64 v[64:65], 1, v[64:65]
	v_lshl_add_u64 v[66:67], s[72:73], 0, v[64:65]
	global_load_dwordx4 v[100:103], v[66:67], off
	v_lshl_add_u64 v[64:65], s[70:71], 0, v[64:65]
	global_load_dwordx4 v[104:107], v[64:65], off
	global_load_dwordx4 v[86:89], v[66:67], off offset:256
	global_load_dwordx4 v[82:85], v[64:65], off offset:256
	v_add_u32_e32 v90, 0x90, v150
	v_ashrrev_i32_e32 v91, 31, v90
	v_lshlrev_b64 v[92:93], 10, v[90:91]
	v_lshl_add_u64 v[64:65], v[92:93], 0, v[148:149]
	v_lshlrev_b64 v[64:65], 1, v[64:65]
	v_lshl_add_u64 v[66:67], s[72:73], 0, v[64:65]
	v_lshl_add_u64 v[64:65], s[70:71], 0, v[64:65]
	global_load_dwordx4 v[76:79], v[66:67], off
	global_load_dwordx4 v[72:75], v[64:65], off
	global_load_dwordx4 v[68:71], v[66:67], off offset:256
	s_nop 0
	global_load_dwordx4 v[64:67], v[64:65], off offset:256
	ds_read_b32 v98, v160 offset:512
	s_waitcnt lgkmcnt(0)
	v_pk_mul_f32 v[56:57], v[56:57], v[98:99] op_sel_hi:[1,0]
	s_nop 0
	v_mul_f32_e32 v56, 0xbfb8aa3b, v56
	v_exp_f32_e32 v56, v56
	v_pk_mul_f32 v[58:59], v[58:59], v[98:99] op_sel_hi:[1,0]
	v_pk_mul_f32 v[60:61], v[60:61], v[98:99] op_sel_hi:[1,0]
	v_pk_mul_f32 v[62:63], v[62:63], v[98:99] op_sel_hi:[1,0]
	v_add_f32_e32 v56, 1.0, v56
	v_rcp_f32_e32 v96, v56
	v_mul_f32_e32 v56, 0xbfb8aa3b, v57
	v_exp_f32_e32 v56, v56
	v_mul_f32_e32 v60, 0xbfb8aa3b, v60
	v_mul_f32_e32 v61, 0xbfb8aa3b, v61
	v_exp_f32_e32 v60, v60
	v_add_f32_e32 v56, 1.0, v56
	v_rcp_f32_e32 v97, v56
	v_mul_f32_e32 v56, 0xbfb8aa3b, v58
	v_exp_f32_e32 v56, v56
	v_exp_f32_e32 v61, v61
	v_mul_f32_e32 v62, 0xbfb8aa3b, v62
	v_mul_f32_e32 v63, 0xbfb8aa3b, v63
	v_add_f32_e32 v56, 1.0, v56
	v_rcp_f32_e32 v108, v56
	v_mul_f32_e32 v56, 0xbfb8aa3b, v59
	v_exp_f32_e32 v56, v56
	v_add_f32_e32 v60, 1.0, v60
	v_add_f32_e32 v61, 1.0, v61
	v_exp_f32_e32 v62, v62
	v_exp_f32_e32 v63, v63
	v_add_f32_e32 v56, 1.0, v56
	v_rcp_f32_e32 v60, v60
	v_rcp_f32_e32 v61, v61
	v_rcp_f32_e32 v109, v56
	v_pk_mul_f32 v[48:49], v[48:49], v[98:99] op_sel_hi:[1,0]
	v_add_f32_e32 v62, 1.0, v62
	v_mul_f32_e32 v48, 0xbfb8aa3b, v48
	v_exp_f32_e32 v48, v48
	v_add_f32_e32 v63, 1.0, v63
	v_rcp_f32_e32 v62, v62
	v_rcp_f32_e32 v63, v63
	v_add_f32_e32 v48, 1.0, v48
	v_pk_mul_f32 v[54:55], v[54:55], v[98:99] op_sel_hi:[1,0]
	v_pk_mul_f32 v[52:53], v[52:53], v[98:99] op_sel_hi:[1,0]
	v_pk_mul_f32 v[50:51], v[50:51], v[98:99] op_sel_hi:[1,0]
	v_rcp_f32_e32 v98, v48
	v_mul_f32_e32 v48, 0xbfb8aa3b, v49
	v_exp_f32_e32 v48, v48
	v_mul_f32_e32 v52, 0xbfb8aa3b, v52
	v_mul_f32_e32 v53, 0xbfb8aa3b, v53
	v_exp_f32_e32 v52, v52
	v_add_f32_e32 v48, 1.0, v48
	v_rcp_f32_e32 v99, v48
	v_mul_f32_e32 v48, 0xbfb8aa3b, v50
	v_exp_f32_e32 v48, v48
	v_exp_f32_e32 v53, v53
	v_mul_f32_e32 v54, 0xbfb8aa3b, v54
	v_mul_f32_e32 v55, 0xbfb8aa3b, v55
	v_add_f32_e32 v48, 1.0, v48
	v_add_f32_e32 v52, 1.0, v52
	v_add_f32_e32 v53, 1.0, v53
	v_exp_f32_e32 v54, v54
	v_exp_f32_e32 v55, v55
	v_rcp_f32_e32 v52, v52
	v_rcp_f32_e32 v53, v53
	s_waitcnt vmcnt(0)
	v_cvt_f32_f16_e32 v56, v100
	v_cvt_f32_f16_sdwa v57, v100 dst_sel:DWORD dst_unused:UNUSED_PAD src0_sel:WORD_1
	v_lshlrev_b32_e32 v58, 16, v104
	v_and_b32_e32 v59, 0xffff0000, v104
	v_lshlrev_b32_e32 v100, 16, v105
	v_pk_fma_f32 v[60:61], v[60:61], v[58:59], v[56:57]
	v_cvt_f32_f16_e32 v58, v101
	v_cvt_f32_f16_sdwa v59, v101 dst_sel:DWORD dst_unused:UNUSED_PAD src0_sel:WORD_1
	v_and_b32_e32 v101, 0xffff0000, v105
	v_cvt_pk_f16_f32 v56, v60, v61
	v_cvt_f32_f16_sdwa v49, v86 dst_sel:DWORD dst_unused:UNUSED_PAD src0_sel:WORD_1
	v_pk_fma_f32 v[62:63], v[62:63], v[100:101], v[58:59]
	v_cvt_f32_f16_e32 v58, v102
	v_cvt_f32_f16_sdwa v59, v102 dst_sel:DWORD dst_unused:UNUSED_PAD src0_sel:WORD_1
	v_lshlrev_b32_e32 v100, 16, v106
	v_and_b32_e32 v101, 0xffff0000, v106
	v_lshlrev_b32_e32 v102, 16, v107
	v_pk_fma_f32 v[100:101], v[96:97], v[100:101], v[58:59]
	v_cvt_f32_f16_e32 v96, v103
	v_cvt_f32_f16_sdwa v97, v103 dst_sel:DWORD dst_unused:UNUSED_PAD src0_sel:WORD_1
	v_and_b32_e32 v103, 0xffff0000, v107
	v_cvt_pk_f16_f32 v57, v62, v63
	v_cvt_pk_f16_f32 v58, v100, v101
	v_pk_fma_f32 v[102:103], v[108:109], v[102:103], v[96:97]
	v_lshlrev_b64 v[96:97], 11, v[94:95]
	v_lshl_add_u64 v[96:97], s[56:57], 0, v[96:97]
	v_cvt_pk_f16_f32 v59, v102, v103
	v_lshl_add_u64 v[96:97], v[148:149], 1, v[96:97]
	global_store_dwordx4 v[96:97], v[56:59], off
	v_add_f32_e32 v54, 1.0, v54
	v_add_f32_e32 v55, 1.0, v55
	v_pk_mul_f32 v[56:57], v[60:61], v[60:61]
	v_pk_mul_f32 v[60:61], v[100:101], v[100:101]
	v_rcp_f32_e32 v100, v48
	v_mul_f32_e32 v48, 0xbfb8aa3b, v51
	v_exp_f32_e32 v48, v48
	v_lshlrev_b32_e32 v50, 16, v82
	v_and_b32_e32 v51, 0xffff0000, v82
	v_rcp_f32_e32 v54, v54
	v_add_f32_e32 v48, 1.0, v48
	v_rcp_f32_e32 v101, v48
	v_cvt_f32_f16_e32 v48, v86
	v_rcp_f32_e32 v55, v55
	v_lshlrev_b32_e32 v82, 16, v83
	v_and_b32_e32 v83, 0xffff0000, v83
	v_pk_fma_f32 v[52:53], v[52:53], v[50:51], v[48:49]
	v_cvt_f32_f16_e32 v50, v87
	v_cvt_f32_f16_sdwa v51, v87 dst_sel:DWORD dst_unused:UNUSED_PAD src0_sel:WORD_1
	v_cvt_f32_f16_e32 v86, v89
	v_cvt_f32_f16_sdwa v87, v89 dst_sel:DWORD dst_unused:UNUSED_PAD src0_sel:WORD_1
	v_cvt_pk_f16_f32 v48, v52, v53
	v_pk_fma_f32 v[54:55], v[54:55], v[82:83], v[50:51]
	v_cvt_f32_f16_e32 v50, v88
	v_cvt_f32_f16_sdwa v51, v88 dst_sel:DWORD dst_unused:UNUSED_PAD src0_sel:WORD_1
	v_lshlrev_b32_e32 v82, 16, v84
	v_and_b32_e32 v83, 0xffff0000, v84
	v_lshlrev_b32_e32 v84, 16, v85
	v_and_b32_e32 v85, 0xffff0000, v85
	v_pk_fma_f32 v[82:83], v[98:99], v[82:83], v[50:51]
	v_pk_fma_f32 v[84:85], v[100:101], v[84:85], v[86:87]
	v_cvt_pk_f16_f32 v49, v54, v55
	v_cvt_pk_f16_f32 v50, v82, v83
	v_cvt_pk_f16_f32 v51, v84, v85
	global_store_dwordx4 v[96:97], v[48:51], off offset:256
	v_pk_mul_f32 v[58:59], v[62:63], v[62:63]
	v_pk_mul_f32 v[62:63], v[102:103], v[102:103]
	v_pk_mul_f32 v[48:49], v[52:53], v[52:53]
	v_pk_mul_f32 v[50:51], v[54:55], v[54:55]
	v_add_f32_e32 v48, v48, v49
	v_add_f32_e32 v50, v50, v51
	v_pk_mul_f32 v[52:53], v[82:83], v[82:83]
	v_pk_mul_f32 v[54:55], v[84:85], v[84:85]
	v_add_f32_e32 v48, v48, v50
	v_add_f32_e32 v49, v62, v63
	v_add_f32_e32 v50, v60, v61
	v_add_f32_e32 v54, v54, v55
	v_add_f32_e32 v52, v52, v53
	v_add_f32_e32 v49, v50, v49
	v_add_f32_e32 v50, v58, v59
	v_add_f32_e32 v51, v56, v57
	v_add_f32_e32 v52, v52, v54
	v_add_f32_e32 v50, v51, v50
	v_add_f32_e32 v48, v48, v52
	v_add_f32_e32 v49, v50, v49
	v_add_f32_e32 v48, v49, v48
	ds_bpermute_b32 v49, v159, v48
	s_waitcnt lgkmcnt(0)
	v_add_f32_e32 v48, v48, v49
	ds_bpermute_b32 v49, v158, v48
	s_and_saveexec_b64 s[0:1], vcc
	s_cbranch_execz .LBB0_1293
;     __device__ __forceinline__ void operator()(const f32x4 (&acc)[2][2][4][2], const Unit& u, int wr, int wc, int fr, int fq) const {
;         { int z_ = 0; asm volatile("" : "+v"(z_)); const int l_ = (int)__builtin_amdgcn_mbcnt_hi(~0u, __builtin_amdgcn_mbcnt_lo(~0u, (unsigned)z_)); fr = l_ & 15; fq = l_ >> 4; }
;         const int row0 = u.pm * BM + wr * 64 + fr, col0 = u.pn * BM + wc * 32 + 8 * fq, lane = fq * 16 + fr;
; #pragma unroll
;         for (int ai = 0; ai < 2; ++ai)
; #pragma unroll
;             for (int mp = 0; mp < 2; ++mp) {
;                 u32x4 bsv[2][2], tv[2][2];
; #pragma unroll
;                 for (int mm = 0; mm < 2; ++mm)
; #pragma unroll
;                     for (int bj = 0; bj < 2; ++bj) { const size_t o = (size_t)(row0 + ai * HALF + (2 * mp + mm) * 16) * ldc + col0 + bj * HALF; bsv[mm][bj] = *(const u32x4*)(base + o); tv[mm][bj] = *(const u32x4*)(PP + o); }
; #pragma unroll
;                 for (int mm = 0; mm < 2; ++mm) { const int m = 2 * mp + mm; const size_t r = (size_t)(row0 + ai * HALF + m * 16), off = r * ldc + col0; float ss = 0.f;
;                     const float rs = tbl[wr * 64 + fr + ai * HALF + m * 16];
; #pragma unroll
;                     for (int bj = 0; bj < 2; ++bj) { const u32x4 t = tv[mm][bj], b = bsv[mm][bj]; const f32x4 a0 = acc[ai][bj][m][0] * rs, a1 = acc[ai][bj][m][1] * rs;
;                         f32x4 v0, v1; v0[0] = f16_lo(b.x) + bf_lo(t.x) * sigm(a0[0]); v0[1] = f16_hi(b.x) + bf_hi(t.x) * sigm(a0[1]); v0[2] = f16_lo(b.y) + bf_lo(t.y) * sigm(a0[2]); v0[3] = f16_hi(b.y) + bf_hi(t.y) * sigm(a0[3]);
;                         v1[0] = f16_lo(b.z) + bf_lo(t.z) * sigm(a1[0]); v1[1] = f16_hi(b.z) + bf_hi(t.z) * sigm(a1[1]); v1[2] = f16_lo(b.w) + bf_lo(t.w) * sigm(a1[2]); v1[3] = f16_hi(b.w) + bf_hi(t.w) * sigm(a1[3]);
;                         u32x4 w; w.x = pk_f16(v0[0], v0[1]); w.y = pk_f16(v0[2], v0[3]); w.z = pk_f16(v1[0], v1[1]); w.w = pk_f16(v1[2], v1[3]); *(u32x4*)(out + off + bj * HALF) = w;
;                         ss += ((v0[0] * v0[0] + v0[1] * v0[1]) + (v0[2] * v0[2] + v0[3] * v0[3])) + ((v1[0] * v1[0] + v1[1] * v1[1]) + (v1[2] * v1[2] + v1[3] * v1[3])); }
;                     ss = xor_add(ss, lane, 16); ss = xor_add(ss, lane, 32);
;                     if (fq == 0) ssp[r * 16 + (u.pn & 3) * 4 + wc] = ss; }
;                 asm volatile("" ::: "memory");
;             }
;     }
	v_lshlrev_b64 v[50:51], 6, v[94:95]
	v_lshl_add_u64 v[50:51], s[6:7], 0, v[50:51]
	s_lshl_b32 s62, s11, 2
	v_lshl_add_u64 v[50:51], v[50:51], 0, s[62:63]
	s_lshl_b32 s62, s35, 2
	v_lshl_add_u64 v[50:51], v[50:51], 0, s[62:63]
	s_waitcnt lgkmcnt(0)
	v_add_f32_e32 v48, v48, v49
	global_store_dword v[50:51], v48, off
.LBB0_1293:
	s_or_b64 exec, exec, s[0:1]
	ds_read_b32 v48, v160 offset:576
	v_lshlrev_b32_e32 v54, 16, v73
	v_and_b32_e32 v55, 0xffff0000, v73
	v_lshlrev_b32_e32 v56, 16, v75
	v_and_b32_e32 v57, 0xffff0000, v75
	s_waitcnt lgkmcnt(0)
	v_pk_mul_f32 v[40:41], v[40:41], v[48:49] op_sel_hi:[1,0]
	v_pk_mul_f32 v[44:45], v[44:45], v[48:49] op_sel_hi:[1,0]
	v_mul_f32_e32 v40, 0xbfb8aa3b, v40
	v_exp_f32_e32 v40, v40
	v_mul_f32_e32 v41, 0xbfb8aa3b, v41
	v_exp_f32_e32 v41, v41
	v_pk_mul_f32 v[42:43], v[42:43], v[48:49] op_sel_hi:[1,0]
	v_add_f32_e32 v40, 1.0, v40
	v_mul_f32_e32 v44, 0xbfb8aa3b, v44
	v_mul_f32_e32 v45, 0xbfb8aa3b, v45
	v_rcp_f32_e32 v50, v40
	v_add_f32_e32 v40, 1.0, v41
	v_mul_f32_e32 v41, 0xbfb8aa3b, v42
	v_exp_f32_e32 v44, v44
	v_exp_f32_e32 v45, v45
	v_exp_f32_e32 v41, v41
	v_pk_mul_f32 v[46:47], v[46:47], v[48:49] op_sel_hi:[1,0]
	v_mul_f32_e32 v42, 0xbfb8aa3b, v43
	v_mul_f32_e32 v46, 0xbfb8aa3b, v46
	v_mul_f32_e32 v47, 0xbfb8aa3b, v47
	v_exp_f32_e32 v42, v42
	v_add_f32_e32 v44, 1.0, v44
	v_add_f32_e32 v45, 1.0, v45
	v_exp_f32_e32 v46, v46
	v_exp_f32_e32 v47, v47
	v_rcp_f32_e32 v51, v40
	v_add_f32_e32 v40, 1.0, v41
	v_rcp_f32_e32 v44, v44
	v_rcp_f32_e32 v45, v45
	v_rcp_f32_e32 v52, v40
	v_cvt_f32_f16_sdwa v41, v76 dst_sel:DWORD dst_unused:UNUSED_PAD src0_sel:WORD_1
	v_cvt_f32_f16_e32 v40, v76
	v_add_f32_e32 v42, 1.0, v42
	v_add_f32_e32 v46, 1.0, v46
	v_add_f32_e32 v47, 1.0, v47
	v_rcp_f32_e32 v53, v42
	v_lshlrev_b32_e32 v42, 16, v72
	v_and_b32_e32 v43, 0xffff0000, v72
	v_rcp_f32_e32 v46, v46
	v_rcp_f32_e32 v47, v47
	v_pk_fma_f32 v[44:45], v[44:45], v[42:43], v[40:41]
	v_cvt_f32_f16_sdwa v43, v77 dst_sel:DWORD dst_unused:UNUSED_PAD src0_sel:WORD_1
	v_cvt_f32_f16_e32 v42, v77
	v_pk_mul_f32 v[36:37], v[36:37], v[48:49] op_sel_hi:[1,0]
	v_pk_mul_f32 v[38:39], v[38:39], v[48:49] op_sel_hi:[1,0]
	v_mul_f32_e32 v36, 0xbfb8aa3b, v36
	v_pk_fma_f32 v[46:47], v[46:47], v[54:55], v[42:43]
	v_cvt_f32_f16_sdwa v43, v78 dst_sel:DWORD dst_unused:UNUSED_PAD src0_sel:WORD_1
	v_cvt_f32_f16_e32 v42, v78
	v_mul_f32_e32 v37, 0xbfb8aa3b, v37
	v_exp_f32_e32 v36, v36
	v_exp_f32_e32 v37, v37
	v_mul_f32_e32 v38, 0xbfb8aa3b, v38
	v_mul_f32_e32 v39, 0xbfb8aa3b, v39
	v_lshlrev_b32_e32 v54, 16, v74
	v_and_b32_e32 v55, 0xffff0000, v74
	v_exp_f32_e32 v38, v38
	v_exp_f32_e32 v39, v39
	v_pk_fma_f32 v[50:51], v[50:51], v[54:55], v[42:43]
	v_cvt_f32_f16_sdwa v55, v79 dst_sel:DWORD dst_unused:UNUSED_PAD src0_sel:WORD_1
	v_cvt_f32_f16_e32 v54, v79
	v_pk_mul_f32 v[32:33], v[32:33], v[48:49] op_sel_hi:[1,0]
	v_pk_mul_f32 v[34:35], v[34:35], v[48:49] op_sel_hi:[1,0]
	v_add_f32_e32 v36, 1.0, v36
	v_add_f32_e32 v37, 1.0, v37
	v_mul_f32_e32 v32, 0xbfb8aa3b, v32
	v_mul_f32_e32 v33, 0xbfb8aa3b, v33
	v_rcp_f32_e32 v36, v36
	v_rcp_f32_e32 v37, v37
	v_add_f32_e32 v38, 1.0, v38
	v_add_f32_e32 v39, 1.0, v39
	v_exp_f32_e32 v32, v32
	v_exp_f32_e32 v33, v33
	v_mul_f32_e32 v34, 0xbfb8aa3b, v34
	v_mul_f32_e32 v35, 0xbfb8aa3b, v35
	v_cvt_f32_f16_sdwa v49, v68 dst_sel:DWORD dst_unused:UNUSED_PAD src0_sel:WORD_1
	v_cvt_f32_f16_e32 v48, v68
	v_pk_fma_f32 v[52:53], v[52:53], v[56:57], v[54:55]
	v_rcp_f32_e32 v38, v38
	v_rcp_f32_e32 v39, v39
	v_exp_f32_e32 v34, v34
	v_exp_f32_e32 v35, v35
	v_cvt_f32_f16_sdwa v57, v69 dst_sel:DWORD dst_unused:UNUSED_PAD src0_sel:WORD_1
	v_cvt_f32_f16_e32 v56, v69
	v_lshlrev_b32_e32 v54, 16, v64
	v_and_b32_e32 v55, 0xffff0000, v64
	v_add_f32_e32 v32, 1.0, v32
	v_add_f32_e32 v33, 1.0, v33
	v_pk_fma_f32 v[36:37], v[36:37], v[54:55], v[48:49]
	v_lshlrev_b32_e32 v48, 16, v65
	v_and_b32_e32 v49, 0xffff0000, v65
	v_rcp_f32_e32 v32, v32
	v_rcp_f32_e32 v33, v33
	v_add_f32_e32 v34, 1.0, v34
	v_add_f32_e32 v35, 1.0, v35
	v_pk_fma_f32 v[38:39], v[38:39], v[48:49], v[56:57]
	v_cvt_f32_f16_sdwa v49, v70 dst_sel:DWORD dst_unused:UNUSED_PAD src0_sel:WORD_1
	v_cvt_f32_f16_e32 v48, v70
	v_rcp_f32_e32 v34, v34
	v_rcp_f32_e32 v35, v35
	v_cvt_f32_f16_sdwa v57, v71 dst_sel:DWORD dst_unused:UNUSED_PAD src0_sel:WORD_1
	v_cvt_f32_f16_e32 v56, v71
	v_lshlrev_b32_e32 v54, 16, v66
	v_and_b32_e32 v55, 0xffff0000, v66
	v_pk_fma_f32 v[48:49], v[32:33], v[54:55], v[48:49]
	v_lshlrev_b32_e32 v32, 16, v67
	v_and_b32_e32 v33, 0xffff0000, v67
	v_pk_fma_f32 v[54:55], v[34:35], v[32:33], v[56:57]
	v_pk_mul_f32 v[32:33], v[36:37], v[36:37]
	v_pk_mul_f32 v[34:35], v[38:39], v[38:39]
	v_cvt_pk_f16_f32 v42, v50, v51
	v_cvt_pk_f16_f32 v43, v52, v53
	v_pk_mul_f32 v[50:51], v[50:51], v[50:51]
	v_pk_mul_f32 v[52:53], v[52:53], v[52:53]
	v_add_f32_e32 v34, v34, v35
	v_add_f32_e32 v32, v32, v33
	v_cvt_pk_f16_f32 v40, v44, v45
	v_cvt_pk_f16_f32 v41, v46, v47
	v_pk_mul_f32 v[44:45], v[44:45], v[44:45]
	v_pk_mul_f32 v[46:47], v[46:47], v[46:47]
	v_pk_mul_f32 v[56:57], v[48:49], v[48:49]
	v_pk_mul_f32 v[58:59], v[54:55], v[54:55]
	v_add_f32_e32 v32, v32, v34
	v_add_f32_e32 v33, v52, v53
	v_add_f32_e32 v34, v50, v51
	v_add_f32_e32 v58, v58, v59
	v_add_f32_e32 v56, v56, v57
	v_add_f32_e32 v33, v34, v33
	v_add_f32_e32 v34, v46, v47
	v_add_f32_e32 v35, v44, v45
	v_add_f32_e32 v56, v56, v58
	v_add_f32_e32 v34, v35, v34
	v_add_f32_e32 v32, v32, v56
	v_add_f32_e32 v33, v34, v33
	v_add_f32_e32 v35, v33, v32
	ds_bpermute_b32 v46, v159, v35
	v_lshl_add_u64 v[32:33], v[92:93], 1, s[56:57]
	v_lshl_add_u64 v[44:45], v[148:149], 1, v[32:33]
	v_cvt_pk_f16_f32 v34, v36, v37
	v_cvt_pk_f16_f32 v36, v48, v49
	s_waitcnt lgkmcnt(0)
	v_add_f32_e32 v32, v35, v46
	ds_bpermute_b32 v33, v158, v32
	v_cvt_pk_f16_f32 v35, v38, v39
	v_cvt_pk_f16_f32 v37, v54, v55
	global_store_dwordx4 v[44:45], v[40:43], off
	global_store_dwordx4 v[44:45], v[34:37], off offset:256
	s_and_saveexec_b64 s[0:1], vcc
	s_cbranch_execz .LBB0_1295
	v_lshlrev_b64 v[34:35], 6, v[90:91]
	v_lshl_add_u64 v[34:35], s[6:7], 0, v[34:35]
	s_lshl_b32 s62, s11, 2
	v_lshl_add_u64 v[34:35], v[34:35], 0, s[62:63]
	s_lshl_b32 s62, s35, 2
	v_lshl_add_u64 v[34:35], v[34:35], 0, s[62:63]
	s_waitcnt lgkmcnt(0)
	v_add_f32_e32 v32, v32, v33
	global_store_dword v[34:35], v32, off
;     __device__ __forceinline__ void operator()(const f32x4 (&acc)[2][2][4][2], const Unit& u, int wr, int wc, int fr, int fq) const {
;         { int z_ = 0; asm volatile("" : "+v"(z_)); const int l_ = (int)__builtin_amdgcn_mbcnt_hi(~0u, __builtin_amdgcn_mbcnt_lo(~0u, (unsigned)z_)); fr = l_ & 15; fq = l_ >> 4; }
;         const int row0 = u.pm * BM + wr * 64 + fr, col0 = u.pn * BM + wc * 32 + 8 * fq, lane = fq * 16 + fr;
; #pragma unroll
;         for (int ai = 0; ai < 2; ++ai)
; #pragma unroll
;             for (int mp = 0; mp < 2; ++mp) {
;                 u32x4 bsv[2][2], tv[2][2];
; #pragma unroll
;                 for (int mm = 0; mm < 2; ++mm)
; #pragma unroll
;                     for (int bj = 0; bj < 2; ++bj) { const size_t o = (size_t)(row0 + ai * HALF + (2 * mp + mm) * 16) * ldc + col0 + bj * HALF; bsv[mm][bj] = *(const u32x4*)(base + o); tv[mm][bj] = *(const u32x4*)(PP + o); }
; #pragma unroll
;                 for (int mm = 0; mm < 2; ++mm) { const int m = 2 * mp + mm; const size_t r = (size_t)(row0 + ai * HALF + m * 16), off = r * ldc + col0; float ss = 0.f;
;                     const float rs = tbl[wr * 64 + fr + ai * HALF + m * 16];
; #pragma unroll
;                     for (int bj = 0; bj < 2; ++bj) { const u32x4 t = tv[mm][bj], b = bsv[mm][bj]; const f32x4 a0 = acc[ai][bj][m][0] * rs, a1 = acc[ai][bj][m][1] * rs;
;                         f32x4 v0, v1; v0[0] = f16_lo(b.x) + bf_lo(t.x) * sigm(a0[0]); v0[1] = f16_hi(b.x) + bf_hi(t.x) * sigm(a0[1]); v0[2] = f16_lo(b.y) + bf_lo(t.y) * sigm(a0[2]); v0[3] = f16_hi(b.y) + bf_hi(t.y) * sigm(a0[3]);
;                         v1[0] = f16_lo(b.z) + bf_lo(t.z) * sigm(a1[0]); v1[1] = f16_hi(b.z) + bf_hi(t.z) * sigm(a1[1]); v1[2] = f16_lo(b.w) + bf_lo(t.w) * sigm(a1[2]); v1[3] = f16_hi(b.w) + bf_hi(t.w) * sigm(a1[3]);
;                         u32x4 w; w.x = pk_f16(v0[0], v0[1]); w.y = pk_f16(v0[2], v0[3]); w.z = pk_f16(v1[0], v1[1]); w.w = pk_f16(v1[2], v1[3]); *(u32x4*)(out + off + bj * HALF) = w;
;                         ss += ((v0[0] * v0[0] + v0[1] * v0[1]) + (v0[2] * v0[2] + v0[3] * v0[3])) + ((v1[0] * v1[0] + v1[1] * v1[1]) + (v1[2] * v1[2] + v1[3] * v1[3])); }
;                     ss = xor_add(ss, lane, 16); ss = xor_add(ss, lane, 32);
;                     if (fq == 0) ssp[r * 16 + (u.pn & 3) * 4 + wc] = ss; }
;                 asm volatile("" ::: "memory");
;             }
;     }
.LBB0_1295:
	s_or_b64 exec, exec, s[0:1]
	v_add_u32_e32 v60, 0xa0, v150
	v_ashrrev_i32_e32 v61, 31, v60
	s_waitcnt lgkmcnt(0)
	v_lshlrev_b64 v[32:33], 10, v[60:61]
	v_lshl_add_u64 v[32:33], v[32:33], 0, v[148:149]
	v_lshlrev_b64 v[32:33], 1, v[32:33]
	v_lshl_add_u64 v[34:35], s[72:73], 0, v[32:33]
	global_load_dwordx4 v[66:69], v[34:35], off
	v_lshl_add_u64 v[32:33], s[70:71], 0, v[32:33]
	global_load_dwordx4 v[70:73], v[32:33], off
	global_load_dwordx4 v[52:55], v[34:35], off offset:256
	global_load_dwordx4 v[48:51], v[32:33], off offset:256
	v_add_u32_e32 v56, 0xb0, v150
	v_ashrrev_i32_e32 v57, 31, v56
	v_lshlrev_b64 v[58:59], 10, v[56:57]
	v_lshl_add_u64 v[32:33], v[58:59], 0, v[148:149]
	v_lshlrev_b64 v[32:33], 1, v[32:33]
	v_lshl_add_u64 v[34:35], s[72:73], 0, v[32:33]
	v_lshl_add_u64 v[32:33], s[70:71], 0, v[32:33]
	global_load_dwordx4 v[44:47], v[34:35], off
	global_load_dwordx4 v[40:43], v[32:33], off
	global_load_dwordx4 v[36:39], v[34:35], off offset:256
	s_nop 0
	global_load_dwordx4 v[32:35], v[32:33], off offset:256
	ds_read_b32 v64, v160 offset:640
	s_waitcnt lgkmcnt(0)
	v_pk_mul_f32 v[24:25], v[24:25], v[64:65] op_sel_hi:[1,0]
	s_nop 0
	v_mul_f32_e32 v24, 0xbfb8aa3b, v24
	v_exp_f32_e32 v24, v24
	v_pk_mul_f32 v[26:27], v[26:27], v[64:65] op_sel_hi:[1,0]
	v_pk_mul_f32 v[28:29], v[28:29], v[64:65] op_sel_hi:[1,0]
	v_pk_mul_f32 v[30:31], v[30:31], v[64:65] op_sel_hi:[1,0]
	v_add_f32_e32 v24, 1.0, v24
	v_rcp_f32_e32 v62, v24
	v_mul_f32_e32 v24, 0xbfb8aa3b, v25
	v_exp_f32_e32 v24, v24
	v_mul_f32_e32 v28, 0xbfb8aa3b, v28
	v_mul_f32_e32 v29, 0xbfb8aa3b, v29
	v_exp_f32_e32 v28, v28
	v_add_f32_e32 v24, 1.0, v24
	v_rcp_f32_e32 v63, v24
	v_mul_f32_e32 v24, 0xbfb8aa3b, v26
	v_exp_f32_e32 v24, v24
	v_exp_f32_e32 v29, v29
	v_mul_f32_e32 v30, 0xbfb8aa3b, v30
	v_mul_f32_e32 v31, 0xbfb8aa3b, v31
	v_add_f32_e32 v24, 1.0, v24
	v_rcp_f32_e32 v74, v24
	v_mul_f32_e32 v24, 0xbfb8aa3b, v27
	v_exp_f32_e32 v24, v24
	v_add_f32_e32 v28, 1.0, v28
	v_add_f32_e32 v29, 1.0, v29
	v_exp_f32_e32 v30, v30
	v_exp_f32_e32 v31, v31
	v_add_f32_e32 v24, 1.0, v24
	v_rcp_f32_e32 v28, v28
	v_rcp_f32_e32 v29, v29
	v_rcp_f32_e32 v75, v24
	v_pk_mul_f32 v[16:17], v[16:17], v[64:65] op_sel_hi:[1,0]
	v_add_f32_e32 v30, 1.0, v30
	v_mul_f32_e32 v16, 0xbfb8aa3b, v16
	v_exp_f32_e32 v16, v16
	v_add_f32_e32 v31, 1.0, v31
	v_rcp_f32_e32 v30, v30
	v_rcp_f32_e32 v31, v31
	v_add_f32_e32 v16, 1.0, v16
	v_pk_mul_f32 v[22:23], v[22:23], v[64:65] op_sel_hi:[1,0]
	v_pk_mul_f32 v[20:21], v[20:21], v[64:65] op_sel_hi:[1,0]
	v_pk_mul_f32 v[18:19], v[18:19], v[64:65] op_sel_hi:[1,0]
	v_rcp_f32_e32 v64, v16
	v_mul_f32_e32 v16, 0xbfb8aa3b, v17
	v_exp_f32_e32 v16, v16
	v_mul_f32_e32 v20, 0xbfb8aa3b, v20
	v_mul_f32_e32 v21, 0xbfb8aa3b, v21
	v_exp_f32_e32 v20, v20
	v_add_f32_e32 v16, 1.0, v16
	v_rcp_f32_e32 v65, v16
	v_mul_f32_e32 v16, 0xbfb8aa3b, v18
	v_exp_f32_e32 v16, v16
	v_exp_f32_e32 v21, v21
	v_mul_f32_e32 v22, 0xbfb8aa3b, v22
	v_mul_f32_e32 v23, 0xbfb8aa3b, v23
	v_add_f32_e32 v16, 1.0, v16
	v_add_f32_e32 v20, 1.0, v20
	v_add_f32_e32 v21, 1.0, v21
	v_exp_f32_e32 v22, v22
	v_exp_f32_e32 v23, v23
	v_rcp_f32_e32 v20, v20
	v_rcp_f32_e32 v21, v21
	s_waitcnt vmcnt(0)
	v_cvt_f32_f16_e32 v24, v66
	v_cvt_f32_f16_sdwa v25, v66 dst_sel:DWORD dst_unused:UNUSED_PAD src0_sel:WORD_1
	v_lshlrev_b32_e32 v26, 16, v70
	v_and_b32_e32 v27, 0xffff0000, v70
	v_lshlrev_b32_e32 v66, 16, v71
	v_pk_fma_f32 v[28:29], v[28:29], v[26:27], v[24:25]
	v_cvt_f32_f16_e32 v26, v67
	v_cvt_f32_f16_sdwa v27, v67 dst_sel:DWORD dst_unused:UNUSED_PAD src0_sel:WORD_1
	v_and_b32_e32 v67, 0xffff0000, v71
	v_cvt_pk_f16_f32 v24, v28, v29
	v_cvt_f32_f16_sdwa v17, v52 dst_sel:DWORD dst_unused:UNUSED_PAD src0_sel:WORD_1
	v_pk_fma_f32 v[30:31], v[30:31], v[66:67], v[26:27]
	v_cvt_f32_f16_e32 v26, v68
	v_cvt_f32_f16_sdwa v27, v68 dst_sel:DWORD dst_unused:UNUSED_PAD src0_sel:WORD_1
	v_lshlrev_b32_e32 v66, 16, v72
	v_and_b32_e32 v67, 0xffff0000, v72
	v_lshlrev_b32_e32 v68, 16, v73
	v_pk_fma_f32 v[66:67], v[62:63], v[66:67], v[26:27]
	v_cvt_f32_f16_e32 v62, v69
	v_cvt_f32_f16_sdwa v63, v69 dst_sel:DWORD dst_unused:UNUSED_PAD src0_sel:WORD_1
	v_and_b32_e32 v69, 0xffff0000, v73
	v_cvt_pk_f16_f32 v25, v30, v31
	v_cvt_pk_f16_f32 v26, v66, v67
	v_pk_fma_f32 v[68:69], v[74:75], v[68:69], v[62:63]
	v_lshlrev_b64 v[62:63], 11, v[60:61]
	v_lshl_add_u64 v[62:63], s[56:57], 0, v[62:63]
	v_cvt_pk_f16_f32 v27, v68, v69
	v_lshl_add_u64 v[62:63], v[148:149], 1, v[62:63]
	global_store_dwordx4 v[62:63], v[24:27], off
	v_add_f32_e32 v22, 1.0, v22
	v_add_f32_e32 v23, 1.0, v23
	v_pk_mul_f32 v[24:25], v[28:29], v[28:29]
	v_pk_mul_f32 v[28:29], v[66:67], v[66:67]
	v_rcp_f32_e32 v66, v16
	v_mul_f32_e32 v16, 0xbfb8aa3b, v19
	v_exp_f32_e32 v16, v16
	v_lshlrev_b32_e32 v18, 16, v48
	v_and_b32_e32 v19, 0xffff0000, v48
	v_rcp_f32_e32 v22, v22
	v_add_f32_e32 v16, 1.0, v16
	v_rcp_f32_e32 v67, v16
	v_cvt_f32_f16_e32 v16, v52
	v_rcp_f32_e32 v23, v23
	v_lshlrev_b32_e32 v48, 16, v49
	v_and_b32_e32 v49, 0xffff0000, v49
	v_pk_fma_f32 v[20:21], v[20:21], v[18:19], v[16:17]
	v_cvt_f32_f16_e32 v18, v53
	v_cvt_f32_f16_sdwa v19, v53 dst_sel:DWORD dst_unused:UNUSED_PAD src0_sel:WORD_1
	v_cvt_f32_f16_e32 v52, v55
	v_cvt_f32_f16_sdwa v53, v55 dst_sel:DWORD dst_unused:UNUSED_PAD src0_sel:WORD_1
	v_cvt_pk_f16_f32 v16, v20, v21
	v_pk_fma_f32 v[22:23], v[22:23], v[48:49], v[18:19]
	v_cvt_f32_f16_e32 v18, v54
	v_cvt_f32_f16_sdwa v19, v54 dst_sel:DWORD dst_unused:UNUSED_PAD src0_sel:WORD_1
	v_lshlrev_b32_e32 v48, 16, v50
	v_and_b32_e32 v49, 0xffff0000, v50
	v_lshlrev_b32_e32 v50, 16, v51
	v_and_b32_e32 v51, 0xffff0000, v51
	v_pk_fma_f32 v[48:49], v[64:65], v[48:49], v[18:19]
	v_pk_fma_f32 v[50:51], v[66:67], v[50:51], v[52:53]
	v_cvt_pk_f16_f32 v17, v22, v23
	v_cvt_pk_f16_f32 v18, v48, v49
	v_cvt_pk_f16_f32 v19, v50, v51
	global_store_dwordx4 v[62:63], v[16:19], off offset:256
	v_pk_mul_f32 v[26:27], v[30:31], v[30:31]
	v_pk_mul_f32 v[30:31], v[68:69], v[68:69]
	v_pk_mul_f32 v[16:17], v[20:21], v[20:21]
	v_pk_mul_f32 v[18:19], v[22:23], v[22:23]
	v_add_f32_e32 v16, v16, v17
	v_add_f32_e32 v18, v18, v19
	v_pk_mul_f32 v[20:21], v[48:49], v[48:49]
	v_pk_mul_f32 v[22:23], v[50:51], v[50:51]
	v_add_f32_e32 v16, v16, v18
	v_add_f32_e32 v17, v30, v31
	v_add_f32_e32 v18, v28, v29
	v_add_f32_e32 v22, v22, v23
	v_add_f32_e32 v20, v20, v21
	v_add_f32_e32 v17, v18, v17
	v_add_f32_e32 v18, v26, v27
	v_add_f32_e32 v19, v24, v25
	v_add_f32_e32 v20, v20, v22
	v_add_f32_e32 v18, v19, v18
	v_add_f32_e32 v16, v16, v20
	v_add_f32_e32 v17, v18, v17
	v_add_f32_e32 v16, v17, v16
	ds_bpermute_b32 v17, v159, v16
	s_waitcnt lgkmcnt(0)
	v_add_f32_e32 v16, v16, v17
	ds_bpermute_b32 v17, v158, v16
	s_and_saveexec_b64 s[0:1], vcc
	s_cbranch_execz .LBB0_1297
	v_lshlrev_b64 v[18:19], 6, v[60:61]
	v_lshl_add_u64 v[18:19], s[6:7], 0, v[18:19]
	s_lshl_b32 s62, s11, 2
	v_lshl_add_u64 v[18:19], v[18:19], 0, s[62:63]
	s_lshl_b32 s62, s35, 2
	v_lshl_add_u64 v[18:19], v[18:19], 0, s[62:63]
	s_waitcnt lgkmcnt(0)
	v_add_f32_e32 v16, v16, v17
	global_store_dword v[18:19], v16, off
; __device__ __forceinline__ float bf_lo(unsigned u) { return __uint_as_float(u << 16); }
; __device__ __forceinline__ float bf_hi(unsigned u) { return __uint_as_float(u & 0xffff0000u); }
; __device__ __forceinline__ float sigm(float x) { return __builtin_amdgcn_rcpf(1.f + __expf(-x)); }
; __device__ __forceinline__ float xor_add(float v, int lane, int o) { return v + __builtin_bit_cast(float, __builtin_amdgcn_ds_bpermute((lane ^ o) << 2, __builtin_bit_cast(int, v))); }
; __device__ __forceinline__ float f16_lo(unsigned u) { return (float)__builtin_bit_cast(h16x2, u)[0]; }
; __device__ __forceinline__ float f16_hi(unsigned u) { return (float)__builtin_bit_cast(h16x2, u)[1]; }
;     __device__ __forceinline__ void operator()(const f32x4 (&acc)[2][2][4][2], const Unit& u, int wr, int wc, int fr, int fq) const {
;     ...
;                 for (int mm = 0; mm < 2; ++mm) { const int m = 2 * mp + mm; const size_t r = (size_t)(row0 + ai * HALF + m * 16), off = r * ldc + col0; float ss = 0.f;
;                     const float rs = tbl[wr * 64 + fr + ai * HALF + m * 16];
; #pragma unroll
;                     for (int bj = 0; bj < 2; ++bj) { const u32x4 t = tv[mm][bj], b = bsv[mm][bj]; const f32x4 a0 = acc[ai][bj][m][0] * rs, a1 = acc[ai][bj][m][1] * rs;
;                         f32x4 v0, v1; v0[0] = f16_lo(b.x) + bf_lo(t.x) * sigm(a0[0]); v0[1] = f16_hi(b.x) + bf_hi(t.x) * sigm(a0[1]); v0[2] = f16_lo(b.y) + bf_lo(t.y) * sigm(a0[2]); v0[3] = f16_hi(b.y) + bf_hi(t.y) * sigm(a0[3]);
;                         v1[0] = f16_lo(b.z) + bf_lo(t.z) * sigm(a1[0]); v1[1] = f16_hi(b.z) + bf_hi(t.z) * sigm(a1[1]); v1[2] = f16_lo(b.w) + bf_lo(t.w) * sigm(a1[2]); v1[3] = f16_hi(b.w) + bf_hi(t.w) * sigm(a1[3]);
;                         u32x4 w; w.x = pk_f16(v0[0], v0[1]); w.y = pk_f16(v0[2], v0[3]); w.z = pk_f16(v1[0], v1[1]); w.w = pk_f16(v1[2], v1[3]); *(u32x4*)(out + off + bj * HALF) = w;
;                         ss += ((v0[0] * v0[0] + v0[1] * v0[1]) + (v0[2] * v0[2] + v0[3] * v0[3])) + ((v1[0] * v1[0] + v1[1] * v1[1]) + (v1[2] * v1[2] + v1[3] * v1[3])); }
;                     ss = xor_add(ss, lane, 16); ss = xor_add(ss, lane, 32);
;                     if (fq == 0) ssp[r * 16 + (u.pn & 3) * 4 + wc] = ss; }
.LBB0_1297:
	s_or_b64 exec, exec, s[0:1]
	ds_read_b32 v16, v160 offset:704
	v_lshlrev_b32_e32 v22, 16, v41
	v_and_b32_e32 v23, 0xffff0000, v41
	v_lshlrev_b32_e32 v24, 16, v43
	v_and_b32_e32 v25, 0xffff0000, v43
	s_waitcnt lgkmcnt(0)
	v_pk_mul_f32 v[8:9], v[8:9], v[16:17] op_sel_hi:[1,0]
	v_pk_mul_f32 v[12:13], v[12:13], v[16:17] op_sel_hi:[1,0]
	v_mul_f32_e32 v8, 0xbfb8aa3b, v8
	v_exp_f32_e32 v8, v8
	v_mul_f32_e32 v9, 0xbfb8aa3b, v9
	v_exp_f32_e32 v9, v9
	v_pk_mul_f32 v[10:11], v[10:11], v[16:17] op_sel_hi:[1,0]
	v_add_f32_e32 v8, 1.0, v8
	v_mul_f32_e32 v12, 0xbfb8aa3b, v12
	v_mul_f32_e32 v13, 0xbfb8aa3b, v13
	v_rcp_f32_e32 v18, v8
	v_add_f32_e32 v8, 1.0, v9
	v_mul_f32_e32 v9, 0xbfb8aa3b, v10
	v_exp_f32_e32 v12, v12
	v_exp_f32_e32 v13, v13
	v_exp_f32_e32 v9, v9
	v_pk_mul_f32 v[14:15], v[14:15], v[16:17] op_sel_hi:[1,0]
	v_mul_f32_e32 v10, 0xbfb8aa3b, v11
	v_mul_f32_e32 v14, 0xbfb8aa3b, v14
	v_mul_f32_e32 v15, 0xbfb8aa3b, v15
	v_exp_f32_e32 v10, v10
	v_add_f32_e32 v12, 1.0, v12
	v_add_f32_e32 v13, 1.0, v13
	v_exp_f32_e32 v14, v14
	v_exp_f32_e32 v15, v15
	v_rcp_f32_e32 v19, v8
	v_add_f32_e32 v8, 1.0, v9
	v_rcp_f32_e32 v12, v12
	v_rcp_f32_e32 v13, v13
	v_rcp_f32_e32 v20, v8
	v_cvt_f32_f16_sdwa v9, v44 dst_sel:DWORD dst_unused:UNUSED_PAD src0_sel:WORD_1
	v_cvt_f32_f16_e32 v8, v44
	v_add_f32_e32 v10, 1.0, v10
	v_add_f32_e32 v14, 1.0, v14
	v_add_f32_e32 v15, 1.0, v15
	v_rcp_f32_e32 v21, v10
	v_lshlrev_b32_e32 v10, 16, v40
	v_and_b32_e32 v11, 0xffff0000, v40
	v_rcp_f32_e32 v14, v14
	v_rcp_f32_e32 v15, v15
	v_pk_fma_f32 v[12:13], v[12:13], v[10:11], v[8:9]
	v_cvt_f32_f16_sdwa v11, v45 dst_sel:DWORD dst_unused:UNUSED_PAD src0_sel:WORD_1
	v_cvt_f32_f16_e32 v10, v45
	v_pk_mul_f32 v[4:5], v[4:5], v[16:17] op_sel_hi:[1,0]
	v_pk_mul_f32 v[6:7], v[6:7], v[16:17] op_sel_hi:[1,0]
	v_mul_f32_e32 v4, 0xbfb8aa3b, v4
	v_pk_fma_f32 v[14:15], v[14:15], v[22:23], v[10:11]
	v_cvt_f32_f16_sdwa v11, v46 dst_sel:DWORD dst_unused:UNUSED_PAD src0_sel:WORD_1
	v_cvt_f32_f16_e32 v10, v46
	v_mul_f32_e32 v5, 0xbfb8aa3b, v5
	v_exp_f32_e32 v4, v4
	v_exp_f32_e32 v5, v5
	v_mul_f32_e32 v6, 0xbfb8aa3b, v6
	v_mul_f32_e32 v7, 0xbfb8aa3b, v7
	v_lshlrev_b32_e32 v22, 16, v42
	v_and_b32_e32 v23, 0xffff0000, v42
	v_exp_f32_e32 v6, v6
	v_exp_f32_e32 v7, v7
	v_pk_fma_f32 v[18:19], v[18:19], v[22:23], v[10:11]
	v_cvt_f32_f16_sdwa v23, v47 dst_sel:DWORD dst_unused:UNUSED_PAD src0_sel:WORD_1
	v_cvt_f32_f16_e32 v22, v47
	v_pk_mul_f32 v[0:1], v[0:1], v[16:17] op_sel_hi:[1,0]
	v_pk_mul_f32 v[2:3], v[2:3], v[16:17] op_sel_hi:[1,0]
	v_add_f32_e32 v4, 1.0, v4
	v_add_f32_e32 v5, 1.0, v5
	v_mul_f32_e32 v0, 0xbfb8aa3b, v0
	v_mul_f32_e32 v1, 0xbfb8aa3b, v1
	v_rcp_f32_e32 v4, v4
	v_rcp_f32_e32 v5, v5
	v_add_f32_e32 v6, 1.0, v6
	v_add_f32_e32 v7, 1.0, v7
	v_exp_f32_e32 v0, v0
	v_exp_f32_e32 v1, v1
	v_mul_f32_e32 v2, 0xbfb8aa3b, v2
	v_mul_f32_e32 v3, 0xbfb8aa3b, v3
	v_cvt_f32_f16_sdwa v17, v36 dst_sel:DWORD dst_unused:UNUSED_PAD src0_sel:WORD_1
	v_cvt_f32_f16_e32 v16, v36
	v_pk_fma_f32 v[20:21], v[20:21], v[24:25], v[22:23]
	v_rcp_f32_e32 v6, v6
	v_rcp_f32_e32 v7, v7
	v_exp_f32_e32 v2, v2
	v_exp_f32_e32 v3, v3
	v_cvt_f32_f16_sdwa v25, v37 dst_sel:DWORD dst_unused:UNUSED_PAD src0_sel:WORD_1
	v_cvt_f32_f16_e32 v24, v37
	v_lshlrev_b32_e32 v22, 16, v32
	v_and_b32_e32 v23, 0xffff0000, v32
	v_add_f32_e32 v0, 1.0, v0
	v_add_f32_e32 v1, 1.0, v1
	v_pk_fma_f32 v[4:5], v[4:5], v[22:23], v[16:17]
	v_lshlrev_b32_e32 v16, 16, v33
	v_and_b32_e32 v17, 0xffff0000, v33
	v_rcp_f32_e32 v0, v0
	v_rcp_f32_e32 v1, v1
	v_add_f32_e32 v2, 1.0, v2
	v_add_f32_e32 v3, 1.0, v3
	v_pk_fma_f32 v[6:7], v[6:7], v[16:17], v[24:25]
	v_cvt_f32_f16_sdwa v17, v38 dst_sel:DWORD dst_unused:UNUSED_PAD src0_sel:WORD_1
	v_cvt_f32_f16_e32 v16, v38
	v_rcp_f32_e32 v2, v2
	v_rcp_f32_e32 v3, v3
	v_cvt_f32_f16_sdwa v25, v39 dst_sel:DWORD dst_unused:UNUSED_PAD src0_sel:WORD_1
	v_cvt_f32_f16_e32 v24, v39
	v_lshlrev_b32_e32 v22, 16, v34
	v_and_b32_e32 v23, 0xffff0000, v34
	v_pk_fma_f32 v[16:17], v[0:1], v[22:23], v[16:17]
	v_lshlrev_b32_e32 v0, 16, v35
	v_and_b32_e32 v1, 0xffff0000, v35
	v_pk_fma_f32 v[22:23], v[2:3], v[0:1], v[24:25]
	v_pk_mul_f32 v[0:1], v[4:5], v[4:5]
	v_pk_mul_f32 v[2:3], v[6:7], v[6:7]
	v_cvt_pk_f16_f32 v10, v18, v19
	v_cvt_pk_f16_f32 v11, v20, v21
	v_pk_mul_f32 v[18:19], v[18:19], v[18:19]
	v_pk_mul_f32 v[20:21], v[20:21], v[20:21]
	v_add_f32_e32 v2, v2, v3
	v_add_f32_e32 v0, v0, v1
	v_cvt_pk_f16_f32 v8, v12, v13
	v_cvt_pk_f16_f32 v9, v14, v15
	v_pk_mul_f32 v[12:13], v[12:13], v[12:13]
	v_pk_mul_f32 v[14:15], v[14:15], v[14:15]
	v_pk_mul_f32 v[24:25], v[16:17], v[16:17]
	v_pk_mul_f32 v[26:27], v[22:23], v[22:23]
	v_add_f32_e32 v0, v0, v2
	v_add_f32_e32 v1, v20, v21
	v_add_f32_e32 v2, v18, v19
	v_add_f32_e32 v26, v26, v27
	v_add_f32_e32 v24, v24, v25
	v_add_f32_e32 v1, v2, v1
	v_add_f32_e32 v2, v14, v15
	v_add_f32_e32 v3, v12, v13
	v_add_f32_e32 v24, v24, v26
	v_add_f32_e32 v2, v3, v2
	v_add_f32_e32 v0, v0, v24
	v_add_f32_e32 v1, v2, v1
	v_add_f32_e32 v3, v1, v0
	ds_bpermute_b32 v14, v159, v3
	v_lshl_add_u64 v[0:1], v[58:59], 1, s[56:57]
	v_lshl_add_u64 v[12:13], v[148:149], 1, v[0:1]
	v_cvt_pk_f16_f32 v2, v4, v5
	v_cvt_pk_f16_f32 v4, v16, v17
	s_waitcnt lgkmcnt(0)
	v_add_f32_e32 v0, v3, v14
	ds_bpermute_b32 v1, v158, v0
	v_cvt_pk_f16_f32 v3, v6, v7
	v_cvt_pk_f16_f32 v5, v22, v23
	global_store_dwordx4 v[12:13], v[8:11], off
	global_store_dwordx4 v[12:13], v[2:5], off offset:256
	s_and_saveexec_b64 s[0:1], vcc
	s_cbranch_execz .LBB0_1299
	v_lshlrev_b64 v[2:3], 6, v[56:57]
	v_lshl_add_u64 v[2:3], s[6:7], 0, v[2:3]
	s_lshl_b32 s62, s11, 2
	v_lshl_add_u64 v[2:3], v[2:3], 0, s[62:63]
	s_lshl_b32 s62, s35, 2
	v_lshl_add_u64 v[2:3], v[2:3], 0, s[62:63]
	s_waitcnt lgkmcnt(0)
	v_add_f32_e32 v0, v0, v1
	global_store_dword v[2:3], v0, off
